# K-loop: blocks C1+C2 of each K-step run back to back under one barrier pair (6 barriers per K-step instead of 8): B1 reads hoisted to L1, B(b,0) DMA moved one segment later, waits re-derived; 11 of 14
# baseline (speedup 1.0000x reference)
.LBB0_366:
	s_add_i32 s73, s64, 0x18000
	s_lshl_b32 s4, s4, 12
	v_lshl_add_u64 v[8:9], v[8:9], 0, s[24:25]
	s_mov_b32 m0, s73
	s_add_i32 s74, s64, 0x1a000
	s_lshl_b32 s72, s5, 13
	s_and_b32 s10, s4, 0x3000
	s_waitcnt vmcnt(2)
	s_barrier
	global_load_lds_dwordx4 v[8:9], off
	v_lshl_add_u64 v[6:7], v[6:7], 0, s[24:25]
	s_mov_b32 m0, s74
	s_add_i32 s75, s64, 0x8000
	s_add_i32 s76, s64, 0xa000
	global_load_lds_dwordx4 v[6:7], off
	v_lshl_add_u64 v[4:5], v[4:5], 0, s[24:25]
	s_mov_b32 m0, s75
	s_add_u32 s4, s6, 0x20080
	global_load_lds_dwordx4 v[4:5], off
	v_lshl_add_u64 v[2:3], v[2:3], 0, s[24:25]
	s_mov_b32 m0, s76
	s_addc_u32 s5, s7, 0
	s_add_i32 s77, s64, 0x1c000
	global_load_lds_dwordx4 v[2:3], off
	v_lshl_add_u64 v[2:3], s[4:5], 0, v[0:1]
	s_mov_b32 m0, s77
	s_add_i32 s78, s64, 0x1e000
	global_load_lds_dwordx4 v[2:3], off
	v_lshl_add_u64 v[2:3], s[4:5], 0, v[146:147]
	s_mov_b32 m0, s78
	s_add_u32 s79, s20, 0x4d000000
	global_load_lds_dwordx4 v[2:3], off
	v_and_b32_e32 v2, 15, v12
	v_and_b32_e32 v3, 48, v12
	v_lshl_or_b32 v2, v2, 6, v3
	v_lshlrev_b32_e32 v3, 2, v12
	v_and_b32_e32 v3, 32, v3
	v_xad_u32 v164, v2, v3, 0
	v_add_u32_e32 v2, s10, v164
	v_add_u32_e32 v165, 0x10000, v2
	v_add_u32_e32 v166, 0x10400, v2
	v_add_u32_e32 v167, 0x10800, v2
	v_add_u32_e32 v168, 0x10c00, v2
	v_add_u32_e32 v169, 0x14000, v2
	v_add_u32_e32 v170, 0x14400, v2
	v_add_u32_e32 v171, 0x14800, v2
	v_add_u32_e32 v172, 0x14c00, v2
	v_add_u32_e32 v173, 0x18000, v2
	v_add_u32_e32 v174, 0x18400, v2
	v_add_u32_e32 v175, 0x18800, v2
	v_add_u32_e32 v176, 0x18c00, v2
	v_add_u32_e32 v177, 0x1c000, v2
	v_add_u32_e32 v178, 0x1c400, v2
	v_add_u32_e32 v179, 0x1c800, v2
	v_add_u32_e32 v180, 0x1cc00, v2
	v_lshlrev_b32_e32 v2, 13, v15
	v_and_b32_e32 v2, 0xffffc000, v2
	v_lshl_add_u32 v2, v14, 10, v2
	v_and_b32_e32 v3, 1, v15
	v_lshl_or_b32 v2, v3, 6, v2
	v_lshl_add_u32 v152, v16, 1, v2
	v_lshlrev_b32_e32 v2, 13, v10
	v_and_b32_e32 v2, 0xffffc000, v2
	s_waitcnt vmcnt(6)
	s_addc_u32 s80, s21, 0
	v_lshl_add_u32 v2, v11, 10, v2
	v_and_b32_e32 v3, 1, v10
	s_add_u32 s34, s20, 0x61000000
	v_lshl_or_b32 v2, v3, 6, v2
	s_addc_u32 s35, s21, 0
	v_mov_b32_e32 v153, v1
	v_lshl_add_u32 v154, v13, 1, v2
	v_mov_b32_e32 v155, v1
	s_mov_b32 s81, 0
	v_readlane_b32 s82, v253, 14
	v_readlane_b32 s46, v253, 61
	s_barrier
	v_readlane_b32 s47, v253, 62
	s_branch .LBB0_368

.LBB0_374:
	v_mov_b64_e32 v[2:3], 0x800
	s_ashr_i32 s45, s44, 31
	v_cmp_lt_i64_e32 vcc, s[10:11], v[2:3]
	s_lshl_b64 s[10:11], s[44:45], 18
	s_add_u32 s48, s27, s10
	s_addc_u32 s49, s60, s11
	s_and_b64 s[10:11], vcc, exec
	ds_read_b128 v[2:5], v165
	ds_read_b128 v[6:9], v166
	ds_read_b128 v[10:13], v167
	ds_read_b128 v[14:17], v168
	s_cselect_b32 s12, s49, s9
	s_cselect_b32 s13, s48, s8
	s_ashr_i32 s43, s42, 31
	s_lshl_b64 s[10:11], s[42:43], 18
	s_add_u32 s50, s62, s10
	s_addc_u32 s51, s63, s11
	s_and_b64 s[10:11], vcc, exec
	s_cselect_b32 s28, s51, s7
	s_cselect_b32 s43, s50, s6
	s_add_u32 s10, s8, 0x20080
	s_addc_u32 s11, s9, 0
	s_add_i32 s45, s64, 0xc000
	v_add_u32_e32 v181, s72, v164
	v_lshl_add_u64 v[50:51], s[10:11], 0, v[150:151]
	s_mov_b32 m0, s45
	s_add_i32 s47, s64, 0xe000
	ds_read_b128 v[18:21], v181
	ds_read_b128 v[22:25], v181 offset:1024
	ds_read_b128 v[26:29], v181 offset:2048
	ds_read_b128 v[30:33], v181 offset:3072
	ds_read_b128 v[34:37], v181 offset:4096
	ds_read_b128 v[38:41], v181 offset:5120
	ds_read_b128 v[42:45], v181 offset:6144
	ds_read_b128 v[46:49], v181 offset:7168
	global_load_lds_dwordx4 v[50:51], off
	v_lshl_add_u64 v[50:51], s[10:11], 0, v[148:149]
	s_mov_b32 m0, s47
	s_nop 0
	global_load_lds_dwordx4 v[50:51], off
	ds_read_b128 v[188:191], v169
	ds_read_b128 v[192:195], v170
	ds_read_b128 v[196:199], v171
	ds_read_b128 v[200:203], v172
	s_waitcnt lgkmcnt(4)
	s_waitcnt vmcnt(8)
	s_barrier
	s_waitcnt lgkmcnt(0)
	s_setprio 1
	s_waitcnt lgkmcnt(0)
	v_mfma_f32_16x16x128_f8f6f4 v[142:145], v[2:9], v[18:25], 0
	v_mfma_f32_16x16x128_f8f6f4 v[138:141], v[10:17], v[18:25], 0
	v_mfma_f32_16x16x128_f8f6f4 v[126:129], v[2:9], v[26:33], 0
	v_mfma_f32_16x16x128_f8f6f4 v[122:125], v[10:17], v[26:33], 0
	v_mfma_f32_16x16x128_f8f6f4 v[110:113], v[2:9], v[34:41], 0
	v_mfma_f32_16x16x128_f8f6f4 v[106:109], v[10:17], v[34:41], 0
	v_mfma_f32_16x16x128_f8f6f4 v[94:97], v[2:9], v[42:49], 0
	v_mfma_f32_16x16x128_f8f6f4 v[90:93], v[10:17], v[42:49], 0
	v_lshl_add_u64 v[160:161], s[6:7], 0, v[0:1]
	s_mov_b64 s[10:11], 0x100
	v_lshl_add_u64 v[162:163], s[6:7], 0, v[146:147]
	v_mfma_f32_16x16x128_f8f6f4 v[134:137], v[188:195], v[18:25], 0
	v_mfma_f32_16x16x128_f8f6f4 v[130:133], v[196:203], v[18:25], 0
	v_mfma_f32_16x16x128_f8f6f4 v[118:121], v[188:195], v[26:33], 0
	v_mfma_f32_16x16x128_f8f6f4 v[114:117], v[196:203], v[26:33], 0
	v_mfma_f32_16x16x128_f8f6f4 v[102:105], v[188:195], v[34:41], 0
	v_mfma_f32_16x16x128_f8f6f4 v[98:101], v[196:203], v[34:41], 0
	v_mfma_f32_16x16x128_f8f6f4 v[86:89], v[188:195], v[42:49], 0
	v_mfma_f32_16x16x128_f8f6f4 v[82:85], v[196:203], v[42:49], 0
	s_setprio 0
	v_lshl_add_u64 v[156:157], s[8:9], 0, v[150:151]
	s_mov_b32 m0, s64
	v_lshl_add_u64 v[26:27], v[156:157], 0, s[10:11]
	v_lshl_add_u64 v[158:159], s[8:9], 0, v[148:149]
	s_barrier
	ds_read_b128 v[18:21], v181 offset:16384
	ds_read_b128 v[22:25], v181 offset:17408
	ds_read_b128 v[34:37], v181 offset:18432
	ds_read_b128 v[38:41], v181 offset:19456
	ds_read_b128 v[204:207], v181 offset:20480
	ds_read_b128 v[208:211], v181 offset:21504
	ds_read_b128 v[212:215], v181 offset:22528
	ds_read_b128 v[216:219], v181 offset:23552
	global_load_lds_dwordx4 v[26:27], off
	v_lshl_add_u64 v[26:27], v[158:159], 0, s[10:11]
	s_mov_b32 m0, s67
	s_nop 0
	global_load_lds_dwordx4 v[26:27], off
	s_mov_b32 m0, s65
	v_lshl_add_u64 v[50:51], v[160:161], 0, s[10:11]
	global_load_lds_dwordx4 v[50:51], off
	v_lshl_add_u64 v[50:51], v[162:163], 0, s[10:11]
	s_mov_b32 m0, s66
	s_nop 0
	global_load_lds_dwordx4 v[50:51], off
	s_barrier
	s_waitcnt lgkmcnt(0)
	s_setprio 1
	s_waitcnt lgkmcnt(0)
	v_mfma_f32_16x16x128_f8f6f4 v[78:81], v[2:9], v[18:25], 0
	v_mfma_f32_16x16x128_f8f6f4 v[74:77], v[10:17], v[18:25], 0
	v_mfma_f32_16x16x128_f8f6f4 v[62:65], v[2:9], v[34:41], 0
	v_mfma_f32_16x16x128_f8f6f4 v[58:61], v[10:17], v[34:41], 0
	v_mfma_f32_16x16x128_f8f6f4 v[46:49], v[2:9], v[204:211], 0
	v_mfma_f32_16x16x128_f8f6f4 v[42:45], v[10:17], v[204:211], 0
	v_mfma_f32_16x16x128_f8f6f4 v[30:33], v[2:9], v[212:219], 0
	v_mfma_f32_16x16x128_f8f6f4 v[26:29], v[10:17], v[212:219], 0
	s_setprio 0
	s_barrier
	s_add_u32 s10, s6, 0x20100
	s_addc_u32 s11, s7, 0
	s_mov_b32 m0, s68
	v_lshl_add_u64 v[2:3], s[10:11], 0, v[0:1]
	global_load_lds_dwordx4 v[2:3], off
	v_lshl_add_u64 v[2:3], s[10:11], 0, v[146:147]
	s_mov_b32 m0, s69
	s_nop 0
	global_load_lds_dwordx4 v[2:3], off
	s_waitcnt vmcnt(8)
	s_barrier
	s_setprio 1
	v_mfma_f32_16x16x128_f8f6f4 v[70:73], v[188:195], v[18:25], 0
	v_mfma_f32_16x16x128_f8f6f4 v[66:69], v[196:203], v[18:25], 0
	v_mfma_f32_16x16x128_f8f6f4 v[54:57], v[188:195], v[34:41], 0
	v_mfma_f32_16x16x128_f8f6f4 v[50:53], v[196:203], v[34:41], 0
	v_mfma_f32_16x16x128_f8f6f4 v[38:41], v[188:195], v[204:211], 0
	v_mfma_f32_16x16x128_f8f6f4 v[34:37], v[196:203], v[204:211], 0
	v_mfma_f32_16x16x128_f8f6f4 v[22:25], v[188:195], v[212:219], 0
	v_mfma_f32_16x16x128_f8f6f4 v[18:21], v[196:203], v[212:219], 0
	s_setprio 0
	s_barrier
	ds_read_b128 v[2:5], v173
	ds_read_b128 v[6:9], v174
	ds_read_b128 v[10:13], v175
	ds_read_b128 v[14:17], v176
	s_add_u32 s10, s8, 0x20100
	s_addc_u32 s11, s9, 0
	s_mov_b32 m0, s70
	v_lshl_add_u64 v[182:183], s[10:11], 0, v[150:151]
	ds_read_b128 v[188:191], v181 offset:32768
	ds_read_b128 v[192:195], v181 offset:33792
	ds_read_b128 v[196:199], v181 offset:34816
	ds_read_b128 v[200:203], v181 offset:35840
	ds_read_b128 v[204:207], v181 offset:36864
	ds_read_b128 v[208:211], v181 offset:37888
	ds_read_b128 v[212:215], v181 offset:38912
	ds_read_b128 v[216:219], v181 offset:39936
	global_load_lds_dwordx4 v[182:183], off
	v_lshl_add_u64 v[182:183], s[10:11], 0, v[148:149]
	s_mov_b32 m0, s71
	s_nop 0
	global_load_lds_dwordx4 v[182:183], off
	ds_read_b128 v[232:235], v177
	ds_read_b128 v[236:239], v178
	ds_read_b128 v[240:243], v179
	ds_read_b128 v[244:247], v180
	s_waitcnt lgkmcnt(4)
	s_waitcnt vmcnt(8)
	s_barrier
	s_waitcnt lgkmcnt(0)
	s_setprio 1
	s_waitcnt lgkmcnt(0)
	v_mfma_f32_16x16x128_f8f6f4 v[142:145], v[2:9], v[188:195], v[142:145]
	v_mfma_f32_16x16x128_f8f6f4 v[138:141], v[10:17], v[188:195], v[138:141]
	v_mfma_f32_16x16x128_f8f6f4 v[126:129], v[2:9], v[196:203], v[126:129]
	v_mfma_f32_16x16x128_f8f6f4 v[122:125], v[10:17], v[196:203], v[122:125]
	v_mfma_f32_16x16x128_f8f6f4 v[110:113], v[2:9], v[204:211], v[110:113]
	v_mfma_f32_16x16x128_f8f6f4 v[106:109], v[10:17], v[204:211], v[106:109]
	v_mfma_f32_16x16x128_f8f6f4 v[94:97], v[2:9], v[212:219], v[94:97]
	v_mfma_f32_16x16x128_f8f6f4 v[90:93], v[10:17], v[212:219], v[90:93]
	s_mov_b64 s[10:11], 0x180
	v_mfma_f32_16x16x128_f8f6f4 v[134:137], v[232:239], v[188:195], v[134:137]
	v_mfma_f32_16x16x128_f8f6f4 v[130:133], v[240:247], v[188:195], v[130:133]
	v_mfma_f32_16x16x128_f8f6f4 v[118:121], v[232:239], v[196:203], v[118:121]
	v_mfma_f32_16x16x128_f8f6f4 v[114:117], v[240:247], v[196:203], v[114:117]
	v_mfma_f32_16x16x128_f8f6f4 v[102:105], v[232:239], v[204:211], v[102:105]
	v_mfma_f32_16x16x128_f8f6f4 v[98:101], v[240:247], v[204:211], v[98:101]
	v_mfma_f32_16x16x128_f8f6f4 v[86:89], v[232:239], v[212:219], v[86:89]
	v_mfma_f32_16x16x128_f8f6f4 v[82:85], v[240:247], v[212:219], v[82:85]
	s_setprio 0
	s_mov_b32 m0, s75
	v_lshl_add_u64 v[156:157], v[156:157], 0, s[10:11]
	s_barrier
	ds_read_b128 v[188:191], v181 offset:49152
	ds_read_b128 v[192:195], v181 offset:50176
	ds_read_b128 v[196:199], v181 offset:51200
	ds_read_b128 v[200:203], v181 offset:52224
	ds_read_b128 v[204:207], v181 offset:53248
	ds_read_b128 v[208:211], v181 offset:54272
	ds_read_b128 v[212:215], v181 offset:55296
	ds_read_b128 v[216:219], v181 offset:56320
	global_load_lds_dwordx4 v[156:157], off
	v_lshl_add_u64 v[156:157], v[158:159], 0, s[10:11]
	s_mov_b32 m0, s76
	s_nop 0
	global_load_lds_dwordx4 v[156:157], off
	s_mov_b32 m0, s73
	v_lshl_add_u64 v[160:161], v[160:161], 0, s[10:11]
	global_load_lds_dwordx4 v[160:161], off
	v_lshl_add_u64 v[160:161], v[162:163], 0, s[10:11]
	s_mov_b32 m0, s74
	s_nop 0
	global_load_lds_dwordx4 v[160:161], off
	s_barrier
	s_waitcnt lgkmcnt(0)
	s_setprio 1
	s_waitcnt lgkmcnt(0)
	v_mfma_f32_16x16x128_f8f6f4 v[78:81], v[2:9], v[188:195], v[78:81]
	v_mfma_f32_16x16x128_f8f6f4 v[74:77], v[10:17], v[188:195], v[74:77]
	v_mfma_f32_16x16x128_f8f6f4 v[62:65], v[2:9], v[196:203], v[62:65]
	v_mfma_f32_16x16x128_f8f6f4 v[58:61], v[10:17], v[196:203], v[58:61]
	v_mfma_f32_16x16x128_f8f6f4 v[46:49], v[2:9], v[204:211], v[46:49]
	v_mfma_f32_16x16x128_f8f6f4 v[42:45], v[10:17], v[204:211], v[42:45]
	v_mfma_f32_16x16x128_f8f6f4 v[30:33], v[2:9], v[212:219], v[30:33]
	v_mfma_f32_16x16x128_f8f6f4 v[26:29], v[10:17], v[212:219], v[26:29]
	s_setprio 0
	s_barrier
	s_add_u32 s10, s6, 0x20180
	s_addc_u32 s11, s7, 0
	s_mov_b32 m0, s77
	v_lshl_add_u64 v[2:3], s[10:11], 0, v[0:1]
	global_load_lds_dwordx4 v[2:3], off
	v_lshl_add_u64 v[2:3], s[10:11], 0, v[146:147]
	s_mov_b32 m0, s78
	s_nop 0
	global_load_lds_dwordx4 v[2:3], off
	s_waitcnt vmcnt(8)
	s_barrier
	s_setprio 1
	v_mfma_f32_16x16x128_f8f6f4 v[70:73], v[232:239], v[188:195], v[70:73]
	v_mfma_f32_16x16x128_f8f6f4 v[66:69], v[240:247], v[188:195], v[66:69]
	v_mfma_f32_16x16x128_f8f6f4 v[54:57], v[232:239], v[196:203], v[54:57]
	v_mfma_f32_16x16x128_f8f6f4 v[50:53], v[240:247], v[196:203], v[50:53]
	v_mfma_f32_16x16x128_f8f6f4 v[38:41], v[232:239], v[204:211], v[38:41]
	v_mfma_f32_16x16x128_f8f6f4 v[34:37], v[240:247], v[204:211], v[34:37]
	v_mfma_f32_16x16x128_f8f6f4 v[22:25], v[232:239], v[212:219], v[22:25]
	v_mfma_f32_16x16x128_f8f6f4 v[18:21], v[240:247], v[212:219], v[18:21]
	s_setprio 0
	s_add_u32 s8, s8, 0x20180
	s_addc_u32 s9, s9, 0
	s_add_u32 s52, s6, 0x200
	s_addc_u32 s53, s7, 0
	s_mov_b32 s54, 0
	s_barrier
.LBB0_375:
	ds_read_b128 v[10:13], v165
	ds_read_b128 v[14:17], v166
	ds_read_b128 v[156:159], v167
	ds_read_b128 v[160:163], v168
	s_add_u32 s6, s8, 0xfffe0080
	s_addc_u32 s7, s9, -1
	s_cmp_eq_u32 s54, 4
	s_cselect_b32 s11, s12, s7
	s_cselect_b32 s10, s13, s6
	s_cselect_b32 s7, s28, s53
	s_cselect_b32 s6, s43, s52
	s_mov_b32 m0, s45
	v_lshl_add_u64 v[2:3], s[8:9], 0, v[152:153]
	ds_read_b128 v[188:191], v181
	ds_read_b128 v[192:195], v181 offset:1024
	ds_read_b128 v[196:199], v181 offset:2048
	ds_read_b128 v[200:203], v181 offset:3072
	ds_read_b128 v[204:207], v181 offset:4096
	ds_read_b128 v[208:211], v181 offset:5120
	ds_read_b128 v[212:215], v181 offset:6144
	ds_read_b128 v[216:219], v181 offset:7168
	global_load_lds_dwordx4 v[2:3], off
	v_lshl_add_u64 v[2:3], s[8:9], 0, v[154:155]
	s_mov_b32 m0, s47
	s_nop 0
	global_load_lds_dwordx4 v[2:3], off
	ds_read_b128 v[232:235], v169
	ds_read_b128 v[236:239], v170
	ds_read_b128 v[240:243], v171
	ds_read_b128 v[244:247], v172
	s_waitcnt lgkmcnt(4)
	s_waitcnt vmcnt(8)
	s_barrier
	s_waitcnt lgkmcnt(0)
	s_setprio 1
	s_waitcnt lgkmcnt(0)
	v_mfma_f32_16x16x128_f8f6f4 v[142:145], v[10:17], v[188:195], v[142:145]
	v_mfma_f32_16x16x128_f8f6f4 v[138:141], v[156:163], v[188:195], v[138:141]
	v_mfma_f32_16x16x128_f8f6f4 v[126:129], v[10:17], v[196:203], v[126:129]
	v_mfma_f32_16x16x128_f8f6f4 v[122:125], v[156:163], v[196:203], v[122:125]
	v_mfma_f32_16x16x128_f8f6f4 v[110:113], v[10:17], v[204:211], v[110:113]
	v_mfma_f32_16x16x128_f8f6f4 v[106:109], v[156:163], v[204:211], v[106:109]
	v_mfma_f32_16x16x128_f8f6f4 v[94:97], v[10:17], v[212:219], v[94:97]
	v_mfma_f32_16x16x128_f8f6f4 v[90:93], v[156:163], v[212:219], v[90:93]
	v_mfma_f32_16x16x128_f8f6f4 v[134:137], v[232:239], v[188:195], v[134:137]
	v_mfma_f32_16x16x128_f8f6f4 v[130:133], v[240:247], v[188:195], v[130:133]
	v_mfma_f32_16x16x128_f8f6f4 v[118:121], v[232:239], v[196:203], v[118:121]
	v_mfma_f32_16x16x128_f8f6f4 v[114:117], v[240:247], v[196:203], v[114:117]
	v_mfma_f32_16x16x128_f8f6f4 v[102:105], v[232:239], v[204:211], v[102:105]
	v_mfma_f32_16x16x128_f8f6f4 v[98:101], v[240:247], v[204:211], v[98:101]
	v_mfma_f32_16x16x128_f8f6f4 v[86:89], v[232:239], v[212:219], v[86:89]
	v_mfma_f32_16x16x128_f8f6f4 v[82:85], v[240:247], v[212:219], v[82:85]
	s_setprio 0
	s_mov_b32 m0, s64
	v_lshl_add_u64 v[2:3], s[10:11], 0, v[150:151]
	s_barrier
	ds_read_b128 v[188:191], v181 offset:16384
	ds_read_b128 v[192:195], v181 offset:17408
	ds_read_b128 v[196:199], v181 offset:18432
	ds_read_b128 v[200:203], v181 offset:19456
	ds_read_b128 v[204:207], v181 offset:20480
	ds_read_b128 v[208:211], v181 offset:21504
	ds_read_b128 v[212:215], v181 offset:22528
	ds_read_b128 v[216:219], v181 offset:23552
	global_load_lds_dwordx4 v[2:3], off
	v_lshl_add_u64 v[4:5], s[10:11], 0, v[148:149]
	s_mov_b32 m0, s67
	s_nop 0
	global_load_lds_dwordx4 v[4:5], off
	s_mov_b32 m0, s65
	v_lshl_add_u64 v[6:7], s[6:7], 0, v[0:1]
	global_load_lds_dwordx4 v[6:7], off
	v_lshl_add_u64 v[8:9], s[6:7], 0, v[146:147]
	s_mov_b32 m0, s66
	s_nop 0
	global_load_lds_dwordx4 v[8:9], off
	s_barrier
	s_waitcnt lgkmcnt(0)
	s_setprio 1
	s_waitcnt lgkmcnt(0)
	v_mfma_f32_16x16x128_f8f6f4 v[78:81], v[10:17], v[188:195], v[78:81]
	v_mfma_f32_16x16x128_f8f6f4 v[74:77], v[156:163], v[188:195], v[74:77]
	v_mfma_f32_16x16x128_f8f6f4 v[62:65], v[10:17], v[196:203], v[62:65]
	v_mfma_f32_16x16x128_f8f6f4 v[58:61], v[156:163], v[196:203], v[58:61]
	v_mfma_f32_16x16x128_f8f6f4 v[46:49], v[10:17], v[204:211], v[46:49]
	v_mfma_f32_16x16x128_f8f6f4 v[42:45], v[156:163], v[204:211], v[42:45]
	v_mfma_f32_16x16x128_f8f6f4 v[30:33], v[10:17], v[212:219], v[30:33]
	v_mfma_f32_16x16x128_f8f6f4 v[26:29], v[156:163], v[212:219], v[26:29]
	s_setprio 0
	s_barrier
	s_add_u32 s56, s6, 0x20000
	s_addc_u32 s57, s7, 0
	s_mov_b32 m0, s68
	v_lshl_add_u64 v[10:11], s[56:57], 0, v[0:1]
	global_load_lds_dwordx4 v[10:11], off
	v_lshl_add_u64 v[10:11], s[56:57], 0, v[146:147]
	s_mov_b32 m0, s69
	s_nop 0
	global_load_lds_dwordx4 v[10:11], off
	s_waitcnt vmcnt(8)
	s_barrier
	s_setprio 1
	v_mfma_f32_16x16x128_f8f6f4 v[70:73], v[232:239], v[188:195], v[70:73]
	v_mfma_f32_16x16x128_f8f6f4 v[66:69], v[240:247], v[188:195], v[66:69]
	v_mfma_f32_16x16x128_f8f6f4 v[54:57], v[232:239], v[196:203], v[54:57]
	v_mfma_f32_16x16x128_f8f6f4 v[50:53], v[240:247], v[196:203], v[50:53]
	v_mfma_f32_16x16x128_f8f6f4 v[38:41], v[232:239], v[204:211], v[38:41]
	v_mfma_f32_16x16x128_f8f6f4 v[34:37], v[240:247], v[204:211], v[34:37]
	v_mfma_f32_16x16x128_f8f6f4 v[22:25], v[232:239], v[212:219], v[22:25]
	v_mfma_f32_16x16x128_f8f6f4 v[18:21], v[240:247], v[212:219], v[18:21]
	s_setprio 0
	s_barrier
	ds_read_b128 v[10:13], v173
	ds_read_b128 v[14:17], v174
	ds_read_b128 v[156:159], v175
	ds_read_b128 v[160:163], v176
	s_add_u32 s10, s10, 0x20000
	s_addc_u32 s11, s11, 0
	s_mov_b32 m0, s70
	v_lshl_add_u64 v[182:183], s[10:11], 0, v[150:151]
	ds_read_b128 v[188:191], v181 offset:32768
	ds_read_b128 v[192:195], v181 offset:33792
	ds_read_b128 v[196:199], v181 offset:34816
	ds_read_b128 v[200:203], v181 offset:35840
	ds_read_b128 v[204:207], v181 offset:36864
	ds_read_b128 v[208:211], v181 offset:37888
	ds_read_b128 v[212:215], v181 offset:38912
	ds_read_b128 v[216:219], v181 offset:39936
	global_load_lds_dwordx4 v[182:183], off
	v_lshl_add_u64 v[182:183], s[10:11], 0, v[148:149]
	s_mov_b32 m0, s71
	s_nop 0
	global_load_lds_dwordx4 v[182:183], off
	ds_read_b128 v[232:235], v177
	ds_read_b128 v[236:239], v178
	ds_read_b128 v[240:243], v179
	ds_read_b128 v[244:247], v180
	s_waitcnt lgkmcnt(4)
	s_waitcnt vmcnt(8)
	s_barrier
	s_waitcnt lgkmcnt(0)
	s_setprio 1
	s_waitcnt lgkmcnt(0)
	v_mfma_f32_16x16x128_f8f6f4 v[142:145], v[10:17], v[188:195], v[142:145]
	v_mfma_f32_16x16x128_f8f6f4 v[138:141], v[156:163], v[188:195], v[138:141]
	v_mfma_f32_16x16x128_f8f6f4 v[126:129], v[10:17], v[196:203], v[126:129]
	v_mfma_f32_16x16x128_f8f6f4 v[122:125], v[156:163], v[196:203], v[122:125]
	v_mfma_f32_16x16x128_f8f6f4 v[110:113], v[10:17], v[204:211], v[110:113]
	v_mfma_f32_16x16x128_f8f6f4 v[106:109], v[156:163], v[204:211], v[106:109]
	v_mfma_f32_16x16x128_f8f6f4 v[94:97], v[10:17], v[212:219], v[94:97]
	v_mfma_f32_16x16x128_f8f6f4 v[90:93], v[156:163], v[212:219], v[90:93]
	v_mfma_f32_16x16x128_f8f6f4 v[134:137], v[232:239], v[188:195], v[134:137]
	v_mfma_f32_16x16x128_f8f6f4 v[130:133], v[240:247], v[188:195], v[130:133]
	v_mfma_f32_16x16x128_f8f6f4 v[118:121], v[232:239], v[196:203], v[118:121]
	v_mfma_f32_16x16x128_f8f6f4 v[114:117], v[240:247], v[196:203], v[114:117]
	v_mfma_f32_16x16x128_f8f6f4 v[102:105], v[232:239], v[204:211], v[102:105]
	v_mfma_f32_16x16x128_f8f6f4 v[98:101], v[240:247], v[204:211], v[98:101]
	v_mfma_f32_16x16x128_f8f6f4 v[86:89], v[232:239], v[212:219], v[86:89]
	v_mfma_f32_16x16x128_f8f6f4 v[82:85], v[240:247], v[212:219], v[82:85]
	s_setprio 0
	s_mov_b32 m0, s75
	v_lshl_add_u64 v[2:3], v[2:3], 0, s[24:25]
	s_barrier
	ds_read_b128 v[188:191], v181 offset:49152
	ds_read_b128 v[192:195], v181 offset:50176
	ds_read_b128 v[196:199], v181 offset:51200
	ds_read_b128 v[200:203], v181 offset:52224
	ds_read_b128 v[204:207], v181 offset:53248
	ds_read_b128 v[208:211], v181 offset:54272
	ds_read_b128 v[212:215], v181 offset:55296
	ds_read_b128 v[216:219], v181 offset:56320
	global_load_lds_dwordx4 v[2:3], off
	v_lshl_add_u64 v[2:3], v[4:5], 0, s[24:25]
	s_mov_b32 m0, s76
	s_nop 0
	global_load_lds_dwordx4 v[2:3], off
	s_mov_b32 m0, s73
	v_lshl_add_u64 v[6:7], v[6:7], 0, s[24:25]
	global_load_lds_dwordx4 v[6:7], off
	v_lshl_add_u64 v[6:7], v[8:9], 0, s[24:25]
	s_mov_b32 m0, s74
	s_nop 0
	global_load_lds_dwordx4 v[6:7], off
	s_barrier
	s_waitcnt lgkmcnt(0)
	s_setprio 1
	s_waitcnt lgkmcnt(0)
	v_mfma_f32_16x16x128_f8f6f4 v[78:81], v[10:17], v[188:195], v[78:81]
	v_mfma_f32_16x16x128_f8f6f4 v[74:77], v[156:163], v[188:195], v[74:77]
	v_mfma_f32_16x16x128_f8f6f4 v[62:65], v[10:17], v[196:203], v[62:65]
	v_mfma_f32_16x16x128_f8f6f4 v[58:61], v[156:163], v[196:203], v[58:61]
	v_mfma_f32_16x16x128_f8f6f4 v[46:49], v[10:17], v[204:211], v[46:49]
	v_mfma_f32_16x16x128_f8f6f4 v[42:45], v[156:163], v[204:211], v[42:45]
	v_mfma_f32_16x16x128_f8f6f4 v[30:33], v[10:17], v[212:219], v[30:33]
	v_mfma_f32_16x16x128_f8f6f4 v[26:29], v[156:163], v[212:219], v[26:29]
	s_setprio 0
	s_barrier
	s_add_u32 s6, s6, 0x20080
	s_addc_u32 s7, s7, 0
	s_mov_b32 m0, s77
	v_lshl_add_u64 v[2:3], s[6:7], 0, v[0:1]
	global_load_lds_dwordx4 v[2:3], off
	v_lshl_add_u64 v[2:3], s[6:7], 0, v[146:147]
	s_mov_b32 m0, s78
	s_nop 0
	global_load_lds_dwordx4 v[2:3], off
	s_waitcnt vmcnt(8)
	s_barrier
	s_setprio 1
	v_mfma_f32_16x16x128_f8f6f4 v[70:73], v[232:239], v[188:195], v[70:73]
	v_mfma_f32_16x16x128_f8f6f4 v[66:69], v[240:247], v[188:195], v[66:69]
	v_mfma_f32_16x16x128_f8f6f4 v[54:57], v[232:239], v[196:203], v[54:57]
	v_mfma_f32_16x16x128_f8f6f4 v[50:53], v[240:247], v[196:203], v[50:53]
	v_mfma_f32_16x16x128_f8f6f4 v[38:41], v[232:239], v[204:211], v[38:41]
	v_mfma_f32_16x16x128_f8f6f4 v[34:37], v[240:247], v[204:211], v[34:37]
	v_mfma_f32_16x16x128_f8f6f4 v[22:25], v[232:239], v[212:219], v[22:25]
	v_mfma_f32_16x16x128_f8f6f4 v[18:21], v[240:247], v[212:219], v[18:21]
	s_setprio 0
	s_add_i32 s54, s54, 2
	s_add_u32 s8, s8, 0x100
	s_addc_u32 s9, s9, 0
	s_add_u32 s52, s52, 0x100
	s_addc_u32 s53, s53, 0
	s_cmp_gt_u32 s54, 5
	s_barrier
	s_cbranch_scc0 .LBB0_375
	s_and_b32 s43, s82, 3
	s_cmp_lt_i32 s82, 4
	s_cselect_b64 s[6:7], -1, 0
	s_cmp_gt_i32 s82, 3
	s_nop 15
	s_nop 15
	v_mbcnt_lo_u32_b32 v2, -1, 0
	v_mbcnt_hi_u32_b32 v2, -1, v2
	s_cselect_b64 s[58:59], -1, 0
	s_cmp_lt_i32 s82, 8
	s_cselect_b64 s[8:9], -1, 0
	s_cmp_gt_i32 s82, 7
	v_readlane_b32 s47, v252, 51
	v_readlane_b32 s45, v252, 52
	s_cselect_b64 s[12:13], -1, 0
	s_mov_b64 s[10:11], -1
	s_and_b64 vcc, exec, s[58:59]
	s_cbranch_vccz .LBB0_382
	s_and_b64 vcc, exec, s[12:13]
	s_cbranch_vccz .LBB0_379
	s_lshl_b32 s10, s82, 8
	s_add_i32 s28, s10, 0xfffff800
	s_mov_b64 s[10:11], 0

.LBB0_518:
	s_add_i32 s55, s46, 0x18000
	s_lshl_b32 s4, s4, 12
	v_lshl_add_u64 v[8:9], v[8:9], 0, s[24:25]
	s_mov_b32 m0, s55
	s_add_i32 s56, s46, 0x1a000
	s_lshl_b32 s54, s5, 13
	s_and_b32 s6, s4, 0x3000
	s_waitcnt vmcnt(2)
	s_barrier
	global_load_lds_dwordx4 v[8:9], off
	v_lshl_add_u64 v[6:7], v[6:7], 0, s[24:25]
	s_mov_b32 m0, s56
	s_add_i32 s57, s46, 0x8000
	s_add_i32 s58, s46, 0xa000
	global_load_lds_dwordx4 v[6:7], off
	v_lshl_add_u64 v[4:5], v[4:5], 0, s[24:25]
	s_mov_b32 m0, s57
	s_add_u32 s4, s34, 0x20080
	global_load_lds_dwordx4 v[4:5], off
	v_lshl_add_u64 v[2:3], v[2:3], 0, s[24:25]
	s_mov_b32 m0, s58
	s_addc_u32 s5, s35, 0
	s_add_i32 s59, s46, 0x1c000
	global_load_lds_dwordx4 v[2:3], off
	v_lshl_add_u64 v[2:3], s[4:5], 0, v[0:1]
	s_mov_b32 m0, s59
	s_add_i32 s61, s46, 0x1e000
	global_load_lds_dwordx4 v[2:3], off
	v_lshl_add_u64 v[2:3], s[4:5], 0, v[146:147]
	s_mov_b32 m0, s61
	s_add_u32 s62, s20, 0x51000000
	global_load_lds_dwordx4 v[2:3], off
	v_and_b32_e32 v2, 15, v12
	v_and_b32_e32 v3, 48, v12
	v_lshl_or_b32 v2, v2, 6, v3
	v_lshlrev_b32_e32 v3, 2, v12
	v_and_b32_e32 v3, 32, v3
	v_xad_u32 v164, v2, v3, 0
	v_add_u32_e32 v2, s6, v164
	v_add_u32_e32 v165, 0x10000, v2
	v_add_u32_e32 v166, 0x10400, v2
	v_add_u32_e32 v167, 0x10800, v2
	v_add_u32_e32 v168, 0x10c00, v2
	v_add_u32_e32 v169, 0x14000, v2
	v_add_u32_e32 v170, 0x14400, v2
	v_add_u32_e32 v171, 0x14800, v2
	v_add_u32_e32 v172, 0x14c00, v2
	v_add_u32_e32 v173, 0x18000, v2
	v_add_u32_e32 v174, 0x18400, v2
	v_add_u32_e32 v175, 0x18800, v2
	v_add_u32_e32 v176, 0x18c00, v2
	v_add_u32_e32 v177, 0x1c000, v2
	v_add_u32_e32 v178, 0x1c400, v2
	v_add_u32_e32 v179, 0x1c800, v2
	v_add_u32_e32 v180, 0x1cc00, v2
	v_lshlrev_b32_e32 v2, 13, v15
	v_and_b32_e32 v2, 0xffffc000, v2
	v_lshl_add_u32 v2, v14, 10, v2
	v_and_b32_e32 v3, 1, v15
	v_lshl_or_b32 v2, v3, 6, v2
	v_lshl_add_u32 v152, v16, 1, v2
	v_lshlrev_b32_e32 v2, 13, v10
	v_and_b32_e32 v2, 0xffffc000, v2
	s_waitcnt vmcnt(6)
	v_lshl_add_u32 v2, v11, 10, v2
	v_and_b32_e32 v3, 1, v10
	v_lshl_or_b32 v2, v3, 6, v2
	v_readlane_b32 s4, v253, 18
	s_addc_u32 s63, s21, 0
	v_mov_b32_e32 v153, v1
	v_lshl_add_u32 v154, v13, 1, v2
	v_mov_b32_e32 v155, v1
	s_mov_b32 s64, 0
	v_readlane_b32 s66, v253, 15
	s_mov_b32 s65, s4
	s_barrier
	v_readlane_b32 s5, v253, 19

.LBB0_525:
	s_ashr_i32 s9, s8, 31
	v_cmp_lt_i64_e32 vcc, s[10:11], v[248:249]
	s_lshl_b64 s[10:11], s[8:9], 18
	s_add_u32 s10, s44, s10
	s_addc_u32 s11, s45, s11
	s_and_b64 s[12:13], vcc, exec
	ds_read_b128 v[2:5], v165
	ds_read_b128 v[6:9], v166
	ds_read_b128 v[10:13], v167
	ds_read_b128 v[14:17], v168
	s_cselect_b32 s9, s11, s43
	s_cselect_b32 s67, s10, s42
	s_ashr_i32 s7, s6, 31
	s_lshl_b64 s[12:13], s[6:7], 18
	s_add_u32 s12, s27, s12
	s_addc_u32 s13, s60, s13
	s_and_b64 s[20:21], vcc, exec
	s_cselect_b32 s7, s13, s35
	s_cselect_b32 s68, s12, s34
	s_add_u32 s20, s42, 0x20080
	s_addc_u32 s21, s43, 0
	s_add_i32 s69, s46, 0xc000
	v_add_u32_e32 v181, s54, v164
	v_lshl_add_u64 v[42:43], s[20:21], 0, v[150:151]
	s_mov_b32 m0, s69
	s_add_i32 s70, s46, 0xe000
	ds_read_b128 v[18:21], v181
	ds_read_b128 v[22:25], v181 offset:1024
	ds_read_b128 v[26:29], v181 offset:2048
	ds_read_b128 v[30:33], v181 offset:3072
	ds_read_b128 v[34:37], v181 offset:4096
	ds_read_b128 v[38:41], v181 offset:5120
	ds_read_b128 v[50:53], v181 offset:6144
	ds_read_b128 v[54:57], v181 offset:7168
	global_load_lds_dwordx4 v[42:43], off
	v_lshl_add_u64 v[42:43], s[20:21], 0, v[148:149]
	s_mov_b32 m0, s70
	s_nop 0
	global_load_lds_dwordx4 v[42:43], off
	ds_read_b128 v[188:191], v169
	ds_read_b128 v[192:195], v170
	ds_read_b128 v[196:199], v171
	ds_read_b128 v[200:203], v172
	s_waitcnt lgkmcnt(4)
	s_waitcnt vmcnt(8)
	s_barrier
	s_waitcnt lgkmcnt(0)
	s_setprio 1
	s_waitcnt lgkmcnt(0)
	v_mfma_f32_16x16x128_f8f6f4 v[130:133], v[2:9], v[18:25], 0
	v_mfma_f32_16x16x128_f8f6f4 v[122:125], v[10:17], v[18:25], 0
	v_mfma_f32_16x16x128_f8f6f4 v[114:117], v[2:9], v[26:33], 0
	v_mfma_f32_16x16x128_f8f6f4 v[106:109], v[10:17], v[26:33], 0
	v_mfma_f32_16x16x128_f8f6f4 v[98:101], v[2:9], v[34:41], 0
	v_mfma_f32_16x16x128_f8f6f4 v[90:93], v[10:17], v[34:41], 0
	v_mfma_f32_16x16x128_f8f6f4 v[86:89], v[2:9], v[50:57], 0
	v_mfma_f32_16x16x128_f8f6f4 v[82:85], v[10:17], v[50:57], 0
	v_lshl_add_u64 v[160:161], s[34:35], 0, v[0:1]
	s_mov_b64 s[20:21], 0x100
	v_lshl_add_u64 v[162:163], s[34:35], 0, v[146:147]
	v_mfma_f32_16x16x128_f8f6f4 v[62:65], v[188:195], v[18:25], 0
	v_mfma_f32_16x16x128_f8f6f4 v[58:61], v[196:203], v[18:25], 0
	v_mfma_f32_16x16x128_f8f6f4 v[46:49], v[188:195], v[26:33], 0
	v_mfma_f32_16x16x128_f8f6f4 v[42:45], v[196:203], v[26:33], 0
	v_mfma_f32_16x16x128_f8f6f4 v[30:33], v[188:195], v[34:41], 0
	v_mfma_f32_16x16x128_f8f6f4 v[26:29], v[196:203], v[34:41], 0
	v_mfma_f32_16x16x128_f8f6f4 v[22:25], v[188:195], v[50:57], 0
	v_mfma_f32_16x16x128_f8f6f4 v[18:21], v[196:203], v[50:57], 0
	s_setprio 0
	v_lshl_add_u64 v[156:157], s[42:43], 0, v[150:151]
	s_mov_b32 m0, s46
	v_lshl_add_u64 v[66:67], v[156:157], 0, s[20:21]
	v_lshl_add_u64 v[158:159], s[42:43], 0, v[148:149]
	s_barrier
	ds_read_b128 v[34:37], v181 offset:16384
	ds_read_b128 v[38:41], v181 offset:17408
	ds_read_b128 v[50:53], v181 offset:18432
	ds_read_b128 v[54:57], v181 offset:19456
	ds_read_b128 v[204:207], v181 offset:20480
	ds_read_b128 v[208:211], v181 offset:21504
	ds_read_b128 v[212:215], v181 offset:22528
	ds_read_b128 v[216:219], v181 offset:23552
	global_load_lds_dwordx4 v[66:67], off
	v_lshl_add_u64 v[66:67], v[158:159], 0, s[20:21]
	s_mov_b32 m0, s49
	s_nop 0
	global_load_lds_dwordx4 v[66:67], off
	s_mov_b32 m0, s47
	v_lshl_add_u64 v[66:67], v[160:161], 0, s[20:21]
	global_load_lds_dwordx4 v[66:67], off
	v_lshl_add_u64 v[66:67], v[162:163], 0, s[20:21]
	s_mov_b32 m0, s48
	s_nop 0
	global_load_lds_dwordx4 v[66:67], off
	s_barrier
	s_waitcnt lgkmcnt(0)
	s_setprio 1
	s_waitcnt lgkmcnt(0)
	v_mfma_f32_16x16x128_f8f6f4 v[142:145], v[2:9], v[34:41], 0
	v_mfma_f32_16x16x128_f8f6f4 v[138:141], v[10:17], v[34:41], 0
	v_mfma_f32_16x16x128_f8f6f4 v[134:137], v[2:9], v[50:57], 0
	v_mfma_f32_16x16x128_f8f6f4 v[126:129], v[10:17], v[50:57], 0
	v_mfma_f32_16x16x128_f8f6f4 v[118:121], v[2:9], v[204:211], 0
	v_mfma_f32_16x16x128_f8f6f4 v[110:113], v[10:17], v[204:211], 0
	v_mfma_f32_16x16x128_f8f6f4 v[102:105], v[2:9], v[212:219], 0
	v_mfma_f32_16x16x128_f8f6f4 v[94:97], v[10:17], v[212:219], 0
	s_setprio 0
	s_barrier
	s_add_u32 s20, s34, 0x20100
	s_addc_u32 s21, s35, 0
	s_mov_b32 m0, s50
	v_lshl_add_u64 v[2:3], s[20:21], 0, v[0:1]
	global_load_lds_dwordx4 v[2:3], off
	v_lshl_add_u64 v[2:3], s[20:21], 0, v[146:147]
	s_mov_b32 m0, s51
	s_nop 0
	global_load_lds_dwordx4 v[2:3], off
	s_waitcnt vmcnt(8)
	s_barrier
	s_setprio 1
	v_mfma_f32_16x16x128_f8f6f4 v[78:81], v[188:195], v[34:41], 0
	v_mfma_f32_16x16x128_f8f6f4 v[74:77], v[196:203], v[34:41], 0
	v_mfma_f32_16x16x128_f8f6f4 v[70:73], v[188:195], v[50:57], 0
	v_mfma_f32_16x16x128_f8f6f4 v[66:69], v[196:203], v[50:57], 0
	v_mfma_f32_16x16x128_f8f6f4 v[54:57], v[188:195], v[204:211], 0
	v_mfma_f32_16x16x128_f8f6f4 v[50:53], v[196:203], v[204:211], 0
	v_mfma_f32_16x16x128_f8f6f4 v[38:41], v[188:195], v[212:219], 0
	v_mfma_f32_16x16x128_f8f6f4 v[34:37], v[196:203], v[212:219], 0
	s_setprio 0
	s_barrier
	ds_read_b128 v[2:5], v173
	ds_read_b128 v[6:9], v174
	ds_read_b128 v[10:13], v175
	ds_read_b128 v[14:17], v176
	s_add_u32 s20, s42, 0x20100
	s_addc_u32 s21, s43, 0
	s_mov_b32 m0, s52
	v_lshl_add_u64 v[182:183], s[20:21], 0, v[150:151]
	ds_read_b128 v[188:191], v181 offset:32768
	ds_read_b128 v[192:195], v181 offset:33792
	ds_read_b128 v[196:199], v181 offset:34816
	ds_read_b128 v[200:203], v181 offset:35840
	ds_read_b128 v[204:207], v181 offset:36864
	ds_read_b128 v[208:211], v181 offset:37888
	ds_read_b128 v[212:215], v181 offset:38912
	ds_read_b128 v[216:219], v181 offset:39936
	global_load_lds_dwordx4 v[182:183], off
	v_lshl_add_u64 v[182:183], s[20:21], 0, v[148:149]
	s_mov_b32 m0, s53
	s_nop 0
	global_load_lds_dwordx4 v[182:183], off
	ds_read_b128 v[232:235], v177
	ds_read_b128 v[236:239], v178
	ds_read_b128 v[240:243], v179
	ds_read_b128 v[244:247], v180
	s_waitcnt lgkmcnt(4)
	s_waitcnt vmcnt(8)
	s_barrier
	s_waitcnt lgkmcnt(0)
	s_setprio 1
	s_waitcnt lgkmcnt(0)
	v_mfma_f32_16x16x128_f8f6f4 v[130:133], v[2:9], v[188:195], v[130:133]
	v_mfma_f32_16x16x128_f8f6f4 v[122:125], v[10:17], v[188:195], v[122:125]
	v_mfma_f32_16x16x128_f8f6f4 v[114:117], v[2:9], v[196:203], v[114:117]
	v_mfma_f32_16x16x128_f8f6f4 v[106:109], v[10:17], v[196:203], v[106:109]
	v_mfma_f32_16x16x128_f8f6f4 v[98:101], v[2:9], v[204:211], v[98:101]
	v_mfma_f32_16x16x128_f8f6f4 v[90:93], v[10:17], v[204:211], v[90:93]
	v_mfma_f32_16x16x128_f8f6f4 v[86:89], v[2:9], v[212:219], v[86:89]
	v_mfma_f32_16x16x128_f8f6f4 v[82:85], v[10:17], v[212:219], v[82:85]
	s_mov_b64 s[20:21], 0x180
	v_mfma_f32_16x16x128_f8f6f4 v[62:65], v[232:239], v[188:195], v[62:65]
	v_mfma_f32_16x16x128_f8f6f4 v[58:61], v[240:247], v[188:195], v[58:61]
	v_mfma_f32_16x16x128_f8f6f4 v[46:49], v[232:239], v[196:203], v[46:49]
	v_mfma_f32_16x16x128_f8f6f4 v[42:45], v[240:247], v[196:203], v[42:45]
	v_mfma_f32_16x16x128_f8f6f4 v[30:33], v[232:239], v[204:211], v[30:33]
	v_mfma_f32_16x16x128_f8f6f4 v[26:29], v[240:247], v[204:211], v[26:29]
	v_mfma_f32_16x16x128_f8f6f4 v[22:25], v[232:239], v[212:219], v[22:25]
	v_mfma_f32_16x16x128_f8f6f4 v[18:21], v[240:247], v[212:219], v[18:21]
	s_setprio 0
	s_mov_b32 m0, s57
	v_lshl_add_u64 v[156:157], v[156:157], 0, s[20:21]
	s_barrier
	ds_read_b128 v[188:191], v181 offset:49152
	ds_read_b128 v[192:195], v181 offset:50176
	ds_read_b128 v[196:199], v181 offset:51200
	ds_read_b128 v[200:203], v181 offset:52224
	ds_read_b128 v[204:207], v181 offset:53248
	ds_read_b128 v[208:211], v181 offset:54272
	ds_read_b128 v[212:215], v181 offset:55296
	ds_read_b128 v[216:219], v181 offset:56320
	global_load_lds_dwordx4 v[156:157], off
	v_lshl_add_u64 v[156:157], v[158:159], 0, s[20:21]
	s_mov_b32 m0, s58
	s_nop 0
	global_load_lds_dwordx4 v[156:157], off
	s_mov_b32 m0, s55
	v_lshl_add_u64 v[160:161], v[160:161], 0, s[20:21]
	global_load_lds_dwordx4 v[160:161], off
	v_lshl_add_u64 v[160:161], v[162:163], 0, s[20:21]
	s_mov_b32 m0, s56
	s_nop 0
	global_load_lds_dwordx4 v[160:161], off
	s_barrier
	s_waitcnt lgkmcnt(0)
	s_setprio 1
	s_waitcnt lgkmcnt(0)
	v_mfma_f32_16x16x128_f8f6f4 v[142:145], v[2:9], v[188:195], v[142:145]
	v_mfma_f32_16x16x128_f8f6f4 v[138:141], v[10:17], v[188:195], v[138:141]
	v_mfma_f32_16x16x128_f8f6f4 v[134:137], v[2:9], v[196:203], v[134:137]
	v_mfma_f32_16x16x128_f8f6f4 v[126:129], v[10:17], v[196:203], v[126:129]
	v_mfma_f32_16x16x128_f8f6f4 v[118:121], v[2:9], v[204:211], v[118:121]
	v_mfma_f32_16x16x128_f8f6f4 v[110:113], v[10:17], v[204:211], v[110:113]
	v_mfma_f32_16x16x128_f8f6f4 v[102:105], v[2:9], v[212:219], v[102:105]
	v_mfma_f32_16x16x128_f8f6f4 v[94:97], v[10:17], v[212:219], v[94:97]
	s_setprio 0
	s_barrier
	s_add_u32 s20, s34, 0x20180
	s_addc_u32 s21, s35, 0
	s_mov_b32 m0, s59
	v_lshl_add_u64 v[2:3], s[20:21], 0, v[0:1]
	global_load_lds_dwordx4 v[2:3], off
	v_lshl_add_u64 v[2:3], s[20:21], 0, v[146:147]
	s_mov_b32 m0, s61
	s_nop 0
	global_load_lds_dwordx4 v[2:3], off
	s_waitcnt vmcnt(8)
	s_barrier
	s_setprio 1
	v_mfma_f32_16x16x128_f8f6f4 v[78:81], v[232:239], v[188:195], v[78:81]
	v_mfma_f32_16x16x128_f8f6f4 v[74:77], v[240:247], v[188:195], v[74:77]
	v_mfma_f32_16x16x128_f8f6f4 v[70:73], v[232:239], v[196:203], v[70:73]
	v_mfma_f32_16x16x128_f8f6f4 v[66:69], v[240:247], v[196:203], v[66:69]
	v_mfma_f32_16x16x128_f8f6f4 v[54:57], v[232:239], v[204:211], v[54:57]
	v_mfma_f32_16x16x128_f8f6f4 v[50:53], v[240:247], v[204:211], v[50:53]
	v_mfma_f32_16x16x128_f8f6f4 v[38:41], v[232:239], v[212:219], v[38:41]
	v_mfma_f32_16x16x128_f8f6f4 v[34:37], v[240:247], v[212:219], v[34:37]
	s_setprio 0
	s_add_u32 s20, s42, 0x20180
	s_addc_u32 s21, s43, 0
	s_add_u32 s71, s34, 0x200
	s_addc_u32 s72, s35, 0
	s_mov_b32 s73, 0
	s_barrier
.LBB0_526:
	ds_read_b128 v[10:13], v165
	ds_read_b128 v[14:17], v166
	ds_read_b128 v[156:159], v167
	ds_read_b128 v[160:163], v168
	s_add_u32 s34, s20, 0xfffe0080
	s_addc_u32 s35, s21, -1
	s_cmp_eq_u32 s73, 4
	s_cselect_b32 s43, s9, s35
	s_cselect_b32 s42, s67, s34
	s_cselect_b32 s35, s7, s72
	s_cselect_b32 s34, s68, s71
	s_mov_b32 m0, s69
	v_lshl_add_u64 v[2:3], s[20:21], 0, v[152:153]
	ds_read_b128 v[188:191], v181
	ds_read_b128 v[192:195], v181 offset:1024
	ds_read_b128 v[196:199], v181 offset:2048
	ds_read_b128 v[200:203], v181 offset:3072
	ds_read_b128 v[204:207], v181 offset:4096
	ds_read_b128 v[208:211], v181 offset:5120
	ds_read_b128 v[212:215], v181 offset:6144
	ds_read_b128 v[216:219], v181 offset:7168
	global_load_lds_dwordx4 v[2:3], off
	v_lshl_add_u64 v[2:3], s[20:21], 0, v[154:155]
	s_mov_b32 m0, s70
	s_nop 0
	global_load_lds_dwordx4 v[2:3], off
	ds_read_b128 v[232:235], v169
	ds_read_b128 v[236:239], v170
	ds_read_b128 v[240:243], v171
	ds_read_b128 v[244:247], v172
	s_waitcnt lgkmcnt(4)
	s_waitcnt vmcnt(8)
	s_barrier
	s_waitcnt lgkmcnt(0)
	s_setprio 1
	s_waitcnt lgkmcnt(0)
	v_mfma_f32_16x16x128_f8f6f4 v[130:133], v[10:17], v[188:195], v[130:133]
	v_mfma_f32_16x16x128_f8f6f4 v[122:125], v[156:163], v[188:195], v[122:125]
	v_mfma_f32_16x16x128_f8f6f4 v[114:117], v[10:17], v[196:203], v[114:117]
	v_mfma_f32_16x16x128_f8f6f4 v[106:109], v[156:163], v[196:203], v[106:109]
	v_mfma_f32_16x16x128_f8f6f4 v[98:101], v[10:17], v[204:211], v[98:101]
	v_mfma_f32_16x16x128_f8f6f4 v[90:93], v[156:163], v[204:211], v[90:93]
	v_mfma_f32_16x16x128_f8f6f4 v[86:89], v[10:17], v[212:219], v[86:89]
	v_mfma_f32_16x16x128_f8f6f4 v[82:85], v[156:163], v[212:219], v[82:85]
	v_mfma_f32_16x16x128_f8f6f4 v[62:65], v[232:239], v[188:195], v[62:65]
	v_mfma_f32_16x16x128_f8f6f4 v[58:61], v[240:247], v[188:195], v[58:61]
	v_mfma_f32_16x16x128_f8f6f4 v[46:49], v[232:239], v[196:203], v[46:49]
	v_mfma_f32_16x16x128_f8f6f4 v[42:45], v[240:247], v[196:203], v[42:45]
	v_mfma_f32_16x16x128_f8f6f4 v[30:33], v[232:239], v[204:211], v[30:33]
	v_mfma_f32_16x16x128_f8f6f4 v[26:29], v[240:247], v[204:211], v[26:29]
	v_mfma_f32_16x16x128_f8f6f4 v[22:25], v[232:239], v[212:219], v[22:25]
	v_mfma_f32_16x16x128_f8f6f4 v[18:21], v[240:247], v[212:219], v[18:21]
	s_setprio 0
	s_mov_b32 m0, s46
	v_lshl_add_u64 v[2:3], s[42:43], 0, v[150:151]
	s_barrier
	ds_read_b128 v[188:191], v181 offset:16384
	ds_read_b128 v[192:195], v181 offset:17408
	ds_read_b128 v[196:199], v181 offset:18432
	ds_read_b128 v[200:203], v181 offset:19456
	ds_read_b128 v[204:207], v181 offset:20480
	ds_read_b128 v[208:211], v181 offset:21504
	ds_read_b128 v[212:215], v181 offset:22528
	ds_read_b128 v[216:219], v181 offset:23552
	global_load_lds_dwordx4 v[2:3], off
	v_lshl_add_u64 v[4:5], s[42:43], 0, v[148:149]
	s_mov_b32 m0, s49
	s_nop 0
	global_load_lds_dwordx4 v[4:5], off
	s_mov_b32 m0, s47
	v_lshl_add_u64 v[6:7], s[34:35], 0, v[0:1]
	global_load_lds_dwordx4 v[6:7], off
	v_lshl_add_u64 v[8:9], s[34:35], 0, v[146:147]
	s_mov_b32 m0, s48
	s_nop 0
	global_load_lds_dwordx4 v[8:9], off
	s_barrier
	s_waitcnt lgkmcnt(0)
	s_setprio 1
	s_waitcnt lgkmcnt(0)
	v_mfma_f32_16x16x128_f8f6f4 v[142:145], v[10:17], v[188:195], v[142:145]
	v_mfma_f32_16x16x128_f8f6f4 v[138:141], v[156:163], v[188:195], v[138:141]
	v_mfma_f32_16x16x128_f8f6f4 v[134:137], v[10:17], v[196:203], v[134:137]
	v_mfma_f32_16x16x128_f8f6f4 v[126:129], v[156:163], v[196:203], v[126:129]
	v_mfma_f32_16x16x128_f8f6f4 v[118:121], v[10:17], v[204:211], v[118:121]
	v_mfma_f32_16x16x128_f8f6f4 v[110:113], v[156:163], v[204:211], v[110:113]
	v_mfma_f32_16x16x128_f8f6f4 v[102:105], v[10:17], v[212:219], v[102:105]
	v_mfma_f32_16x16x128_f8f6f4 v[94:97], v[156:163], v[212:219], v[94:97]
	s_setprio 0
	s_barrier
	s_add_u32 s74, s34, 0x20000
	s_addc_u32 s75, s35, 0
	s_mov_b32 m0, s50
	v_lshl_add_u64 v[10:11], s[74:75], 0, v[0:1]
	global_load_lds_dwordx4 v[10:11], off
	v_lshl_add_u64 v[10:11], s[74:75], 0, v[146:147]
	s_mov_b32 m0, s51
	s_nop 0
	global_load_lds_dwordx4 v[10:11], off
	s_waitcnt vmcnt(8)
	s_barrier
	s_setprio 1
	v_mfma_f32_16x16x128_f8f6f4 v[78:81], v[232:239], v[188:195], v[78:81]
	v_mfma_f32_16x16x128_f8f6f4 v[74:77], v[240:247], v[188:195], v[74:77]
	v_mfma_f32_16x16x128_f8f6f4 v[70:73], v[232:239], v[196:203], v[70:73]
	v_mfma_f32_16x16x128_f8f6f4 v[66:69], v[240:247], v[196:203], v[66:69]
	v_mfma_f32_16x16x128_f8f6f4 v[54:57], v[232:239], v[204:211], v[54:57]
	v_mfma_f32_16x16x128_f8f6f4 v[50:53], v[240:247], v[204:211], v[50:53]
	v_mfma_f32_16x16x128_f8f6f4 v[38:41], v[232:239], v[212:219], v[38:41]
	v_mfma_f32_16x16x128_f8f6f4 v[34:37], v[240:247], v[212:219], v[34:37]
	s_setprio 0
	s_barrier
	ds_read_b128 v[10:13], v173
	ds_read_b128 v[14:17], v174
	ds_read_b128 v[156:159], v175
	ds_read_b128 v[160:163], v176
	s_add_u32 s42, s42, 0x20000
	s_addc_u32 s43, s43, 0
	s_mov_b32 m0, s52
	v_lshl_add_u64 v[182:183], s[42:43], 0, v[150:151]
	ds_read_b128 v[188:191], v181 offset:32768
	ds_read_b128 v[192:195], v181 offset:33792
	ds_read_b128 v[196:199], v181 offset:34816
	ds_read_b128 v[200:203], v181 offset:35840
	ds_read_b128 v[204:207], v181 offset:36864
	ds_read_b128 v[208:211], v181 offset:37888
	ds_read_b128 v[212:215], v181 offset:38912
	ds_read_b128 v[216:219], v181 offset:39936
	global_load_lds_dwordx4 v[182:183], off
	v_lshl_add_u64 v[182:183], s[42:43], 0, v[148:149]
	s_mov_b32 m0, s53
	s_nop 0
	global_load_lds_dwordx4 v[182:183], off
	ds_read_b128 v[232:235], v177
	ds_read_b128 v[236:239], v178
	ds_read_b128 v[240:243], v179
	ds_read_b128 v[244:247], v180
	s_waitcnt lgkmcnt(4)
	s_waitcnt vmcnt(8)
	s_barrier
	s_waitcnt lgkmcnt(0)
	s_setprio 1
	s_waitcnt lgkmcnt(0)
	v_mfma_f32_16x16x128_f8f6f4 v[130:133], v[10:17], v[188:195], v[130:133]
	v_mfma_f32_16x16x128_f8f6f4 v[122:125], v[156:163], v[188:195], v[122:125]
	v_mfma_f32_16x16x128_f8f6f4 v[114:117], v[10:17], v[196:203], v[114:117]
	v_mfma_f32_16x16x128_f8f6f4 v[106:109], v[156:163], v[196:203], v[106:109]
	v_mfma_f32_16x16x128_f8f6f4 v[98:101], v[10:17], v[204:211], v[98:101]
	v_mfma_f32_16x16x128_f8f6f4 v[90:93], v[156:163], v[204:211], v[90:93]
	v_mfma_f32_16x16x128_f8f6f4 v[86:89], v[10:17], v[212:219], v[86:89]
	v_mfma_f32_16x16x128_f8f6f4 v[82:85], v[156:163], v[212:219], v[82:85]
	v_mfma_f32_16x16x128_f8f6f4 v[62:65], v[232:239], v[188:195], v[62:65]
	v_mfma_f32_16x16x128_f8f6f4 v[58:61], v[240:247], v[188:195], v[58:61]
	v_mfma_f32_16x16x128_f8f6f4 v[46:49], v[232:239], v[196:203], v[46:49]
	v_mfma_f32_16x16x128_f8f6f4 v[42:45], v[240:247], v[196:203], v[42:45]
	v_mfma_f32_16x16x128_f8f6f4 v[30:33], v[232:239], v[204:211], v[30:33]
	v_mfma_f32_16x16x128_f8f6f4 v[26:29], v[240:247], v[204:211], v[26:29]
	v_mfma_f32_16x16x128_f8f6f4 v[22:25], v[232:239], v[212:219], v[22:25]
	v_mfma_f32_16x16x128_f8f6f4 v[18:21], v[240:247], v[212:219], v[18:21]
	s_setprio 0
	s_mov_b32 m0, s57
	v_lshl_add_u64 v[2:3], v[2:3], 0, s[24:25]
	s_barrier
	ds_read_b128 v[188:191], v181 offset:49152
	ds_read_b128 v[192:195], v181 offset:50176
	ds_read_b128 v[196:199], v181 offset:51200
	ds_read_b128 v[200:203], v181 offset:52224
	ds_read_b128 v[204:207], v181 offset:53248
	ds_read_b128 v[208:211], v181 offset:54272
	ds_read_b128 v[212:215], v181 offset:55296
	ds_read_b128 v[216:219], v181 offset:56320
	global_load_lds_dwordx4 v[2:3], off
	v_lshl_add_u64 v[2:3], v[4:5], 0, s[24:25]
	s_mov_b32 m0, s58
	s_nop 0
	global_load_lds_dwordx4 v[2:3], off
	s_mov_b32 m0, s55
	v_lshl_add_u64 v[6:7], v[6:7], 0, s[24:25]
	global_load_lds_dwordx4 v[6:7], off
	v_lshl_add_u64 v[6:7], v[8:9], 0, s[24:25]
	s_mov_b32 m0, s56
	s_nop 0
	global_load_lds_dwordx4 v[6:7], off
	s_barrier
	s_waitcnt lgkmcnt(0)
	s_setprio 1
	s_waitcnt lgkmcnt(0)
	v_mfma_f32_16x16x128_f8f6f4 v[142:145], v[10:17], v[188:195], v[142:145]
	v_mfma_f32_16x16x128_f8f6f4 v[138:141], v[156:163], v[188:195], v[138:141]
	v_mfma_f32_16x16x128_f8f6f4 v[134:137], v[10:17], v[196:203], v[134:137]
	v_mfma_f32_16x16x128_f8f6f4 v[126:129], v[156:163], v[196:203], v[126:129]
	v_mfma_f32_16x16x128_f8f6f4 v[118:121], v[10:17], v[204:211], v[118:121]
	v_mfma_f32_16x16x128_f8f6f4 v[110:113], v[156:163], v[204:211], v[110:113]
	v_mfma_f32_16x16x128_f8f6f4 v[102:105], v[10:17], v[212:219], v[102:105]
	v_mfma_f32_16x16x128_f8f6f4 v[94:97], v[156:163], v[212:219], v[94:97]
	s_setprio 0
	s_barrier
	s_add_u32 s34, s34, 0x20080
	s_addc_u32 s35, s35, 0
	s_mov_b32 m0, s59
	v_lshl_add_u64 v[2:3], s[34:35], 0, v[0:1]
	global_load_lds_dwordx4 v[2:3], off
	v_lshl_add_u64 v[2:3], s[34:35], 0, v[146:147]
	s_mov_b32 m0, s61
	s_nop 0
	global_load_lds_dwordx4 v[2:3], off
	s_waitcnt vmcnt(8)
	s_barrier
	s_setprio 1
	v_mfma_f32_16x16x128_f8f6f4 v[78:81], v[232:239], v[188:195], v[78:81]
	v_mfma_f32_16x16x128_f8f6f4 v[74:77], v[240:247], v[188:195], v[74:77]
	v_mfma_f32_16x16x128_f8f6f4 v[70:73], v[232:239], v[196:203], v[70:73]
	v_mfma_f32_16x16x128_f8f6f4 v[66:69], v[240:247], v[196:203], v[66:69]
	v_mfma_f32_16x16x128_f8f6f4 v[54:57], v[232:239], v[204:211], v[54:57]
	v_mfma_f32_16x16x128_f8f6f4 v[50:53], v[240:247], v[204:211], v[50:53]
	v_mfma_f32_16x16x128_f8f6f4 v[38:41], v[232:239], v[212:219], v[38:41]
	v_mfma_f32_16x16x128_f8f6f4 v[34:37], v[240:247], v[212:219], v[34:37]
	s_setprio 0
	s_add_i32 s73, s73, 2
	s_add_u32 s20, s20, 0x100
	s_addc_u32 s21, s21, 0
	s_add_u32 s71, s71, 0x100
	s_addc_u32 s72, s72, 0
	s_cmp_gt_u32 s73, 5
	s_barrier
	s_cbranch_scc0 .LBB0_526
	s_ashr_i32 s21, s66, 1
	s_ashr_i32 s20, s65, 1
	s_and_b32 s21, s21, -4
	s_add_i32 s20, s21, s20
	s_ashr_i32 s21, s20, 31
	s_lshl_b64 s[20:21], s[20:21], 22
	s_add_u32 s20, s62, s20
	s_addc_u32 s21, s63, s21
	s_lshl_b32 s34, s66, 19
	s_and_b32 s34, s34, 0x380000
	s_nop 15
	s_nop 15
	v_mbcnt_lo_u32_b32 v2, -1, 0
	v_mbcnt_hi_u32_b32 v2, -1, v2
	s_add_u32 s20, s20, s34
	v_and_b32_e32 v3, 15, v2
	s_addc_u32 s21, s21, 0
	s_lshl_b32 s34, s65, 18
	v_lshrrev_b32_e32 v2, 1, v2
	v_readlane_b32 s7, v252, 51
	v_readlane_b32 s9, v252, 52
	s_and_b32 s34, s34, 0x40000
	v_and_b32_e32 v2, 24, v2
	s_add_u32 s20, s20, s34
	v_lshl_or_b32 v6, s9, 5, v2
	v_lshl_or_b32 v8, s7, 6, v3
	s_addc_u32 s21, s21, 0
	v_ashrrev_i32_e32 v7, 31, v6
	v_pk_mul_f32 v[4:5], v[132:133], s[22:23] op_sel_hi:[1,0]
	v_pk_mul_f32 v[2:3], v[130:131], s[22:23] op_sel_hi:[1,0]
	v_pk_mul_f32 v[12:13], v[124:125], s[22:23] op_sel_hi:[1,0]
	v_ashrrev_i32_e32 v9, 31, v8
	v_lshl_add_u64 v[10:11], v[6:7], 1, s[20:21]
	v_pk_mul_f32 v[14:15], v[122:123], s[22:23] op_sel_hi:[1,0]
	v_cvt_pk_bf16_f32 v2, v2, v3
	v_cvt_pk_bf16_f32 v3, v4, v5
	v_cvt_pk_bf16_f32 v5, v12, v13
	v_lshlrev_b64 v[12:13], 10, v[8:9]
	v_cvt_pk_bf16_f32 v4, v14, v15
	v_lshl_add_u64 v[14:15], v[10:11], 0, v[12:13]
	global_store_dwordx4 v[14:15], v[2:5], off
	v_pk_mul_f32 v[14:15], v[108:109], s[22:23] op_sel_hi:[1,0]
	v_pk_mul_f32 v[16:17], v[106:107], s[22:23] op_sel_hi:[1,0]
	v_pk_mul_f32 v[4:5], v[116:117], s[22:23] op_sel_hi:[1,0]
	v_pk_mul_f32 v[2:3], v[114:115], s[22:23] op_sel_hi:[1,0]
	v_pk_mul_f32 v[90:91], v[90:91], s[22:23] op_sel_hi:[1,0]
	v_cvt_pk_bf16_f32 v2, v2, v3
	v_cvt_pk_bf16_f32 v3, v4, v5
	v_cvt_pk_bf16_f32 v5, v14, v15
	v_or_b32_e32 v14, 16, v8
	v_ashrrev_i32_e32 v15, 31, v14
	v_lshlrev_b64 v[14:15], 10, v[14:15]
	v_cvt_pk_bf16_f32 v4, v16, v17
	v_lshl_add_u64 v[16:17], v[10:11], 0, v[14:15]
	global_store_dwordx4 v[16:17], v[2:5], off
	v_pk_mul_f32 v[16:17], v[92:93], s[22:23] op_sel_hi:[1,0]
	v_pk_mul_f32 v[82:83], v[82:83], s[22:23] op_sel_hi:[1,0]
	v_pk_mul_f32 v[4:5], v[100:101], s[22:23] op_sel_hi:[1,0]
	v_pk_mul_f32 v[2:3], v[98:99], s[22:23] op_sel_hi:[1,0]
	v_pk_mul_f32 v[84:85], v[84:85], s[22:23] op_sel_hi:[1,0]
	v_cvt_pk_bf16_f32 v2, v2, v3
	v_cvt_pk_bf16_f32 v3, v4, v5
	v_cvt_pk_bf16_f32 v5, v16, v17
	v_or_b32_e32 v16, 32, v8
	v_ashrrev_i32_e32 v17, 31, v16
	v_lshlrev_b64 v[16:17], 10, v[16:17]
	v_cvt_pk_bf16_f32 v4, v90, v91
	v_lshl_add_u64 v[90:91], v[10:11], 0, v[16:17]
	global_store_dwordx4 v[90:91], v[2:5], off
	v_pk_mul_f32 v[90:91], v[110:111], s[22:23] op_sel_hi:[1,0]
	v_pk_mul_f32 v[92:93], v[94:95], s[22:23] op_sel_hi:[1,0]
	v_pk_mul_f32 v[4:5], v[88:89], s[22:23] op_sel_hi:[1,0]
	v_pk_mul_f32 v[2:3], v[86:87], s[22:23] op_sel_hi:[1,0]
	v_pk_mul_f32 v[86:87], v[140:141], s[22:23] op_sel_hi:[1,0]
	v_cvt_pk_bf16_f32 v2, v2, v3
	v_cvt_pk_bf16_f32 v3, v4, v5
	v_cvt_pk_bf16_f32 v4, v82, v83
	v_or_b32_e32 v82, 48, v8
	v_ashrrev_i32_e32 v83, 31, v82
	v_lshlrev_b64 v[82:83], 10, v[82:83]
	v_cvt_pk_bf16_f32 v5, v84, v85
	v_lshl_add_u64 v[84:85], v[10:11], 0, v[82:83]
	global_store_dwordx4 v[84:85], v[2:5], off
	v_add_u32_e32 v84, 0x80, v8
	v_ashrrev_i32_e32 v85, 31, v84
	v_pk_mul_f32 v[4:5], v[144:145], s[22:23] op_sel_hi:[1,0]
	v_pk_mul_f32 v[2:3], v[142:143], s[22:23] op_sel_hi:[1,0]
	v_pk_mul_f32 v[88:89], v[138:139], s[22:23] op_sel_hi:[1,0]
	v_lshlrev_b64 v[84:85], 10, v[84:85]
	v_cvt_pk_bf16_f32 v2, v2, v3
	v_cvt_pk_bf16_f32 v3, v4, v5
	v_cvt_pk_bf16_f32 v4, v88, v89
	v_cvt_pk_bf16_f32 v5, v86, v87
	v_lshl_add_u64 v[86:87], v[10:11], 0, v[84:85]
	global_store_dwordx4 v[86:87], v[2:5], off
	v_pk_mul_f32 v[86:87], v[128:129], s[22:23] op_sel_hi:[1,0]
	v_pk_mul_f32 v[88:89], v[126:127], s[22:23] op_sel_hi:[1,0]
	v_pk_mul_f32 v[4:5], v[136:137], s[22:23] op_sel_hi:[1,0]
	v_pk_mul_f32 v[2:3], v[134:135], s[22:23] op_sel_hi:[1,0]
	v_pk_mul_f32 v[58:59], v[58:59], s[22:23] op_sel_hi:[1,0]
	v_cvt_pk_bf16_f32 v2, v2, v3
	v_cvt_pk_bf16_f32 v3, v4, v5
	v_cvt_pk_bf16_f32 v5, v86, v87
	v_add_u32_e32 v86, 0x90, v8
	v_ashrrev_i32_e32 v87, 31, v86
	v_lshlrev_b64 v[86:87], 10, v[86:87]
	v_cvt_pk_bf16_f32 v4, v88, v89
	v_lshl_add_u64 v[88:89], v[10:11], 0, v[86:87]
	global_store_dwordx4 v[88:89], v[2:5], off
	v_pk_mul_f32 v[88:89], v[112:113], s[22:23] op_sel_hi:[1,0]
	s_and_b64 vcc, exec, s[4:5]
	v_pk_mul_f32 v[4:5], v[120:121], s[22:23] op_sel_hi:[1,0]
	v_pk_mul_f32 v[2:3], v[118:119], s[22:23] op_sel_hi:[1,0]
	s_mov_b32 s66, s6
	v_cvt_pk_bf16_f32 v2, v2, v3
	v_cvt_pk_bf16_f32 v3, v4, v5
	v_cvt_pk_bf16_f32 v5, v88, v89
	v_add_u32_e32 v88, 0xa0, v8
	v_ashrrev_i32_e32 v89, 31, v88
	v_lshlrev_b64 v[88:89], 10, v[88:89]
	v_add_u32_e32 v8, 0xb0, v8
	v_cvt_pk_bf16_f32 v4, v90, v91
	v_lshl_add_u64 v[90:91], v[10:11], 0, v[88:89]
	v_ashrrev_i32_e32 v9, 31, v8
	global_store_dwordx4 v[90:91], v[2:5], off
	v_pk_mul_f32 v[90:91], v[96:97], s[22:23] op_sel_hi:[1,0]
	v_lshlrev_b64 v[8:9], 10, v[8:9]
	v_pk_mul_f32 v[4:5], v[104:105], s[22:23] op_sel_hi:[1,0]
	v_pk_mul_f32 v[2:3], v[102:103], s[22:23] op_sel_hi:[1,0]
	v_lshl_add_u64 v[10:11], v[10:11], 0, v[8:9]
	v_cvt_pk_bf16_f32 v2, v2, v3
	v_cvt_pk_bf16_f32 v3, v4, v5
	v_cvt_pk_bf16_f32 v4, v92, v93
	v_cvt_pk_bf16_f32 v5, v90, v91
	global_store_dwordx4 v[10:11], v[2:5], off
	v_pk_mul_f32 v[10:11], v[60:61], s[22:23] op_sel_hi:[1,0]
	s_mov_b32 s65, s8
	v_add_u32_e32 v2, 0x80, v6
	v_ashrrev_i32_e32 v3, 31, v2
	v_lshl_add_u64 v[6:7], v[2:3], 1, s[20:21]
	v_pk_mul_f32 v[4:5], v[64:65], s[22:23] op_sel_hi:[1,0]
	v_pk_mul_f32 v[2:3], v[62:63], s[22:23] op_sel_hi:[1,0]
	s_mov_b64 s[34:35], s[12:13]
	v_cvt_pk_bf16_f32 v2, v2, v3
	v_cvt_pk_bf16_f32 v3, v4, v5
	v_cvt_pk_bf16_f32 v4, v58, v59
	v_cvt_pk_bf16_f32 v5, v10, v11
	v_lshl_add_u64 v[10:11], v[6:7], 0, v[12:13]
	global_store_dwordx4 v[10:11], v[2:5], off
	v_pk_mul_f32 v[10:11], v[44:45], s[22:23] op_sel_hi:[1,0]
	v_pk_mul_f32 v[12:13], v[42:43], s[22:23] op_sel_hi:[1,0]
	v_pk_mul_f32 v[4:5], v[48:49], s[22:23] op_sel_hi:[1,0]
	v_pk_mul_f32 v[2:3], v[46:47], s[22:23] op_sel_hi:[1,0]
	s_mov_b64 s[42:43], s[10:11]
	v_cvt_pk_bf16_f32 v2, v2, v3
	v_cvt_pk_bf16_f32 v3, v4, v5
	v_cvt_pk_bf16_f32 v4, v12, v13
	v_cvt_pk_bf16_f32 v5, v10, v11
	v_lshl_add_u64 v[10:11], v[6:7], 0, v[14:15]
	global_store_dwordx4 v[10:11], v[2:5], off
	v_pk_mul_f32 v[10:11], v[28:29], s[22:23] op_sel_hi:[1,0]
	v_pk_mul_f32 v[12:13], v[26:27], s[22:23] op_sel_hi:[1,0]
	v_pk_mul_f32 v[4:5], v[32:33], s[22:23] op_sel_hi:[1,0]
	v_pk_mul_f32 v[2:3], v[30:31], s[22:23] op_sel_hi:[1,0]
	s_nop 0
	v_cvt_pk_bf16_f32 v2, v2, v3
	v_cvt_pk_bf16_f32 v3, v4, v5
	v_cvt_pk_bf16_f32 v4, v12, v13
	v_cvt_pk_bf16_f32 v5, v10, v11
	v_lshl_add_u64 v[10:11], v[6:7], 0, v[16:17]
	global_store_dwordx4 v[10:11], v[2:5], off
	v_pk_mul_f32 v[10:11], v[20:21], s[22:23] op_sel_hi:[1,0]
	v_pk_mul_f32 v[12:13], v[18:19], s[22:23] op_sel_hi:[1,0]
	v_pk_mul_f32 v[4:5], v[24:25], s[22:23] op_sel_hi:[1,0]
	v_pk_mul_f32 v[2:3], v[22:23], s[22:23] op_sel_hi:[1,0]
	s_nop 0
	v_cvt_pk_bf16_f32 v2, v2, v3
	v_cvt_pk_bf16_f32 v3, v4, v5
	v_cvt_pk_bf16_f32 v4, v12, v13
	v_cvt_pk_bf16_f32 v5, v10, v11
	v_lshl_add_u64 v[10:11], v[6:7], 0, v[82:83]
	global_store_dwordx4 v[10:11], v[2:5], off
	v_pk_mul_f32 v[10:11], v[76:77], s[22:23] op_sel_hi:[1,0]
	v_pk_mul_f32 v[12:13], v[74:75], s[22:23] op_sel_hi:[1,0]
	v_pk_mul_f32 v[4:5], v[80:81], s[22:23] op_sel_hi:[1,0]
	v_pk_mul_f32 v[2:3], v[78:79], s[22:23] op_sel_hi:[1,0]
	s_nop 0
	v_cvt_pk_bf16_f32 v2, v2, v3
	v_cvt_pk_bf16_f32 v3, v4, v5
	v_cvt_pk_bf16_f32 v4, v12, v13
	v_cvt_pk_bf16_f32 v5, v10, v11
	v_lshl_add_u64 v[10:11], v[6:7], 0, v[84:85]
	global_store_dwordx4 v[10:11], v[2:5], off
	v_pk_mul_f32 v[10:11], v[68:69], s[22:23] op_sel_hi:[1,0]
	v_pk_mul_f32 v[12:13], v[66:67], s[22:23] op_sel_hi:[1,0]
	v_pk_mul_f32 v[4:5], v[72:73], s[22:23] op_sel_hi:[1,0]
	v_pk_mul_f32 v[2:3], v[70:71], s[22:23] op_sel_hi:[1,0]
	s_nop 0
	v_cvt_pk_bf16_f32 v2, v2, v3
	v_cvt_pk_bf16_f32 v3, v4, v5
	v_cvt_pk_bf16_f32 v4, v12, v13
	v_cvt_pk_bf16_f32 v5, v10, v11
	v_lshl_add_u64 v[10:11], v[6:7], 0, v[86:87]
	global_store_dwordx4 v[10:11], v[2:5], off
	v_pk_mul_f32 v[10:11], v[52:53], s[22:23] op_sel_hi:[1,0]
	v_pk_mul_f32 v[12:13], v[50:51], s[22:23] op_sel_hi:[1,0]
	v_pk_mul_f32 v[4:5], v[56:57], s[22:23] op_sel_hi:[1,0]
	v_pk_mul_f32 v[2:3], v[54:55], s[22:23] op_sel_hi:[1,0]
	s_nop 0
	v_cvt_pk_bf16_f32 v2, v2, v3
	v_cvt_pk_bf16_f32 v3, v4, v5
	v_cvt_pk_bf16_f32 v4, v12, v13
	v_cvt_pk_bf16_f32 v5, v10, v11
	v_lshl_add_u64 v[10:11], v[6:7], 0, v[88:89]
	global_store_dwordx4 v[10:11], v[2:5], off
	v_pk_mul_f32 v[10:11], v[36:37], s[22:23] op_sel_hi:[1,0]
	v_pk_mul_f32 v[12:13], v[34:35], s[22:23] op_sel_hi:[1,0]
	v_pk_mul_f32 v[4:5], v[40:41], s[22:23] op_sel_hi:[1,0]
	v_pk_mul_f32 v[2:3], v[38:39], s[22:23] op_sel_hi:[1,0]
	v_lshl_add_u64 v[6:7], v[6:7], 0, v[8:9]
	v_cvt_pk_bf16_f32 v2, v2, v3
	v_cvt_pk_bf16_f32 v3, v4, v5
	v_cvt_pk_bf16_f32 v4, v12, v13
	v_cvt_pk_bf16_f32 v5, v10, v11
	global_store_dwordx4 v[6:7], v[2:5], off
	s_cbranch_vccz .LBB0_519
	s_waitcnt vmcnt(0)
	s_cmpk_gt_u32 s28, 0xff
	s_cbranch_scc1 .LBB0_530
	s_barrier

.LBB0_582:
	s_add_i32 s64, s55, 0x18000
	s_lshl_b32 s12, s12, 12
	v_lshl_add_u64 v[8:9], v[8:9], 0, s[24:25]
	s_mov_b32 m0, s64
	s_add_i32 s65, s55, 0x1a000
	s_lshl_b32 s63, s13, 13
	s_and_b32 s20, s12, 0x3000
	s_waitcnt vmcnt(2)
	s_barrier
	global_load_lds_dwordx4 v[8:9], off
	v_lshl_add_u64 v[6:7], v[6:7], 0, s[24:25]
	s_mov_b32 m0, s65
	s_add_i32 s66, s55, 0x8000
	s_add_i32 s67, s55, 0xa000
	global_load_lds_dwordx4 v[6:7], off
	v_lshl_add_u64 v[4:5], v[4:5], 0, s[24:25]
	s_mov_b32 m0, s66
	s_add_u32 s12, s8, 0x10080
	global_load_lds_dwordx4 v[4:5], off
	v_lshl_add_u64 v[2:3], v[2:3], 0, s[24:25]
	s_mov_b32 m0, s67
	s_addc_u32 s13, s9, 0
	s_add_i32 s68, s55, 0x1c000
	global_load_lds_dwordx4 v[2:3], off
	v_lshl_add_u64 v[2:3], s[12:13], 0, v[136:137]
	s_mov_b32 m0, s68
	s_add_i32 s69, s55, 0x1e000
	global_load_lds_dwordx4 v[2:3], off
	v_lshl_add_u64 v[2:3], s[12:13], 0, v[132:133]
	s_mov_b32 m0, s69
	s_mov_b32 s70, 0
	global_load_lds_dwordx4 v[2:3], off
	v_and_b32_e32 v2, 15, v0
	v_and_b32_e32 v3, 48, v0
	v_lshlrev_b32_e32 v0, 2, v0
	v_lshl_or_b32 v2, v2, 6, v3
	v_and_b32_e32 v0, 32, v0
	v_xad_u32 v148, v2, v0, 0
	s_waitcnt vmcnt(6)
	v_add_u32_e32 v0, s20, v148
	v_mov_b32_e32 v2, v1
	v_mov_b32_e32 v3, v1
	v_add_u32_e32 v149, 0x10000, v0
	v_add_u32_e32 v150, 0x10400, v0
	v_add_u32_e32 v151, 0x10800, v0
	v_add_u32_e32 v152, 0x10c00, v0
	v_add_u32_e32 v153, 0x14000, v0
	v_add_u32_e32 v154, 0x14400, v0
	v_add_u32_e32 v155, 0x14800, v0
	v_add_u32_e32 v156, 0x14c00, v0
	v_add_u32_e32 v157, 0x18000, v0
	v_add_u32_e32 v158, 0x18400, v0
	v_add_u32_e32 v159, 0x18800, v0
	v_add_u32_e32 v160, 0x18c00, v0
	v_add_u32_e32 v161, 0x1c000, v0
	v_add_u32_e32 v162, 0x1c400, v0
	v_add_u32_e32 v163, 0x1c800, v0
	v_add_u32_e32 v164, 0x1cc00, v0
	v_mov_b32_e32 v0, v1
	v_mov_b64_e32 v[6:7], v[2:3]
	v_mov_b64_e32 v[10:11], v[2:3]
	v_mov_b64_e32 v[14:15], v[2:3]
	v_mov_b64_e32 v[18:19], v[2:3]
	v_mov_b64_e32 v[22:23], v[2:3]
	v_mov_b64_e32 v[26:27], v[2:3]
	v_mov_b64_e32 v[30:31], v[2:3]
	v_mov_b64_e32 v[34:35], v[2:3]
	v_mov_b64_e32 v[38:39], v[2:3]
	v_mov_b64_e32 v[42:43], v[2:3]
	v_mov_b64_e32 v[46:47], v[2:3]
	v_mov_b64_e32 v[50:51], v[2:3]
	v_mov_b64_e32 v[54:55], v[2:3]
	v_mov_b64_e32 v[58:59], v[2:3]
	v_mov_b64_e32 v[62:63], v[2:3]
	v_mov_b64_e32 v[66:67], v[2:3]
	v_mov_b64_e32 v[70:71], v[2:3]
	v_mov_b64_e32 v[74:75], v[2:3]
	v_mov_b64_e32 v[78:79], v[2:3]
	v_mov_b64_e32 v[82:83], v[2:3]
	v_mov_b64_e32 v[86:87], v[2:3]
	v_mov_b64_e32 v[90:91], v[2:3]
	v_mov_b64_e32 v[94:95], v[2:3]
	v_mov_b64_e32 v[98:99], v[2:3]
	v_mov_b64_e32 v[102:103], v[2:3]
	v_mov_b64_e32 v[106:107], v[2:3]
	v_mov_b64_e32 v[110:111], v[2:3]
	v_mov_b64_e32 v[114:115], v[2:3]
	v_mov_b64_e32 v[118:119], v[2:3]
	v_mov_b64_e32 v[122:123], v[2:3]
	v_mov_b64_e32 v[126:127], v[2:3]
	v_mov_b64_e32 v[130:131], v[2:3]
	v_mov_b64_e32 v[4:5], v[0:1]
	v_mov_b64_e32 v[8:9], v[0:1]
	v_mov_b64_e32 v[12:13], v[0:1]
	v_mov_b64_e32 v[16:17], v[0:1]
	v_mov_b64_e32 v[20:21], v[0:1]
	v_mov_b64_e32 v[24:25], v[0:1]
	v_mov_b64_e32 v[28:29], v[0:1]
	v_mov_b64_e32 v[32:33], v[0:1]
	v_mov_b64_e32 v[36:37], v[0:1]
	v_mov_b64_e32 v[40:41], v[0:1]
	v_mov_b64_e32 v[44:45], v[0:1]
	v_mov_b64_e32 v[48:49], v[0:1]
	v_mov_b64_e32 v[52:53], v[0:1]
	v_mov_b64_e32 v[56:57], v[0:1]
	v_mov_b64_e32 v[60:61], v[0:1]
	v_mov_b64_e32 v[64:65], v[0:1]
	v_mov_b64_e32 v[68:69], v[0:1]
	v_mov_b64_e32 v[72:73], v[0:1]
	v_mov_b64_e32 v[76:77], v[0:1]
	v_mov_b64_e32 v[80:81], v[0:1]
	v_mov_b64_e32 v[84:85], v[0:1]
	v_mov_b64_e32 v[88:89], v[0:1]
	v_mov_b64_e32 v[92:93], v[0:1]
	v_mov_b64_e32 v[96:97], v[0:1]
	v_mov_b64_e32 v[100:101], v[0:1]
	v_mov_b64_e32 v[104:105], v[0:1]
	v_mov_b64_e32 v[108:109], v[0:1]
	v_mov_b64_e32 v[112:113], v[0:1]
	v_mov_b64_e32 v[116:117], v[0:1]
	v_mov_b64_e32 v[120:121], v[0:1]
	v_mov_b64_e32 v[124:125], v[0:1]
	v_mov_b64_e32 v[128:129], v[0:1]
	v_readlane_b32 s71, v252, 56
	s_barrier
	s_branch .LBB0_584

.LBB0_585:
	s_add_u32 s47, s20, s46
	s_addc_u32 s77, s21, 0
	s_add_u32 s50, s47, 0x100
	s_addc_u32 s51, s77, 0
	s_and_b64 s[48:49], s[44:45], exec
	s_cselect_b32 s51, s73, s51
	s_cselect_b32 s50, s74, s50
	s_add_u32 s46, s34, s46
	s_addc_u32 s48, s35, 0
	s_add_u32 s46, s46, 0x100
	s_addc_u32 s48, s48, 0
	s_and_b64 s[44:45], s[44:45], exec
	s_cselect_b32 s53, s75, s48
	s_cselect_b32 s52, s76, s46
	s_add_u32 s78, s47, 0x20080
	s_addc_u32 s79, s77, 0
	s_add_i32 m0, s55, 0xc000
	s_add_i32 s77, s55, 0xe000
	ds_read_b128 v[140:143], v149
	ds_read_b128 v[144:147], v150
	ds_read_b128 v[166:169], v151
	ds_read_b128 v[170:173], v152
	s_add_u32 s48, s52, 0x10000
	s_addc_u32 s49, s53, 0
	s_add_u32 s46, s50, 0x20000
	s_addc_u32 s47, s51, 0
	s_add_u32 s44, s52, 0x10080
	s_addc_u32 s45, s53, 0
	v_add_u32_e32 v0, s63, v148
	v_lshl_add_u64 v[2:3], s[78:79], 0, v[138:139]
	ds_read_b128 v[174:177], v0
	ds_read_b128 v[178:181], v0 offset:1024
	ds_read_b128 v[182:185], v0 offset:2048
	ds_read_b128 v[188:191], v0 offset:3072
	ds_read_b128 v[192:195], v0 offset:4096
	ds_read_b128 v[196:199], v0 offset:5120
	ds_read_b128 v[200:203], v0 offset:6144
	ds_read_b128 v[204:207], v0 offset:7168
	global_load_lds_dwordx4 v[2:3], off
	v_lshl_add_u64 v[2:3], s[78:79], 0, v[134:135]
	s_mov_b32 m0, s77
	s_nop 0
	global_load_lds_dwordx4 v[2:3], off
	ds_read_b128 v[208:211], v153
	ds_read_b128 v[212:215], v154
	ds_read_b128 v[216:219], v155
	ds_read_b128 v[232:235], v156
	s_waitcnt lgkmcnt(4)
	s_waitcnt vmcnt(8)
	s_barrier
	s_waitcnt lgkmcnt(0)
	s_setprio 1
	s_waitcnt lgkmcnt(0)
	v_mfma_f32_16x16x32_bf16 v[128:131], v[140:143], v[174:177], v[128:131]
	v_mfma_f32_16x16x32_bf16 v[124:127], v[166:169], v[174:177], v[124:127]
	v_mfma_f32_16x16x32_bf16 v[120:123], v[140:143], v[182:185], v[120:123]
	v_mfma_f32_16x16x32_bf16 v[116:119], v[166:169], v[182:185], v[116:119]
	v_mfma_f32_16x16x32_bf16 v[112:115], v[140:143], v[192:195], v[112:115]
	v_mfma_f32_16x16x32_bf16 v[108:111], v[166:169], v[192:195], v[108:111]
	v_mfma_f32_16x16x32_bf16 v[104:107], v[140:143], v[200:203], v[104:107]
	v_mfma_f32_16x16x32_bf16 v[100:103], v[166:169], v[200:203], v[100:103]
	v_mfma_f32_16x16x32_bf16 v[128:131], v[144:147], v[178:181], v[128:131]
	v_mfma_f32_16x16x32_bf16 v[124:127], v[170:173], v[178:181], v[124:127]
	v_mfma_f32_16x16x32_bf16 v[120:123], v[144:147], v[188:191], v[120:123]
	v_mfma_f32_16x16x32_bf16 v[116:119], v[170:173], v[188:191], v[116:119]
	v_mfma_f32_16x16x32_bf16 v[112:115], v[144:147], v[196:199], v[112:115]
	v_mfma_f32_16x16x32_bf16 v[108:111], v[170:173], v[196:199], v[108:111]
	v_mfma_f32_16x16x32_bf16 v[104:107], v[144:147], v[204:207], v[104:107]
	v_mfma_f32_16x16x32_bf16 v[100:103], v[170:173], v[204:207], v[100:103]
	v_mfma_f32_16x16x32_bf16 v[96:99], v[208:211], v[174:177], v[96:99]
	v_mfma_f32_16x16x32_bf16 v[92:95], v[216:219], v[174:177], v[92:95]
	v_mfma_f32_16x16x32_bf16 v[88:91], v[208:211], v[182:185], v[88:91]
	v_mfma_f32_16x16x32_bf16 v[84:87], v[216:219], v[182:185], v[84:87]
	v_mfma_f32_16x16x32_bf16 v[80:83], v[208:211], v[192:195], v[80:83]
	v_mfma_f32_16x16x32_bf16 v[76:79], v[216:219], v[192:195], v[76:79]
	v_mfma_f32_16x16x32_bf16 v[72:75], v[208:211], v[200:203], v[72:75]
	v_mfma_f32_16x16x32_bf16 v[68:71], v[216:219], v[200:203], v[68:71]
	v_mfma_f32_16x16x32_bf16 v[96:99], v[212:215], v[178:181], v[96:99]
	v_mfma_f32_16x16x32_bf16 v[92:95], v[232:235], v[178:181], v[92:95]
	v_mfma_f32_16x16x32_bf16 v[88:91], v[212:215], v[188:191], v[88:91]
	v_mfma_f32_16x16x32_bf16 v[84:87], v[232:235], v[188:191], v[84:87]
	v_mfma_f32_16x16x32_bf16 v[80:83], v[212:215], v[196:199], v[80:83]
	v_mfma_f32_16x16x32_bf16 v[76:79], v[232:235], v[196:199], v[76:79]
	v_mfma_f32_16x16x32_bf16 v[72:75], v[212:215], v[204:207], v[72:75]
	v_mfma_f32_16x16x32_bf16 v[68:71], v[232:235], v[204:207], v[68:71]
	s_setprio 0
	s_mov_b32 m0, s55
	v_lshl_add_u64 v[236:237], s[50:51], 0, v[138:139]
	s_barrier
	ds_read_b128 v[174:177], v0 offset:16384
	ds_read_b128 v[178:181], v0 offset:17408
	ds_read_b128 v[182:185], v0 offset:18432
	ds_read_b128 v[188:191], v0 offset:19456
	ds_read_b128 v[192:195], v0 offset:20480
	ds_read_b128 v[196:199], v0 offset:21504
	ds_read_b128 v[200:203], v0 offset:22528
	ds_read_b128 v[204:207], v0 offset:23552
	global_load_lds_dwordx4 v[236:237], off
	v_lshl_add_u64 v[238:239], s[50:51], 0, v[134:135]
	s_mov_b32 m0, s58
	s_nop 0
	global_load_lds_dwordx4 v[238:239], off
	s_mov_b32 m0, s56
	v_lshl_add_u64 v[220:221], s[52:53], 0, v[136:137]
	global_load_lds_dwordx4 v[220:221], off
	v_lshl_add_u64 v[226:227], s[52:53], 0, v[132:133]
	s_mov_b32 m0, s57
	s_nop 0
	global_load_lds_dwordx4 v[226:227], off
	s_barrier
	s_waitcnt lgkmcnt(0)
	s_setprio 1
	s_waitcnt lgkmcnt(0)
	v_mfma_f32_16x16x32_bf16 v[64:67], v[140:143], v[174:177], v[64:67]
	v_mfma_f32_16x16x32_bf16 v[60:63], v[166:169], v[174:177], v[60:63]
	v_mfma_f32_16x16x32_bf16 v[56:59], v[140:143], v[182:185], v[56:59]
	v_mfma_f32_16x16x32_bf16 v[52:55], v[166:169], v[182:185], v[52:55]
	v_mfma_f32_16x16x32_bf16 v[48:51], v[140:143], v[192:195], v[48:51]
	v_mfma_f32_16x16x32_bf16 v[44:47], v[166:169], v[192:195], v[44:47]
	v_mfma_f32_16x16x32_bf16 v[40:43], v[140:143], v[200:203], v[40:43]
	v_mfma_f32_16x16x32_bf16 v[36:39], v[166:169], v[200:203], v[36:39]
	v_mfma_f32_16x16x32_bf16 v[64:67], v[144:147], v[178:181], v[64:67]
	v_mfma_f32_16x16x32_bf16 v[60:63], v[170:173], v[178:181], v[60:63]
	v_mfma_f32_16x16x32_bf16 v[56:59], v[144:147], v[188:191], v[56:59]
	v_mfma_f32_16x16x32_bf16 v[52:55], v[170:173], v[188:191], v[52:55]
	v_mfma_f32_16x16x32_bf16 v[48:51], v[144:147], v[196:199], v[48:51]
	v_mfma_f32_16x16x32_bf16 v[44:47], v[170:173], v[196:199], v[44:47]
	v_mfma_f32_16x16x32_bf16 v[40:43], v[144:147], v[204:207], v[40:43]
	v_mfma_f32_16x16x32_bf16 v[36:39], v[170:173], v[204:207], v[36:39]
	s_setprio 0
	s_barrier
	s_mov_b32 m0, s59
	v_lshl_add_u64 v[2:3], s[48:49], 0, v[136:137]
	global_load_lds_dwordx4 v[2:3], off
	v_lshl_add_u64 v[2:3], s[48:49], 0, v[132:133]
	s_mov_b32 m0, s60
	s_nop 0
	global_load_lds_dwordx4 v[2:3], off
	s_waitcnt vmcnt(8)
	s_barrier
	s_setprio 1
	v_mfma_f32_16x16x32_bf16 v[32:35], v[208:211], v[174:177], v[32:35]
	v_mfma_f32_16x16x32_bf16 v[28:31], v[216:219], v[174:177], v[28:31]
	v_mfma_f32_16x16x32_bf16 v[24:27], v[208:211], v[182:185], v[24:27]
	v_mfma_f32_16x16x32_bf16 v[20:23], v[216:219], v[182:185], v[20:23]
	v_mfma_f32_16x16x32_bf16 v[16:19], v[208:211], v[192:195], v[16:19]
	v_mfma_f32_16x16x32_bf16 v[12:15], v[216:219], v[192:195], v[12:15]
	v_mfma_f32_16x16x32_bf16 v[8:11], v[208:211], v[200:203], v[8:11]
	v_mfma_f32_16x16x32_bf16 v[2:5], v[216:219], v[200:203], v[4:7]
	v_mfma_f32_16x16x32_bf16 v[32:35], v[212:215], v[178:181], v[32:35]
	v_mfma_f32_16x16x32_bf16 v[28:31], v[232:235], v[178:181], v[28:31]
	v_mfma_f32_16x16x32_bf16 v[24:27], v[212:215], v[188:191], v[24:27]
	v_mfma_f32_16x16x32_bf16 v[20:23], v[232:235], v[188:191], v[20:23]
	v_mfma_f32_16x16x32_bf16 v[16:19], v[212:215], v[196:199], v[16:19]
	v_mfma_f32_16x16x32_bf16 v[12:15], v[232:235], v[196:199], v[12:15]
	v_mfma_f32_16x16x32_bf16 v[8:11], v[212:215], v[204:207], v[8:11]
	v_mfma_f32_16x16x32_bf16 v[2:5], v[232:235], v[204:207], v[2:5]
	s_setprio 0
	s_barrier
	ds_read_b128 v[140:143], v157
	ds_read_b128 v[144:147], v158
	ds_read_b128 v[166:169], v159
	ds_read_b128 v[170:173], v160
	s_mov_b32 m0, s61
	v_lshl_add_u64 v[6:7], s[46:47], 0, v[138:139]
	ds_read_b128 v[174:177], v0 offset:32768
	ds_read_b128 v[178:181], v0 offset:33792
	ds_read_b128 v[182:185], v0 offset:34816
	ds_read_b128 v[188:191], v0 offset:35840
	ds_read_b128 v[192:195], v0 offset:36864
	ds_read_b128 v[196:199], v0 offset:37888
	ds_read_b128 v[200:203], v0 offset:38912
	ds_read_b128 v[204:207], v0 offset:39936
	global_load_lds_dwordx4 v[6:7], off
	v_lshl_add_u64 v[6:7], s[46:47], 0, v[134:135]
	s_mov_b32 m0, s62
	s_nop 0
	global_load_lds_dwordx4 v[6:7], off
	ds_read_b128 v[208:211], v161
	ds_read_b128 v[212:215], v162
	ds_read_b128 v[216:219], v163
	ds_read_b128 v[232:235], v164
	s_waitcnt lgkmcnt(4)
	s_waitcnt vmcnt(8)
	s_barrier
	s_waitcnt lgkmcnt(0)
	s_setprio 1
	s_waitcnt lgkmcnt(0)
	v_mfma_f32_16x16x32_bf16 v[128:131], v[140:143], v[174:177], v[128:131]
	v_mfma_f32_16x16x32_bf16 v[124:127], v[166:169], v[174:177], v[124:127]
	v_mfma_f32_16x16x32_bf16 v[120:123], v[140:143], v[182:185], v[120:123]
	v_mfma_f32_16x16x32_bf16 v[116:119], v[166:169], v[182:185], v[116:119]
	v_mfma_f32_16x16x32_bf16 v[112:115], v[140:143], v[192:195], v[112:115]
	v_mfma_f32_16x16x32_bf16 v[108:111], v[166:169], v[192:195], v[108:111]
	v_mfma_f32_16x16x32_bf16 v[104:107], v[140:143], v[200:203], v[104:107]
	v_mfma_f32_16x16x32_bf16 v[100:103], v[166:169], v[200:203], v[100:103]
	v_mfma_f32_16x16x32_bf16 v[128:131], v[144:147], v[178:181], v[128:131]
	v_mfma_f32_16x16x32_bf16 v[124:127], v[170:173], v[178:181], v[124:127]
	v_mfma_f32_16x16x32_bf16 v[120:123], v[144:147], v[188:191], v[120:123]
	v_mfma_f32_16x16x32_bf16 v[116:119], v[170:173], v[188:191], v[116:119]
	v_mfma_f32_16x16x32_bf16 v[112:115], v[144:147], v[196:199], v[112:115]
	v_mfma_f32_16x16x32_bf16 v[108:111], v[170:173], v[196:199], v[108:111]
	v_mfma_f32_16x16x32_bf16 v[104:107], v[144:147], v[204:207], v[104:107]
	v_mfma_f32_16x16x32_bf16 v[100:103], v[170:173], v[204:207], v[100:103]
	v_mfma_f32_16x16x32_bf16 v[96:99], v[208:211], v[174:177], v[96:99]
	v_mfma_f32_16x16x32_bf16 v[92:95], v[216:219], v[174:177], v[92:95]
	v_mfma_f32_16x16x32_bf16 v[88:91], v[208:211], v[182:185], v[88:91]
	v_mfma_f32_16x16x32_bf16 v[84:87], v[216:219], v[182:185], v[84:87]
	v_mfma_f32_16x16x32_bf16 v[80:83], v[208:211], v[192:195], v[80:83]
	v_mfma_f32_16x16x32_bf16 v[76:79], v[216:219], v[192:195], v[76:79]
	v_mfma_f32_16x16x32_bf16 v[72:75], v[208:211], v[200:203], v[72:75]
	v_mfma_f32_16x16x32_bf16 v[68:71], v[216:219], v[200:203], v[68:71]
	v_mfma_f32_16x16x32_bf16 v[96:99], v[212:215], v[178:181], v[96:99]
	v_mfma_f32_16x16x32_bf16 v[92:95], v[232:235], v[178:181], v[92:95]
	v_mfma_f32_16x16x32_bf16 v[88:91], v[212:215], v[188:191], v[88:91]
	v_mfma_f32_16x16x32_bf16 v[84:87], v[232:235], v[188:191], v[84:87]
	v_mfma_f32_16x16x32_bf16 v[80:83], v[212:215], v[196:199], v[80:83]
	v_mfma_f32_16x16x32_bf16 v[76:79], v[232:235], v[196:199], v[76:79]
	v_mfma_f32_16x16x32_bf16 v[72:75], v[212:215], v[204:207], v[72:75]
	v_mfma_f32_16x16x32_bf16 v[68:71], v[232:235], v[204:207], v[68:71]
	s_setprio 0
	s_barrier
	ds_read_b128 v[174:177], v0 offset:49152
	ds_read_b128 v[178:181], v0 offset:50176
	ds_read_b128 v[182:185], v0 offset:51200
	ds_read_b128 v[188:191], v0 offset:52224
	ds_read_b128 v[192:195], v0 offset:53248
	ds_read_b128 v[196:199], v0 offset:54272
	ds_read_b128 v[200:203], v0 offset:55296
	ds_read_b128 v[204:207], v0 offset:56320
	s_mov_b32 m0, s64
	v_lshl_add_u64 v[6:7], v[220:221], 0, s[24:25]
	global_load_lds_dwordx4 v[6:7], off
	v_lshl_add_u64 v[6:7], v[226:227], 0, s[24:25]
	s_mov_b32 m0, s65
	s_nop 0
	global_load_lds_dwordx4 v[6:7], off
	s_mov_b32 m0, s66
	v_lshl_add_u64 v[6:7], v[236:237], 0, s[24:25]
	global_load_lds_dwordx4 v[6:7], off
	v_lshl_add_u64 v[6:7], v[238:239], 0, s[24:25]
	s_mov_b32 m0, s67
	s_nop 0
	global_load_lds_dwordx4 v[6:7], off
	s_barrier
	s_waitcnt lgkmcnt(0)
	s_setprio 1
	s_waitcnt lgkmcnt(0)
	v_mfma_f32_16x16x32_bf16 v[64:67], v[140:143], v[174:177], v[64:67]
	v_mfma_f32_16x16x32_bf16 v[60:63], v[166:169], v[174:177], v[60:63]
	v_mfma_f32_16x16x32_bf16 v[56:59], v[140:143], v[182:185], v[56:59]
	v_mfma_f32_16x16x32_bf16 v[52:55], v[166:169], v[182:185], v[52:55]
	v_mfma_f32_16x16x32_bf16 v[48:51], v[140:143], v[192:195], v[48:51]
	v_mfma_f32_16x16x32_bf16 v[44:47], v[166:169], v[192:195], v[44:47]
	v_mfma_f32_16x16x32_bf16 v[40:43], v[140:143], v[200:203], v[40:43]
	v_mfma_f32_16x16x32_bf16 v[36:39], v[166:169], v[200:203], v[36:39]
	v_mfma_f32_16x16x32_bf16 v[64:67], v[144:147], v[178:181], v[64:67]
	v_mfma_f32_16x16x32_bf16 v[60:63], v[170:173], v[178:181], v[60:63]
	v_mfma_f32_16x16x32_bf16 v[56:59], v[144:147], v[188:191], v[56:59]
	v_mfma_f32_16x16x32_bf16 v[52:55], v[170:173], v[188:191], v[52:55]
	v_mfma_f32_16x16x32_bf16 v[48:51], v[144:147], v[196:199], v[48:51]
	v_mfma_f32_16x16x32_bf16 v[44:47], v[170:173], v[196:199], v[44:47]
	v_mfma_f32_16x16x32_bf16 v[40:43], v[144:147], v[204:207], v[40:43]
	v_mfma_f32_16x16x32_bf16 v[36:39], v[170:173], v[204:207], v[36:39]
	s_setprio 0
	s_barrier
	s_mov_b32 m0, s68
	v_lshl_add_u64 v[6:7], s[44:45], 0, v[136:137]
	global_load_lds_dwordx4 v[6:7], off
	v_lshl_add_u64 v[6:7], s[44:45], 0, v[132:133]
	s_mov_b32 m0, s69
	s_nop 0
	global_load_lds_dwordx4 v[6:7], off
	s_waitcnt vmcnt(8)
	s_barrier
	s_setprio 1
	v_mfma_f32_16x16x32_bf16 v[32:35], v[208:211], v[174:177], v[32:35]
	v_mfma_f32_16x16x32_bf16 v[28:31], v[216:219], v[174:177], v[28:31]
	v_mfma_f32_16x16x32_bf16 v[24:27], v[208:211], v[182:185], v[24:27]
	v_mfma_f32_16x16x32_bf16 v[20:23], v[216:219], v[182:185], v[20:23]
	v_mfma_f32_16x16x32_bf16 v[16:19], v[208:211], v[192:195], v[16:19]
	v_mfma_f32_16x16x32_bf16 v[12:15], v[216:219], v[192:195], v[12:15]
	v_mfma_f32_16x16x32_bf16 v[6:9], v[208:211], v[200:203], v[8:11]
	v_mfma_f32_16x16x32_bf16 v[2:5], v[216:219], v[200:203], v[2:5]
	v_mfma_f32_16x16x32_bf16 v[32:35], v[212:215], v[178:181], v[32:35]
	v_mfma_f32_16x16x32_bf16 v[28:31], v[232:235], v[178:181], v[28:31]
	v_mfma_f32_16x16x32_bf16 v[24:27], v[212:215], v[188:191], v[24:27]
	v_mfma_f32_16x16x32_bf16 v[20:23], v[232:235], v[188:191], v[20:23]
	v_mfma_f32_16x16x32_bf16 v[16:19], v[212:215], v[196:199], v[16:19]
	v_mfma_f32_16x16x32_bf16 v[12:15], v[232:235], v[196:199], v[12:15]
	v_mfma_f32_16x16x32_bf16 v[8:11], v[212:215], v[204:207], v[6:9]
	v_mfma_f32_16x16x32_bf16 v[4:7], v[232:235], v[204:207], v[2:5]
	s_setprio 0
	s_movk_i32 s46, 0x100
	s_andn2_b64 vcc, exec, s[42:43]
	s_mov_b64 s[44:45], -1
	s_mov_b64 s[42:43], 0
	s_barrier
	s_cbranch_vccz .LBB0_585
	s_bfe_u32 s42, s72, 0x20004
	v_cvt_f32_ubyte0_e32 v2, s42
	v_sub_f32_e32 v2, 0xc0a00000, v2
	s_mov_b32 s46, 0xc2fc0000
	v_cmp_gt_f32_e32 vcc, s46, v2
	s_ashr_i32 s20, s72, 1
	s_ashr_i32 s21, s20, 31
	v_cndmask_b32_e32 v3, 0, v224, vcc
	v_add_f32_e32 v2, v2, v3
	v_exp_f32_e32 v2, v2
	s_and_b32 s42, s20, 7
	s_and_b64 s[44:45], vcc, exec
	s_cselect_b32 s43, 0xffffffc0, 0
	v_ldexp_f32 v2, v2, s43
	v_sub_f32_e32 v2, 1.0, v2
	v_log_f32_e32 v2, v2
	v_readlane_b32 s34, v252, 51
	v_readlane_b32 s35, v252, 52
	v_mbcnt_lo_u32_b32 v0, -1, 0
	v_mbcnt_hi_u32_b32 v0, -1, v0
	v_mul_f32_e32 v3, 0x43800000, v2
	v_cmp_gt_f32_e32 vcc, s46, v3
	s_and_b64 s[44:45], vcc, exec
	s_cselect_b32 s43, 0xffffffc0, 0
	v_cndmask_b32_e32 v3, 0, v224, vcc
	v_fmac_f32_e32 v3, 0x43800000, v2
	v_exp_f32_e32 v2, v3
	v_and_b32_e32 v3, 15, v0
	s_lshl_b64 s[20:21], s[20:21], 9
	v_ldexp_f32 v2, v2, s43
	s_lshl_b32 s43, s72, 8
	s_and_b32 s43, s43, 0x100
	v_lshl_or_b32 v142, s34, 6, v3
	s_lshl_b32 s34, s35, 5
	v_lshrrev_b32_e32 v0, 1, v0
	s_or_b32 s20, s20, s43
	s_ashr_i32 s35, s34, 31
	v_and_b32_e32 v0, 24, v0
	v_mov_b32_e32 v140, v2
	v_mov_b32_e32 v141, v2
	s_cmp_gt_i32 s42, 6
	v_lshlrev_b32_e32 v0, 1, v0
	s_cbranch_scc1 .LBB0_611
	v_ashrrev_i32_e32 v143, 31, v142
	v_lshl_add_u64 v[144:145], s[20:21], 0, v[142:143]
	v_lshlrev_b64 v[144:145], 10, v[144:145]
	v_lshl_add_u64 v[144:145], s[6:7], 0, v[144:145]
	v_lshl_add_u64 v[144:145], s[34:35], 1, v[144:145]
	v_lshl_add_u64 v[146:147], v[144:145], 0, v[0:1]
	s_mov_b64 s[44:45], 0x200
	s_cmp_lg_u32 s42, 0
	v_lshl_add_u64 v[144:145], v[146:147], 0, s[44:45]
	s_cbranch_scc1 .LBB0_589
	v_mov_b32 v166, 0
	s_nop 0
	v_mov_b32_e32 v167, v166
	v_mov_b32_e32 v168, v166
	v_mov_b32_e32 v169, v166
	global_store_dwordx4 v[144:145], v[166:169], off

.LBB0_642:
	s_add_u32 s20, s4, 0x200
	s_addc_u32 s21, s5, 0
	s_add_i32 s65, s56, 0x18000
	s_lshl_b32 s4, s8, 12
	v_lshl_add_u64 v[6:7], v[6:7], 0, s[24:25]
	s_mov_b32 m0, s65
	s_add_i32 s66, s56, 0x1a000
	s_and_b32 s8, s4, 0x3000
	s_waitcnt vmcnt(2)
	s_barrier
	global_load_lds_dwordx4 v[6:7], off
	v_lshl_add_u64 v[6:7], v[8:9], 0, s[24:25]
	s_mov_b32 m0, s66
	s_mov_b64 s[4:5], 0x280
	s_add_i32 s67, s56, 0x8000
	s_lshl_b32 s64, s9, 13
	global_load_lds_dwordx4 v[6:7], off
	v_lshl_add_u64 v[2:3], v[2:3], 0, s[4:5]
	s_mov_b32 m0, s67
	s_add_i32 s68, s56, 0xa000
	global_load_lds_dwordx4 v[2:3], off
	v_lshl_add_u64 v[2:3], v[4:5], 0, s[4:5]
	s_add_u32 s4, s12, 0x40080
	s_mov_b32 m0, s68
	s_addc_u32 s5, s13, 0
	s_add_i32 s69, s56, 0x1c000
	global_load_lds_dwordx4 v[2:3], off
	v_lshl_add_u64 v[2:3], s[4:5], 0, v[0:1]
	s_mov_b32 m0, s69
	s_add_i32 s70, s56, 0x1e000
	global_load_lds_dwordx4 v[2:3], off
	v_lshl_add_u64 v[2:3], s[4:5], 0, v[130:131]
	s_mov_b32 m0, s70
	s_mov_b32 s71, 0
	global_load_lds_dwordx4 v[2:3], off
	v_and_b32_e32 v2, 15, v10
	v_and_b32_e32 v3, 48, v10
	v_lshl_or_b32 v2, v2, 6, v3
	v_lshlrev_b32_e32 v3, 2, v10
	v_and_b32_e32 v3, 32, v3
	s_waitcnt vmcnt(6)
	v_xad_u32 v140, v2, v3, 0
	v_add_u32_e32 v2, s8, v140
	v_add_u32_e32 v141, 0x10000, v2
	v_add_u32_e32 v142, 0x10400, v2
	v_add_u32_e32 v143, 0x10800, v2
	v_add_u32_e32 v144, 0x10c00, v2
	v_add_u32_e32 v145, 0x14000, v2
	v_add_u32_e32 v146, 0x14400, v2
	v_add_u32_e32 v147, 0x14800, v2
	v_add_u32_e32 v148, 0x14c00, v2
	v_add_u32_e32 v149, 0x18000, v2
	v_add_u32_e32 v150, 0x18400, v2
	v_add_u32_e32 v151, 0x18800, v2
	v_add_u32_e32 v152, 0x18c00, v2
	v_add_u32_e32 v153, 0x1c000, v2
	v_add_u32_e32 v154, 0x1c400, v2
	v_add_u32_e32 v155, 0x1c800, v2
	v_add_u32_e32 v156, 0x1cc00, v2
	v_readlane_b32 s28, v254, 9
	s_barrier

.LBB0_648:
	s_add_u32 s45, s20, s44
	s_addc_u32 s53, s21, 0
	s_add_u32 s48, s45, 0x100
	s_addc_u32 s49, s53, 0
	s_and_b64 s[46:47], s[42:43], exec
	s_cselect_b32 s49, s9, s49
	s_cselect_b32 s48, s8, s48
	s_add_u32 s44, s12, s44
	s_addc_u32 s46, s13, 0
	s_add_u32 s44, s44, 0x100
	s_addc_u32 s46, s46, 0
	s_and_b64 s[42:43], s[42:43], exec
	s_cselect_b32 s51, s73, s46
	s_cselect_b32 s50, s74, s44
	s_add_u32 s52, s45, 0x80080
	s_addc_u32 s53, s53, 0
	s_add_i32 m0, s56, 0xc000
	s_add_i32 s75, s56, 0xe000
	ds_read_b128 v[136:139], v141
	ds_read_b128 v[158:161], v142
	ds_read_b128 v[162:165], v143
	ds_read_b128 v[166:169], v144
	s_add_u32 s46, s50, 0x40000
	s_addc_u32 s47, s51, 0
	s_add_u32 s44, s48, 0x80000
	s_addc_u32 s45, s49, 0
	s_add_u32 s42, s50, 0x40080
	s_addc_u32 s43, s51, 0
	v_add_u32_e32 v157, s64, v140
	v_lshl_add_u64 v[204:205], s[52:53], 0, v[134:135]
	ds_read_b128 v[170:173], v157
	ds_read_b128 v[174:177], v157 offset:1024
	ds_read_b128 v[178:181], v157 offset:2048
	ds_read_b128 v[182:185], v157 offset:3072
	ds_read_b128 v[188:191], v157 offset:4096
	ds_read_b128 v[192:195], v157 offset:5120
	ds_read_b128 v[196:199], v157 offset:6144
	ds_read_b128 v[200:203], v157 offset:7168
	global_load_lds_dwordx4 v[204:205], off
	v_lshl_add_u64 v[204:205], s[52:53], 0, v[132:133]
	s_mov_b32 m0, s75
	s_nop 0
	global_load_lds_dwordx4 v[204:205], off
	ds_read_b128 v[204:207], v145
	ds_read_b128 v[208:211], v146
	ds_read_b128 v[212:215], v147
	ds_read_b128 v[216:219], v148
	s_waitcnt lgkmcnt(4)
	s_waitcnt vmcnt(8)
	s_barrier
	s_waitcnt lgkmcnt(0)
	s_setprio 1
	s_waitcnt lgkmcnt(0)
	v_mfma_f32_16x16x32_bf16 v[126:129], v[136:139], v[170:173], v[126:129]
	v_mfma_f32_16x16x32_bf16 v[122:125], v[162:165], v[170:173], v[122:125]
	v_mfma_f32_16x16x32_bf16 v[110:113], v[136:139], v[178:181], v[110:113]
	v_mfma_f32_16x16x32_bf16 v[106:109], v[162:165], v[178:181], v[106:109]
	v_mfma_f32_16x16x32_bf16 v[94:97], v[136:139], v[188:191], v[94:97]
	v_mfma_f32_16x16x32_bf16 v[90:93], v[162:165], v[188:191], v[90:93]
	v_mfma_f32_16x16x32_bf16 v[78:81], v[136:139], v[196:199], v[78:81]
	v_mfma_f32_16x16x32_bf16 v[74:77], v[162:165], v[196:199], v[74:77]
	v_mfma_f32_16x16x32_bf16 v[126:129], v[158:161], v[174:177], v[126:129]
	v_mfma_f32_16x16x32_bf16 v[122:125], v[166:169], v[174:177], v[122:125]
	v_mfma_f32_16x16x32_bf16 v[110:113], v[158:161], v[182:185], v[110:113]
	v_mfma_f32_16x16x32_bf16 v[106:109], v[166:169], v[182:185], v[106:109]
	v_mfma_f32_16x16x32_bf16 v[94:97], v[158:161], v[192:195], v[94:97]
	v_mfma_f32_16x16x32_bf16 v[90:93], v[166:169], v[192:195], v[90:93]
	v_mfma_f32_16x16x32_bf16 v[78:81], v[158:161], v[200:203], v[78:81]
	v_mfma_f32_16x16x32_bf16 v[74:77], v[166:169], v[200:203], v[74:77]
	v_mfma_f32_16x16x32_bf16 v[118:121], v[204:207], v[170:173], v[118:121]
	v_mfma_f32_16x16x32_bf16 v[114:117], v[212:215], v[170:173], v[114:117]
	v_mfma_f32_16x16x32_bf16 v[102:105], v[204:207], v[178:181], v[102:105]
	v_mfma_f32_16x16x32_bf16 v[98:101], v[212:215], v[178:181], v[98:101]
	v_mfma_f32_16x16x32_bf16 v[86:89], v[204:207], v[188:191], v[86:89]
	v_mfma_f32_16x16x32_bf16 v[82:85], v[212:215], v[188:191], v[82:85]
	v_mfma_f32_16x16x32_bf16 v[70:73], v[204:207], v[196:199], v[70:73]
	v_mfma_f32_16x16x32_bf16 v[66:69], v[212:215], v[196:199], v[66:69]
	v_mfma_f32_16x16x32_bf16 v[118:121], v[208:211], v[174:177], v[118:121]
	v_mfma_f32_16x16x32_bf16 v[114:117], v[216:219], v[174:177], v[114:117]
	v_mfma_f32_16x16x32_bf16 v[102:105], v[208:211], v[182:185], v[102:105]
	v_mfma_f32_16x16x32_bf16 v[98:101], v[216:219], v[182:185], v[98:101]
	v_mfma_f32_16x16x32_bf16 v[86:89], v[208:211], v[192:195], v[86:89]
	v_mfma_f32_16x16x32_bf16 v[82:85], v[216:219], v[192:195], v[82:85]
	v_mfma_f32_16x16x32_bf16 v[70:73], v[208:211], v[200:203], v[70:73]
	v_mfma_f32_16x16x32_bf16 v[66:69], v[216:219], v[200:203], v[66:69]
	s_setprio 0
	s_mov_b32 m0, s56
	v_lshl_add_u64 v[232:233], s[48:49], 0, v[134:135]
	s_barrier
	ds_read_b128 v[170:173], v157 offset:16384
	ds_read_b128 v[174:177], v157 offset:17408
	ds_read_b128 v[178:181], v157 offset:18432
	ds_read_b128 v[182:185], v157 offset:19456
	ds_read_b128 v[188:191], v157 offset:20480
	ds_read_b128 v[192:195], v157 offset:21504
	ds_read_b128 v[196:199], v157 offset:22528
	ds_read_b128 v[200:203], v157 offset:23552
	global_load_lds_dwordx4 v[232:233], off
	v_lshl_add_u64 v[234:235], s[48:49], 0, v[132:133]
	s_mov_b32 m0, s59
	s_nop 0
	global_load_lds_dwordx4 v[234:235], off
	s_mov_b32 m0, s57
	v_lshl_add_u64 v[220:221], s[50:51], 0, v[0:1]
	global_load_lds_dwordx4 v[220:221], off
	v_lshl_add_u64 v[226:227], s[50:51], 0, v[130:131]
	s_mov_b32 m0, s58
	s_nop 0
	global_load_lds_dwordx4 v[226:227], off
	s_barrier
	s_waitcnt lgkmcnt(0)
	s_setprio 1
	s_waitcnt lgkmcnt(0)
	v_mfma_f32_16x16x32_bf16 v[62:65], v[136:139], v[170:173], v[62:65]
	v_mfma_f32_16x16x32_bf16 v[58:61], v[162:165], v[170:173], v[58:61]
	v_mfma_f32_16x16x32_bf16 v[46:49], v[136:139], v[178:181], v[46:49]
	v_mfma_f32_16x16x32_bf16 v[42:45], v[162:165], v[178:181], v[42:45]
	v_mfma_f32_16x16x32_bf16 v[30:33], v[136:139], v[188:191], v[30:33]
	v_mfma_f32_16x16x32_bf16 v[26:29], v[162:165], v[188:191], v[26:29]
	v_mfma_f32_16x16x32_bf16 v[14:17], v[136:139], v[196:199], v[14:17]
	v_mfma_f32_16x16x32_bf16 v[10:13], v[162:165], v[196:199], v[10:13]
	v_mfma_f32_16x16x32_bf16 v[62:65], v[158:161], v[174:177], v[62:65]
	v_mfma_f32_16x16x32_bf16 v[58:61], v[166:169], v[174:177], v[58:61]
	v_mfma_f32_16x16x32_bf16 v[46:49], v[158:161], v[182:185], v[46:49]
	v_mfma_f32_16x16x32_bf16 v[42:45], v[166:169], v[182:185], v[42:45]
	v_mfma_f32_16x16x32_bf16 v[30:33], v[158:161], v[192:195], v[30:33]
	v_mfma_f32_16x16x32_bf16 v[26:29], v[166:169], v[192:195], v[26:29]
	v_mfma_f32_16x16x32_bf16 v[14:17], v[158:161], v[200:203], v[14:17]
	v_mfma_f32_16x16x32_bf16 v[10:13], v[166:169], v[200:203], v[10:13]
	s_setprio 0
	s_barrier
	s_mov_b32 m0, s60
	v_lshl_add_u64 v[136:137], s[46:47], 0, v[0:1]
	global_load_lds_dwordx4 v[136:137], off
	v_lshl_add_u64 v[136:137], s[46:47], 0, v[130:131]
	s_mov_b32 m0, s61
	s_nop 0
	global_load_lds_dwordx4 v[136:137], off
	s_waitcnt vmcnt(8)
	s_barrier
	s_setprio 1
	v_mfma_f32_16x16x32_bf16 v[54:57], v[204:207], v[170:173], v[54:57]
	v_mfma_f32_16x16x32_bf16 v[50:53], v[212:215], v[170:173], v[50:53]
	v_mfma_f32_16x16x32_bf16 v[38:41], v[204:207], v[178:181], v[38:41]
	v_mfma_f32_16x16x32_bf16 v[34:37], v[212:215], v[178:181], v[34:37]
	v_mfma_f32_16x16x32_bf16 v[22:25], v[204:207], v[188:191], v[22:25]
	v_mfma_f32_16x16x32_bf16 v[18:21], v[212:215], v[188:191], v[18:21]
	v_mfma_f32_16x16x32_bf16 v[6:9], v[204:207], v[196:199], v[6:9]
	v_mfma_f32_16x16x32_bf16 v[2:5], v[212:215], v[196:199], v[2:5]
	v_mfma_f32_16x16x32_bf16 v[54:57], v[208:211], v[174:177], v[54:57]
	v_mfma_f32_16x16x32_bf16 v[50:53], v[216:219], v[174:177], v[50:53]
	v_mfma_f32_16x16x32_bf16 v[38:41], v[208:211], v[182:185], v[38:41]
	v_mfma_f32_16x16x32_bf16 v[34:37], v[216:219], v[182:185], v[34:37]
	v_mfma_f32_16x16x32_bf16 v[22:25], v[208:211], v[192:195], v[22:25]
	v_mfma_f32_16x16x32_bf16 v[18:21], v[216:219], v[192:195], v[18:21]
	v_mfma_f32_16x16x32_bf16 v[6:9], v[208:211], v[200:203], v[6:9]
	v_mfma_f32_16x16x32_bf16 v[2:5], v[216:219], v[200:203], v[2:5]
	s_setprio 0
	s_barrier
	ds_read_b128 v[136:139], v149
	ds_read_b128 v[158:161], v150
	ds_read_b128 v[162:165], v151
	ds_read_b128 v[166:169], v152
	s_mov_b32 m0, s62
	v_lshl_add_u64 v[204:205], s[44:45], 0, v[134:135]
	ds_read_b128 v[170:173], v157 offset:32768
	ds_read_b128 v[174:177], v157 offset:33792
	ds_read_b128 v[178:181], v157 offset:34816
	ds_read_b128 v[182:185], v157 offset:35840
	ds_read_b128 v[188:191], v157 offset:36864
	ds_read_b128 v[192:195], v157 offset:37888
	ds_read_b128 v[196:199], v157 offset:38912
	ds_read_b128 v[200:203], v157 offset:39936
	global_load_lds_dwordx4 v[204:205], off
	v_lshl_add_u64 v[204:205], s[44:45], 0, v[132:133]
	s_mov_b32 m0, s63
	s_nop 0
	global_load_lds_dwordx4 v[204:205], off
	ds_read_b128 v[204:207], v153
	ds_read_b128 v[208:211], v154
	ds_read_b128 v[212:215], v155
	ds_read_b128 v[216:219], v156
	s_waitcnt lgkmcnt(4)
	s_waitcnt vmcnt(8)
	s_barrier
	s_waitcnt lgkmcnt(0)
	s_setprio 1
	s_waitcnt lgkmcnt(0)
	v_mfma_f32_16x16x32_bf16 v[126:129], v[136:139], v[170:173], v[126:129]
	v_mfma_f32_16x16x32_bf16 v[122:125], v[162:165], v[170:173], v[122:125]
	v_mfma_f32_16x16x32_bf16 v[110:113], v[136:139], v[178:181], v[110:113]
	v_mfma_f32_16x16x32_bf16 v[106:109], v[162:165], v[178:181], v[106:109]
	v_mfma_f32_16x16x32_bf16 v[94:97], v[136:139], v[188:191], v[94:97]
	v_mfma_f32_16x16x32_bf16 v[90:93], v[162:165], v[188:191], v[90:93]
	v_mfma_f32_16x16x32_bf16 v[78:81], v[136:139], v[196:199], v[78:81]
	v_mfma_f32_16x16x32_bf16 v[74:77], v[162:165], v[196:199], v[74:77]
	v_mfma_f32_16x16x32_bf16 v[126:129], v[158:161], v[174:177], v[126:129]
	v_mfma_f32_16x16x32_bf16 v[122:125], v[166:169], v[174:177], v[122:125]
	v_mfma_f32_16x16x32_bf16 v[110:113], v[158:161], v[182:185], v[110:113]
	v_mfma_f32_16x16x32_bf16 v[106:109], v[166:169], v[182:185], v[106:109]
	v_mfma_f32_16x16x32_bf16 v[94:97], v[158:161], v[192:195], v[94:97]
	v_mfma_f32_16x16x32_bf16 v[90:93], v[166:169], v[192:195], v[90:93]
	v_mfma_f32_16x16x32_bf16 v[78:81], v[158:161], v[200:203], v[78:81]
	v_mfma_f32_16x16x32_bf16 v[74:77], v[166:169], v[200:203], v[74:77]
	v_mfma_f32_16x16x32_bf16 v[118:121], v[204:207], v[170:173], v[118:121]
	v_mfma_f32_16x16x32_bf16 v[114:117], v[212:215], v[170:173], v[114:117]
	v_mfma_f32_16x16x32_bf16 v[102:105], v[204:207], v[178:181], v[102:105]
	v_mfma_f32_16x16x32_bf16 v[98:101], v[212:215], v[178:181], v[98:101]
	v_mfma_f32_16x16x32_bf16 v[86:89], v[204:207], v[188:191], v[86:89]
	v_mfma_f32_16x16x32_bf16 v[82:85], v[212:215], v[188:191], v[82:85]
	v_mfma_f32_16x16x32_bf16 v[70:73], v[204:207], v[196:199], v[70:73]
	v_mfma_f32_16x16x32_bf16 v[66:69], v[212:215], v[196:199], v[66:69]
	v_mfma_f32_16x16x32_bf16 v[118:121], v[208:211], v[174:177], v[118:121]
	v_mfma_f32_16x16x32_bf16 v[114:117], v[216:219], v[174:177], v[114:117]
	v_mfma_f32_16x16x32_bf16 v[102:105], v[208:211], v[182:185], v[102:105]
	v_mfma_f32_16x16x32_bf16 v[98:101], v[216:219], v[182:185], v[98:101]
	v_mfma_f32_16x16x32_bf16 v[86:89], v[208:211], v[192:195], v[86:89]
	v_mfma_f32_16x16x32_bf16 v[82:85], v[216:219], v[192:195], v[82:85]
	v_mfma_f32_16x16x32_bf16 v[70:73], v[208:211], v[200:203], v[70:73]
	v_mfma_f32_16x16x32_bf16 v[66:69], v[216:219], v[200:203], v[66:69]
	s_setprio 0
	s_barrier
	ds_read_b128 v[170:173], v157 offset:49152
	ds_read_b128 v[174:177], v157 offset:50176
	ds_read_b128 v[178:181], v157 offset:51200
	ds_read_b128 v[182:185], v157 offset:52224
	ds_read_b128 v[188:191], v157 offset:53248
	ds_read_b128 v[192:195], v157 offset:54272
	ds_read_b128 v[196:199], v157 offset:55296
	ds_read_b128 v[200:203], v157 offset:56320
	s_mov_b32 m0, s65
	v_lshl_add_u64 v[220:221], v[220:221], 0, s[24:25]
	global_load_lds_dwordx4 v[220:221], off
	v_lshl_add_u64 v[220:221], v[226:227], 0, s[24:25]
	s_mov_b32 m0, s66
	s_nop 0
	global_load_lds_dwordx4 v[220:221], off
	s_mov_b32 m0, s67
	v_lshl_add_u64 v[220:221], v[232:233], 0, s[24:25]
	global_load_lds_dwordx4 v[220:221], off
	v_lshl_add_u64 v[220:221], v[234:235], 0, s[24:25]
	s_mov_b32 m0, s68
	s_nop 0
	global_load_lds_dwordx4 v[220:221], off
	s_barrier
	s_waitcnt lgkmcnt(0)
	s_setprio 1
	s_waitcnt lgkmcnt(0)
	v_mfma_f32_16x16x32_bf16 v[62:65], v[136:139], v[170:173], v[62:65]
	v_mfma_f32_16x16x32_bf16 v[58:61], v[162:165], v[170:173], v[58:61]
	v_mfma_f32_16x16x32_bf16 v[46:49], v[136:139], v[178:181], v[46:49]
	v_mfma_f32_16x16x32_bf16 v[42:45], v[162:165], v[178:181], v[42:45]
	v_mfma_f32_16x16x32_bf16 v[30:33], v[136:139], v[188:191], v[30:33]
	v_mfma_f32_16x16x32_bf16 v[26:29], v[162:165], v[188:191], v[26:29]
	v_mfma_f32_16x16x32_bf16 v[14:17], v[136:139], v[196:199], v[14:17]
	v_mfma_f32_16x16x32_bf16 v[10:13], v[162:165], v[196:199], v[10:13]
	v_mfma_f32_16x16x32_bf16 v[62:65], v[158:161], v[174:177], v[62:65]
	v_mfma_f32_16x16x32_bf16 v[58:61], v[166:169], v[174:177], v[58:61]
	v_mfma_f32_16x16x32_bf16 v[46:49], v[158:161], v[182:185], v[46:49]
	v_mfma_f32_16x16x32_bf16 v[42:45], v[166:169], v[182:185], v[42:45]
	v_mfma_f32_16x16x32_bf16 v[30:33], v[158:161], v[192:195], v[30:33]
	v_mfma_f32_16x16x32_bf16 v[26:29], v[166:169], v[192:195], v[26:29]
	v_mfma_f32_16x16x32_bf16 v[14:17], v[158:161], v[200:203], v[14:17]
	v_mfma_f32_16x16x32_bf16 v[10:13], v[166:169], v[200:203], v[10:13]
	s_setprio 0
	s_barrier
	s_mov_b32 m0, s69
	v_lshl_add_u64 v[136:137], s[42:43], 0, v[0:1]
	global_load_lds_dwordx4 v[136:137], off
	v_lshl_add_u64 v[136:137], s[42:43], 0, v[130:131]
	s_mov_b32 m0, s70
	s_nop 0
	global_load_lds_dwordx4 v[136:137], off
	s_waitcnt vmcnt(8)
	s_barrier
	s_setprio 1
	v_mfma_f32_16x16x32_bf16 v[54:57], v[204:207], v[170:173], v[54:57]
	v_mfma_f32_16x16x32_bf16 v[50:53], v[212:215], v[170:173], v[50:53]
	v_mfma_f32_16x16x32_bf16 v[38:41], v[204:207], v[178:181], v[38:41]
	v_mfma_f32_16x16x32_bf16 v[34:37], v[212:215], v[178:181], v[34:37]
	v_mfma_f32_16x16x32_bf16 v[22:25], v[204:207], v[188:191], v[22:25]
	v_mfma_f32_16x16x32_bf16 v[18:21], v[212:215], v[188:191], v[18:21]
	v_mfma_f32_16x16x32_bf16 v[6:9], v[204:207], v[196:199], v[6:9]
	v_mfma_f32_16x16x32_bf16 v[2:5], v[212:215], v[196:199], v[2:5]
	v_mfma_f32_16x16x32_bf16 v[54:57], v[208:211], v[174:177], v[54:57]
	v_mfma_f32_16x16x32_bf16 v[50:53], v[216:219], v[174:177], v[50:53]
	v_mfma_f32_16x16x32_bf16 v[38:41], v[208:211], v[182:185], v[38:41]
	v_mfma_f32_16x16x32_bf16 v[34:37], v[216:219], v[182:185], v[34:37]
	v_mfma_f32_16x16x32_bf16 v[22:25], v[208:211], v[192:195], v[22:25]
	v_mfma_f32_16x16x32_bf16 v[18:21], v[216:219], v[192:195], v[18:21]
	v_mfma_f32_16x16x32_bf16 v[6:9], v[208:211], v[200:203], v[6:9]
	v_mfma_f32_16x16x32_bf16 v[2:5], v[216:219], v[200:203], v[2:5]
	s_setprio 0
	s_movk_i32 s44, 0x100
	s_andn2_b64 vcc, exec, s[34:35]
	s_mov_b64 s[42:43], -1
	s_mov_b64 s[34:35], 0
	s_barrier
	s_cbranch_vccz .LBB0_648
	v_mbcnt_lo_u32_b32 v136, -1, 0
	v_mbcnt_hi_u32_b32 v136, -1, v136
	s_ashr_i32 s12, s28, 5
	v_readlane_b32 s20, v252, 51
	v_readlane_b32 s21, v252, 52
	v_and_b32_e32 v137, 15, v136
	s_ashr_i32 s13, s12, 31
	s_lshl_b32 s34, s28, 8
	v_lshrrev_b32_e32 v136, 1, v136
	s_lshl_b64 s[12:13], s[12:13], 11
	s_and_b32 s34, s34, 0x700
	v_lshl_or_b32 v138, s20, 6, v137
	v_and_b32_e32 v136, 24, v136
	s_or_b32 s12, s12, s34
	v_lshl_or_b32 v136, s21, 5, v136
	v_ashrrev_i32_e32 v139, 31, v138
	v_lshl_add_u64 v[158:159], s[12:13], 0, v[138:139]
	v_cmp_ge_i32_e32 vcc, v138, v136
	v_or_b32_e32 v139, 4, v136
	v_or_b32_e32 v157, 5, v136
	v_cndmask_b32_e32 v126, 0, v126, vcc
	v_cmp_ge_i32_e32 vcc, v138, v139
	v_or_b32_e32 v160, 2, v136
	v_or_b32_e32 v161, 6, v136
	v_cndmask_b32_e32 v122, 0, v122, vcc
	v_cmp_gt_i32_e32 vcc, v138, v136
	v_or_b32_e32 v162, 3, v136
	v_or_b32_e32 v163, 7, v136
	v_cndmask_b32_e32 v127, 0, v127, vcc
	v_cmp_ge_i32_e32 vcc, v138, v157
	v_lshlrev_b64 v[158:159], 12, v[158:159]
	s_lshl_b32 s20, s28, 7
	v_cndmask_b32_e32 v123, 0, v123, vcc
	v_cmp_ge_i32_e32 vcc, v138, v160
	s_and_b32 s28, s20, 0xc00
	s_mov_b64 s[20:21], s[8:9]
	v_cndmask_b32_e32 v128, 0, v128, vcc
	v_cmp_ge_i32_e32 vcc, v138, v161
	s_nop 1
	v_cndmask_b32_e32 v137, 0, v124, vcc
	v_cmp_ge_i32_e32 vcc, v138, v162
	v_cvt_pk_bf16_f32 v124, v126, v127
	v_cvt_pk_bf16_f32 v126, v122, v123
	v_cndmask_b32_e32 v129, 0, v129, vcc
	v_cmp_ge_i32_e32 vcc, v138, v163
	v_lshl_add_u64 v[122:123], s[6:7], 0, v[158:159]
	v_add_u32_e32 v159, 0x83, v136
	v_cndmask_b32_e32 v164, 0, v125, vcc
	v_cvt_pk_bf16_f32 v127, v137, v164
	v_ashrrev_i32_e32 v137, 31, v136
	v_cvt_pk_bf16_f32 v125, v128, v129
	v_lshl_add_u64 v[128:129], v[122:123], 0, s[28:29]
	v_lshlrev_b64 v[122:123], 1, v[136:137]
	v_lshl_add_u64 v[128:129], v[128:129], 0, v[122:123]
	global_store_dwordx4 v[128:129], v[124:127], off
	v_add_u32_e32 v137, 0x82, v136
	s_nop 0
	v_add_u32_e32 v124, 0x80, v136
	v_cmp_ge_i32_e32 vcc, v138, v124
	v_add_u32_e32 v125, 0x84, v136
	s_nop 0
	v_cndmask_b32_e32 v118, 0, v118, vcc
	v_cmp_ge_i32_e32 vcc, v138, v125
	s_nop 1
	v_cndmask_b32_e32 v126, 0, v114, vcc
	v_cmp_gt_i32_e32 vcc, v138, v124
	s_nop 1
	v_cndmask_b32_e32 v114, 0, v119, vcc
	v_add_u32_e32 v119, 0x85, v136
	v_cmp_ge_i32_e32 vcc, v138, v119
	v_cvt_pk_bf16_f32 v114, v118, v114
	s_nop 0
	v_cndmask_b32_e32 v127, 0, v115, vcc
	v_cmp_ge_i32_e32 vcc, v138, v137
	s_nop 1
	v_cndmask_b32_e32 v115, 0, v120, vcc
	v_add_u32_e32 v120, 0x86, v136
	v_cmp_ge_i32_e32 vcc, v138, v120
	s_nop 1
	v_cndmask_b32_e32 v158, 0, v116, vcc
	v_cmp_ge_i32_e32 vcc, v138, v159
	s_nop 1
	v_cndmask_b32_e32 v116, 0, v121, vcc
	v_add_u32_e32 v121, 0x87, v136
	v_cmp_ge_i32_e32 vcc, v138, v121
	v_cvt_pk_bf16_f32 v115, v115, v116
	v_cvt_pk_bf16_f32 v116, v126, v127
	v_cndmask_b32_e32 v117, 0, v117, vcc
	v_cvt_pk_bf16_f32 v117, v158, v117
	global_store_dwordx4 v[128:129], v[114:117], off offset:256
	s_nop 1
	v_or_b32_e32 v114, 16, v138
	v_cmp_ge_i32_e32 vcc, v114, v136
	v_ashrrev_i32_e32 v115, 31, v114
	v_lshl_add_u64 v[116:117], s[12:13], 0, v[114:115]
	v_cndmask_b32_e32 v110, 0, v110, vcc
	v_cmp_ge_i32_e32 vcc, v114, v139
	v_lshlrev_b64 v[116:117], 12, v[116:117]
	s_nop 0
	v_cndmask_b32_e32 v115, 0, v106, vcc
	v_cmp_gt_i32_e32 vcc, v114, v136
	s_nop 1
	v_cndmask_b32_e32 v106, 0, v111, vcc
	v_cmp_ge_i32_e32 vcc, v114, v157
	v_cvt_pk_bf16_f32 v106, v110, v106
	s_nop 0
	v_cndmask_b32_e32 v111, 0, v107, vcc
	v_cmp_ge_i32_e32 vcc, v114, v160
	s_nop 1
	v_cndmask_b32_e32 v107, 0, v112, vcc
	v_cmp_ge_i32_e32 vcc, v114, v161
	s_nop 1
	v_cndmask_b32_e32 v112, 0, v108, vcc
	v_cmp_ge_i32_e32 vcc, v114, v162
	s_nop 1
	v_cndmask_b32_e32 v108, 0, v113, vcc
	v_cmp_ge_i32_e32 vcc, v114, v163
	v_cvt_pk_bf16_f32 v107, v107, v108
	v_cvt_pk_bf16_f32 v108, v115, v111
	v_lshl_add_u64 v[110:111], s[6:7], 0, v[116:117]
	v_cndmask_b32_e32 v109, 0, v109, vcc
	v_lshl_add_u64 v[110:111], v[110:111], 0, s[28:29]
	v_cmp_ge_i32_e32 vcc, v114, v124
	v_cvt_pk_bf16_f32 v109, v112, v109
	v_lshl_add_u64 v[110:111], v[110:111], 0, v[122:123]
	v_cndmask_b32_e32 v102, 0, v102, vcc
	v_cmp_ge_i32_e32 vcc, v114, v125
	global_store_dwordx4 v[110:111], v[106:109], off
	s_nop 1
	v_cndmask_b32_e32 v106, 0, v98, vcc
	v_cmp_gt_i32_e32 vcc, v114, v124
	s_nop 1
	v_cndmask_b32_e32 v98, 0, v103, vcc
	v_cmp_ge_i32_e32 vcc, v114, v119
	v_cvt_pk_bf16_f32 v98, v102, v98
	s_nop 0
	v_cndmask_b32_e32 v103, 0, v99, vcc
	v_cmp_ge_i32_e32 vcc, v114, v137
	s_nop 1
	v_cndmask_b32_e32 v99, 0, v104, vcc
	v_cmp_ge_i32_e32 vcc, v114, v120
	s_nop 1
	v_cndmask_b32_e32 v104, 0, v100, vcc
	v_cmp_ge_i32_e32 vcc, v114, v159
	s_nop 1
	v_cndmask_b32_e32 v100, 0, v105, vcc
	v_cmp_ge_i32_e32 vcc, v114, v121
	v_cvt_pk_bf16_f32 v99, v99, v100
	v_cvt_pk_bf16_f32 v100, v106, v103
	v_cndmask_b32_e32 v101, 0, v101, vcc
	v_cvt_pk_bf16_f32 v101, v104, v101
	global_store_dwordx4 v[110:111], v[98:101], off offset:256
	s_nop 1
	v_or_b32_e32 v98, 32, v138
	v_cmp_ge_i32_e32 vcc, v98, v136
	v_ashrrev_i32_e32 v99, 31, v98
	v_lshl_add_u64 v[100:101], s[12:13], 0, v[98:99]
	v_cndmask_b32_e32 v94, 0, v94, vcc
	v_cmp_ge_i32_e32 vcc, v98, v139
	v_lshlrev_b64 v[100:101], 12, v[100:101]
	s_nop 0
	v_cndmask_b32_e32 v99, 0, v90, vcc
	v_cmp_gt_i32_e32 vcc, v98, v136
	s_nop 1
	v_cndmask_b32_e32 v90, 0, v95, vcc
	v_cmp_ge_i32_e32 vcc, v98, v157
	v_cvt_pk_bf16_f32 v90, v94, v90
	s_nop 0
	v_cndmask_b32_e32 v95, 0, v91, vcc
	v_cmp_ge_i32_e32 vcc, v98, v160
	s_nop 1
	v_cndmask_b32_e32 v91, 0, v96, vcc
	v_cmp_ge_i32_e32 vcc, v98, v161
	s_nop 1
	v_cndmask_b32_e32 v96, 0, v92, vcc
	v_cmp_ge_i32_e32 vcc, v98, v162
	s_nop 1
	v_cndmask_b32_e32 v92, 0, v97, vcc
	v_cmp_ge_i32_e32 vcc, v98, v163
	v_cvt_pk_bf16_f32 v91, v91, v92
	v_cvt_pk_bf16_f32 v92, v99, v95
	v_lshl_add_u64 v[94:95], s[6:7], 0, v[100:101]
	v_cndmask_b32_e32 v93, 0, v93, vcc
	v_lshl_add_u64 v[94:95], v[94:95], 0, s[28:29]
	v_cmp_ge_i32_e32 vcc, v98, v124
	v_cvt_pk_bf16_f32 v93, v96, v93
	v_lshl_add_u64 v[94:95], v[94:95], 0, v[122:123]
	v_cndmask_b32_e32 v86, 0, v86, vcc
	v_cmp_ge_i32_e32 vcc, v98, v125
	global_store_dwordx4 v[94:95], v[90:93], off
	s_nop 1
	v_cndmask_b32_e32 v90, 0, v82, vcc
	v_cmp_gt_i32_e32 vcc, v98, v124
	s_nop 1
	v_cndmask_b32_e32 v82, 0, v87, vcc
	v_cmp_ge_i32_e32 vcc, v98, v119
	v_cvt_pk_bf16_f32 v82, v86, v82
	s_nop 0
	v_cndmask_b32_e32 v87, 0, v83, vcc
	v_cmp_ge_i32_e32 vcc, v98, v137
	s_nop 1
	v_cndmask_b32_e32 v83, 0, v88, vcc
	v_cmp_ge_i32_e32 vcc, v98, v120
	s_nop 1
	v_cndmask_b32_e32 v88, 0, v84, vcc
	v_cmp_ge_i32_e32 vcc, v98, v159
	s_nop 1
	v_cndmask_b32_e32 v84, 0, v89, vcc
	v_cmp_ge_i32_e32 vcc, v98, v121
	v_cvt_pk_bf16_f32 v83, v83, v84
	v_cvt_pk_bf16_f32 v84, v90, v87
	v_cndmask_b32_e32 v85, 0, v85, vcc
	v_cvt_pk_bf16_f32 v85, v88, v85
	global_store_dwordx4 v[94:95], v[82:85], off offset:256
	s_nop 1
	v_or_b32_e32 v82, 48, v138
	v_cmp_ge_i32_e32 vcc, v82, v136
	v_ashrrev_i32_e32 v83, 31, v82
	v_lshl_add_u64 v[84:85], s[12:13], 0, v[82:83]
	v_cndmask_b32_e32 v78, 0, v78, vcc
	v_cmp_ge_i32_e32 vcc, v82, v139
	v_lshlrev_b64 v[84:85], 12, v[84:85]
	s_nop 0
	v_cndmask_b32_e32 v83, 0, v74, vcc
	v_cmp_gt_i32_e32 vcc, v82, v136
	s_nop 1
	v_cndmask_b32_e32 v74, 0, v79, vcc
	v_cmp_ge_i32_e32 vcc, v82, v157
	v_cvt_pk_bf16_f32 v74, v78, v74
	s_nop 0
	v_cndmask_b32_e32 v79, 0, v75, vcc
	v_cmp_ge_i32_e32 vcc, v82, v160
	s_nop 1
	v_cndmask_b32_e32 v75, 0, v80, vcc
	v_cmp_ge_i32_e32 vcc, v82, v161
	s_nop 1
	v_cndmask_b32_e32 v80, 0, v76, vcc
	v_cmp_ge_i32_e32 vcc, v82, v162
	s_nop 1
	v_cndmask_b32_e32 v76, 0, v81, vcc
	v_cmp_ge_i32_e32 vcc, v82, v163
	v_cvt_pk_bf16_f32 v75, v75, v76
	v_cvt_pk_bf16_f32 v76, v83, v79
	v_lshl_add_u64 v[78:79], s[6:7], 0, v[84:85]
	v_cndmask_b32_e32 v77, 0, v77, vcc
	v_lshl_add_u64 v[78:79], v[78:79], 0, s[28:29]
	v_cmp_ge_i32_e32 vcc, v82, v124
	v_cvt_pk_bf16_f32 v77, v80, v77
	v_lshl_add_u64 v[78:79], v[78:79], 0, v[122:123]
	v_cndmask_b32_e32 v70, 0, v70, vcc
	v_cmp_ge_i32_e32 vcc, v82, v125
	global_store_dwordx4 v[78:79], v[74:77], off
	s_nop 1
	v_cndmask_b32_e32 v74, 0, v66, vcc
	v_cmp_gt_i32_e32 vcc, v82, v124
	s_nop 1
	v_cndmask_b32_e32 v66, 0, v71, vcc
	v_cmp_ge_i32_e32 vcc, v82, v119
	v_cvt_pk_bf16_f32 v66, v70, v66
	s_nop 0
	v_cndmask_b32_e32 v71, 0, v67, vcc
	v_cmp_ge_i32_e32 vcc, v82, v137
	s_nop 1
	v_cndmask_b32_e32 v67, 0, v72, vcc
	v_cmp_ge_i32_e32 vcc, v82, v120
	s_nop 1
	v_cndmask_b32_e32 v72, 0, v68, vcc
	v_cmp_ge_i32_e32 vcc, v82, v159
	s_nop 1
	v_cndmask_b32_e32 v68, 0, v73, vcc
	v_cmp_ge_i32_e32 vcc, v82, v121
	v_cvt_pk_bf16_f32 v67, v67, v68
	v_cvt_pk_bf16_f32 v68, v74, v71
	v_cndmask_b32_e32 v69, 0, v69, vcc
	v_cvt_pk_bf16_f32 v69, v72, v69
	global_store_dwordx4 v[78:79], v[66:69], off offset:256
	s_nop 1
	v_add_u32_e32 v66, 0x80, v138
	v_cmp_ge_i32_e32 vcc, v66, v136
	v_ashrrev_i32_e32 v67, 31, v66
	v_lshl_add_u64 v[68:69], s[12:13], 0, v[66:67]
	v_cndmask_b32_e32 v62, 0, v62, vcc
	v_cmp_ge_i32_e32 vcc, v66, v139
	v_lshlrev_b64 v[68:69], 12, v[68:69]
	s_nop 0
	v_cndmask_b32_e32 v67, 0, v58, vcc
	v_cmp_gt_i32_e32 vcc, v66, v136
	s_nop 1
	v_cndmask_b32_e32 v58, 0, v63, vcc
	v_cmp_ge_i32_e32 vcc, v66, v157
	v_cvt_pk_bf16_f32 v58, v62, v58
	s_nop 0
	v_cndmask_b32_e32 v63, 0, v59, vcc
	v_cmp_ge_i32_e32 vcc, v66, v160
	s_nop 1
	v_cndmask_b32_e32 v59, 0, v64, vcc
	v_cmp_ge_i32_e32 vcc, v66, v161
	s_nop 1
	v_cndmask_b32_e32 v64, 0, v60, vcc
	v_cmp_ge_i32_e32 vcc, v66, v162
	s_nop 1
	v_cndmask_b32_e32 v60, 0, v65, vcc
	v_cmp_ge_i32_e32 vcc, v66, v163
	v_cvt_pk_bf16_f32 v59, v59, v60
	v_cvt_pk_bf16_f32 v60, v67, v63
	v_lshl_add_u64 v[62:63], s[6:7], 0, v[68:69]
	v_cndmask_b32_e32 v61, 0, v61, vcc
	v_lshl_add_u64 v[62:63], v[62:63], 0, s[28:29]
	v_cmp_ge_i32_e32 vcc, v66, v124
	v_cvt_pk_bf16_f32 v61, v64, v61
	v_lshl_add_u64 v[62:63], v[62:63], 0, v[122:123]
	v_cndmask_b32_e32 v54, 0, v54, vcc
	v_cmp_ge_i32_e32 vcc, v66, v125
	global_store_dwordx4 v[62:63], v[58:61], off
	s_nop 1
	v_cndmask_b32_e32 v58, 0, v50, vcc
	v_cmp_gt_i32_e32 vcc, v66, v124
	s_nop 1
	v_cndmask_b32_e32 v50, 0, v55, vcc
	v_cmp_ge_i32_e32 vcc, v66, v119
	v_cvt_pk_bf16_f32 v50, v54, v50
	s_nop 0
	v_cndmask_b32_e32 v55, 0, v51, vcc
	v_cmp_ge_i32_e32 vcc, v66, v137
	s_nop 1
	v_cndmask_b32_e32 v51, 0, v56, vcc
	v_cmp_ge_i32_e32 vcc, v66, v120
	s_nop 1
	v_cndmask_b32_e32 v56, 0, v52, vcc
	v_cmp_ge_i32_e32 vcc, v66, v159
	s_nop 1
	v_cndmask_b32_e32 v52, 0, v57, vcc
	v_cmp_ge_i32_e32 vcc, v66, v121
	v_cvt_pk_bf16_f32 v51, v51, v52
	v_cvt_pk_bf16_f32 v52, v58, v55
	v_cndmask_b32_e32 v53, 0, v53, vcc
	v_cvt_pk_bf16_f32 v53, v56, v53
	global_store_dwordx4 v[62:63], v[50:53], off offset:256
	s_nop 1
	v_add_u32_e32 v50, 0x90, v138
	v_cmp_ge_i32_e32 vcc, v50, v136
	v_ashrrev_i32_e32 v51, 31, v50
	v_lshl_add_u64 v[52:53], s[12:13], 0, v[50:51]
	v_cndmask_b32_e32 v46, 0, v46, vcc
	v_cmp_ge_i32_e32 vcc, v50, v139
	v_lshlrev_b64 v[52:53], 12, v[52:53]
	s_nop 0
	v_cndmask_b32_e32 v51, 0, v42, vcc
	v_cmp_gt_i32_e32 vcc, v50, v136
	s_nop 1
	v_cndmask_b32_e32 v42, 0, v47, vcc
	v_cmp_ge_i32_e32 vcc, v50, v157
	v_cvt_pk_bf16_f32 v42, v46, v42
	s_nop 0
	v_cndmask_b32_e32 v47, 0, v43, vcc
	v_cmp_ge_i32_e32 vcc, v50, v160
	s_nop 1
	v_cndmask_b32_e32 v43, 0, v48, vcc
	v_cmp_ge_i32_e32 vcc, v50, v161
	s_nop 1
	v_cndmask_b32_e32 v48, 0, v44, vcc
	v_cmp_ge_i32_e32 vcc, v50, v162
	s_nop 1
	v_cndmask_b32_e32 v44, 0, v49, vcc
	v_cmp_ge_i32_e32 vcc, v50, v163
	v_cvt_pk_bf16_f32 v43, v43, v44
	v_cvt_pk_bf16_f32 v44, v51, v47
	v_lshl_add_u64 v[46:47], s[6:7], 0, v[52:53]
	v_cndmask_b32_e32 v45, 0, v45, vcc
	v_lshl_add_u64 v[46:47], v[46:47], 0, s[28:29]
	v_cmp_ge_i32_e32 vcc, v50, v124
	v_cvt_pk_bf16_f32 v45, v48, v45
	v_lshl_add_u64 v[46:47], v[46:47], 0, v[122:123]
	v_cndmask_b32_e32 v38, 0, v38, vcc
	v_cmp_ge_i32_e32 vcc, v50, v125
	global_store_dwordx4 v[46:47], v[42:45], off
	s_nop 1
	v_cndmask_b32_e32 v42, 0, v34, vcc
	v_cmp_gt_i32_e32 vcc, v50, v124
	s_nop 1
	v_cndmask_b32_e32 v34, 0, v39, vcc
	v_cmp_ge_i32_e32 vcc, v50, v119
	v_cvt_pk_bf16_f32 v34, v38, v34
	s_nop 0
	v_cndmask_b32_e32 v39, 0, v35, vcc
	v_cmp_ge_i32_e32 vcc, v50, v137
	s_nop 1
	v_cndmask_b32_e32 v35, 0, v40, vcc
	v_cmp_ge_i32_e32 vcc, v50, v120
	s_nop 1
	v_cndmask_b32_e32 v40, 0, v36, vcc
	v_cmp_ge_i32_e32 vcc, v50, v159
	s_nop 1
	v_cndmask_b32_e32 v36, 0, v41, vcc
	v_cmp_ge_i32_e32 vcc, v50, v121
	v_cvt_pk_bf16_f32 v35, v35, v36
	v_cvt_pk_bf16_f32 v36, v42, v39
	v_cndmask_b32_e32 v37, 0, v37, vcc
	v_cvt_pk_bf16_f32 v37, v40, v37
	global_store_dwordx4 v[46:47], v[34:37], off offset:256
	s_nop 1
	v_add_u32_e32 v34, 0xa0, v138
	v_cmp_ge_i32_e32 vcc, v34, v136
	v_ashrrev_i32_e32 v35, 31, v34
	v_lshl_add_u64 v[36:37], s[12:13], 0, v[34:35]
	v_cndmask_b32_e32 v30, 0, v30, vcc
	v_cmp_ge_i32_e32 vcc, v34, v139
	v_lshlrev_b64 v[36:37], 12, v[36:37]
	s_nop 0
	v_cndmask_b32_e32 v35, 0, v26, vcc
	v_cmp_gt_i32_e32 vcc, v34, v136
	s_nop 1
	v_cndmask_b32_e32 v26, 0, v31, vcc
	v_cmp_ge_i32_e32 vcc, v34, v157
	v_cvt_pk_bf16_f32 v26, v30, v26
	s_nop 0
	v_cndmask_b32_e32 v31, 0, v27, vcc
	v_cmp_ge_i32_e32 vcc, v34, v160
	s_nop 1
	v_cndmask_b32_e32 v27, 0, v32, vcc
	v_cmp_ge_i32_e32 vcc, v34, v161
	s_nop 1
	v_cndmask_b32_e32 v32, 0, v28, vcc
	v_cmp_ge_i32_e32 vcc, v34, v162
	s_nop 1
	v_cndmask_b32_e32 v28, 0, v33, vcc
	v_cmp_ge_i32_e32 vcc, v34, v163
	v_cvt_pk_bf16_f32 v27, v27, v28
	v_cvt_pk_bf16_f32 v28, v35, v31
	v_lshl_add_u64 v[30:31], s[6:7], 0, v[36:37]
	v_cndmask_b32_e32 v29, 0, v29, vcc
	v_lshl_add_u64 v[30:31], v[30:31], 0, s[28:29]
	v_cmp_ge_i32_e32 vcc, v34, v124
	v_cvt_pk_bf16_f32 v29, v32, v29
	v_lshl_add_u64 v[30:31], v[30:31], 0, v[122:123]
	v_cndmask_b32_e32 v22, 0, v22, vcc
	v_cmp_ge_i32_e32 vcc, v34, v125
	global_store_dwordx4 v[30:31], v[26:29], off
	s_nop 1
	v_cndmask_b32_e32 v26, 0, v18, vcc
	v_cmp_gt_i32_e32 vcc, v34, v124
	s_nop 1
	v_cndmask_b32_e32 v18, 0, v23, vcc
	v_cmp_ge_i32_e32 vcc, v34, v119
	v_cvt_pk_bf16_f32 v18, v22, v18
	s_nop 0
	v_cndmask_b32_e32 v23, 0, v19, vcc
	v_cmp_ge_i32_e32 vcc, v34, v137
	s_nop 1
	v_cndmask_b32_e32 v19, 0, v24, vcc
	v_cmp_ge_i32_e32 vcc, v34, v120
	s_nop 1
	v_cndmask_b32_e32 v24, 0, v20, vcc
	v_cmp_ge_i32_e32 vcc, v34, v159
	s_nop 1
	v_cndmask_b32_e32 v20, 0, v25, vcc
	v_cmp_ge_i32_e32 vcc, v34, v121
	v_cvt_pk_bf16_f32 v19, v19, v20
	v_cvt_pk_bf16_f32 v20, v26, v23
	v_cndmask_b32_e32 v21, 0, v21, vcc
	v_cvt_pk_bf16_f32 v21, v24, v21
	global_store_dwordx4 v[30:31], v[18:21], off offset:256
	s_nop 1
	v_add_u32_e32 v18, 0xb0, v138
	v_cmp_ge_i32_e32 vcc, v18, v136
	v_ashrrev_i32_e32 v19, 31, v18
	v_lshl_add_u64 v[20:21], s[12:13], 0, v[18:19]
	v_cndmask_b32_e32 v14, 0, v14, vcc
	v_cmp_ge_i32_e32 vcc, v18, v139
	v_lshlrev_b64 v[20:21], 12, v[20:21]
	s_mov_b64 s[12:13], s[10:11]
	v_cndmask_b32_e32 v19, 0, v10, vcc
	v_cmp_gt_i32_e32 vcc, v18, v136
	s_nop 1
	v_cndmask_b32_e32 v10, 0, v15, vcc
	v_cmp_ge_i32_e32 vcc, v18, v157
	v_cvt_pk_bf16_f32 v10, v14, v10
	s_nop 0
	v_cndmask_b32_e32 v15, 0, v11, vcc
	v_cmp_ge_i32_e32 vcc, v18, v160
	s_nop 1
	v_cndmask_b32_e32 v11, 0, v16, vcc
	v_cmp_ge_i32_e32 vcc, v18, v161
	s_nop 1
	v_cndmask_b32_e32 v16, 0, v12, vcc
	v_cmp_ge_i32_e32 vcc, v18, v162
	s_nop 1
	v_cndmask_b32_e32 v12, 0, v17, vcc
	v_cmp_ge_i32_e32 vcc, v18, v163
	v_cvt_pk_bf16_f32 v11, v11, v12
	v_cvt_pk_bf16_f32 v12, v19, v15
	v_lshl_add_u64 v[14:15], s[6:7], 0, v[20:21]
	v_cndmask_b32_e32 v13, 0, v13, vcc
	v_lshl_add_u64 v[14:15], v[14:15], 0, s[28:29]
	v_cmp_ge_i32_e32 vcc, v18, v124
	v_cvt_pk_bf16_f32 v13, v16, v13
	v_lshl_add_u64 v[14:15], v[14:15], 0, v[122:123]
	v_cndmask_b32_e32 v6, 0, v6, vcc
	v_cmp_ge_i32_e32 vcc, v18, v125
	global_store_dwordx4 v[14:15], v[10:13], off
	s_mov_b32 s28, s72
	s_nop 0
	v_cndmask_b32_e32 v10, 0, v2, vcc
	v_cmp_gt_i32_e32 vcc, v18, v124
	s_nop 1
	v_cndmask_b32_e32 v2, 0, v7, vcc
	v_cmp_ge_i32_e32 vcc, v18, v119
	v_cvt_pk_bf16_f32 v2, v6, v2
	s_nop 0
	v_cndmask_b32_e32 v7, 0, v3, vcc
	v_cmp_ge_i32_e32 vcc, v18, v137
	s_nop 1
	v_cndmask_b32_e32 v3, 0, v8, vcc
	v_cmp_ge_i32_e32 vcc, v18, v120
	s_nop 1
	v_cndmask_b32_e32 v8, 0, v4, vcc
	v_cmp_ge_i32_e32 vcc, v18, v159
	s_nop 1
	v_cndmask_b32_e32 v4, 0, v9, vcc
	v_cmp_ge_i32_e32 vcc, v18, v121
	v_cvt_pk_bf16_f32 v3, v3, v4
	v_cvt_pk_bf16_f32 v4, v10, v7
	v_cndmask_b32_e32 v5, 0, v5, vcc
	v_cvt_pk_bf16_f32 v5, v8, v5
	s_and_b64 vcc, exec, s[4:5]
	global_store_dwordx4 v[14:15], v[2:5], off offset:256
	s_cbranch_vccz .LBB0_643
	s_branch .LBB0_652

.LBB0_706:
	s_add_u32 s8, s4, 0x79000000
	s_addc_u32 s9, s5, 0
	s_add_i32 s59, s50, 0x18000
	s_lshl_b32 s4, s6, 12
	v_lshl_add_u64 v[8:9], v[8:9], 0, s[24:25]
	s_mov_b32 m0, s59
	s_add_i32 s60, s50, 0x1a000
	s_lshl_b32 s58, s7, 13
	s_and_b32 s6, s4, 0x3000
	s_waitcnt vmcnt(2)
	s_barrier
	global_load_lds_dwordx4 v[8:9], off
	v_lshl_add_u64 v[6:7], v[6:7], 0, s[24:25]
	s_mov_b32 m0, s60
	s_add_i32 s61, s50, 0x8000
	s_add_i32 s62, s50, 0xa000
	global_load_lds_dwordx4 v[6:7], off
	v_lshl_add_u64 v[4:5], v[4:5], 0, s[24:25]
	s_mov_b32 m0, s61
	s_add_u32 s4, s42, 0x20080
	global_load_lds_dwordx4 v[4:5], off
	v_lshl_add_u64 v[2:3], v[2:3], 0, s[24:25]
	s_mov_b32 m0, s62
	s_addc_u32 s5, s43, 0
	s_add_i32 s63, s50, 0x1c000
	global_load_lds_dwordx4 v[2:3], off
	v_lshl_add_u64 v[2:3], s[4:5], 0, v[134:135]
	s_mov_b32 m0, s63
	s_add_i32 s64, s50, 0x1e000
	global_load_lds_dwordx4 v[2:3], off
	v_lshl_add_u64 v[2:3], s[4:5], 0, v[130:131]
	s_mov_b32 m0, s64
	v_readlane_b32 s4, v253, 32
	global_load_lds_dwordx4 v[2:3], off
	v_and_b32_e32 v2, 15, v10
	v_and_b32_e32 v3, 48, v10
	v_lshl_or_b32 v2, v2, 6, v3
	v_lshlrev_b32_e32 v3, 2, v10
	v_and_b32_e32 v3, 32, v3
	v_xad_u32 v144, v2, v3, 0
	v_add_u32_e32 v2, s6, v144
	v_add_u32_e32 v145, 0x10000, v2
	v_add_u32_e32 v146, 0x10400, v2
	v_add_u32_e32 v147, 0x10800, v2
	v_add_u32_e32 v148, 0x10c00, v2
	v_add_u32_e32 v149, 0x14000, v2
	v_add_u32_e32 v150, 0x14400, v2
	v_add_u32_e32 v151, 0x14800, v2
	v_add_u32_e32 v152, 0x14c00, v2
	v_add_u32_e32 v153, 0x18000, v2
	v_add_u32_e32 v154, 0x18400, v2
	v_add_u32_e32 v155, 0x18800, v2
	v_add_u32_e32 v156, 0x18c00, v2
	v_add_u32_e32 v157, 0x1c000, v2
	v_add_u32_e32 v158, 0x1c400, v2
	v_add_u32_e32 v159, 0x1c800, v2
	v_add_u32_e32 v160, 0x1cc00, v2
	v_lshlrev_b32_e32 v2, 15, v14
	v_and_b32_e32 v2, 0xffff0000, v2
	v_lshl_add_u32 v2, v13, 12, v2
	v_and_b32_e32 v3, 1, v14
	v_lshl_or_b32 v2, v3, 6, v2
	v_lshl_add_u32 v138, v15, 1, v2
	v_lshlrev_b32_e32 v2, 15, v0
	v_and_b32_e32 v2, 0xffff0000, v2
	s_waitcnt vmcnt(6)
	v_lshl_add_u32 v2, v11, 12, v2
	v_and_b32_e32 v0, 1, v0
	v_lshl_or_b32 v0, v0, 6, v2
	v_mov_b32_e32 v139, v1
	v_lshl_add_u32 v140, v12, 1, v0
	v_mov_b32_e32 v141, v1
	s_mov_b32 s65, 0
	v_readlane_b32 s66, v253, 26
	s_mov_b32 s28, s4
	s_barrier
	v_readlane_b32 s5, v253, 33

.LBB0_716:
	ds_read_b128 v[162:165], v145
	ds_read_b128 v[166:169], v146
	ds_read_b128 v[170:173], v147
	ds_read_b128 v[174:177], v148
	s_add_u32 s42, s6, 0xfff80080
	s_addc_u32 s43, s7, -1
	s_cmp_eq_u32 s69, 4
	s_cselect_b32 s45, s21, s43
	s_cselect_b32 s44, s20, s42
	s_cselect_b32 s43, s11, s68
	s_cselect_b32 s42, s13, s67
	v_add_u32_e32 v0, s58, v144
	v_lshl_add_u64 v[142:143], s[6:7], 0, v[138:139]
	s_add_i32 m0, s50, 0xc000
	ds_read_b128 v[178:181], v0
	ds_read_b128 v[182:185], v0 offset:1024
	ds_read_b128 v[188:191], v0 offset:2048
	ds_read_b128 v[192:195], v0 offset:3072
	ds_read_b128 v[196:199], v0 offset:4096
	ds_read_b128 v[200:203], v0 offset:5120
	ds_read_b128 v[204:207], v0 offset:6144
	ds_read_b128 v[208:211], v0 offset:7168
	global_load_lds_dwordx4 v[142:143], off
	v_lshl_add_u64 v[142:143], s[6:7], 0, v[140:141]
	s_add_i32 m0, s50, 0xe000
	s_nop 0
	global_load_lds_dwordx4 v[142:143], off
	ds_read_b128 v[212:215], v149
	ds_read_b128 v[216:219], v150
	ds_read_b128 v[232:235], v151
	ds_read_b128 v[236:239], v152
	s_waitcnt lgkmcnt(4)
	s_waitcnt vmcnt(8)
	s_barrier
	s_waitcnt lgkmcnt(0)
	s_setprio 1
	s_waitcnt lgkmcnt(0)
	v_mfma_f32_16x16x32_bf16 v[126:129], v[162:165], v[178:181], v[126:129]
	v_mfma_f32_16x16x32_bf16 v[122:125], v[170:173], v[178:181], v[122:125]
	v_mfma_f32_16x16x32_bf16 v[110:113], v[162:165], v[188:191], v[110:113]
	v_mfma_f32_16x16x32_bf16 v[106:109], v[170:173], v[188:191], v[106:109]
	v_mfma_f32_16x16x32_bf16 v[94:97], v[162:165], v[196:199], v[94:97]
	v_mfma_f32_16x16x32_bf16 v[90:93], v[170:173], v[196:199], v[90:93]
	v_mfma_f32_16x16x32_bf16 v[78:81], v[162:165], v[204:207], v[78:81]
	v_mfma_f32_16x16x32_bf16 v[74:77], v[170:173], v[204:207], v[74:77]
	v_mfma_f32_16x16x32_bf16 v[126:129], v[166:169], v[182:185], v[126:129]
	v_mfma_f32_16x16x32_bf16 v[122:125], v[174:177], v[182:185], v[122:125]
	v_mfma_f32_16x16x32_bf16 v[110:113], v[166:169], v[192:195], v[110:113]
	v_mfma_f32_16x16x32_bf16 v[106:109], v[174:177], v[192:195], v[106:109]
	v_mfma_f32_16x16x32_bf16 v[94:97], v[166:169], v[200:203], v[94:97]
	v_mfma_f32_16x16x32_bf16 v[90:93], v[174:177], v[200:203], v[90:93]
	v_mfma_f32_16x16x32_bf16 v[78:81], v[166:169], v[208:211], v[78:81]
	v_mfma_f32_16x16x32_bf16 v[74:77], v[174:177], v[208:211], v[74:77]
	v_mfma_f32_16x16x32_bf16 v[118:121], v[212:215], v[178:181], v[118:121]
	v_mfma_f32_16x16x32_bf16 v[114:117], v[232:235], v[178:181], v[114:117]
	v_mfma_f32_16x16x32_bf16 v[102:105], v[212:215], v[188:191], v[102:105]
	v_mfma_f32_16x16x32_bf16 v[98:101], v[232:235], v[188:191], v[98:101]
	v_mfma_f32_16x16x32_bf16 v[86:89], v[212:215], v[196:199], v[86:89]
	v_mfma_f32_16x16x32_bf16 v[82:85], v[232:235], v[196:199], v[82:85]
	v_mfma_f32_16x16x32_bf16 v[70:73], v[212:215], v[204:207], v[70:73]
	v_mfma_f32_16x16x32_bf16 v[66:69], v[232:235], v[204:207], v[66:69]
	v_mfma_f32_16x16x32_bf16 v[118:121], v[216:219], v[182:185], v[118:121]
	v_mfma_f32_16x16x32_bf16 v[114:117], v[236:239], v[182:185], v[114:117]
	v_mfma_f32_16x16x32_bf16 v[102:105], v[216:219], v[192:195], v[102:105]
	v_mfma_f32_16x16x32_bf16 v[98:101], v[236:239], v[192:195], v[98:101]
	v_mfma_f32_16x16x32_bf16 v[86:89], v[216:219], v[200:203], v[86:89]
	v_mfma_f32_16x16x32_bf16 v[82:85], v[236:239], v[200:203], v[82:85]
	v_mfma_f32_16x16x32_bf16 v[70:73], v[216:219], v[208:211], v[70:73]
	v_mfma_f32_16x16x32_bf16 v[66:69], v[236:239], v[208:211], v[66:69]
	s_setprio 0
	s_mov_b32 m0, s50
	v_lshl_add_u64 v[226:227], s[44:45], 0, v[136:137]
	s_barrier
	ds_read_b128 v[178:181], v0 offset:16384
	ds_read_b128 v[182:185], v0 offset:17408
	ds_read_b128 v[188:191], v0 offset:18432
	ds_read_b128 v[192:195], v0 offset:19456
	ds_read_b128 v[196:199], v0 offset:20480
	ds_read_b128 v[200:203], v0 offset:21504
	ds_read_b128 v[204:207], v0 offset:22528
	ds_read_b128 v[208:211], v0 offset:23552
	global_load_lds_dwordx4 v[226:227], off
	v_lshl_add_u64 v[240:241], s[44:45], 0, v[132:133]
	s_mov_b32 m0, s53
	s_nop 0
	global_load_lds_dwordx4 v[240:241], off
	s_mov_b32 m0, s51
	v_lshl_add_u64 v[142:143], s[42:43], 0, v[134:135]
	global_load_lds_dwordx4 v[142:143], off
	v_lshl_add_u64 v[220:221], s[42:43], 0, v[130:131]
	s_mov_b32 m0, s52
	s_nop 0
	global_load_lds_dwordx4 v[220:221], off
	s_barrier
	s_waitcnt lgkmcnt(0)
	s_setprio 1
	s_waitcnt lgkmcnt(0)
	v_mfma_f32_16x16x32_bf16 v[62:65], v[162:165], v[178:181], v[62:65]
	v_mfma_f32_16x16x32_bf16 v[58:61], v[170:173], v[178:181], v[58:61]
	v_mfma_f32_16x16x32_bf16 v[46:49], v[162:165], v[188:191], v[46:49]
	v_mfma_f32_16x16x32_bf16 v[42:45], v[170:173], v[188:191], v[42:45]
	v_mfma_f32_16x16x32_bf16 v[30:33], v[162:165], v[196:199], v[30:33]
	v_mfma_f32_16x16x32_bf16 v[26:29], v[170:173], v[196:199], v[26:29]
	v_mfma_f32_16x16x32_bf16 v[14:17], v[162:165], v[204:207], v[14:17]
	v_mfma_f32_16x16x32_bf16 v[10:13], v[170:173], v[204:207], v[10:13]
	v_mfma_f32_16x16x32_bf16 v[62:65], v[166:169], v[182:185], v[62:65]
	v_mfma_f32_16x16x32_bf16 v[58:61], v[174:177], v[182:185], v[58:61]
	v_mfma_f32_16x16x32_bf16 v[46:49], v[166:169], v[192:195], v[46:49]
	v_mfma_f32_16x16x32_bf16 v[42:45], v[174:177], v[192:195], v[42:45]
	v_mfma_f32_16x16x32_bf16 v[30:33], v[166:169], v[200:203], v[30:33]
	v_mfma_f32_16x16x32_bf16 v[26:29], v[174:177], v[200:203], v[26:29]
	v_mfma_f32_16x16x32_bf16 v[14:17], v[166:169], v[208:211], v[14:17]
	v_mfma_f32_16x16x32_bf16 v[10:13], v[174:177], v[208:211], v[10:13]
	s_setprio 0
	s_barrier
	s_add_u32 s70, s42, 0x20000
	s_addc_u32 s71, s43, 0
	s_mov_b32 m0, s54
	v_lshl_add_u64 v[162:163], s[70:71], 0, v[134:135]
	global_load_lds_dwordx4 v[162:163], off
	v_lshl_add_u64 v[162:163], s[70:71], 0, v[130:131]
	s_mov_b32 m0, s55
	s_nop 0
	global_load_lds_dwordx4 v[162:163], off
	s_waitcnt vmcnt(8)
	s_barrier
	s_setprio 1
	v_mfma_f32_16x16x32_bf16 v[54:57], v[212:215], v[178:181], v[54:57]
	v_mfma_f32_16x16x32_bf16 v[50:53], v[232:235], v[178:181], v[50:53]
	v_mfma_f32_16x16x32_bf16 v[38:41], v[212:215], v[188:191], v[38:41]
	v_mfma_f32_16x16x32_bf16 v[34:37], v[232:235], v[188:191], v[34:37]
	v_mfma_f32_16x16x32_bf16 v[22:25], v[212:215], v[196:199], v[22:25]
	v_mfma_f32_16x16x32_bf16 v[18:21], v[232:235], v[196:199], v[18:21]
	v_mfma_f32_16x16x32_bf16 v[6:9], v[212:215], v[204:207], v[6:9]
	v_mfma_f32_16x16x32_bf16 v[2:5], v[232:235], v[204:207], v[2:5]
	v_mfma_f32_16x16x32_bf16 v[54:57], v[216:219], v[182:185], v[54:57]
	v_mfma_f32_16x16x32_bf16 v[50:53], v[236:239], v[182:185], v[50:53]
	v_mfma_f32_16x16x32_bf16 v[38:41], v[216:219], v[192:195], v[38:41]
	v_mfma_f32_16x16x32_bf16 v[34:37], v[236:239], v[192:195], v[34:37]
	v_mfma_f32_16x16x32_bf16 v[22:25], v[216:219], v[200:203], v[22:25]
	v_mfma_f32_16x16x32_bf16 v[18:21], v[236:239], v[200:203], v[18:21]
	v_mfma_f32_16x16x32_bf16 v[6:9], v[216:219], v[208:211], v[6:9]
	v_mfma_f32_16x16x32_bf16 v[2:5], v[236:239], v[208:211], v[2:5]
	s_setprio 0
	s_barrier
	ds_read_b128 v[162:165], v153
	ds_read_b128 v[166:169], v154
	ds_read_b128 v[170:173], v155
	ds_read_b128 v[174:177], v156
	s_add_u32 s44, s44, 0x80000
	s_addc_u32 s45, s45, 0
	s_mov_b32 m0, s56
	v_lshl_add_u64 v[212:213], s[44:45], 0, v[136:137]
	ds_read_b128 v[178:181], v0 offset:32768
	ds_read_b128 v[182:185], v0 offset:33792
	ds_read_b128 v[188:191], v0 offset:34816
	ds_read_b128 v[192:195], v0 offset:35840
	ds_read_b128 v[196:199], v0 offset:36864
	ds_read_b128 v[200:203], v0 offset:37888
	ds_read_b128 v[204:207], v0 offset:38912
	ds_read_b128 v[208:211], v0 offset:39936
	global_load_lds_dwordx4 v[212:213], off
	v_lshl_add_u64 v[212:213], s[44:45], 0, v[132:133]
	s_mov_b32 m0, s57
	s_nop 0
	global_load_lds_dwordx4 v[212:213], off
	ds_read_b128 v[212:215], v157
	ds_read_b128 v[216:219], v158
	ds_read_b128 v[232:235], v159
	ds_read_b128 v[236:239], v160
	s_waitcnt lgkmcnt(4)
	s_waitcnt vmcnt(8)
	s_barrier
	s_waitcnt lgkmcnt(0)
	s_setprio 1
	s_waitcnt lgkmcnt(0)
	v_mfma_f32_16x16x32_bf16 v[126:129], v[162:165], v[178:181], v[126:129]
	v_mfma_f32_16x16x32_bf16 v[122:125], v[170:173], v[178:181], v[122:125]
	v_mfma_f32_16x16x32_bf16 v[110:113], v[162:165], v[188:191], v[110:113]
	v_mfma_f32_16x16x32_bf16 v[106:109], v[170:173], v[188:191], v[106:109]
	v_mfma_f32_16x16x32_bf16 v[94:97], v[162:165], v[196:199], v[94:97]
	v_mfma_f32_16x16x32_bf16 v[90:93], v[170:173], v[196:199], v[90:93]
	v_mfma_f32_16x16x32_bf16 v[78:81], v[162:165], v[204:207], v[78:81]
	v_mfma_f32_16x16x32_bf16 v[74:77], v[170:173], v[204:207], v[74:77]
	v_mfma_f32_16x16x32_bf16 v[126:129], v[166:169], v[182:185], v[126:129]
	v_mfma_f32_16x16x32_bf16 v[122:125], v[174:177], v[182:185], v[122:125]
	v_mfma_f32_16x16x32_bf16 v[110:113], v[166:169], v[192:195], v[110:113]
	v_mfma_f32_16x16x32_bf16 v[106:109], v[174:177], v[192:195], v[106:109]
	v_mfma_f32_16x16x32_bf16 v[94:97], v[166:169], v[200:203], v[94:97]
	v_mfma_f32_16x16x32_bf16 v[90:93], v[174:177], v[200:203], v[90:93]
	v_mfma_f32_16x16x32_bf16 v[78:81], v[166:169], v[208:211], v[78:81]
	v_mfma_f32_16x16x32_bf16 v[74:77], v[174:177], v[208:211], v[74:77]
	v_mfma_f32_16x16x32_bf16 v[118:121], v[212:215], v[178:181], v[118:121]
	v_mfma_f32_16x16x32_bf16 v[114:117], v[232:235], v[178:181], v[114:117]
	v_mfma_f32_16x16x32_bf16 v[102:105], v[212:215], v[188:191], v[102:105]
	v_mfma_f32_16x16x32_bf16 v[98:101], v[232:235], v[188:191], v[98:101]
	v_mfma_f32_16x16x32_bf16 v[86:89], v[212:215], v[196:199], v[86:89]
	v_mfma_f32_16x16x32_bf16 v[82:85], v[232:235], v[196:199], v[82:85]
	v_mfma_f32_16x16x32_bf16 v[70:73], v[212:215], v[204:207], v[70:73]
	v_mfma_f32_16x16x32_bf16 v[66:69], v[232:235], v[204:207], v[66:69]
	v_mfma_f32_16x16x32_bf16 v[118:121], v[216:219], v[182:185], v[118:121]
	v_mfma_f32_16x16x32_bf16 v[114:117], v[236:239], v[182:185], v[114:117]
	v_mfma_f32_16x16x32_bf16 v[102:105], v[216:219], v[192:195], v[102:105]
	v_mfma_f32_16x16x32_bf16 v[98:101], v[236:239], v[192:195], v[98:101]
	v_mfma_f32_16x16x32_bf16 v[86:89], v[216:219], v[200:203], v[86:89]
	v_mfma_f32_16x16x32_bf16 v[82:85], v[236:239], v[200:203], v[82:85]
	v_mfma_f32_16x16x32_bf16 v[70:73], v[216:219], v[208:211], v[70:73]
	v_mfma_f32_16x16x32_bf16 v[66:69], v[236:239], v[208:211], v[66:69]
	s_setprio 0
	s_barrier
	ds_read_b128 v[178:181], v0 offset:49152
	ds_read_b128 v[182:185], v0 offset:50176
	ds_read_b128 v[188:191], v0 offset:51200
	ds_read_b128 v[192:195], v0 offset:52224
	ds_read_b128 v[196:199], v0 offset:53248
	ds_read_b128 v[200:203], v0 offset:54272
	ds_read_b128 v[204:207], v0 offset:55296
	ds_read_b128 v[208:211], v0 offset:56320
	s_mov_b32 m0, s59
	v_lshl_add_u64 v[142:143], v[142:143], 0, s[24:25]
	global_load_lds_dwordx4 v[142:143], off
	v_lshl_add_u64 v[142:143], v[220:221], 0, s[24:25]
	s_mov_b32 m0, s60
	s_nop 0
	global_load_lds_dwordx4 v[142:143], off
	s_mov_b32 m0, s61
	v_lshl_add_u64 v[142:143], v[226:227], 0, s[24:25]
	global_load_lds_dwordx4 v[142:143], off
	v_lshl_add_u64 v[142:143], v[240:241], 0, s[24:25]
	s_mov_b32 m0, s62
	s_nop 0
	global_load_lds_dwordx4 v[142:143], off
	s_barrier
	s_waitcnt lgkmcnt(0)
	s_setprio 1
	s_waitcnt lgkmcnt(0)
	v_mfma_f32_16x16x32_bf16 v[62:65], v[162:165], v[178:181], v[62:65]
	v_mfma_f32_16x16x32_bf16 v[58:61], v[170:173], v[178:181], v[58:61]
	v_mfma_f32_16x16x32_bf16 v[46:49], v[162:165], v[188:191], v[46:49]
	v_mfma_f32_16x16x32_bf16 v[42:45], v[170:173], v[188:191], v[42:45]
	v_mfma_f32_16x16x32_bf16 v[30:33], v[162:165], v[196:199], v[30:33]
	v_mfma_f32_16x16x32_bf16 v[26:29], v[170:173], v[196:199], v[26:29]
	v_mfma_f32_16x16x32_bf16 v[14:17], v[162:165], v[204:207], v[14:17]
	v_mfma_f32_16x16x32_bf16 v[10:13], v[170:173], v[204:207], v[10:13]
	v_mfma_f32_16x16x32_bf16 v[62:65], v[166:169], v[182:185], v[62:65]
	v_mfma_f32_16x16x32_bf16 v[58:61], v[174:177], v[182:185], v[58:61]
	v_mfma_f32_16x16x32_bf16 v[46:49], v[166:169], v[192:195], v[46:49]
	v_mfma_f32_16x16x32_bf16 v[42:45], v[174:177], v[192:195], v[42:45]
	v_mfma_f32_16x16x32_bf16 v[30:33], v[166:169], v[200:203], v[30:33]
	v_mfma_f32_16x16x32_bf16 v[26:29], v[174:177], v[200:203], v[26:29]
	v_mfma_f32_16x16x32_bf16 v[14:17], v[166:169], v[208:211], v[14:17]
	v_mfma_f32_16x16x32_bf16 v[10:13], v[174:177], v[208:211], v[10:13]
	s_setprio 0
	s_barrier
	s_add_u32 s42, s42, 0x20080
	s_addc_u32 s43, s43, 0
	s_mov_b32 m0, s63
	v_lshl_add_u64 v[142:143], s[42:43], 0, v[134:135]
	global_load_lds_dwordx4 v[142:143], off
	v_lshl_add_u64 v[142:143], s[42:43], 0, v[130:131]
	s_mov_b32 m0, s64
	s_nop 0
	global_load_lds_dwordx4 v[142:143], off
	s_waitcnt vmcnt(8)
	s_barrier
	s_setprio 1
	v_mfma_f32_16x16x32_bf16 v[54:57], v[212:215], v[178:181], v[54:57]
	v_mfma_f32_16x16x32_bf16 v[50:53], v[232:235], v[178:181], v[50:53]
	v_mfma_f32_16x16x32_bf16 v[38:41], v[212:215], v[188:191], v[38:41]
	v_mfma_f32_16x16x32_bf16 v[34:37], v[232:235], v[188:191], v[34:37]
	v_mfma_f32_16x16x32_bf16 v[22:25], v[212:215], v[196:199], v[22:25]
	v_mfma_f32_16x16x32_bf16 v[18:21], v[232:235], v[196:199], v[18:21]
	v_mfma_f32_16x16x32_bf16 v[6:9], v[212:215], v[204:207], v[6:9]
	v_mfma_f32_16x16x32_bf16 v[2:5], v[232:235], v[204:207], v[2:5]
	v_mfma_f32_16x16x32_bf16 v[54:57], v[216:219], v[182:185], v[54:57]
	v_mfma_f32_16x16x32_bf16 v[50:53], v[236:239], v[182:185], v[50:53]
	v_mfma_f32_16x16x32_bf16 v[38:41], v[216:219], v[192:195], v[38:41]
	v_mfma_f32_16x16x32_bf16 v[34:37], v[236:239], v[192:195], v[34:37]
	v_mfma_f32_16x16x32_bf16 v[22:25], v[216:219], v[200:203], v[22:25]
	v_mfma_f32_16x16x32_bf16 v[18:21], v[236:239], v[200:203], v[18:21]
	v_mfma_f32_16x16x32_bf16 v[6:9], v[216:219], v[208:211], v[6:9]
	v_mfma_f32_16x16x32_bf16 v[2:5], v[236:239], v[208:211], v[2:5]
	s_setprio 0
	s_add_i32 s69, s69, 2
	s_add_u32 s6, s6, 0x100
	s_addc_u32 s7, s7, 0
	s_add_u32 s67, s67, 0x100
	s_addc_u32 s68, s68, 0
	s_cmp_gt_u32 s69, 5
	s_barrier
	s_cbranch_scc0 .LBB0_716
	v_pk_mul_f32 v[122:123], v[122:123], 4.0 op_sel_hi:[1,0]
	v_mov_b32_e32 v165, v1
	v_cvt_pk_fp8_f32 v165, v122, v123
	v_pk_mul_f32 v[114:115], v[114:115], 4.0 op_sel_hi:[1,0]
	v_mov_b32_e32 v123, v1
	v_cvt_pk_fp8_f32 v123, v114, v115
	v_pk_mul_f32 v[116:117], v[116:117], 4.0 op_sel_hi:[1,0]
	v_pk_mul_f32 v[106:107], v[106:107], 4.0 op_sel_hi:[1,0]
	v_pk_mul_f32 v[98:99], v[98:99], 4.0 op_sel_hi:[1,0]
	v_cvt_pk_fp8_f32 v123, v116, v117 op_sel:[0,0,1]
	v_mov_b32_e32 v117, v1
	v_cvt_pk_fp8_f32 v117, v106, v107
	v_mov_b32_e32 v107, v1
	v_cvt_pk_fp8_f32 v107, v98, v99
	v_pk_mul_f32 v[100:101], v[100:101], 4.0 op_sel_hi:[1,0]
	v_pk_mul_f32 v[90:91], v[90:91], 4.0 op_sel_hi:[1,0]
	v_pk_mul_f32 v[82:83], v[82:83], 4.0 op_sel_hi:[1,0]
	v_cvt_pk_fp8_f32 v107, v100, v101 op_sel:[0,0,1]
	v_mov_b32_e32 v101, v1
	v_cvt_pk_fp8_f32 v101, v90, v91
	v_mov_b32_e32 v91, v1
	v_cvt_pk_fp8_f32 v91, v82, v83
	v_pk_mul_f32 v[84:85], v[84:85], 4.0 op_sel_hi:[1,0]
	v_pk_mul_f32 v[74:75], v[74:75], 4.0 op_sel_hi:[1,0]
	v_pk_mul_f32 v[66:67], v[66:67], 4.0 op_sel_hi:[1,0]
	v_cvt_pk_fp8_f32 v91, v84, v85 op_sel:[0,0,1]
	v_mov_b32_e32 v85, v1
	v_cvt_pk_fp8_f32 v85, v74, v75
	v_mov_b32_e32 v75, v1
	v_cvt_pk_fp8_f32 v75, v66, v67
	v_pk_mul_f32 v[68:69], v[68:69], 4.0 op_sel_hi:[1,0]
	v_pk_mul_f32 v[58:59], v[58:59], 4.0 op_sel_hi:[1,0]
	v_pk_mul_f32 v[50:51], v[50:51], 4.0 op_sel_hi:[1,0]
	v_cvt_pk_fp8_f32 v75, v68, v69 op_sel:[0,0,1]
	v_mov_b32_e32 v69, v1
	v_cvt_pk_fp8_f32 v69, v58, v59
	v_mov_b32_e32 v59, v1
	v_cvt_pk_fp8_f32 v59, v50, v51
	v_pk_mul_f32 v[52:53], v[52:53], 4.0 op_sel_hi:[1,0]
	v_pk_mul_f32 v[42:43], v[42:43], 4.0 op_sel_hi:[1,0]
	v_pk_mul_f32 v[34:35], v[34:35], 4.0 op_sel_hi:[1,0]
	v_cvt_pk_fp8_f32 v59, v52, v53 op_sel:[0,0,1]
	v_mov_b32_e32 v53, v1
	v_cvt_pk_fp8_f32 v53, v42, v43
	v_mov_b32_e32 v43, v1
	v_cvt_pk_fp8_f32 v43, v34, v35
	v_pk_mul_f32 v[36:37], v[36:37], 4.0 op_sel_hi:[1,0]
	v_pk_mul_f32 v[26:27], v[26:27], 4.0 op_sel_hi:[1,0]
	v_pk_mul_f32 v[18:19], v[18:19], 4.0 op_sel_hi:[1,0]
	v_cvt_pk_fp8_f32 v43, v36, v37 op_sel:[0,0,1]
	v_mov_b32_e32 v37, v1
	v_cvt_pk_fp8_f32 v37, v26, v27
	v_mov_b32_e32 v27, v1
	v_cvt_pk_fp8_f32 v27, v18, v19
	v_mbcnt_lo_u32_b32 v0, -1, 0
	v_mbcnt_hi_u32_b32 v0, -1, v0
	v_readlane_b32 s11, v252, 51
	v_and_b32_e32 v142, 15, v0
	v_readlane_b32 s13, v252, 52
	s_ashr_i32 s6, s28, 5
	v_pk_mul_f32 v[20:21], v[20:21], 4.0 op_sel_hi:[1,0]
	s_ashr_i32 s7, s6, 31
	s_lshl_b32 s42, s28, 8
	v_lshl_or_b32 v142, s11, 6, v142
	v_cvt_pk_fp8_f32 v27, v20, v21 op_sel:[0,0,1]
	v_pk_mul_f32 v[10:11], v[10:11], 4.0 op_sel_hi:[1,0]
	v_mov_b32_e32 v21, v1
	s_lshl_b64 s[6:7], s[6:7], 11
	s_and_b32 s42, s42, 0x700
	v_pk_mul_f32 v[126:127], v[126:127], 4.0 op_sel_hi:[1,0]
	v_mov_b32_e32 v164, v1
	v_pk_mul_f32 v[118:119], v[118:119], 4.0 op_sel_hi:[1,0]
	v_mov_b32_e32 v122, v1
	v_or_b32_e32 v114, 16, v142
	v_pk_mul_f32 v[110:111], v[110:111], 4.0 op_sel_hi:[1,0]
	v_mov_b32_e32 v116, v1
	v_pk_mul_f32 v[102:103], v[102:103], 4.0 op_sel_hi:[1,0]
	v_mov_b32_e32 v106, v1
	v_or_b32_e32 v98, 32, v142
	v_pk_mul_f32 v[94:95], v[94:95], 4.0 op_sel_hi:[1,0]
	v_mov_b32_e32 v100, v1
	v_pk_mul_f32 v[86:87], v[86:87], 4.0 op_sel_hi:[1,0]
	v_mov_b32_e32 v90, v1
	v_or_b32_e32 v82, 48, v142
	v_pk_mul_f32 v[78:79], v[78:79], 4.0 op_sel_hi:[1,0]
	v_mov_b32_e32 v84, v1
	v_pk_mul_f32 v[70:71], v[70:71], 4.0 op_sel_hi:[1,0]
	v_mov_b32_e32 v74, v1
	v_add_u32_e32 v66, 0x80, v142
	v_pk_mul_f32 v[62:63], v[62:63], 4.0 op_sel_hi:[1,0]
	v_mov_b32_e32 v68, v1
	v_pk_mul_f32 v[54:55], v[54:55], 4.0 op_sel_hi:[1,0]
	v_mov_b32_e32 v58, v1
	v_add_u32_e32 v50, 0x90, v142
	v_pk_mul_f32 v[46:47], v[46:47], 4.0 op_sel_hi:[1,0]
	v_mov_b32_e32 v52, v1
	v_pk_mul_f32 v[38:39], v[38:39], 4.0 op_sel_hi:[1,0]
	v_mov_b32_e32 v42, v1
	v_add_u32_e32 v34, 0xa0, v142
	v_pk_mul_f32 v[30:31], v[30:31], 4.0 op_sel_hi:[1,0]
	v_mov_b32_e32 v36, v1
	v_pk_mul_f32 v[22:23], v[22:23], 4.0 op_sel_hi:[1,0]
	v_mov_b32_e32 v26, v1
	v_add_u32_e32 v18, 0xb0, v142
	v_pk_mul_f32 v[14:15], v[14:15], 4.0 op_sel_hi:[1,0]
	v_mov_b32_e32 v20, v1
	v_cvt_pk_fp8_f32 v21, v10, v11
	v_pk_mul_f32 v[6:7], v[6:7], 4.0 op_sel_hi:[1,0]
	v_pk_mul_f32 v[2:3], v[2:3], 4.0 op_sel_hi:[1,0]
	v_mov_b32_e32 v10, v1
	v_mov_b32_e32 v11, v1
	s_or_b32 s6, s6, s42
	v_ashrrev_i32_e32 v143, 31, v142
	v_cvt_pk_fp8_f32 v164, v126, v127
	v_cvt_pk_fp8_f32 v122, v118, v119
	v_ashrrev_i32_e32 v115, 31, v114
	v_cvt_pk_fp8_f32 v116, v110, v111
	v_cvt_pk_fp8_f32 v106, v102, v103
	v_ashrrev_i32_e32 v99, 31, v98
	v_cvt_pk_fp8_f32 v100, v94, v95
	v_cvt_pk_fp8_f32 v90, v86, v87
	v_ashrrev_i32_e32 v83, 31, v82
	v_cvt_pk_fp8_f32 v84, v78, v79
	v_cvt_pk_fp8_f32 v74, v70, v71
	v_ashrrev_i32_e32 v67, 31, v66
	v_cvt_pk_fp8_f32 v68, v62, v63
	v_cvt_pk_fp8_f32 v58, v54, v55
	v_ashrrev_i32_e32 v51, 31, v50
	v_cvt_pk_fp8_f32 v52, v46, v47
	v_cvt_pk_fp8_f32 v42, v38, v39
	v_ashrrev_i32_e32 v35, 31, v34
	v_cvt_pk_fp8_f32 v36, v30, v31
	v_cvt_pk_fp8_f32 v26, v22, v23
	v_ashrrev_i32_e32 v19, 31, v18
	v_cvt_pk_fp8_f32 v20, v14, v15
	v_cvt_pk_fp8_f32 v10, v6, v7
	v_cvt_pk_fp8_f32 v11, v2, v3
	v_lshl_add_u64 v[162:163], s[6:7], 0, v[142:143]
	v_lshl_add_u64 v[114:115], s[6:7], 0, v[114:115]
	v_lshl_add_u64 v[98:99], s[6:7], 0, v[98:99]
	v_lshl_add_u64 v[82:83], s[6:7], 0, v[82:83]
	v_lshl_add_u64 v[66:67], s[6:7], 0, v[66:67]
	v_lshl_add_u64 v[50:51], s[6:7], 0, v[50:51]
	v_lshl_add_u64 v[34:35], s[6:7], 0, v[34:35]
	v_lshl_add_u64 v[18:19], s[6:7], 0, v[18:19]
	s_lshl_b32 s11, s28, 6
	v_lshlrev_b64 v[162:163], 11, v[162:163]
	v_lshlrev_b64 v[114:115], 11, v[114:115]
	v_lshlrev_b64 v[98:99], 11, v[98:99]
	v_lshlrev_b64 v[82:83], 11, v[82:83]
	v_lshlrev_b64 v[66:67], 11, v[66:67]
	v_lshlrev_b64 v[50:51], 11, v[50:51]
	v_lshlrev_b64 v[34:35], 11, v[34:35]
	v_lshlrev_b64 v[18:19], 11, v[18:19]
	s_and_b32 s28, s11, 0x600
	v_lshl_add_u64 v[162:163], s[8:9], 0, v[162:163]
	s_lshl_b32 s44, s66, 8
	v_pk_mul_f32 v[128:129], v[128:129], 4.0 op_sel_hi:[1,0]
	v_pk_mul_f32 v[124:125], v[124:125], 4.0 op_sel_hi:[1,0]
	v_pk_mul_f32 v[120:121], v[120:121], 4.0 op_sel_hi:[1,0]
	v_lshl_add_u64 v[114:115], s[8:9], 0, v[114:115]
	v_pk_mul_f32 v[112:113], v[112:113], 4.0 op_sel_hi:[1,0]
	v_pk_mul_f32 v[108:109], v[108:109], 4.0 op_sel_hi:[1,0]
	v_pk_mul_f32 v[104:105], v[104:105], 4.0 op_sel_hi:[1,0]
	v_lshl_add_u64 v[98:99], s[8:9], 0, v[98:99]
	v_pk_mul_f32 v[96:97], v[96:97], 4.0 op_sel_hi:[1,0]
	v_pk_mul_f32 v[92:93], v[92:93], 4.0 op_sel_hi:[1,0]
	v_pk_mul_f32 v[88:89], v[88:89], 4.0 op_sel_hi:[1,0]
	v_lshl_add_u64 v[82:83], s[8:9], 0, v[82:83]
	v_pk_mul_f32 v[80:81], v[80:81], 4.0 op_sel_hi:[1,0]
	v_pk_mul_f32 v[76:77], v[76:77], 4.0 op_sel_hi:[1,0]
	v_pk_mul_f32 v[72:73], v[72:73], 4.0 op_sel_hi:[1,0]
	v_lshl_add_u64 v[66:67], s[8:9], 0, v[66:67]
	v_pk_mul_f32 v[64:65], v[64:65], 4.0 op_sel_hi:[1,0]
	v_pk_mul_f32 v[60:61], v[60:61], 4.0 op_sel_hi:[1,0]
	v_pk_mul_f32 v[56:57], v[56:57], 4.0 op_sel_hi:[1,0]
	v_lshl_add_u64 v[50:51], s[8:9], 0, v[50:51]
	v_pk_mul_f32 v[48:49], v[48:49], 4.0 op_sel_hi:[1,0]
	v_pk_mul_f32 v[44:45], v[44:45], 4.0 op_sel_hi:[1,0]
	v_pk_mul_f32 v[40:41], v[40:41], 4.0 op_sel_hi:[1,0]
	v_lshl_add_u64 v[34:35], s[8:9], 0, v[34:35]
	v_pk_mul_f32 v[32:33], v[32:33], 4.0 op_sel_hi:[1,0]
	v_pk_mul_f32 v[28:29], v[28:29], 4.0 op_sel_hi:[1,0]
	v_pk_mul_f32 v[24:25], v[24:25], 4.0 op_sel_hi:[1,0]
	v_lshl_add_u64 v[18:19], s[8:9], 0, v[18:19]
	v_pk_mul_f32 v[16:17], v[16:17], 4.0 op_sel_hi:[1,0]
	v_pk_mul_f32 v[12:13], v[12:13], 4.0 op_sel_hi:[1,0]
	v_pk_mul_f32 v[8:9], v[8:9], 4.0 op_sel_hi:[1,0]
	v_pk_mul_f32 v[4:5], v[4:5], 4.0 op_sel_hi:[1,0]
	s_lshl_b32 s42, s13, 5
	v_lshl_add_u64 v[162:163], v[162:163], 0, s[28:29]
	s_ashr_i32 s45, s44, 31
	v_cvt_pk_fp8_f32 v164, v128, v129 op_sel:[0,0,1]
	v_cvt_pk_fp8_f32 v165, v124, v125 op_sel:[0,0,1]
	v_cvt_pk_fp8_f32 v122, v120, v121 op_sel:[0,0,1]
	v_lshl_add_u64 v[114:115], v[114:115], 0, s[28:29]
	v_cvt_pk_fp8_f32 v116, v112, v113 op_sel:[0,0,1]
	v_cvt_pk_fp8_f32 v117, v108, v109 op_sel:[0,0,1]
	v_cvt_pk_fp8_f32 v106, v104, v105 op_sel:[0,0,1]
	v_lshl_add_u64 v[98:99], v[98:99], 0, s[28:29]
	v_cvt_pk_fp8_f32 v100, v96, v97 op_sel:[0,0,1]
	v_cvt_pk_fp8_f32 v101, v92, v93 op_sel:[0,0,1]
	v_cvt_pk_fp8_f32 v90, v88, v89 op_sel:[0,0,1]
	v_lshl_add_u64 v[82:83], v[82:83], 0, s[28:29]
	v_cvt_pk_fp8_f32 v84, v80, v81 op_sel:[0,0,1]
	v_cvt_pk_fp8_f32 v85, v76, v77 op_sel:[0,0,1]
	v_cvt_pk_fp8_f32 v74, v72, v73 op_sel:[0,0,1]
	v_lshl_add_u64 v[66:67], v[66:67], 0, s[28:29]
	v_cvt_pk_fp8_f32 v68, v64, v65 op_sel:[0,0,1]
	v_cvt_pk_fp8_f32 v69, v60, v61 op_sel:[0,0,1]
	v_cvt_pk_fp8_f32 v58, v56, v57 op_sel:[0,0,1]
	v_lshl_add_u64 v[50:51], v[50:51], 0, s[28:29]
	v_cvt_pk_fp8_f32 v52, v48, v49 op_sel:[0,0,1]
	v_cvt_pk_fp8_f32 v53, v44, v45 op_sel:[0,0,1]
	v_cvt_pk_fp8_f32 v42, v40, v41 op_sel:[0,0,1]
	v_lshl_add_u64 v[34:35], v[34:35], 0, s[28:29]
	v_cvt_pk_fp8_f32 v36, v32, v33 op_sel:[0,0,1]
	v_cvt_pk_fp8_f32 v37, v28, v29 op_sel:[0,0,1]
	v_cvt_pk_fp8_f32 v26, v24, v25 op_sel:[0,0,1]
	v_lshl_add_u64 v[18:19], v[18:19], 0, s[28:29]
	v_cvt_pk_fp8_f32 v20, v16, v17 op_sel:[0,0,1]
	v_cvt_pk_fp8_f32 v21, v12, v13 op_sel:[0,0,1]
	v_cvt_pk_fp8_f32 v10, v8, v9 op_sel:[0,0,1]
	v_cvt_pk_fp8_f32 v11, v4, v5 op_sel:[0,0,1]
	s_ashr_i32 s43, s42, 31
	v_lshrrev_b32_e32 v0, 1, v0
	v_lshl_add_u64 v[162:163], v[162:163], 0, s[44:45]
	v_lshl_add_u64 v[114:115], v[114:115], 0, s[44:45]
	v_lshl_add_u64 v[98:99], v[98:99], 0, s[44:45]
	v_lshl_add_u64 v[82:83], v[82:83], 0, s[44:45]
	v_lshl_add_u64 v[66:67], v[66:67], 0, s[44:45]
	v_lshl_add_u64 v[50:51], v[50:51], 0, s[44:45]
	v_lshl_add_u64 v[34:35], v[34:35], 0, s[44:45]
	v_lshl_add_u64 v[18:19], v[18:19], 0, s[44:45]
	v_and_b32_e32 v0, 24, v0
	v_lshl_add_u64 v[162:163], v[162:163], 0, s[42:43]
	v_lshl_add_u64 v[114:115], v[114:115], 0, s[42:43]
	v_lshl_add_u64 v[98:99], v[98:99], 0, s[42:43]
	v_lshl_add_u64 v[82:83], v[82:83], 0, s[42:43]
	v_lshl_add_u64 v[66:67], v[66:67], 0, s[42:43]
	v_lshl_add_u64 v[50:51], v[50:51], 0, s[42:43]
	v_lshl_add_u64 v[34:35], v[34:35], 0, s[42:43]
	v_lshl_add_u64 v[18:19], v[18:19], 0, s[42:43]
	v_lshl_add_u64 v[162:163], v[162:163], 0, v[0:1]
	v_lshl_add_u64 v[114:115], v[114:115], 0, v[0:1]
	v_lshl_add_u64 v[98:99], v[98:99], 0, v[0:1]
	v_lshl_add_u64 v[82:83], v[82:83], 0, v[0:1]
	v_lshl_add_u64 v[66:67], v[66:67], 0, v[0:1]
	v_lshl_add_u64 v[50:51], v[50:51], 0, v[0:1]
	v_lshl_add_u64 v[34:35], v[34:35], 0, v[0:1]
	v_lshl_add_u64 v[18:19], v[18:19], 0, v[0:1]
	s_and_b64 vcc, exec, s[4:5]
	s_mov_b32 s66, s10
	s_mov_b32 s28, s12
	s_mov_b64 s[42:43], s[34:35]
	s_mov_b64 s[44:45], s[20:21]
	global_store_dwordx2 v[162:163], v[164:165], off
	global_store_dwordx2 v[162:163], v[122:123], off offset:128
	global_store_dwordx2 v[114:115], v[116:117], off
	global_store_dwordx2 v[114:115], v[106:107], off offset:128
	global_store_dwordx2 v[98:99], v[100:101], off
	global_store_dwordx2 v[98:99], v[90:91], off offset:128
	global_store_dwordx2 v[82:83], v[84:85], off
	global_store_dwordx2 v[82:83], v[74:75], off offset:128
	global_store_dwordx2 v[66:67], v[68:69], off
	global_store_dwordx2 v[66:67], v[58:59], off offset:128
	global_store_dwordx2 v[50:51], v[52:53], off
	global_store_dwordx2 v[50:51], v[42:43], off offset:128
	global_store_dwordx2 v[34:35], v[36:37], off
	global_store_dwordx2 v[34:35], v[26:27], off offset:128
	global_store_dwordx2 v[18:19], v[20:21], off
	global_store_dwordx2 v[18:19], v[10:11], off offset:128
	s_cbranch_vccz .LBB0_707
	s_waitcnt vmcnt(0)
	s_cmpk_gt_u32 s27, 0xff
	s_cbranch_scc1 .LBB0_720
	s_barrier

.LBB0_964:
	s_lshl_b32 s28, s84, 8
	s_lshl_b64 s[12:13], s[28:29], 2
	s_add_u32 s12, s10, s12
	s_addc_u32 s13, s11, s13
	s_add_u32 s66, s12, 0x4304000
	s_addc_u32 s67, s13, 0
	s_add_i32 s69, s58, 0x18000
	s_lshl_b32 s4, s4, 12
	v_lshl_add_u64 v[8:9], v[8:9], 0, s[24:25]
	s_mov_b32 m0, s69
	s_add_i32 s70, s58, 0x1a000
	s_lshl_b32 s68, s5, 13
	s_and_b32 s12, s4, 0x3000
	s_waitcnt vmcnt(2)
	s_barrier
	global_load_lds_dwordx4 v[8:9], off
	v_lshl_add_u64 v[6:7], v[6:7], 0, s[24:25]
	s_mov_b32 m0, s70
	s_add_i32 s71, s58, 0x8000
	s_add_i32 s72, s58, 0xa000
	global_load_lds_dwordx4 v[6:7], off
	v_lshl_add_u64 v[4:5], v[4:5], 0, s[24:25]
	s_mov_b32 m0, s71
	s_add_u32 s4, s8, 0x40080
	global_load_lds_dwordx4 v[4:5], off
	v_lshl_add_u64 v[2:3], v[2:3], 0, s[24:25]
	s_mov_b32 m0, s72
	s_addc_u32 s5, s9, 0
	s_add_i32 s73, s58, 0x1c000
	global_load_lds_dwordx4 v[2:3], off
	v_lshl_add_u64 v[2:3], s[4:5], 0, v[150:151]
	s_mov_b32 m0, s73
	s_add_i32 s74, s58, 0x1e000
	global_load_lds_dwordx4 v[2:3], off
	v_lshl_add_u64 v[2:3], s[4:5], 0, v[146:147]
	s_mov_b32 m0, s74
	v_readlane_b32 s4, v254, 1
	global_load_lds_dwordx4 v[2:3], off
	v_and_b32_e32 v2, 15, v11
	v_and_b32_e32 v3, 48, v11
	v_lshl_or_b32 v2, v2, 6, v3
	v_lshlrev_b32_e32 v3, 2, v11
	v_and_b32_e32 v3, 32, v3
	v_xad_u32 v163, v2, v3, 0
	v_add_u32_e32 v2, s12, v163
	v_add_u32_e32 v166, 0x10000, v2
	v_add_u32_e32 v167, 0x10400, v2
	v_add_u32_e32 v168, 0x10800, v2
	v_add_u32_e32 v169, 0x10c00, v2
	v_add_u32_e32 v170, 0x14000, v2
	v_add_u32_e32 v171, 0x14400, v2
	v_add_u32_e32 v172, 0x14800, v2
	v_add_u32_e32 v173, 0x14c00, v2
	v_add_u32_e32 v174, 0x18000, v2
	v_add_u32_e32 v175, 0x18400, v2
	v_add_u32_e32 v176, 0x18800, v2
	v_add_u32_e32 v177, 0x18c00, v2
	v_add_u32_e32 v178, 0x1c000, v2
	v_add_u32_e32 v179, 0x1c400, v2
	v_add_u32_e32 v180, 0x1c800, v2
	v_add_u32_e32 v181, 0x1cc00, v2
	v_lshlrev_b32_e32 v2, 14, v14
	v_and_b32_e32 v2, 0xffff8000, v2
	v_lshl_add_u32 v2, v13, 11, v2
	v_and_b32_e32 v3, 1, v14
	v_lshl_or_b32 v2, v3, 6, v2
	v_lshl_add_u32 v154, v15, 1, v2
	v_lshlrev_b32_e32 v2, 14, v0
	v_and_b32_e32 v2, 0xffff8000, v2
	s_waitcnt vmcnt(6)
	v_lshl_add_u32 v2, v10, 11, v2
	v_and_b32_e32 v0, 1, v0
	v_lshl_or_b32 v0, v0, 6, v2
	v_mov_b32_e32 v155, v1
	v_lshl_add_u32 v156, v12, 1, v0
	v_mov_b32_e32 v157, v1
	s_mov_b32 s75, 0
	v_readlane_b32 s76, v253, 31
	s_mov_b32 s43, s4
	s_barrier
	v_readlane_b32 s5, v254, 2
	s_branch .LBB0_966

.LBB0_973:
	ds_read_b128 v[90:93], v166
	ds_read_b128 v[94:97], v167
	ds_read_b128 v[98:101], v168
	ds_read_b128 v[102:105], v169
	s_add_u32 s8, s6, 0xfffc0080
	s_addc_u32 s9, s7, -1
	s_cmp_eq_u32 s44, 12
	s_cselect_b32 s39, s15, s9
	s_cselect_b32 s38, s28, s8
	s_cselect_b32 s9, s13, s42
	s_cselect_b32 s8, s40, s41
	v_add_u32_e32 v0, s68, v163
	v_lshl_add_u64 v[164:165], s[6:7], 0, v[154:155]
	s_add_i32 m0, s58, 0xc000
	ds_read_b128 v[158:161], v0
	ds_read_b128 v[182:185], v0 offset:1024
	ds_read_b128 v[188:191], v0 offset:2048
	ds_read_b128 v[192:195], v0 offset:3072
	ds_read_b128 v[196:199], v0 offset:4096
	ds_read_b128 v[200:203], v0 offset:5120
	ds_read_b128 v[204:207], v0 offset:6144
	ds_read_b128 v[208:211], v0 offset:7168
	global_load_lds_dwordx4 v[164:165], off
	v_lshl_add_u64 v[164:165], s[6:7], 0, v[156:157]
	s_add_i32 m0, s58, 0xe000
	s_nop 0
	global_load_lds_dwordx4 v[164:165], off
	ds_read_b128 v[212:215], v170
	ds_read_b128 v[216:219], v171
	ds_read_b128 v[232:235], v172
	ds_read_b128 v[236:239], v173
	s_waitcnt lgkmcnt(4)
	s_waitcnt vmcnt(8)
	s_barrier
	s_waitcnt lgkmcnt(0)
	s_setprio 1
	s_waitcnt lgkmcnt(0)
	v_mfma_f32_16x16x32_bf16 v[142:145], v[90:93], v[158:161], v[142:145]
	v_mfma_f32_16x16x32_bf16 v[138:141], v[98:101], v[158:161], v[138:141]
	v_mfma_f32_16x16x32_bf16 v[126:129], v[90:93], v[188:191], v[126:129]
	v_mfma_f32_16x16x32_bf16 v[122:125], v[98:101], v[188:191], v[122:125]
	v_mfma_f32_16x16x32_bf16 v[110:113], v[90:93], v[196:199], v[110:113]
	v_mfma_f32_16x16x32_bf16 v[106:109], v[98:101], v[196:199], v[106:109]
	v_mfma_f32_16x16x32_bf16 v[78:81], v[90:93], v[204:207], v[78:81]
	v_mfma_f32_16x16x32_bf16 v[74:77], v[98:101], v[204:207], v[74:77]
	v_mfma_f32_16x16x32_bf16 v[142:145], v[94:97], v[182:185], v[142:145]
	v_mfma_f32_16x16x32_bf16 v[138:141], v[102:105], v[182:185], v[138:141]
	v_mfma_f32_16x16x32_bf16 v[126:129], v[94:97], v[192:195], v[126:129]
	v_mfma_f32_16x16x32_bf16 v[122:125], v[102:105], v[192:195], v[122:125]
	v_mfma_f32_16x16x32_bf16 v[110:113], v[94:97], v[200:203], v[110:113]
	v_mfma_f32_16x16x32_bf16 v[106:109], v[102:105], v[200:203], v[106:109]
	v_mfma_f32_16x16x32_bf16 v[78:81], v[94:97], v[208:211], v[78:81]
	v_mfma_f32_16x16x32_bf16 v[74:77], v[102:105], v[208:211], v[74:77]
	v_mfma_f32_16x16x32_bf16 v[134:137], v[212:215], v[158:161], v[134:137]
	v_mfma_f32_16x16x32_bf16 v[130:133], v[232:235], v[158:161], v[130:133]
	v_mfma_f32_16x16x32_bf16 v[118:121], v[212:215], v[188:191], v[118:121]
	v_mfma_f32_16x16x32_bf16 v[114:117], v[232:235], v[188:191], v[114:117]
	v_mfma_f32_16x16x32_bf16 v[86:89], v[212:215], v[196:199], v[86:89]
	v_mfma_f32_16x16x32_bf16 v[82:85], v[232:235], v[196:199], v[82:85]
	v_mfma_f32_16x16x32_bf16 v[70:73], v[212:215], v[204:207], v[70:73]
	v_mfma_f32_16x16x32_bf16 v[66:69], v[232:235], v[204:207], v[66:69]
	v_mfma_f32_16x16x32_bf16 v[134:137], v[216:219], v[182:185], v[134:137]
	v_mfma_f32_16x16x32_bf16 v[130:133], v[236:239], v[182:185], v[130:133]
	v_mfma_f32_16x16x32_bf16 v[118:121], v[216:219], v[192:195], v[118:121]
	v_mfma_f32_16x16x32_bf16 v[114:117], v[236:239], v[192:195], v[114:117]
	v_mfma_f32_16x16x32_bf16 v[86:89], v[216:219], v[200:203], v[86:89]
	v_mfma_f32_16x16x32_bf16 v[82:85], v[236:239], v[200:203], v[82:85]
	v_mfma_f32_16x16x32_bf16 v[70:73], v[216:219], v[208:211], v[70:73]
	v_mfma_f32_16x16x32_bf16 v[66:69], v[236:239], v[208:211], v[66:69]
	s_setprio 0
	s_mov_b32 m0, s58
	v_lshl_add_u64 v[240:241], s[38:39], 0, v[152:153]
	s_barrier
	ds_read_b128 v[158:161], v0 offset:16384
	ds_read_b128 v[182:185], v0 offset:17408
	ds_read_b128 v[188:191], v0 offset:18432
	ds_read_b128 v[192:195], v0 offset:19456
	ds_read_b128 v[196:199], v0 offset:20480
	ds_read_b128 v[200:203], v0 offset:21504
	ds_read_b128 v[204:207], v0 offset:22528
	ds_read_b128 v[208:211], v0 offset:23552
	global_load_lds_dwordx4 v[240:241], off
	v_lshl_add_u64 v[242:243], s[38:39], 0, v[148:149]
	s_mov_b32 m0, s61
	s_nop 0
	global_load_lds_dwordx4 v[242:243], off
	s_mov_b32 m0, s59
	v_lshl_add_u64 v[164:165], s[8:9], 0, v[150:151]
	global_load_lds_dwordx4 v[164:165], off
	v_lshl_add_u64 v[220:221], s[8:9], 0, v[146:147]
	s_mov_b32 m0, s60
	s_nop 0
	global_load_lds_dwordx4 v[220:221], off
	s_barrier
	s_waitcnt lgkmcnt(0)
	s_setprio 1
	s_waitcnt lgkmcnt(0)
	v_mfma_f32_16x16x32_bf16 v[62:65], v[90:93], v[158:161], v[62:65]
	v_mfma_f32_16x16x32_bf16 v[58:61], v[98:101], v[158:161], v[58:61]
	v_mfma_f32_16x16x32_bf16 v[46:49], v[90:93], v[188:191], v[46:49]
	v_mfma_f32_16x16x32_bf16 v[42:45], v[98:101], v[188:191], v[42:45]
	v_mfma_f32_16x16x32_bf16 v[30:33], v[90:93], v[196:199], v[30:33]
	v_mfma_f32_16x16x32_bf16 v[26:29], v[98:101], v[196:199], v[26:29]
	v_mfma_f32_16x16x32_bf16 v[14:17], v[90:93], v[204:207], v[14:17]
	v_mfma_f32_16x16x32_bf16 v[10:13], v[98:101], v[204:207], v[10:13]
	v_mfma_f32_16x16x32_bf16 v[62:65], v[94:97], v[182:185], v[62:65]
	v_mfma_f32_16x16x32_bf16 v[58:61], v[102:105], v[182:185], v[58:61]
	v_mfma_f32_16x16x32_bf16 v[46:49], v[94:97], v[192:195], v[46:49]
	v_mfma_f32_16x16x32_bf16 v[42:45], v[102:105], v[192:195], v[42:45]
	v_mfma_f32_16x16x32_bf16 v[30:33], v[94:97], v[200:203], v[30:33]
	v_mfma_f32_16x16x32_bf16 v[26:29], v[102:105], v[200:203], v[26:29]
	v_mfma_f32_16x16x32_bf16 v[14:17], v[94:97], v[208:211], v[14:17]
	v_mfma_f32_16x16x32_bf16 v[10:13], v[102:105], v[208:211], v[10:13]
	s_setprio 0
	s_barrier
	s_add_u32 s46, s8, 0x40000
	s_addc_u32 s47, s9, 0
	s_mov_b32 m0, s62
	v_lshl_add_u64 v[90:91], s[46:47], 0, v[150:151]
	global_load_lds_dwordx4 v[90:91], off
	v_lshl_add_u64 v[90:91], s[46:47], 0, v[146:147]
	s_mov_b32 m0, s63
	s_nop 0
	global_load_lds_dwordx4 v[90:91], off
	s_waitcnt vmcnt(8)
	s_barrier
	s_setprio 1
	v_mfma_f32_16x16x32_bf16 v[54:57], v[212:215], v[158:161], v[54:57]
	v_mfma_f32_16x16x32_bf16 v[50:53], v[232:235], v[158:161], v[50:53]
	v_mfma_f32_16x16x32_bf16 v[38:41], v[212:215], v[188:191], v[38:41]
	v_mfma_f32_16x16x32_bf16 v[34:37], v[232:235], v[188:191], v[34:37]
	v_mfma_f32_16x16x32_bf16 v[22:25], v[212:215], v[196:199], v[22:25]
	v_mfma_f32_16x16x32_bf16 v[18:21], v[232:235], v[196:199], v[18:21]
	v_mfma_f32_16x16x32_bf16 v[6:9], v[212:215], v[204:207], v[6:9]
	v_mfma_f32_16x16x32_bf16 v[2:5], v[232:235], v[204:207], v[2:5]
	v_mfma_f32_16x16x32_bf16 v[54:57], v[216:219], v[182:185], v[54:57]
	v_mfma_f32_16x16x32_bf16 v[50:53], v[236:239], v[182:185], v[50:53]
	v_mfma_f32_16x16x32_bf16 v[38:41], v[216:219], v[192:195], v[38:41]
	v_mfma_f32_16x16x32_bf16 v[34:37], v[236:239], v[192:195], v[34:37]
	v_mfma_f32_16x16x32_bf16 v[22:25], v[216:219], v[200:203], v[22:25]
	v_mfma_f32_16x16x32_bf16 v[18:21], v[236:239], v[200:203], v[18:21]
	v_mfma_f32_16x16x32_bf16 v[6:9], v[216:219], v[208:211], v[6:9]
	v_mfma_f32_16x16x32_bf16 v[2:5], v[236:239], v[208:211], v[2:5]
	s_setprio 0
	s_barrier
	ds_read_b128 v[90:93], v174
	ds_read_b128 v[94:97], v175
	ds_read_b128 v[98:101], v176
	ds_read_b128 v[102:105], v177
	s_add_u32 s38, s38, 0x40000
	s_addc_u32 s39, s39, 0
	s_mov_b32 m0, s64
	v_lshl_add_u64 v[212:213], s[38:39], 0, v[152:153]
	ds_read_b128 v[158:161], v0 offset:32768
	ds_read_b128 v[182:185], v0 offset:33792
	ds_read_b128 v[188:191], v0 offset:34816
	ds_read_b128 v[192:195], v0 offset:35840
	ds_read_b128 v[196:199], v0 offset:36864
	ds_read_b128 v[200:203], v0 offset:37888
	ds_read_b128 v[204:207], v0 offset:38912
	ds_read_b128 v[208:211], v0 offset:39936
	global_load_lds_dwordx4 v[212:213], off
	v_lshl_add_u64 v[212:213], s[38:39], 0, v[148:149]
	s_mov_b32 m0, s65
	s_nop 0
	global_load_lds_dwordx4 v[212:213], off
	ds_read_b128 v[212:215], v178
	ds_read_b128 v[216:219], v179
	ds_read_b128 v[232:235], v180
	ds_read_b128 v[236:239], v181
	s_waitcnt lgkmcnt(4)
	s_waitcnt vmcnt(8)
	s_barrier
	s_waitcnt lgkmcnt(0)
	s_setprio 1
	s_waitcnt lgkmcnt(0)
	v_mfma_f32_16x16x32_bf16 v[142:145], v[90:93], v[158:161], v[142:145]
	v_mfma_f32_16x16x32_bf16 v[138:141], v[98:101], v[158:161], v[138:141]
	v_mfma_f32_16x16x32_bf16 v[126:129], v[90:93], v[188:191], v[126:129]
	v_mfma_f32_16x16x32_bf16 v[122:125], v[98:101], v[188:191], v[122:125]
	v_mfma_f32_16x16x32_bf16 v[110:113], v[90:93], v[196:199], v[110:113]
	v_mfma_f32_16x16x32_bf16 v[106:109], v[98:101], v[196:199], v[106:109]
	v_mfma_f32_16x16x32_bf16 v[78:81], v[90:93], v[204:207], v[78:81]
	v_mfma_f32_16x16x32_bf16 v[74:77], v[98:101], v[204:207], v[74:77]
	v_mfma_f32_16x16x32_bf16 v[142:145], v[94:97], v[182:185], v[142:145]
	v_mfma_f32_16x16x32_bf16 v[138:141], v[102:105], v[182:185], v[138:141]
	v_mfma_f32_16x16x32_bf16 v[126:129], v[94:97], v[192:195], v[126:129]
	v_mfma_f32_16x16x32_bf16 v[122:125], v[102:105], v[192:195], v[122:125]
	v_mfma_f32_16x16x32_bf16 v[110:113], v[94:97], v[200:203], v[110:113]
	v_mfma_f32_16x16x32_bf16 v[106:109], v[102:105], v[200:203], v[106:109]
	v_mfma_f32_16x16x32_bf16 v[78:81], v[94:97], v[208:211], v[78:81]
	v_mfma_f32_16x16x32_bf16 v[74:77], v[102:105], v[208:211], v[74:77]
	v_mfma_f32_16x16x32_bf16 v[134:137], v[212:215], v[158:161], v[134:137]
	v_mfma_f32_16x16x32_bf16 v[130:133], v[232:235], v[158:161], v[130:133]
	v_mfma_f32_16x16x32_bf16 v[118:121], v[212:215], v[188:191], v[118:121]
	v_mfma_f32_16x16x32_bf16 v[114:117], v[232:235], v[188:191], v[114:117]
	v_mfma_f32_16x16x32_bf16 v[86:89], v[212:215], v[196:199], v[86:89]
	v_mfma_f32_16x16x32_bf16 v[82:85], v[232:235], v[196:199], v[82:85]
	v_mfma_f32_16x16x32_bf16 v[70:73], v[212:215], v[204:207], v[70:73]
	v_mfma_f32_16x16x32_bf16 v[66:69], v[232:235], v[204:207], v[66:69]
	v_mfma_f32_16x16x32_bf16 v[134:137], v[216:219], v[182:185], v[134:137]
	v_mfma_f32_16x16x32_bf16 v[130:133], v[236:239], v[182:185], v[130:133]
	v_mfma_f32_16x16x32_bf16 v[118:121], v[216:219], v[192:195], v[118:121]
	v_mfma_f32_16x16x32_bf16 v[114:117], v[236:239], v[192:195], v[114:117]
	v_mfma_f32_16x16x32_bf16 v[86:89], v[216:219], v[200:203], v[86:89]
	v_mfma_f32_16x16x32_bf16 v[82:85], v[236:239], v[200:203], v[82:85]
	v_mfma_f32_16x16x32_bf16 v[70:73], v[216:219], v[208:211], v[70:73]
	v_mfma_f32_16x16x32_bf16 v[66:69], v[236:239], v[208:211], v[66:69]
	s_setprio 0
	s_barrier
	ds_read_b128 v[158:161], v0 offset:49152
	ds_read_b128 v[182:185], v0 offset:50176
	ds_read_b128 v[188:191], v0 offset:51200
	ds_read_b128 v[192:195], v0 offset:52224
	ds_read_b128 v[196:199], v0 offset:53248
	ds_read_b128 v[200:203], v0 offset:54272
	ds_read_b128 v[204:207], v0 offset:55296
	ds_read_b128 v[208:211], v0 offset:56320
	s_mov_b32 m0, s69
	v_lshl_add_u64 v[164:165], v[164:165], 0, s[24:25]
	global_load_lds_dwordx4 v[164:165], off
	v_lshl_add_u64 v[164:165], v[220:221], 0, s[24:25]
	s_mov_b32 m0, s70
	s_nop 0
	global_load_lds_dwordx4 v[164:165], off
	s_mov_b32 m0, s71
	v_lshl_add_u64 v[164:165], v[240:241], 0, s[24:25]
	global_load_lds_dwordx4 v[164:165], off
	v_lshl_add_u64 v[164:165], v[242:243], 0, s[24:25]
	s_mov_b32 m0, s72
	s_nop 0
	global_load_lds_dwordx4 v[164:165], off
	s_barrier
	s_waitcnt lgkmcnt(0)
	s_setprio 1
	s_waitcnt lgkmcnt(0)
	v_mfma_f32_16x16x32_bf16 v[62:65], v[90:93], v[158:161], v[62:65]
	v_mfma_f32_16x16x32_bf16 v[58:61], v[98:101], v[158:161], v[58:61]
	v_mfma_f32_16x16x32_bf16 v[46:49], v[90:93], v[188:191], v[46:49]
	v_mfma_f32_16x16x32_bf16 v[42:45], v[98:101], v[188:191], v[42:45]
	v_mfma_f32_16x16x32_bf16 v[30:33], v[90:93], v[196:199], v[30:33]
	v_mfma_f32_16x16x32_bf16 v[26:29], v[98:101], v[196:199], v[26:29]
	v_mfma_f32_16x16x32_bf16 v[14:17], v[90:93], v[204:207], v[14:17]
	v_mfma_f32_16x16x32_bf16 v[10:13], v[98:101], v[204:207], v[10:13]
	v_mfma_f32_16x16x32_bf16 v[62:65], v[94:97], v[182:185], v[62:65]
	v_mfma_f32_16x16x32_bf16 v[58:61], v[102:105], v[182:185], v[58:61]
	v_mfma_f32_16x16x32_bf16 v[46:49], v[94:97], v[192:195], v[46:49]
	v_mfma_f32_16x16x32_bf16 v[42:45], v[102:105], v[192:195], v[42:45]
	v_mfma_f32_16x16x32_bf16 v[30:33], v[94:97], v[200:203], v[30:33]
	v_mfma_f32_16x16x32_bf16 v[26:29], v[102:105], v[200:203], v[26:29]
	v_mfma_f32_16x16x32_bf16 v[14:17], v[94:97], v[208:211], v[14:17]
	v_mfma_f32_16x16x32_bf16 v[10:13], v[102:105], v[208:211], v[10:13]
	s_setprio 0
	s_barrier
	s_add_u32 s8, s8, 0x40080
	s_addc_u32 s9, s9, 0
	s_mov_b32 m0, s73
	v_lshl_add_u64 v[90:91], s[8:9], 0, v[150:151]
	global_load_lds_dwordx4 v[90:91], off
	v_lshl_add_u64 v[90:91], s[8:9], 0, v[146:147]
	s_mov_b32 m0, s74
	s_nop 0
	global_load_lds_dwordx4 v[90:91], off
	s_waitcnt vmcnt(8)
	s_barrier
	s_setprio 1
	v_mfma_f32_16x16x32_bf16 v[54:57], v[212:215], v[158:161], v[54:57]
	v_mfma_f32_16x16x32_bf16 v[50:53], v[232:235], v[158:161], v[50:53]
	v_mfma_f32_16x16x32_bf16 v[38:41], v[212:215], v[188:191], v[38:41]
	v_mfma_f32_16x16x32_bf16 v[34:37], v[232:235], v[188:191], v[34:37]
	v_mfma_f32_16x16x32_bf16 v[22:25], v[212:215], v[196:199], v[22:25]
	v_mfma_f32_16x16x32_bf16 v[18:21], v[232:235], v[196:199], v[18:21]
	v_mfma_f32_16x16x32_bf16 v[6:9], v[212:215], v[204:207], v[6:9]
	v_mfma_f32_16x16x32_bf16 v[2:5], v[232:235], v[204:207], v[2:5]
	v_mfma_f32_16x16x32_bf16 v[54:57], v[216:219], v[182:185], v[54:57]
	v_mfma_f32_16x16x32_bf16 v[50:53], v[236:239], v[182:185], v[50:53]
	v_mfma_f32_16x16x32_bf16 v[38:41], v[216:219], v[192:195], v[38:41]
	v_mfma_f32_16x16x32_bf16 v[34:37], v[236:239], v[192:195], v[34:37]
	v_mfma_f32_16x16x32_bf16 v[22:25], v[216:219], v[200:203], v[22:25]
	v_mfma_f32_16x16x32_bf16 v[18:21], v[236:239], v[200:203], v[18:21]
	v_mfma_f32_16x16x32_bf16 v[6:9], v[216:219], v[208:211], v[6:9]
	v_mfma_f32_16x16x32_bf16 v[2:5], v[236:239], v[208:211], v[2:5]
	s_setprio 0
	s_add_i32 s44, s44, 2
	s_add_u32 s6, s6, 0x100
	s_addc_u32 s7, s7, 0
	s_add_u32 s41, s41, 0x100
	s_addc_u32 s42, s42, 0
	s_cmp_gt_u32 s44, 13
	s_barrier
	s_cbranch_scc0 .LBB0_973
	s_cmp_eq_u32 s76, 6
	s_cselect_b64 s[46:47], -1, 0
	s_cmp_lg_u32 s76, 6
	s_cselect_b64 s[40:41], -1, 0
	s_cmp_gt_i32 s76, 1
	s_cselect_b64 s[38:39], -1, 0
	s_cmp_gt_u32 s76, 5
	s_cselect_b64 s[48:49], -1, 0
	s_cmp_lt_u32 s76, 6
	s_movk_i32 s6, 0xc0
	s_cselect_b32 s8, 0x80, s6
	s_cmp_gt_u32 s76, 3
	s_cselect_b64 s[50:51], -1, 0
	s_and_b64 s[6:7], s[50:51], exec
	s_cselect_b32 s28, s8, 64
	s_cmp_lt_i32 s76, 2
	s_cselect_b64 s[8:9], -1, 0
	s_and_b64 s[6:7], s[8:9], exec
	s_cselect_b32 s6, 0, s28
	v_mbcnt_lo_u32_b32 v161, -1, 0
	v_mbcnt_hi_u32_b32 v161, -1, v161
	s_lshl_b32 s6, s6, 2
	v_lshrrev_b32_e32 v0, 1, v161
	s_add_u32 s6, s66, s6
	v_and_b32_e32 v160, 24, v0
	s_addc_u32 s7, s67, 0
	v_lshlrev_b32_e32 v0, 2, v160
	v_mov_b32_e32 v90, 1.0
	v_readlane_b32 s15, v252, 51
	v_readlane_b32 s13, v252, 52
	v_lshl_add_u64 v[158:159], s[6:7], 0, v[0:1]
	s_and_b64 vcc, exec, s[46:47]
	v_mov_b32_e32 v94, 1.0
	v_mov_b32_e32 v95, v90
	v_mov_b32_e32 v96, 1.0
	v_mov_b32_e32 v97, 1.0
	s_cbranch_vccnz .LBB0_976
	global_load_dwordx4 v[94:97], v[158:159], off

.LBB0_1050:
	s_add_i32 s55, s46, 0x18000
	s_lshl_b32 s53, s4, 13
	s_lshl_b32 s4, s5, 12
	v_lshl_add_u64 v[8:9], v[8:9], 0, s[24:25]
	s_mov_b32 m0, s55
	s_add_i32 s56, s46, 0x1a000
	s_and_b32 s7, s4, 0x3000
	s_waitcnt vmcnt(2)
	s_barrier
	global_load_lds_dwordx4 v[8:9], off
	v_lshl_add_u64 v[6:7], v[6:7], 0, s[24:25]
	s_mov_b32 m0, s56
	s_add_i32 s57, s46, 0x8000
	s_add_i32 s58, s46, 0xa000
	global_load_lds_dwordx4 v[6:7], off
	v_lshl_add_u64 v[4:5], v[4:5], 0, s[24:25]
	s_mov_b32 m0, s57
	s_add_u32 s4, s40, 0x40080
	global_load_lds_dwordx4 v[4:5], off
	v_lshl_add_u64 v[2:3], v[2:3], 0, s[24:25]
	s_mov_b32 m0, s58
	s_addc_u32 s5, s41, 0
	s_add_i32 s59, s46, 0x1c000
	global_load_lds_dwordx4 v[2:3], off
	v_lshl_add_u64 v[2:3], s[4:5], 0, v[132:133]
	s_mov_b32 m0, s59
	s_add_i32 s60, s46, 0x1e000
	global_load_lds_dwordx4 v[2:3], off
	v_lshl_add_u64 v[2:3], s[4:5], 0, v[136:137]
	s_mov_b32 m0, s60
	v_mov_b32_e32 v139, v1
	global_load_lds_dwordx4 v[2:3], off
	v_and_b32_e32 v2, 15, v0
	v_and_b32_e32 v3, 48, v0
	v_lshlrev_b32_e32 v0, 2, v0
	v_lshl_or_b32 v2, v2, 6, v3
	v_and_b32_e32 v0, 32, v0
	v_xad_u32 v148, v2, v0, 0
	v_add_u32_e32 v0, s7, v148
	v_add_u32_e32 v149, 0x10000, v0
	v_add_u32_e32 v150, 0x10400, v0
	v_add_u32_e32 v151, 0x10800, v0
	v_add_u32_e32 v152, 0x10c00, v0
	v_add_u32_e32 v153, 0x14000, v0
	v_add_u32_e32 v154, 0x14400, v0
	v_add_u32_e32 v155, 0x14800, v0
	v_add_u32_e32 v156, 0x14c00, v0
	v_add_u32_e32 v157, 0x18000, v0
	v_add_u32_e32 v158, 0x18400, v0
	v_add_u32_e32 v159, 0x18800, v0
	v_add_u32_e32 v160, 0x18c00, v0
	v_add_u32_e32 v161, 0x1c000, v0
	v_add_u32_e32 v162, 0x1c400, v0
	v_add_u32_e32 v163, 0x1c800, v0
	v_add_u32_e32 v164, 0x1cc00, v0
	v_lshlrev_b32_e32 v0, 14, v10
	v_and_b32_e32 v0, 0xffff8000, v0
	v_lshl_add_u32 v0, v11, 11, v0
	v_and_b32_e32 v2, 1, v10
	v_lshl_or_b32 v0, v2, 6, v0
	v_lshl_add_u32 v138, v12, 1, v0
	v_lshlrev_b32_e32 v0, 14, v13
	v_and_b32_e32 v0, 0xffff8000, v0
	s_waitcnt vmcnt(6)
	v_lshl_add_u32 v0, v14, 11, v0
	v_and_b32_e32 v2, 1, v13
	v_lshl_or_b32 v0, v2, 6, v0
	v_lshl_add_u32 v140, v15, 1, v0
	v_mov_b32_e32 v141, v1
	s_mov_b32 s61, 0
	s_barrier
	s_branch .LBB0_1052

.LBB0_1055:
	ds_read_b128 v[142:145], v149
	ds_read_b128 v[166:169], v150
	ds_read_b128 v[170:173], v151
	ds_read_b128 v[174:177], v152
	s_add_u32 s40, s38, 0xfffc0080
	s_addc_u32 s41, s39, -1
	s_cmp_eq_u32 s65, 12
	s_cselect_b32 s43, s7, s41
	s_cselect_b32 s42, s15, s40
	s_cselect_b32 s41, s13, s64
	s_cselect_b32 s40, s62, s63
	v_add_u32_e32 v0, s53, v148
	v_lshl_add_u64 v[146:147], s[38:39], 0, v[138:139]
	s_add_i32 m0, s46, 0xc000
	ds_read_b128 v[178:181], v0
	ds_read_b128 v[182:185], v0 offset:1024
	ds_read_b128 v[188:191], v0 offset:2048
	ds_read_b128 v[192:195], v0 offset:3072
	ds_read_b128 v[196:199], v0 offset:4096
	ds_read_b128 v[200:203], v0 offset:5120
	ds_read_b128 v[204:207], v0 offset:6144
	ds_read_b128 v[208:211], v0 offset:7168
	global_load_lds_dwordx4 v[146:147], off
	v_lshl_add_u64 v[146:147], s[38:39], 0, v[140:141]
	s_add_i32 m0, s46, 0xe000
	s_nop 0
	global_load_lds_dwordx4 v[146:147], off
	ds_read_b128 v[212:215], v153
	ds_read_b128 v[216:219], v154
	ds_read_b128 v[232:235], v155
	ds_read_b128 v[236:239], v156
	s_waitcnt lgkmcnt(4)
	s_waitcnt vmcnt(8)
	s_barrier
	s_waitcnt lgkmcnt(0)
	s_setprio 1
	s_waitcnt lgkmcnt(0)
	v_mfma_f32_16x16x32_bf16 v[126:129], v[142:145], v[178:181], v[126:129]
	v_mfma_f32_16x16x32_bf16 v[122:125], v[170:173], v[178:181], v[122:125]
	v_mfma_f32_16x16x32_bf16 v[110:113], v[142:145], v[188:191], v[110:113]
	v_mfma_f32_16x16x32_bf16 v[106:109], v[170:173], v[188:191], v[106:109]
	v_mfma_f32_16x16x32_bf16 v[94:97], v[142:145], v[196:199], v[94:97]
	v_mfma_f32_16x16x32_bf16 v[90:93], v[170:173], v[196:199], v[90:93]
	v_mfma_f32_16x16x32_bf16 v[78:81], v[142:145], v[204:207], v[78:81]
	v_mfma_f32_16x16x32_bf16 v[74:77], v[170:173], v[204:207], v[74:77]
	v_mfma_f32_16x16x32_bf16 v[126:129], v[166:169], v[182:185], v[126:129]
	v_mfma_f32_16x16x32_bf16 v[122:125], v[174:177], v[182:185], v[122:125]
	v_mfma_f32_16x16x32_bf16 v[110:113], v[166:169], v[192:195], v[110:113]
	v_mfma_f32_16x16x32_bf16 v[106:109], v[174:177], v[192:195], v[106:109]
	v_mfma_f32_16x16x32_bf16 v[94:97], v[166:169], v[200:203], v[94:97]
	v_mfma_f32_16x16x32_bf16 v[90:93], v[174:177], v[200:203], v[90:93]
	v_mfma_f32_16x16x32_bf16 v[78:81], v[166:169], v[208:211], v[78:81]
	v_mfma_f32_16x16x32_bf16 v[74:77], v[174:177], v[208:211], v[74:77]
	v_mfma_f32_16x16x32_bf16 v[118:121], v[212:215], v[178:181], v[118:121]
	v_mfma_f32_16x16x32_bf16 v[114:117], v[232:235], v[178:181], v[114:117]
	v_mfma_f32_16x16x32_bf16 v[102:105], v[212:215], v[188:191], v[102:105]
	v_mfma_f32_16x16x32_bf16 v[98:101], v[232:235], v[188:191], v[98:101]
	v_mfma_f32_16x16x32_bf16 v[86:89], v[212:215], v[196:199], v[86:89]
	v_mfma_f32_16x16x32_bf16 v[82:85], v[232:235], v[196:199], v[82:85]
	v_mfma_f32_16x16x32_bf16 v[70:73], v[212:215], v[204:207], v[70:73]
	v_mfma_f32_16x16x32_bf16 v[66:69], v[232:235], v[204:207], v[66:69]
	v_mfma_f32_16x16x32_bf16 v[118:121], v[216:219], v[182:185], v[118:121]
	v_mfma_f32_16x16x32_bf16 v[114:117], v[236:239], v[182:185], v[114:117]
	v_mfma_f32_16x16x32_bf16 v[102:105], v[216:219], v[192:195], v[102:105]
	v_mfma_f32_16x16x32_bf16 v[98:101], v[236:239], v[192:195], v[98:101]
	v_mfma_f32_16x16x32_bf16 v[86:89], v[216:219], v[200:203], v[86:89]
	v_mfma_f32_16x16x32_bf16 v[82:85], v[236:239], v[200:203], v[82:85]
	v_mfma_f32_16x16x32_bf16 v[70:73], v[216:219], v[208:211], v[70:73]
	v_mfma_f32_16x16x32_bf16 v[66:69], v[236:239], v[208:211], v[66:69]
	s_setprio 0
	s_mov_b32 m0, s46
	v_lshl_add_u64 v[240:241], s[42:43], 0, v[130:131]
	s_barrier
	ds_read_b128 v[178:181], v0 offset:16384
	ds_read_b128 v[182:185], v0 offset:17408
	ds_read_b128 v[188:191], v0 offset:18432
	ds_read_b128 v[192:195], v0 offset:19456
	ds_read_b128 v[196:199], v0 offset:20480
	ds_read_b128 v[200:203], v0 offset:21504
	ds_read_b128 v[204:207], v0 offset:22528
	ds_read_b128 v[208:211], v0 offset:23552
	global_load_lds_dwordx4 v[240:241], off
	v_lshl_add_u64 v[242:243], s[42:43], 0, v[134:135]
	s_mov_b32 m0, s9
	s_nop 0
	global_load_lds_dwordx4 v[242:243], off
	s_mov_b32 m0, s47
	v_lshl_add_u64 v[146:147], s[40:41], 0, v[132:133]
	global_load_lds_dwordx4 v[146:147], off
	v_lshl_add_u64 v[220:221], s[40:41], 0, v[136:137]
	s_mov_b32 m0, s48
	s_nop 0
	global_load_lds_dwordx4 v[220:221], off
	s_barrier
	s_waitcnt lgkmcnt(0)
	s_setprio 1
	s_waitcnt lgkmcnt(0)
	v_mfma_f32_16x16x32_bf16 v[62:65], v[142:145], v[178:181], v[62:65]
	v_mfma_f32_16x16x32_bf16 v[58:61], v[170:173], v[178:181], v[58:61]
	v_mfma_f32_16x16x32_bf16 v[46:49], v[142:145], v[188:191], v[46:49]
	v_mfma_f32_16x16x32_bf16 v[42:45], v[170:173], v[188:191], v[42:45]
	v_mfma_f32_16x16x32_bf16 v[30:33], v[142:145], v[196:199], v[30:33]
	v_mfma_f32_16x16x32_bf16 v[26:29], v[170:173], v[196:199], v[26:29]
	v_mfma_f32_16x16x32_bf16 v[14:17], v[142:145], v[204:207], v[14:17]
	v_mfma_f32_16x16x32_bf16 v[10:13], v[170:173], v[204:207], v[10:13]
	v_mfma_f32_16x16x32_bf16 v[62:65], v[166:169], v[182:185], v[62:65]
	v_mfma_f32_16x16x32_bf16 v[58:61], v[174:177], v[182:185], v[58:61]
	v_mfma_f32_16x16x32_bf16 v[46:49], v[166:169], v[192:195], v[46:49]
	v_mfma_f32_16x16x32_bf16 v[42:45], v[174:177], v[192:195], v[42:45]
	v_mfma_f32_16x16x32_bf16 v[30:33], v[166:169], v[200:203], v[30:33]
	v_mfma_f32_16x16x32_bf16 v[26:29], v[174:177], v[200:203], v[26:29]
	v_mfma_f32_16x16x32_bf16 v[14:17], v[166:169], v[208:211], v[14:17]
	v_mfma_f32_16x16x32_bf16 v[10:13], v[174:177], v[208:211], v[10:13]
	s_setprio 0
	s_barrier
	s_add_u32 s66, s40, 0x40000
	s_addc_u32 s67, s41, 0
	s_mov_b32 m0, s49
	v_lshl_add_u64 v[142:143], s[66:67], 0, v[132:133]
	global_load_lds_dwordx4 v[142:143], off
	v_lshl_add_u64 v[142:143], s[66:67], 0, v[136:137]
	s_mov_b32 m0, s50
	s_nop 0
	global_load_lds_dwordx4 v[142:143], off
	s_waitcnt vmcnt(8)
	s_barrier
	s_setprio 1
	v_mfma_f32_16x16x32_bf16 v[54:57], v[212:215], v[178:181], v[54:57]
	v_mfma_f32_16x16x32_bf16 v[50:53], v[232:235], v[178:181], v[50:53]
	v_mfma_f32_16x16x32_bf16 v[38:41], v[212:215], v[188:191], v[38:41]
	v_mfma_f32_16x16x32_bf16 v[34:37], v[232:235], v[188:191], v[34:37]
	v_mfma_f32_16x16x32_bf16 v[22:25], v[212:215], v[196:199], v[22:25]
	v_mfma_f32_16x16x32_bf16 v[18:21], v[232:235], v[196:199], v[18:21]
	v_mfma_f32_16x16x32_bf16 v[6:9], v[212:215], v[204:207], v[6:9]
	v_mfma_f32_16x16x32_bf16 v[2:5], v[232:235], v[204:207], v[2:5]
	v_mfma_f32_16x16x32_bf16 v[54:57], v[216:219], v[182:185], v[54:57]
	v_mfma_f32_16x16x32_bf16 v[50:53], v[236:239], v[182:185], v[50:53]
	v_mfma_f32_16x16x32_bf16 v[38:41], v[216:219], v[192:195], v[38:41]
	v_mfma_f32_16x16x32_bf16 v[34:37], v[236:239], v[192:195], v[34:37]
	v_mfma_f32_16x16x32_bf16 v[22:25], v[216:219], v[200:203], v[22:25]
	v_mfma_f32_16x16x32_bf16 v[18:21], v[236:239], v[200:203], v[18:21]
	v_mfma_f32_16x16x32_bf16 v[6:9], v[216:219], v[208:211], v[6:9]
	v_mfma_f32_16x16x32_bf16 v[2:5], v[236:239], v[208:211], v[2:5]
	s_setprio 0
	s_barrier
	ds_read_b128 v[142:145], v157
	ds_read_b128 v[166:169], v158
	ds_read_b128 v[170:173], v159
	ds_read_b128 v[174:177], v160
	s_add_u32 s42, s42, 0x40000
	s_addc_u32 s43, s43, 0
	s_mov_b32 m0, s51
	v_lshl_add_u64 v[212:213], s[42:43], 0, v[130:131]
	ds_read_b128 v[178:181], v0 offset:32768
	ds_read_b128 v[182:185], v0 offset:33792
	ds_read_b128 v[188:191], v0 offset:34816
	ds_read_b128 v[192:195], v0 offset:35840
	ds_read_b128 v[196:199], v0 offset:36864
	ds_read_b128 v[200:203], v0 offset:37888
	ds_read_b128 v[204:207], v0 offset:38912
	ds_read_b128 v[208:211], v0 offset:39936
	global_load_lds_dwordx4 v[212:213], off
	v_lshl_add_u64 v[212:213], s[42:43], 0, v[134:135]
	s_mov_b32 m0, s52
	s_nop 0
	global_load_lds_dwordx4 v[212:213], off
	ds_read_b128 v[212:215], v161
	ds_read_b128 v[216:219], v162
	ds_read_b128 v[232:235], v163
	ds_read_b128 v[236:239], v164
	s_waitcnt lgkmcnt(4)
	s_waitcnt vmcnt(8)
	s_barrier
	s_waitcnt lgkmcnt(0)
	s_setprio 1
	s_waitcnt lgkmcnt(0)
	v_mfma_f32_16x16x32_bf16 v[126:129], v[142:145], v[178:181], v[126:129]
	v_mfma_f32_16x16x32_bf16 v[122:125], v[170:173], v[178:181], v[122:125]
	v_mfma_f32_16x16x32_bf16 v[110:113], v[142:145], v[188:191], v[110:113]
	v_mfma_f32_16x16x32_bf16 v[106:109], v[170:173], v[188:191], v[106:109]
	v_mfma_f32_16x16x32_bf16 v[94:97], v[142:145], v[196:199], v[94:97]
	v_mfma_f32_16x16x32_bf16 v[90:93], v[170:173], v[196:199], v[90:93]
	v_mfma_f32_16x16x32_bf16 v[78:81], v[142:145], v[204:207], v[78:81]
	v_mfma_f32_16x16x32_bf16 v[74:77], v[170:173], v[204:207], v[74:77]
	v_mfma_f32_16x16x32_bf16 v[126:129], v[166:169], v[182:185], v[126:129]
	v_mfma_f32_16x16x32_bf16 v[122:125], v[174:177], v[182:185], v[122:125]
	v_mfma_f32_16x16x32_bf16 v[110:113], v[166:169], v[192:195], v[110:113]
	v_mfma_f32_16x16x32_bf16 v[106:109], v[174:177], v[192:195], v[106:109]
	v_mfma_f32_16x16x32_bf16 v[94:97], v[166:169], v[200:203], v[94:97]
	v_mfma_f32_16x16x32_bf16 v[90:93], v[174:177], v[200:203], v[90:93]
	v_mfma_f32_16x16x32_bf16 v[78:81], v[166:169], v[208:211], v[78:81]
	v_mfma_f32_16x16x32_bf16 v[74:77], v[174:177], v[208:211], v[74:77]
	v_mfma_f32_16x16x32_bf16 v[118:121], v[212:215], v[178:181], v[118:121]
	v_mfma_f32_16x16x32_bf16 v[114:117], v[232:235], v[178:181], v[114:117]
	v_mfma_f32_16x16x32_bf16 v[102:105], v[212:215], v[188:191], v[102:105]
	v_mfma_f32_16x16x32_bf16 v[98:101], v[232:235], v[188:191], v[98:101]
	v_mfma_f32_16x16x32_bf16 v[86:89], v[212:215], v[196:199], v[86:89]
	v_mfma_f32_16x16x32_bf16 v[82:85], v[232:235], v[196:199], v[82:85]
	v_mfma_f32_16x16x32_bf16 v[70:73], v[212:215], v[204:207], v[70:73]
	v_mfma_f32_16x16x32_bf16 v[66:69], v[232:235], v[204:207], v[66:69]
	v_mfma_f32_16x16x32_bf16 v[118:121], v[216:219], v[182:185], v[118:121]
	v_mfma_f32_16x16x32_bf16 v[114:117], v[236:239], v[182:185], v[114:117]
	v_mfma_f32_16x16x32_bf16 v[102:105], v[216:219], v[192:195], v[102:105]
	v_mfma_f32_16x16x32_bf16 v[98:101], v[236:239], v[192:195], v[98:101]
	v_mfma_f32_16x16x32_bf16 v[86:89], v[216:219], v[200:203], v[86:89]
	v_mfma_f32_16x16x32_bf16 v[82:85], v[236:239], v[200:203], v[82:85]
	v_mfma_f32_16x16x32_bf16 v[70:73], v[216:219], v[208:211], v[70:73]
	v_mfma_f32_16x16x32_bf16 v[66:69], v[236:239], v[208:211], v[66:69]
	s_setprio 0
	s_barrier
	ds_read_b128 v[178:181], v0 offset:49152
	ds_read_b128 v[182:185], v0 offset:50176
	ds_read_b128 v[188:191], v0 offset:51200
	ds_read_b128 v[192:195], v0 offset:52224
	ds_read_b128 v[196:199], v0 offset:53248
	ds_read_b128 v[200:203], v0 offset:54272
	ds_read_b128 v[204:207], v0 offset:55296
	ds_read_b128 v[208:211], v0 offset:56320
	s_mov_b32 m0, s55
	v_lshl_add_u64 v[146:147], v[146:147], 0, s[24:25]
	global_load_lds_dwordx4 v[146:147], off
	v_lshl_add_u64 v[146:147], v[220:221], 0, s[24:25]
	s_mov_b32 m0, s56
	s_nop 0
	global_load_lds_dwordx4 v[146:147], off
	s_mov_b32 m0, s57
	v_lshl_add_u64 v[146:147], v[240:241], 0, s[24:25]
	global_load_lds_dwordx4 v[146:147], off
	v_lshl_add_u64 v[146:147], v[242:243], 0, s[24:25]
	s_mov_b32 m0, s58
	s_nop 0
	global_load_lds_dwordx4 v[146:147], off
	s_barrier
	s_waitcnt lgkmcnt(0)
	s_setprio 1
	s_waitcnt lgkmcnt(0)
	v_mfma_f32_16x16x32_bf16 v[62:65], v[142:145], v[178:181], v[62:65]
	v_mfma_f32_16x16x32_bf16 v[58:61], v[170:173], v[178:181], v[58:61]
	v_mfma_f32_16x16x32_bf16 v[46:49], v[142:145], v[188:191], v[46:49]
	v_mfma_f32_16x16x32_bf16 v[42:45], v[170:173], v[188:191], v[42:45]
	v_mfma_f32_16x16x32_bf16 v[30:33], v[142:145], v[196:199], v[30:33]
	v_mfma_f32_16x16x32_bf16 v[26:29], v[170:173], v[196:199], v[26:29]
	v_mfma_f32_16x16x32_bf16 v[14:17], v[142:145], v[204:207], v[14:17]
	v_mfma_f32_16x16x32_bf16 v[10:13], v[170:173], v[204:207], v[10:13]
	v_mfma_f32_16x16x32_bf16 v[62:65], v[166:169], v[182:185], v[62:65]
	v_mfma_f32_16x16x32_bf16 v[58:61], v[174:177], v[182:185], v[58:61]
	v_mfma_f32_16x16x32_bf16 v[46:49], v[166:169], v[192:195], v[46:49]
	v_mfma_f32_16x16x32_bf16 v[42:45], v[174:177], v[192:195], v[42:45]
	v_mfma_f32_16x16x32_bf16 v[30:33], v[166:169], v[200:203], v[30:33]
	v_mfma_f32_16x16x32_bf16 v[26:29], v[174:177], v[200:203], v[26:29]
	v_mfma_f32_16x16x32_bf16 v[14:17], v[166:169], v[208:211], v[14:17]
	v_mfma_f32_16x16x32_bf16 v[10:13], v[174:177], v[208:211], v[10:13]
	s_setprio 0
	s_barrier
	s_add_u32 s40, s40, 0x40080
	s_addc_u32 s41, s41, 0
	s_mov_b32 m0, s59
	v_lshl_add_u64 v[142:143], s[40:41], 0, v[132:133]
	global_load_lds_dwordx4 v[142:143], off
	v_lshl_add_u64 v[142:143], s[40:41], 0, v[136:137]
	s_mov_b32 m0, s60
	s_nop 0
	global_load_lds_dwordx4 v[142:143], off
	s_waitcnt vmcnt(8)
	s_barrier
	s_setprio 1
	v_mfma_f32_16x16x32_bf16 v[54:57], v[212:215], v[178:181], v[54:57]
	v_mfma_f32_16x16x32_bf16 v[50:53], v[232:235], v[178:181], v[50:53]
	v_mfma_f32_16x16x32_bf16 v[38:41], v[212:215], v[188:191], v[38:41]
	v_mfma_f32_16x16x32_bf16 v[34:37], v[232:235], v[188:191], v[34:37]
	v_mfma_f32_16x16x32_bf16 v[22:25], v[212:215], v[196:199], v[22:25]
	v_mfma_f32_16x16x32_bf16 v[18:21], v[232:235], v[196:199], v[18:21]
	v_mfma_f32_16x16x32_bf16 v[6:9], v[212:215], v[204:207], v[6:9]
	v_mfma_f32_16x16x32_bf16 v[2:5], v[232:235], v[204:207], v[2:5]
	v_mfma_f32_16x16x32_bf16 v[54:57], v[216:219], v[182:185], v[54:57]
	v_mfma_f32_16x16x32_bf16 v[50:53], v[236:239], v[182:185], v[50:53]
	v_mfma_f32_16x16x32_bf16 v[38:41], v[216:219], v[192:195], v[38:41]
	v_mfma_f32_16x16x32_bf16 v[34:37], v[236:239], v[192:195], v[34:37]
	v_mfma_f32_16x16x32_bf16 v[22:25], v[216:219], v[200:203], v[22:25]
	v_mfma_f32_16x16x32_bf16 v[18:21], v[236:239], v[200:203], v[18:21]
	v_mfma_f32_16x16x32_bf16 v[6:9], v[216:219], v[208:211], v[6:9]
	v_mfma_f32_16x16x32_bf16 v[2:5], v[236:239], v[208:211], v[2:5]
	s_setprio 0
	s_add_i32 s65, s65, 2
	s_add_u32 s38, s38, 0x100
	s_addc_u32 s39, s39, 0
	s_add_u32 s63, s63, 0x100
	s_addc_u32 s64, s64, 0
	s_cmp_gt_u32 s65, 13
	s_barrier
	s_cbranch_scc0 .LBB0_1055
	v_readlane_b32 s13, v252, 51
	v_readlane_b32 s7, v252, 52
	v_mbcnt_lo_u32_b32 v143, -1, 0
	v_mbcnt_hi_u32_b32 v143, -1, v143
	s_lshl_b32 s15, s13, 6
	s_cmp_gt_i32 s8, 1
	v_and_b32_e32 v144, 15, v143
	s_cselect_b64 s[40:41], -1, 0
	v_or_b32_e32 v142, s15, v144
	s_mov_b64 s[42:43], -1
	s_and_b64 vcc, exec, s[40:41]
	s_cbranch_vccz .LBB0_1058
	s_movk_i32 s38, 0x80
	v_cmp_gt_i32_e32 vcc, s38, v142
	s_mov_b64 s[42:43], 0
	s_nop 0
	v_cndmask_b32_e32 v0, v187, v223, vcc
	v_mov_b64_e32 v[146:147], v[0:1]

.LBB0_1142:
	s_add_u32 s4, s10, 0x4c200000
	s_addc_u32 s5, s11, 0
	s_lshl_b32 s28, s84, 9
	s_lshl_b64 s[12:13], s[28:29], 2
	s_add_u32 s12, s10, s12
	s_addc_u32 s13, s11, s13
	s_add_u32 s28, s12, 0x4300000
	s_addc_u32 s54, s13, 0
	s_add_i32 s56, s46, 0x18000
	s_lshl_b32 s6, s6, 12
	v_lshl_add_u64 v[8:9], v[8:9], 0, s[24:25]
	s_mov_b32 m0, s56
	s_add_i32 s57, s46, 0x1a000
	s_lshl_b32 s55, s7, 13
	s_and_b32 s12, s6, 0x3000
	s_waitcnt vmcnt(2)
	s_barrier
	global_load_lds_dwordx4 v[8:9], off
	v_lshl_add_u64 v[6:7], v[6:7], 0, s[24:25]
	s_mov_b32 m0, s57
	s_add_i32 s58, s46, 0x8000
	s_add_i32 s59, s46, 0xa000
	global_load_lds_dwordx4 v[6:7], off
	v_lshl_add_u64 v[4:5], v[4:5], 0, s[24:25]
	s_mov_b32 m0, s58
	s_add_u32 s6, s34, 0x80080
	global_load_lds_dwordx4 v[4:5], off
	v_lshl_add_u64 v[2:3], v[2:3], 0, s[24:25]
	s_mov_b32 m0, s59
	s_addc_u32 s7, s35, 0
	s_add_i32 s60, s46, 0x1c000
	global_load_lds_dwordx4 v[2:3], off
	v_lshl_add_u64 v[2:3], s[6:7], 0, v[0:1]
	s_mov_b32 m0, s60
	s_add_i32 s61, s46, 0x1e000
	global_load_lds_dwordx4 v[2:3], off
	v_lshl_add_u64 v[2:3], s[6:7], 0, v[138:139]
	s_mov_b32 m0, s61
	v_mov_b32_e32 v145, v1
	global_load_lds_dwordx4 v[2:3], off
	v_and_b32_e32 v2, 15, v11
	v_and_b32_e32 v3, 48, v11
	v_lshl_or_b32 v2, v2, 6, v3
	v_lshlrev_b32_e32 v3, 2, v11
	v_and_b32_e32 v3, 32, v3
	v_xad_u32 v154, v2, v3, 0
	v_add_u32_e32 v2, s12, v154
	v_add_u32_e32 v155, 0x10000, v2
	v_add_u32_e32 v156, 0x10400, v2
	v_add_u32_e32 v157, 0x10800, v2
	v_add_u32_e32 v158, 0x10c00, v2
	v_add_u32_e32 v159, 0x14000, v2
	v_add_u32_e32 v160, 0x14400, v2
	v_add_u32_e32 v161, 0x14800, v2
	v_add_u32_e32 v162, 0x14c00, v2
	v_add_u32_e32 v163, 0x18000, v2
	v_add_u32_e32 v164, 0x18400, v2
	v_add_u32_e32 v165, 0x18800, v2
	v_add_u32_e32 v166, 0x18c00, v2
	v_add_u32_e32 v167, 0x1c000, v2
	v_add_u32_e32 v168, 0x1c400, v2
	v_add_u32_e32 v169, 0x1c800, v2
	v_add_u32_e32 v170, 0x1cc00, v2
	v_lshlrev_b32_e32 v2, 14, v15
	v_and_b32_e32 v2, 0xffff8000, v2
	v_lshl_add_u32 v2, v14, 11, v2
	v_and_b32_e32 v3, 1, v15
	v_lshl_or_b32 v2, v3, 6, v2
	v_lshl_add_u32 v144, v16, 1, v2
	v_lshlrev_b32_e32 v2, 14, v10
	v_and_b32_e32 v2, 0xffff8000, v2
	s_waitcnt vmcnt(6)
	v_lshl_add_u32 v2, v12, 11, v2
	v_and_b32_e32 v3, 1, v10
	v_lshl_or_b32 v2, v3, 6, v2
	v_lshl_add_u32 v146, v13, 1, v2
	v_mov_b32_e32 v147, v1
	s_mov_b32 s62, 0
	v_readlane_b32 s64, v253, 42
	s_barrier

.LBB0_1150:
	ds_read_b128 v[102:105], v155
	ds_read_b128 v[110:113], v156
	ds_read_b128 v[148:151], v157
	ds_read_b128 v[172:175], v158
	s_add_u32 s34, s20, 0xfffc0080
	s_addc_u32 s35, s21, -1
	s_cmp_eq_u32 s71, 28
	s_cselect_b32 s39, s65, s35
	s_cselect_b32 s38, s66, s34
	s_cselect_b32 s35, s67, s70
	s_cselect_b32 s34, s68, s69
	v_add_u32_e32 v171, s55, v154
	v_lshl_add_u64 v[152:153], s[20:21], 0, v[144:145]
	s_add_i32 m0, s46, 0xc000
	ds_read_b128 v[176:179], v171
	ds_read_b128 v[180:183], v171 offset:1024
	ds_read_b128 v[188:191], v171 offset:2048
	ds_read_b128 v[192:195], v171 offset:3072
	ds_read_b128 v[196:199], v171 offset:4096
	ds_read_b128 v[200:203], v171 offset:5120
	ds_read_b128 v[204:207], v171 offset:6144
	ds_read_b128 v[208:211], v171 offset:7168
	global_load_lds_dwordx4 v[152:153], off
	v_lshl_add_u64 v[152:153], s[20:21], 0, v[146:147]
	s_add_i32 m0, s46, 0xe000
	s_nop 0
	global_load_lds_dwordx4 v[152:153], off
	ds_read_b128 v[212:215], v159
	ds_read_b128 v[216:219], v160
	ds_read_b128 v[232:235], v161
	ds_read_b128 v[236:239], v162
	s_waitcnt lgkmcnt(4)
	s_waitcnt vmcnt(8)
	s_barrier
	s_waitcnt lgkmcnt(0)
	s_setprio 1
	s_waitcnt lgkmcnt(0)
	v_mfma_f32_16x16x32_bf16 v[134:137], v[102:105], v[176:179], v[134:137]
	v_mfma_f32_16x16x32_bf16 v[130:133], v[148:151], v[176:179], v[130:133]
	v_mfma_f32_16x16x32_bf16 v[126:129], v[102:105], v[188:191], v[126:129]
	v_mfma_f32_16x16x32_bf16 v[122:125], v[148:151], v[188:191], v[122:125]
	v_mfma_f32_16x16x32_bf16 v[118:121], v[102:105], v[196:199], v[118:121]
	v_mfma_f32_16x16x32_bf16 v[114:117], v[148:151], v[196:199], v[114:117]
	v_mfma_f32_16x16x32_bf16 v[106:109], v[102:105], v[204:207], v[106:109]
	v_mfma_f32_16x16x32_bf16 v[98:101], v[148:151], v[204:207], v[98:101]
	v_mfma_f32_16x16x32_bf16 v[134:137], v[110:113], v[180:183], v[134:137]
	v_mfma_f32_16x16x32_bf16 v[130:133], v[172:175], v[180:183], v[130:133]
	v_mfma_f32_16x16x32_bf16 v[126:129], v[110:113], v[192:195], v[126:129]
	v_mfma_f32_16x16x32_bf16 v[122:125], v[172:175], v[192:195], v[122:125]
	v_mfma_f32_16x16x32_bf16 v[118:121], v[110:113], v[200:203], v[118:121]
	v_mfma_f32_16x16x32_bf16 v[114:117], v[172:175], v[200:203], v[114:117]
	v_mfma_f32_16x16x32_bf16 v[106:109], v[110:113], v[208:211], v[106:109]
	v_mfma_f32_16x16x32_bf16 v[98:101], v[172:175], v[208:211], v[98:101]
	v_mfma_f32_16x16x32_bf16 v[62:65], v[212:215], v[176:179], v[62:65]
	v_mfma_f32_16x16x32_bf16 v[58:61], v[232:235], v[176:179], v[58:61]
	v_mfma_f32_16x16x32_bf16 v[54:57], v[212:215], v[188:191], v[54:57]
	v_mfma_f32_16x16x32_bf16 v[50:53], v[232:235], v[188:191], v[50:53]
	v_mfma_f32_16x16x32_bf16 v[46:49], v[212:215], v[196:199], v[46:49]
	v_mfma_f32_16x16x32_bf16 v[42:45], v[232:235], v[196:199], v[42:45]
	v_mfma_f32_16x16x32_bf16 v[38:41], v[212:215], v[204:207], v[38:41]
	v_mfma_f32_16x16x32_bf16 v[34:37], v[232:235], v[204:207], v[34:37]
	v_mfma_f32_16x16x32_bf16 v[62:65], v[216:219], v[180:183], v[62:65]
	v_mfma_f32_16x16x32_bf16 v[58:61], v[236:239], v[180:183], v[58:61]
	v_mfma_f32_16x16x32_bf16 v[54:57], v[216:219], v[192:195], v[54:57]
	v_mfma_f32_16x16x32_bf16 v[50:53], v[236:239], v[192:195], v[50:53]
	v_mfma_f32_16x16x32_bf16 v[46:49], v[216:219], v[200:203], v[46:49]
	v_mfma_f32_16x16x32_bf16 v[42:45], v[236:239], v[200:203], v[42:45]
	v_mfma_f32_16x16x32_bf16 v[38:41], v[216:219], v[208:211], v[38:41]
	v_mfma_f32_16x16x32_bf16 v[34:37], v[236:239], v[208:211], v[34:37]
	s_setprio 0
	s_mov_b32 m0, s46
	v_lshl_add_u64 v[220:221], s[38:39], 0, v[142:143]
	s_barrier
	ds_read_b128 v[176:179], v171 offset:16384
	ds_read_b128 v[180:183], v171 offset:17408
	ds_read_b128 v[188:191], v171 offset:18432
	ds_read_b128 v[192:195], v171 offset:19456
	ds_read_b128 v[196:199], v171 offset:20480
	ds_read_b128 v[200:203], v171 offset:21504
	ds_read_b128 v[204:207], v171 offset:22528
	ds_read_b128 v[208:211], v171 offset:23552
	global_load_lds_dwordx4 v[220:221], off
	v_lshl_add_u64 v[240:241], s[38:39], 0, v[140:141]
	s_mov_b32 m0, s49
	s_nop 0
	global_load_lds_dwordx4 v[240:241], off
	s_mov_b32 m0, s47
	v_lshl_add_u64 v[152:153], s[34:35], 0, v[0:1]
	global_load_lds_dwordx4 v[152:153], off
	v_lshl_add_u64 v[184:185], s[34:35], 0, v[138:139]
	s_mov_b32 m0, s48
	s_nop 0
	global_load_lds_dwordx4 v[184:185], off
	s_barrier
	s_waitcnt lgkmcnt(0)
	s_setprio 1
	s_waitcnt lgkmcnt(0)
	v_mfma_f32_16x16x32_bf16 v[94:97], v[102:105], v[176:179], v[94:97]
	v_mfma_f32_16x16x32_bf16 v[90:93], v[148:151], v[176:179], v[90:93]
	v_mfma_f32_16x16x32_bf16 v[86:89], v[102:105], v[188:191], v[86:89]
	v_mfma_f32_16x16x32_bf16 v[82:85], v[148:151], v[188:191], v[82:85]
	v_mfma_f32_16x16x32_bf16 v[78:81], v[102:105], v[196:199], v[78:81]
	v_mfma_f32_16x16x32_bf16 v[74:77], v[148:151], v[196:199], v[74:77]
	v_mfma_f32_16x16x32_bf16 v[70:73], v[102:105], v[204:207], v[70:73]
	v_mfma_f32_16x16x32_bf16 v[66:69], v[148:151], v[204:207], v[66:69]
	v_mfma_f32_16x16x32_bf16 v[94:97], v[110:113], v[180:183], v[94:97]
	v_mfma_f32_16x16x32_bf16 v[90:93], v[172:175], v[180:183], v[90:93]
	v_mfma_f32_16x16x32_bf16 v[86:89], v[110:113], v[192:195], v[86:89]
	v_mfma_f32_16x16x32_bf16 v[82:85], v[172:175], v[192:195], v[82:85]
	v_mfma_f32_16x16x32_bf16 v[78:81], v[110:113], v[200:203], v[78:81]
	v_mfma_f32_16x16x32_bf16 v[74:77], v[172:175], v[200:203], v[74:77]
	v_mfma_f32_16x16x32_bf16 v[70:73], v[110:113], v[208:211], v[70:73]
	v_mfma_f32_16x16x32_bf16 v[66:69], v[172:175], v[208:211], v[66:69]
	s_setprio 0
	s_barrier
	s_add_u32 s72, s34, 0x80000
	s_addc_u32 s73, s35, 0
	s_mov_b32 m0, s50
	v_lshl_add_u64 v[102:103], s[72:73], 0, v[0:1]
	global_load_lds_dwordx4 v[102:103], off
	v_lshl_add_u64 v[102:103], s[72:73], 0, v[138:139]
	s_mov_b32 m0, s51
	s_nop 0
	global_load_lds_dwordx4 v[102:103], off
	s_waitcnt vmcnt(8)
	s_barrier
	s_setprio 1
	v_mfma_f32_16x16x32_bf16 v[30:33], v[212:215], v[176:179], v[30:33]
	v_mfma_f32_16x16x32_bf16 v[26:29], v[232:235], v[176:179], v[26:29]
	v_mfma_f32_16x16x32_bf16 v[22:25], v[212:215], v[188:191], v[22:25]
	v_mfma_f32_16x16x32_bf16 v[18:21], v[232:235], v[188:191], v[18:21]
	v_mfma_f32_16x16x32_bf16 v[14:17], v[212:215], v[196:199], v[14:17]
	v_mfma_f32_16x16x32_bf16 v[10:13], v[232:235], v[196:199], v[10:13]
	v_mfma_f32_16x16x32_bf16 v[6:9], v[212:215], v[204:207], v[6:9]
	v_mfma_f32_16x16x32_bf16 v[2:5], v[232:235], v[204:207], v[2:5]
	v_mfma_f32_16x16x32_bf16 v[30:33], v[216:219], v[180:183], v[30:33]
	v_mfma_f32_16x16x32_bf16 v[26:29], v[236:239], v[180:183], v[26:29]
	v_mfma_f32_16x16x32_bf16 v[22:25], v[216:219], v[192:195], v[22:25]
	v_mfma_f32_16x16x32_bf16 v[18:21], v[236:239], v[192:195], v[18:21]
	v_mfma_f32_16x16x32_bf16 v[14:17], v[216:219], v[200:203], v[14:17]
	v_mfma_f32_16x16x32_bf16 v[10:13], v[236:239], v[200:203], v[10:13]
	v_mfma_f32_16x16x32_bf16 v[6:9], v[216:219], v[208:211], v[6:9]
	v_mfma_f32_16x16x32_bf16 v[2:5], v[236:239], v[208:211], v[2:5]
	s_setprio 0
	s_barrier
	ds_read_b128 v[102:105], v163
	ds_read_b128 v[110:113], v164
	ds_read_b128 v[148:151], v165
	ds_read_b128 v[172:175], v166
	s_add_u32 s38, s38, 0x40000
	s_addc_u32 s39, s39, 0
	s_mov_b32 m0, s52
	v_lshl_add_u64 v[212:213], s[38:39], 0, v[142:143]
	ds_read_b128 v[176:179], v171 offset:32768
	ds_read_b128 v[180:183], v171 offset:33792
	ds_read_b128 v[188:191], v171 offset:34816
	ds_read_b128 v[192:195], v171 offset:35840
	ds_read_b128 v[196:199], v171 offset:36864
	ds_read_b128 v[200:203], v171 offset:37888
	ds_read_b128 v[204:207], v171 offset:38912
	ds_read_b128 v[208:211], v171 offset:39936
	global_load_lds_dwordx4 v[212:213], off
	v_lshl_add_u64 v[212:213], s[38:39], 0, v[140:141]
	s_mov_b32 m0, s53
	s_nop 0
	global_load_lds_dwordx4 v[212:213], off
	ds_read_b128 v[212:215], v167
	ds_read_b128 v[216:219], v168
	ds_read_b128 v[232:235], v169
	ds_read_b128 v[236:239], v170
	s_waitcnt lgkmcnt(4)
	s_waitcnt vmcnt(8)
	s_barrier
	s_waitcnt lgkmcnt(0)
	s_setprio 1
	s_waitcnt lgkmcnt(0)
	v_mfma_f32_16x16x32_bf16 v[134:137], v[102:105], v[176:179], v[134:137]
	v_mfma_f32_16x16x32_bf16 v[130:133], v[148:151], v[176:179], v[130:133]
	v_mfma_f32_16x16x32_bf16 v[126:129], v[102:105], v[188:191], v[126:129]
	v_mfma_f32_16x16x32_bf16 v[122:125], v[148:151], v[188:191], v[122:125]
	v_mfma_f32_16x16x32_bf16 v[118:121], v[102:105], v[196:199], v[118:121]
	v_mfma_f32_16x16x32_bf16 v[114:117], v[148:151], v[196:199], v[114:117]
	v_mfma_f32_16x16x32_bf16 v[106:109], v[102:105], v[204:207], v[106:109]
	v_mfma_f32_16x16x32_bf16 v[98:101], v[148:151], v[204:207], v[98:101]
	v_mfma_f32_16x16x32_bf16 v[134:137], v[110:113], v[180:183], v[134:137]
	v_mfma_f32_16x16x32_bf16 v[130:133], v[172:175], v[180:183], v[130:133]
	v_mfma_f32_16x16x32_bf16 v[126:129], v[110:113], v[192:195], v[126:129]
	v_mfma_f32_16x16x32_bf16 v[122:125], v[172:175], v[192:195], v[122:125]
	v_mfma_f32_16x16x32_bf16 v[118:121], v[110:113], v[200:203], v[118:121]
	v_mfma_f32_16x16x32_bf16 v[114:117], v[172:175], v[200:203], v[114:117]
	v_mfma_f32_16x16x32_bf16 v[106:109], v[110:113], v[208:211], v[106:109]
	v_mfma_f32_16x16x32_bf16 v[98:101], v[172:175], v[208:211], v[98:101]
	v_mfma_f32_16x16x32_bf16 v[62:65], v[212:215], v[176:179], v[62:65]
	v_mfma_f32_16x16x32_bf16 v[58:61], v[232:235], v[176:179], v[58:61]
	v_mfma_f32_16x16x32_bf16 v[54:57], v[212:215], v[188:191], v[54:57]
	v_mfma_f32_16x16x32_bf16 v[50:53], v[232:235], v[188:191], v[50:53]
	v_mfma_f32_16x16x32_bf16 v[46:49], v[212:215], v[196:199], v[46:49]
	v_mfma_f32_16x16x32_bf16 v[42:45], v[232:235], v[196:199], v[42:45]
	v_mfma_f32_16x16x32_bf16 v[38:41], v[212:215], v[204:207], v[38:41]
	v_mfma_f32_16x16x32_bf16 v[34:37], v[232:235], v[204:207], v[34:37]
	v_mfma_f32_16x16x32_bf16 v[62:65], v[216:219], v[180:183], v[62:65]
	v_mfma_f32_16x16x32_bf16 v[58:61], v[236:239], v[180:183], v[58:61]
	v_mfma_f32_16x16x32_bf16 v[54:57], v[216:219], v[192:195], v[54:57]
	v_mfma_f32_16x16x32_bf16 v[50:53], v[236:239], v[192:195], v[50:53]
	v_mfma_f32_16x16x32_bf16 v[46:49], v[216:219], v[200:203], v[46:49]
	v_mfma_f32_16x16x32_bf16 v[42:45], v[236:239], v[200:203], v[42:45]
	v_mfma_f32_16x16x32_bf16 v[38:41], v[216:219], v[208:211], v[38:41]
	v_mfma_f32_16x16x32_bf16 v[34:37], v[236:239], v[208:211], v[34:37]
	s_setprio 0
	s_barrier
	ds_read_b128 v[176:179], v171 offset:49152
	ds_read_b128 v[180:183], v171 offset:50176
	ds_read_b128 v[188:191], v171 offset:51200
	ds_read_b128 v[192:195], v171 offset:52224
	ds_read_b128 v[196:199], v171 offset:53248
	ds_read_b128 v[200:203], v171 offset:54272
	ds_read_b128 v[204:207], v171 offset:55296
	ds_read_b128 v[208:211], v171 offset:56320
	s_mov_b32 m0, s56
	v_lshl_add_u64 v[152:153], v[152:153], 0, s[24:25]
	global_load_lds_dwordx4 v[152:153], off
	v_lshl_add_u64 v[152:153], v[184:185], 0, s[24:25]
	s_mov_b32 m0, s57
	s_nop 0
	global_load_lds_dwordx4 v[152:153], off
	s_mov_b32 m0, s58
	v_lshl_add_u64 v[152:153], v[220:221], 0, s[24:25]
	global_load_lds_dwordx4 v[152:153], off
	v_lshl_add_u64 v[152:153], v[240:241], 0, s[24:25]
	s_mov_b32 m0, s59
	s_nop 0
	global_load_lds_dwordx4 v[152:153], off
	s_barrier
	s_waitcnt lgkmcnt(0)
	s_setprio 1
	s_waitcnt lgkmcnt(0)
	v_mfma_f32_16x16x32_bf16 v[94:97], v[102:105], v[176:179], v[94:97]
	v_mfma_f32_16x16x32_bf16 v[90:93], v[148:151], v[176:179], v[90:93]
	v_mfma_f32_16x16x32_bf16 v[86:89], v[102:105], v[188:191], v[86:89]
	v_mfma_f32_16x16x32_bf16 v[82:85], v[148:151], v[188:191], v[82:85]
	v_mfma_f32_16x16x32_bf16 v[78:81], v[102:105], v[196:199], v[78:81]
	v_mfma_f32_16x16x32_bf16 v[74:77], v[148:151], v[196:199], v[74:77]
	v_mfma_f32_16x16x32_bf16 v[70:73], v[102:105], v[204:207], v[70:73]
	v_mfma_f32_16x16x32_bf16 v[66:69], v[148:151], v[204:207], v[66:69]
	v_mfma_f32_16x16x32_bf16 v[94:97], v[110:113], v[180:183], v[94:97]
	v_mfma_f32_16x16x32_bf16 v[90:93], v[172:175], v[180:183], v[90:93]
	v_mfma_f32_16x16x32_bf16 v[86:89], v[110:113], v[192:195], v[86:89]
	v_mfma_f32_16x16x32_bf16 v[82:85], v[172:175], v[192:195], v[82:85]
	v_mfma_f32_16x16x32_bf16 v[78:81], v[110:113], v[200:203], v[78:81]
	v_mfma_f32_16x16x32_bf16 v[74:77], v[172:175], v[200:203], v[74:77]
	v_mfma_f32_16x16x32_bf16 v[70:73], v[110:113], v[208:211], v[70:73]
	v_mfma_f32_16x16x32_bf16 v[66:69], v[172:175], v[208:211], v[66:69]
	s_setprio 0
	s_barrier
	s_add_u32 s34, s34, 0x80080
	s_addc_u32 s35, s35, 0
	s_mov_b32 m0, s60
	v_lshl_add_u64 v[102:103], s[34:35], 0, v[0:1]
	global_load_lds_dwordx4 v[102:103], off
	v_lshl_add_u64 v[102:103], s[34:35], 0, v[138:139]
	s_mov_b32 m0, s61
	s_nop 0
	global_load_lds_dwordx4 v[102:103], off
	s_waitcnt vmcnt(8)
	s_barrier
	s_setprio 1
	v_mfma_f32_16x16x32_bf16 v[30:33], v[212:215], v[176:179], v[30:33]
	v_mfma_f32_16x16x32_bf16 v[26:29], v[232:235], v[176:179], v[26:29]
	v_mfma_f32_16x16x32_bf16 v[22:25], v[212:215], v[188:191], v[22:25]
	v_mfma_f32_16x16x32_bf16 v[18:21], v[232:235], v[188:191], v[18:21]
	v_mfma_f32_16x16x32_bf16 v[14:17], v[212:215], v[196:199], v[14:17]
	v_mfma_f32_16x16x32_bf16 v[10:13], v[232:235], v[196:199], v[10:13]
	v_mfma_f32_16x16x32_bf16 v[6:9], v[212:215], v[204:207], v[6:9]
	v_mfma_f32_16x16x32_bf16 v[2:5], v[232:235], v[204:207], v[2:5]
	v_mfma_f32_16x16x32_bf16 v[30:33], v[216:219], v[180:183], v[30:33]
	v_mfma_f32_16x16x32_bf16 v[26:29], v[236:239], v[180:183], v[26:29]
	v_mfma_f32_16x16x32_bf16 v[22:25], v[216:219], v[192:195], v[22:25]
	v_mfma_f32_16x16x32_bf16 v[18:21], v[236:239], v[192:195], v[18:21]
	v_mfma_f32_16x16x32_bf16 v[14:17], v[216:219], v[200:203], v[14:17]
	v_mfma_f32_16x16x32_bf16 v[10:13], v[236:239], v[200:203], v[10:13]
	v_mfma_f32_16x16x32_bf16 v[6:9], v[216:219], v[208:211], v[6:9]
	v_mfma_f32_16x16x32_bf16 v[2:5], v[236:239], v[208:211], v[2:5]
	s_setprio 0
	s_add_i32 s71, s71, 2
	s_add_u32 s20, s20, 0x100
	s_addc_u32 s21, s21, 0
	s_add_u32 s69, s69, 0x100
	s_addc_u32 s70, s70, 0
	s_cmp_gt_u32 s71, 29
	s_barrier
	s_cbranch_scc0 .LBB0_1150
	v_mbcnt_lo_u32_b32 v102, -1, 0
	v_mbcnt_hi_u32_b32 v102, -1, v102
	v_readlane_b32 s38, v252, 51
	v_and_b32_e32 v103, 15, v102
	v_readlane_b32 s21, v252, 52
	v_lshrrev_b32_e32 v102, 1, v102
	s_ashr_i32 s20, s64, 4
	v_and_b32_e32 v102, 24, v102
	v_lshl_or_b32 v152, s21, 5, v102
	s_lshl_b32 s34, s20, 8
	s_ashr_i32 s21, s20, 31
	s_lshl_b32 s39, s64, 8
	s_ashr_i32 s35, s34, 31
	s_lshl_b64 s[20:21], s[20:21], 12
	s_and_b32 s39, s39, 0xf00
	s_or_b32 s20, s20, s39
	s_lshl_b64 s[34:35], s[34:35], 2
	s_add_u32 s34, s28, s34
	s_addc_u32 s35, s54, s35
	v_ashrrev_i32_e32 v153, 31, v152
	v_lshl_add_u64 v[150:151], v[152:153], 2, s[34:35]
	v_lshl_or_b32 v148, s38, 6, v103
	global_load_dwordx4 v[102:105], v[150:151], off offset:16
	global_load_dwordx4 v[110:113], v[150:151], off
	s_and_b64 vcc, exec, s[6:7]
	s_mov_b32 s64, s63
	s_mov_b64 s[34:35], s[14:15]
	s_waitcnt vmcnt(0)
	v_pk_add_f32 v[130:131], v[130:131], v[102:103]
	v_pk_add_f32 v[134:135], v[134:135], v[110:111]
	v_pk_add_f32 v[136:137], v[136:137], v[112:113]
	v_mul_f32_e32 v149, 0xbfb8aa3b, v134
	v_exp_f32_e32 v149, v149
	v_pk_add_f32 v[132:133], v[132:133], v[104:105]
	v_pk_add_f32 v[126:127], v[126:127], v[110:111]
	v_pk_add_f32 v[128:129], v[128:129], v[112:113]
	v_add_f32_e32 v149, 1.0, v149
	v_rcp_f32_e32 v172, v149
	v_mul_f32_e32 v149, 0xbfb8aa3b, v130
	v_exp_f32_e32 v149, v149
	v_pk_add_f32 v[124:125], v[124:125], v[104:105]
	v_pk_add_f32 v[114:115], v[114:115], v[102:103]
	v_pk_add_f32 v[118:119], v[118:119], v[110:111]
	v_add_f32_e32 v149, 1.0, v149
	v_rcp_f32_e32 v174, v149
	v_mul_f32_e32 v149, 0xbfb8aa3b, v135
	v_exp_f32_e32 v149, v149
	v_pk_add_f32 v[116:117], v[116:117], v[104:105]
	v_pk_add_f32 v[120:121], v[120:121], v[112:113]
	v_pk_add_f32 v[98:99], v[98:99], v[102:103]
	v_add_f32_e32 v149, 1.0, v149
	v_rcp_f32_e32 v173, v149
	v_mul_f32_e32 v149, 0xbfb8aa3b, v131
	v_exp_f32_e32 v149, v149
	v_pk_add_f32 v[106:107], v[106:107], v[110:111]
	v_pk_mul_f32 v[134:135], v[134:135], v[172:173]
	v_pk_add_f32 v[100:101], v[100:101], v[104:105]
	v_add_f32_e32 v149, 1.0, v149
	v_rcp_f32_e32 v175, v149
	v_mul_f32_e32 v149, 0xbfb8aa3b, v136
	v_exp_f32_e32 v149, v149
	v_cvt_pk_bf16_f32 v134, v134, v135
	v_pk_mul_f32 v[130:131], v[130:131], v[174:175]
	v_pk_add_f32 v[108:109], v[108:109], v[112:113]
	v_add_f32_e32 v149, 1.0, v149
	v_rcp_f32_e32 v172, v149
	v_mul_f32_e32 v149, 0xbfb8aa3b, v132
	v_exp_f32_e32 v149, v149
	v_pk_add_f32 v[94:95], v[94:95], v[110:111]
	v_pk_add_f32 v[90:91], v[90:91], v[102:103]
	v_pk_add_f32 v[96:97], v[96:97], v[112:113]
	v_add_f32_e32 v149, 1.0, v149
	v_rcp_f32_e32 v174, v149
	v_mul_f32_e32 v149, 0xbfb8aa3b, v137
	v_exp_f32_e32 v149, v149
	v_pk_add_f32 v[92:93], v[92:93], v[104:105]
	v_pk_add_f32 v[82:83], v[82:83], v[102:103]
	v_pk_add_f32 v[86:87], v[86:87], v[110:111]
	v_add_f32_e32 v149, 1.0, v149
	v_rcp_f32_e32 v173, v149
	v_mul_f32_e32 v149, 0xbfb8aa3b, v133
	v_exp_f32_e32 v149, v149
	v_pk_add_f32 v[84:85], v[84:85], v[104:105]
	v_pk_mul_f32 v[136:137], v[136:137], v[172:173]
	v_pk_add_f32 v[88:89], v[88:89], v[112:113]
	v_add_f32_e32 v149, 1.0, v149
	v_rcp_f32_e32 v175, v149
	v_ashrrev_i32_e32 v149, 31, v148
	v_cvt_pk_bf16_f32 v135, v136, v137
	v_cvt_pk_bf16_f32 v136, v130, v131
	v_lshl_add_u64 v[130:131], s[20:21], 0, v[148:149]
	v_pk_mul_f32 v[132:133], v[132:133], v[174:175]
	v_lshlrev_b64 v[130:131], 9, v[130:131]
	v_cvt_pk_bf16_f32 v137, v132, v133
	v_lshl_add_u64 v[130:131], s[4:5], 0, v[130:131]
	v_lshlrev_b64 v[132:133], 1, v[152:153]
	v_lshl_add_u64 v[130:131], v[130:131], 0, v[132:133]
	global_store_dwordx4 v[130:131], v[134:137], off
	v_pk_add_f32 v[74:75], v[74:75], v[102:103]
	v_pk_add_f32 v[78:79], v[78:79], v[110:111]
	v_pk_add_f32 v[134:135], v[122:123], v[102:103]
	v_mul_f32_e32 v122, 0xbfb8aa3b, v126
	v_mul_f32_e32 v123, 0xbfb8aa3b, v134
	v_exp_f32_e32 v123, v123
	v_exp_f32_e32 v122, v122
	v_pk_add_f32 v[76:77], v[76:77], v[104:105]
	v_pk_add_f32 v[80:81], v[80:81], v[112:113]
	v_add_f32_e32 v123, 1.0, v123
	v_rcp_f32_e32 v136, v123
	v_mul_f32_e32 v123, 0xbfb8aa3b, v127
	v_exp_f32_e32 v123, v123
	v_add_f32_e32 v122, 1.0, v122
	v_rcp_f32_e32 v122, v122
	v_pk_add_f32 v[66:67], v[66:67], v[102:103]
	v_add_f32_e32 v123, 1.0, v123
	v_rcp_f32_e32 v123, v123
	v_pk_add_f32 v[70:71], v[70:71], v[110:111]
	v_pk_add_f32 v[68:69], v[68:69], v[104:105]
	v_pk_add_f32 v[72:73], v[72:73], v[112:113]
	v_pk_mul_f32 v[122:123], v[126:127], v[122:123]
	v_mul_f32_e32 v126, 0xbfb8aa3b, v135
	v_exp_f32_e32 v126, v126
	s_nop 0
	v_add_f32_e32 v126, 1.0, v126
	v_rcp_f32_e32 v137, v126
	s_nop 0
	v_pk_mul_f32 v[126:127], v[134:135], v[136:137]
	v_mul_f32_e32 v134, 0xbfb8aa3b, v128
	v_mul_f32_e32 v135, 0xbfb8aa3b, v129
	v_exp_f32_e32 v134, v134
	v_exp_f32_e32 v135, v135
	v_cvt_pk_bf16_f32 v126, v126, v127
	v_add_f32_e32 v134, 1.0, v134
	v_add_f32_e32 v135, 1.0, v135
	v_rcp_f32_e32 v136, v134
	v_mul_f32_e32 v134, 0xbfb8aa3b, v124
	v_rcp_f32_e32 v137, v135
	v_mul_f32_e32 v135, 0xbfb8aa3b, v125
	v_exp_f32_e32 v134, v134
	v_exp_f32_e32 v135, v135
	v_pk_mul_f32 v[128:129], v[128:129], v[136:137]
	v_add_f32_e32 v134, 1.0, v134
	v_add_f32_e32 v135, 1.0, v135
	v_rcp_f32_e32 v134, v134
	v_rcp_f32_e32 v135, v135
	s_nop 0
	v_pk_mul_f32 v[134:135], v[124:125], v[134:135]
	v_cvt_pk_bf16_f32 v124, v122, v123
	v_or_b32_e32 v122, 16, v148
	v_ashrrev_i32_e32 v123, 31, v122
	v_lshl_add_u64 v[122:123], s[20:21], 0, v[122:123]
	v_lshlrev_b64 v[122:123], 9, v[122:123]
	v_lshl_add_u64 v[122:123], s[4:5], 0, v[122:123]
	v_cvt_pk_bf16_f32 v125, v128, v129
	v_cvt_pk_bf16_f32 v127, v134, v135
	v_lshl_add_u64 v[122:123], v[122:123], 0, v[132:133]
	global_store_dwordx4 v[122:123], v[124:127], off
	s_nop 1
	v_mul_f32_e32 v125, 0xbfb8aa3b, v114
	v_exp_f32_e32 v125, v125
	v_mul_f32_e32 v124, 0xbfb8aa3b, v118
	v_exp_f32_e32 v124, v124
	v_add_f32_e32 v125, 1.0, v125
	v_rcp_f32_e32 v126, v125
	v_mul_f32_e32 v125, 0xbfb8aa3b, v119
	v_exp_f32_e32 v125, v125
	v_add_f32_e32 v124, 1.0, v124
	v_rcp_f32_e32 v124, v124
	v_add_f32_e32 v125, 1.0, v125
	v_rcp_f32_e32 v125, v125
	s_nop 0
	v_pk_mul_f32 v[118:119], v[118:119], v[124:125]
	v_mul_f32_e32 v124, 0xbfb8aa3b, v115
	v_exp_f32_e32 v124, v124
	v_mul_f32_e32 v125, 0xbfb8aa3b, v116
	v_exp_f32_e32 v125, v125
	v_add_f32_e32 v124, 1.0, v124
	v_rcp_f32_e32 v127, v124
	v_add_f32_e32 v125, 1.0, v125
	v_mul_f32_e32 v124, 0xbfb8aa3b, v120
	v_exp_f32_e32 v124, v124
	v_pk_mul_f32 v[114:115], v[114:115], v[126:127]
	v_rcp_f32_e32 v126, v125
	v_mul_f32_e32 v125, 0xbfb8aa3b, v121
	v_exp_f32_e32 v125, v125
	v_add_f32_e32 v124, 1.0, v124
	v_rcp_f32_e32 v124, v124
	v_add_f32_e32 v125, 1.0, v125
	v_rcp_f32_e32 v125, v125
	s_nop 0
	v_pk_mul_f32 v[120:121], v[120:121], v[124:125]
	v_mul_f32_e32 v124, 0xbfb8aa3b, v117
	v_exp_f32_e32 v124, v124
	s_nop 0
	v_add_f32_e32 v124, 1.0, v124
	v_rcp_f32_e32 v127, v124
	s_nop 0
	v_pk_mul_f32 v[124:125], v[116:117], v[126:127]
	v_cvt_pk_bf16_f32 v116, v118, v119
	v_cvt_pk_bf16_f32 v118, v114, v115
	v_or_b32_e32 v114, 32, v148
	v_ashrrev_i32_e32 v115, 31, v114
	v_lshl_add_u64 v[114:115], s[20:21], 0, v[114:115]
	v_lshlrev_b64 v[114:115], 9, v[114:115]
	v_lshl_add_u64 v[114:115], s[4:5], 0, v[114:115]
	v_cvt_pk_bf16_f32 v117, v120, v121
	v_cvt_pk_bf16_f32 v119, v124, v125
	v_lshl_add_u64 v[114:115], v[114:115], 0, v[132:133]
	global_store_dwordx4 v[114:115], v[116:119], off
	s_nop 1
	v_mul_f32_e32 v117, 0xbfb8aa3b, v98
	v_exp_f32_e32 v117, v117
	v_mul_f32_e32 v116, 0xbfb8aa3b, v106
	v_exp_f32_e32 v116, v116
	v_add_f32_e32 v117, 1.0, v117
	v_rcp_f32_e32 v118, v117
	v_mul_f32_e32 v117, 0xbfb8aa3b, v107
	v_exp_f32_e32 v117, v117
	v_add_f32_e32 v116, 1.0, v116
	v_rcp_f32_e32 v116, v116
	v_add_f32_e32 v117, 1.0, v117
	v_rcp_f32_e32 v117, v117
	s_nop 0
	v_pk_mul_f32 v[106:107], v[106:107], v[116:117]
	v_mul_f32_e32 v116, 0xbfb8aa3b, v99
	v_exp_f32_e32 v116, v116
	v_mul_f32_e32 v117, 0xbfb8aa3b, v100
	v_exp_f32_e32 v117, v117
	v_cvt_pk_bf16_f32 v106, v106, v107
	v_add_f32_e32 v116, 1.0, v116
	v_rcp_f32_e32 v119, v116
	v_add_f32_e32 v117, 1.0, v117
	v_mul_f32_e32 v116, 0xbfb8aa3b, v108
	v_exp_f32_e32 v116, v116
	v_pk_mul_f32 v[98:99], v[98:99], v[118:119]
	v_rcp_f32_e32 v118, v117
	v_mul_f32_e32 v117, 0xbfb8aa3b, v109
	v_exp_f32_e32 v117, v117
	v_add_f32_e32 v116, 1.0, v116
	v_rcp_f32_e32 v116, v116
	v_add_f32_e32 v117, 1.0, v117
	v_rcp_f32_e32 v117, v117
	s_nop 0
	v_pk_mul_f32 v[108:109], v[108:109], v[116:117]
	v_mul_f32_e32 v116, 0xbfb8aa3b, v101
	v_exp_f32_e32 v116, v116
	v_cvt_pk_bf16_f32 v107, v108, v109
	v_cvt_pk_bf16_f32 v108, v98, v99
	v_or_b32_e32 v98, 48, v148
	v_add_f32_e32 v116, 1.0, v116
	v_rcp_f32_e32 v119, v116
	v_ashrrev_i32_e32 v99, 31, v98
	v_lshl_add_u64 v[98:99], s[20:21], 0, v[98:99]
	v_lshlrev_b64 v[98:99], 9, v[98:99]
	v_pk_mul_f32 v[100:101], v[100:101], v[118:119]
	v_lshl_add_u64 v[98:99], s[4:5], 0, v[98:99]
	v_cvt_pk_bf16_f32 v109, v100, v101
	v_mul_f32_e32 v101, 0xbfb8aa3b, v94
	v_exp_f32_e32 v101, v101
	v_lshl_add_u64 v[98:99], v[98:99], 0, v[132:133]
	global_store_dwordx4 v[98:99], v[106:109], off
	v_add_u32_e32 v100, 0x80, v148
	v_add_f32_e32 v101, 1.0, v101
	v_rcp_f32_e32 v106, v101
	v_mul_f32_e32 v101, 0xbfb8aa3b, v90
	v_exp_f32_e32 v101, v101
	s_nop 0
	v_add_f32_e32 v101, 1.0, v101
	v_rcp_f32_e32 v108, v101
	v_mul_f32_e32 v101, 0xbfb8aa3b, v95
	v_exp_f32_e32 v101, v101
	s_nop 0
	v_add_f32_e32 v101, 1.0, v101
	v_rcp_f32_e32 v107, v101
	v_mul_f32_e32 v101, 0xbfb8aa3b, v91
	v_exp_f32_e32 v101, v101
	v_pk_mul_f32 v[94:95], v[94:95], v[106:107]
	v_add_f32_e32 v101, 1.0, v101
	v_rcp_f32_e32 v109, v101
	v_mul_f32_e32 v101, 0xbfb8aa3b, v96
	v_exp_f32_e32 v101, v101
	v_pk_mul_f32 v[90:91], v[90:91], v[108:109]
	v_add_f32_e32 v101, 1.0, v101
	v_rcp_f32_e32 v106, v101
	v_mul_f32_e32 v101, 0xbfb8aa3b, v92
	v_exp_f32_e32 v101, v101
	s_nop 0
	v_add_f32_e32 v101, 1.0, v101
	v_rcp_f32_e32 v108, v101
	v_mul_f32_e32 v101, 0xbfb8aa3b, v97
	v_exp_f32_e32 v101, v101
	s_nop 0
	v_add_f32_e32 v101, 1.0, v101
	v_rcp_f32_e32 v107, v101
	v_mul_f32_e32 v101, 0xbfb8aa3b, v93
	v_exp_f32_e32 v101, v101
	v_pk_mul_f32 v[96:97], v[96:97], v[106:107]
	v_add_f32_e32 v101, 1.0, v101
	v_rcp_f32_e32 v109, v101
	v_ashrrev_i32_e32 v101, 31, v100
	v_pk_mul_f32 v[106:107], v[92:93], v[108:109]
	v_cvt_pk_bf16_f32 v92, v94, v95
	v_cvt_pk_bf16_f32 v94, v90, v91
	v_lshl_add_u64 v[90:91], s[20:21], 0, v[100:101]
	v_lshlrev_b64 v[90:91], 9, v[90:91]
	v_lshl_add_u64 v[90:91], s[4:5], 0, v[90:91]
	v_cvt_pk_bf16_f32 v93, v96, v97
	v_cvt_pk_bf16_f32 v95, v106, v107
	v_lshl_add_u64 v[90:91], v[90:91], 0, v[132:133]
	global_store_dwordx4 v[90:91], v[92:95], off
	s_nop 1
	v_mul_f32_e32 v93, 0xbfb8aa3b, v82
	v_exp_f32_e32 v93, v93
	v_mul_f32_e32 v92, 0xbfb8aa3b, v86
	v_exp_f32_e32 v92, v92
	v_add_f32_e32 v93, 1.0, v93
	v_rcp_f32_e32 v94, v93
	v_mul_f32_e32 v93, 0xbfb8aa3b, v87
	v_exp_f32_e32 v93, v93
	v_add_f32_e32 v92, 1.0, v92
	v_rcp_f32_e32 v92, v92
	v_add_f32_e32 v93, 1.0, v93
	v_rcp_f32_e32 v93, v93
	s_nop 0
	v_pk_mul_f32 v[86:87], v[86:87], v[92:93]
	v_mul_f32_e32 v92, 0xbfb8aa3b, v83
	v_exp_f32_e32 v92, v92
	v_mul_f32_e32 v93, 0xbfb8aa3b, v84
	v_exp_f32_e32 v93, v93
	v_add_f32_e32 v92, 1.0, v92
	v_rcp_f32_e32 v95, v92
	v_add_f32_e32 v93, 1.0, v93
	v_mul_f32_e32 v92, 0xbfb8aa3b, v88
	v_exp_f32_e32 v92, v92
	v_pk_mul_f32 v[82:83], v[82:83], v[94:95]
	v_rcp_f32_e32 v94, v93
	v_mul_f32_e32 v93, 0xbfb8aa3b, v89
	v_exp_f32_e32 v93, v93
	v_add_f32_e32 v92, 1.0, v92
	v_rcp_f32_e32 v92, v92
	v_add_f32_e32 v93, 1.0, v93
	v_rcp_f32_e32 v93, v93
	s_nop 0
	v_pk_mul_f32 v[88:89], v[88:89], v[92:93]
	v_mul_f32_e32 v92, 0xbfb8aa3b, v85
	v_exp_f32_e32 v92, v92
	s_nop 0
	v_add_f32_e32 v92, 1.0, v92
	v_rcp_f32_e32 v95, v92
	s_nop 0
	v_pk_mul_f32 v[92:93], v[84:85], v[94:95]
	v_cvt_pk_bf16_f32 v84, v86, v87
	v_cvt_pk_bf16_f32 v86, v82, v83
	v_add_u32_e32 v82, 0x90, v148
	v_ashrrev_i32_e32 v83, 31, v82
	v_lshl_add_u64 v[82:83], s[20:21], 0, v[82:83]
	v_lshlrev_b64 v[82:83], 9, v[82:83]
	v_lshl_add_u64 v[82:83], s[4:5], 0, v[82:83]
	v_cvt_pk_bf16_f32 v85, v88, v89
	v_cvt_pk_bf16_f32 v87, v92, v93
	v_lshl_add_u64 v[82:83], v[82:83], 0, v[132:133]
	global_store_dwordx4 v[82:83], v[84:87], off
	s_nop 1
	v_mul_f32_e32 v85, 0xbfb8aa3b, v74
	v_exp_f32_e32 v85, v85
	v_mul_f32_e32 v84, 0xbfb8aa3b, v78
	v_exp_f32_e32 v84, v84
	v_add_f32_e32 v85, 1.0, v85
	v_rcp_f32_e32 v86, v85
	v_mul_f32_e32 v85, 0xbfb8aa3b, v79
	v_exp_f32_e32 v85, v85
	v_add_f32_e32 v84, 1.0, v84
	v_rcp_f32_e32 v84, v84
	v_add_f32_e32 v85, 1.0, v85
	v_rcp_f32_e32 v85, v85
	s_nop 0
	v_pk_mul_f32 v[78:79], v[78:79], v[84:85]
	v_mul_f32_e32 v84, 0xbfb8aa3b, v75
	v_exp_f32_e32 v84, v84
	v_mul_f32_e32 v85, 0xbfb8aa3b, v76
	v_exp_f32_e32 v85, v85
	v_add_f32_e32 v84, 1.0, v84
	v_rcp_f32_e32 v87, v84
	v_add_f32_e32 v85, 1.0, v85
	v_mul_f32_e32 v84, 0xbfb8aa3b, v80
	v_exp_f32_e32 v84, v84
	v_pk_mul_f32 v[74:75], v[74:75], v[86:87]
	v_rcp_f32_e32 v86, v85
	v_mul_f32_e32 v85, 0xbfb8aa3b, v81
	v_exp_f32_e32 v85, v85
	v_add_f32_e32 v84, 1.0, v84
	v_rcp_f32_e32 v84, v84
	v_add_f32_e32 v85, 1.0, v85
	v_rcp_f32_e32 v85, v85
	s_nop 0
	v_pk_mul_f32 v[80:81], v[80:81], v[84:85]
	v_mul_f32_e32 v84, 0xbfb8aa3b, v77
	v_exp_f32_e32 v84, v84
	s_nop 0
	v_add_f32_e32 v84, 1.0, v84
	v_rcp_f32_e32 v87, v84
	s_nop 0
	v_pk_mul_f32 v[84:85], v[76:77], v[86:87]
	v_cvt_pk_bf16_f32 v76, v78, v79
	v_cvt_pk_bf16_f32 v78, v74, v75
	v_add_u32_e32 v74, 0xa0, v148
	v_ashrrev_i32_e32 v75, 31, v74
	v_lshl_add_u64 v[74:75], s[20:21], 0, v[74:75]
	v_lshlrev_b64 v[74:75], 9, v[74:75]
	v_lshl_add_u64 v[74:75], s[4:5], 0, v[74:75]
	v_cvt_pk_bf16_f32 v77, v80, v81
	v_cvt_pk_bf16_f32 v79, v84, v85
	v_lshl_add_u64 v[74:75], v[74:75], 0, v[132:133]
	global_store_dwordx4 v[74:75], v[76:79], off
	s_nop 1
	v_mul_f32_e32 v77, 0xbfb8aa3b, v66
	v_exp_f32_e32 v77, v77
	v_mul_f32_e32 v76, 0xbfb8aa3b, v70
	v_exp_f32_e32 v76, v76
	v_add_f32_e32 v77, 1.0, v77
	v_rcp_f32_e32 v78, v77
	v_mul_f32_e32 v77, 0xbfb8aa3b, v71
	v_exp_f32_e32 v77, v77
	v_add_f32_e32 v76, 1.0, v76
	v_rcp_f32_e32 v76, v76
	v_add_f32_e32 v77, 1.0, v77
	v_rcp_f32_e32 v77, v77
	s_nop 0
	v_pk_mul_f32 v[70:71], v[70:71], v[76:77]
	v_mul_f32_e32 v76, 0xbfb8aa3b, v67
	v_exp_f32_e32 v76, v76
	s_nop 0
	v_add_f32_e32 v76, 1.0, v76
	v_rcp_f32_e32 v79, v76
	s_nop 0
	v_pk_mul_f32 v[76:77], v[66:67], v[78:79]
	v_mul_f32_e32 v67, 0xbfb8aa3b, v68
	v_exp_f32_e32 v67, v67
	v_mul_f32_e32 v66, 0xbfb8aa3b, v72
	v_exp_f32_e32 v66, v66
	v_add_f32_e32 v67, 1.0, v67
	v_rcp_f32_e32 v78, v67
	v_mul_f32_e32 v67, 0xbfb8aa3b, v73
	v_exp_f32_e32 v67, v67
	v_add_f32_e32 v66, 1.0, v66
	v_rcp_f32_e32 v66, v66
	v_add_f32_e32 v67, 1.0, v67
	v_rcp_f32_e32 v67, v67
	s_nop 0
	v_pk_mul_f32 v[72:73], v[72:73], v[66:67]
	v_mul_f32_e32 v66, 0xbfb8aa3b, v69
	v_exp_f32_e32 v66, v66
	v_cvt_pk_bf16_f32 v67, v72, v73
	v_add_f32_e32 v66, 1.0, v66
	v_rcp_f32_e32 v79, v66
	v_cvt_pk_bf16_f32 v66, v70, v71
	v_add_u32_e32 v70, 0xb0, v148
	v_ashrrev_i32_e32 v71, 31, v70
	v_lshl_add_u64 v[70:71], s[20:21], 0, v[70:71]
	v_lshlrev_b64 v[70:71], 9, v[70:71]
	v_pk_mul_f32 v[78:79], v[68:69], v[78:79]
	v_lshl_add_u64 v[70:71], s[4:5], 0, v[70:71]
	v_cvt_pk_bf16_f32 v68, v76, v77
	v_cvt_pk_bf16_f32 v69, v78, v79
	v_lshl_add_u64 v[76:77], v[70:71], 0, v[132:133]
	global_store_dwordx4 v[76:77], v[66:69], off
	global_load_dwordx4 v[66:69], v[150:151], off offset:528
	s_nop 0
	global_load_dwordx4 v[70:73], v[150:151], off offset:512
	s_mov_b64 s[20:21], s[12:13]
	s_waitcnt vmcnt(0)
	v_pk_add_f32 v[58:59], v[58:59], v[66:67]
	s_nop 0
	v_mul_f32_e32 v79, 0xbfb8aa3b, v58
	v_exp_f32_e32 v79, v79
	v_pk_add_f32 v[62:63], v[62:63], v[70:71]
	v_pk_add_f32 v[60:61], v[60:61], v[68:69]
	v_mul_f32_e32 v78, 0xbfb8aa3b, v62
	v_add_f32_e32 v79, 1.0, v79
	v_rcp_f32_e32 v80, v79
	v_mul_f32_e32 v79, 0xbfb8aa3b, v63
	v_exp_f32_e32 v78, v78
	v_exp_f32_e32 v79, v79
	v_pk_add_f32 v[64:65], v[64:65], v[72:73]
	v_pk_add_f32 v[50:51], v[50:51], v[66:67]
	v_add_f32_e32 v78, 1.0, v78
	v_add_f32_e32 v79, 1.0, v79
	v_rcp_f32_e32 v78, v78
	v_rcp_f32_e32 v79, v79
	v_pk_add_f32 v[54:55], v[54:55], v[70:71]
	v_pk_add_f32 v[52:53], v[52:53], v[68:69]
	v_pk_add_f32 v[56:57], v[56:57], v[72:73]
	v_pk_mul_f32 v[62:63], v[62:63], v[78:79]
	v_mul_f32_e32 v78, 0xbfb8aa3b, v59
	v_exp_f32_e32 v78, v78
	v_pk_add_f32 v[42:43], v[42:43], v[66:67]
	v_pk_add_f32 v[46:47], v[46:47], v[70:71]
	v_pk_add_f32 v[44:45], v[44:45], v[68:69]
	v_add_f32_e32 v78, 1.0, v78
	v_rcp_f32_e32 v81, v78
	v_pk_add_f32 v[48:49], v[48:49], v[72:73]
	v_pk_add_f32 v[34:35], v[34:35], v[66:67]
	v_pk_add_f32 v[38:39], v[38:39], v[70:71]
	v_pk_mul_f32 v[78:79], v[58:59], v[80:81]
	v_mul_f32_e32 v59, 0xbfb8aa3b, v60
	v_exp_f32_e32 v59, v59
	v_mul_f32_e32 v58, 0xbfb8aa3b, v64
	v_exp_f32_e32 v58, v58
	v_pk_add_f32 v[36:37], v[36:37], v[68:69]
	v_add_f32_e32 v59, 1.0, v59
	v_rcp_f32_e32 v80, v59
	v_mul_f32_e32 v59, 0xbfb8aa3b, v65
	v_exp_f32_e32 v59, v59
	v_add_f32_e32 v58, 1.0, v58
	v_rcp_f32_e32 v58, v58
	v_pk_add_f32 v[40:41], v[40:41], v[72:73]
	v_add_f32_e32 v59, 1.0, v59
	v_rcp_f32_e32 v59, v59
	v_pk_add_f32 v[26:27], v[26:27], v[66:67]
	v_pk_add_f32 v[30:31], v[30:31], v[70:71]
	v_pk_add_f32 v[28:29], v[28:29], v[68:69]
	v_pk_mul_f32 v[64:65], v[64:65], v[58:59]
	v_mul_f32_e32 v58, 0xbfb8aa3b, v61
	v_exp_f32_e32 v58, v58
	v_cvt_pk_bf16_f32 v59, v64, v65
	v_pk_add_f32 v[32:33], v[32:33], v[72:73]
	v_pk_add_f32 v[18:19], v[18:19], v[66:67]
	v_add_f32_e32 v58, 1.0, v58
	v_rcp_f32_e32 v81, v58
	v_cvt_pk_bf16_f32 v58, v62, v63
	v_pk_add_f32 v[22:23], v[22:23], v[70:71]
	v_pk_add_f32 v[20:21], v[20:21], v[68:69]
	v_pk_mul_f32 v[80:81], v[60:61], v[80:81]
	v_cvt_pk_bf16_f32 v60, v78, v79
	v_cvt_pk_bf16_f32 v61, v80, v81
	global_store_dwordx4 v[130:131], v[58:61], off offset:256
	v_pk_add_f32 v[24:25], v[24:25], v[72:73]
	v_pk_add_f32 v[10:11], v[10:11], v[66:67]
	v_mul_f32_e32 v59, 0xbfb8aa3b, v50
	v_exp_f32_e32 v59, v59
	v_mul_f32_e32 v58, 0xbfb8aa3b, v54
	v_exp_f32_e32 v58, v58
	v_pk_add_f32 v[14:15], v[14:15], v[70:71]
	v_add_f32_e32 v59, 1.0, v59
	v_rcp_f32_e32 v60, v59
	v_mul_f32_e32 v59, 0xbfb8aa3b, v55
	v_exp_f32_e32 v59, v59
	v_add_f32_e32 v58, 1.0, v58
	v_rcp_f32_e32 v58, v58
	v_pk_add_f32 v[12:13], v[12:13], v[68:69]
	v_add_f32_e32 v59, 1.0, v59
	v_rcp_f32_e32 v59, v59
	v_pk_add_f32 v[16:17], v[16:17], v[72:73]
	v_pk_add_f32 v[2:3], v[2:3], v[66:67]
	v_pk_add_f32 v[6:7], v[6:7], v[70:71]
	v_pk_mul_f32 v[54:55], v[54:55], v[58:59]
	v_mul_f32_e32 v58, 0xbfb8aa3b, v51
	v_exp_f32_e32 v58, v58
	v_pk_add_f32 v[4:5], v[4:5], v[68:69]
	v_pk_add_f32 v[8:9], v[8:9], v[72:73]
	v_add_f32_e32 v58, 1.0, v58
	v_rcp_f32_e32 v61, v58
	s_nop 0
	v_pk_mul_f32 v[58:59], v[50:51], v[60:61]
	v_mul_f32_e32 v51, 0xbfb8aa3b, v52
	v_exp_f32_e32 v51, v51
	v_mul_f32_e32 v50, 0xbfb8aa3b, v56
	v_exp_f32_e32 v50, v50
	v_add_f32_e32 v51, 1.0, v51
	v_rcp_f32_e32 v60, v51
	v_mul_f32_e32 v51, 0xbfb8aa3b, v57
	v_exp_f32_e32 v51, v51
	v_add_f32_e32 v50, 1.0, v50
	v_rcp_f32_e32 v50, v50
	v_add_f32_e32 v51, 1.0, v51
	v_rcp_f32_e32 v51, v51
	s_nop 0
	v_pk_mul_f32 v[56:57], v[56:57], v[50:51]
	v_mul_f32_e32 v50, 0xbfb8aa3b, v53
	v_exp_f32_e32 v50, v50
	v_cvt_pk_bf16_f32 v51, v56, v57
	v_add_f32_e32 v50, 1.0, v50
	v_rcp_f32_e32 v61, v50
	v_cvt_pk_bf16_f32 v50, v54, v55
	v_pk_mul_f32 v[60:61], v[52:53], v[60:61]
	v_cvt_pk_bf16_f32 v52, v58, v59
	v_cvt_pk_bf16_f32 v53, v60, v61
	global_store_dwordx4 v[122:123], v[50:53], off offset:256
	s_nop 1
	v_mul_f32_e32 v51, 0xbfb8aa3b, v42
	v_exp_f32_e32 v51, v51
	v_mul_f32_e32 v50, 0xbfb8aa3b, v46
	v_exp_f32_e32 v50, v50
	v_add_f32_e32 v51, 1.0, v51
	v_rcp_f32_e32 v52, v51
	v_mul_f32_e32 v51, 0xbfb8aa3b, v47
	v_exp_f32_e32 v51, v51
	v_add_f32_e32 v50, 1.0, v50
	v_rcp_f32_e32 v50, v50
	v_add_f32_e32 v51, 1.0, v51
	v_rcp_f32_e32 v51, v51
	s_nop 0
	v_pk_mul_f32 v[46:47], v[46:47], v[50:51]
	v_mul_f32_e32 v50, 0xbfb8aa3b, v43
	v_exp_f32_e32 v50, v50
	s_nop 0
	v_add_f32_e32 v50, 1.0, v50
	v_rcp_f32_e32 v53, v50
	s_nop 0
	v_pk_mul_f32 v[50:51], v[42:43], v[52:53]
	v_mul_f32_e32 v43, 0xbfb8aa3b, v44
	v_exp_f32_e32 v43, v43
	v_mul_f32_e32 v42, 0xbfb8aa3b, v48
	v_exp_f32_e32 v42, v42
	v_add_f32_e32 v43, 1.0, v43
	v_rcp_f32_e32 v52, v43
	v_mul_f32_e32 v43, 0xbfb8aa3b, v49
	v_exp_f32_e32 v43, v43
	v_add_f32_e32 v42, 1.0, v42
	v_rcp_f32_e32 v42, v42
	v_add_f32_e32 v43, 1.0, v43
	v_rcp_f32_e32 v43, v43
	s_nop 0
	v_pk_mul_f32 v[48:49], v[48:49], v[42:43]
	v_mul_f32_e32 v42, 0xbfb8aa3b, v45
	v_exp_f32_e32 v42, v42
	v_cvt_pk_bf16_f32 v43, v48, v49
	v_add_f32_e32 v42, 1.0, v42
	v_rcp_f32_e32 v53, v42
	v_cvt_pk_bf16_f32 v42, v46, v47
	v_pk_mul_f32 v[52:53], v[44:45], v[52:53]
	v_cvt_pk_bf16_f32 v44, v50, v51
	v_cvt_pk_bf16_f32 v45, v52, v53
	global_store_dwordx4 v[114:115], v[42:45], off offset:256
	s_nop 1
	v_mul_f32_e32 v43, 0xbfb8aa3b, v34
	v_exp_f32_e32 v43, v43
	v_mul_f32_e32 v42, 0xbfb8aa3b, v38
	v_exp_f32_e32 v42, v42
	v_add_f32_e32 v43, 1.0, v43
	v_rcp_f32_e32 v44, v43
	v_mul_f32_e32 v43, 0xbfb8aa3b, v39
	v_exp_f32_e32 v43, v43
	v_add_f32_e32 v42, 1.0, v42
	v_rcp_f32_e32 v42, v42
	v_add_f32_e32 v43, 1.0, v43
	v_rcp_f32_e32 v43, v43
	s_nop 0
	v_pk_mul_f32 v[38:39], v[38:39], v[42:43]
	v_mul_f32_e32 v42, 0xbfb8aa3b, v35
	v_exp_f32_e32 v42, v42
	s_nop 0
	v_add_f32_e32 v42, 1.0, v42
	v_rcp_f32_e32 v45, v42
	s_nop 0
	v_pk_mul_f32 v[42:43], v[34:35], v[44:45]
	v_mul_f32_e32 v35, 0xbfb8aa3b, v36
	v_exp_f32_e32 v35, v35
	v_mul_f32_e32 v34, 0xbfb8aa3b, v40
	v_exp_f32_e32 v34, v34
	v_add_f32_e32 v35, 1.0, v35
	v_rcp_f32_e32 v44, v35
	v_mul_f32_e32 v35, 0xbfb8aa3b, v41
	v_exp_f32_e32 v35, v35
	v_add_f32_e32 v34, 1.0, v34
	v_rcp_f32_e32 v34, v34
	v_add_f32_e32 v35, 1.0, v35
	v_rcp_f32_e32 v35, v35
	s_nop 0
	v_pk_mul_f32 v[40:41], v[40:41], v[34:35]
	v_mul_f32_e32 v34, 0xbfb8aa3b, v37
	v_exp_f32_e32 v34, v34
	v_cvt_pk_bf16_f32 v35, v40, v41
	v_add_f32_e32 v34, 1.0, v34
	v_rcp_f32_e32 v45, v34
	v_cvt_pk_bf16_f32 v34, v38, v39
	v_pk_mul_f32 v[44:45], v[36:37], v[44:45]
	v_cvt_pk_bf16_f32 v36, v42, v43
	v_cvt_pk_bf16_f32 v37, v44, v45
	global_store_dwordx4 v[98:99], v[34:37], off offset:256
	s_nop 1
	v_mul_f32_e32 v35, 0xbfb8aa3b, v26
	v_exp_f32_e32 v35, v35
	v_mul_f32_e32 v34, 0xbfb8aa3b, v30
	v_exp_f32_e32 v34, v34
	v_add_f32_e32 v35, 1.0, v35
	v_rcp_f32_e32 v36, v35
	v_mul_f32_e32 v35, 0xbfb8aa3b, v31
	v_exp_f32_e32 v35, v35
	v_add_f32_e32 v34, 1.0, v34
	v_rcp_f32_e32 v34, v34
	v_add_f32_e32 v35, 1.0, v35
	v_rcp_f32_e32 v35, v35
	s_nop 0
	v_pk_mul_f32 v[30:31], v[30:31], v[34:35]
	v_mul_f32_e32 v34, 0xbfb8aa3b, v27
	v_exp_f32_e32 v34, v34
	s_nop 0
	v_add_f32_e32 v34, 1.0, v34
	v_rcp_f32_e32 v37, v34
	s_nop 0
	v_pk_mul_f32 v[34:35], v[26:27], v[36:37]
	v_mul_f32_e32 v27, 0xbfb8aa3b, v28
	v_exp_f32_e32 v27, v27
	v_mul_f32_e32 v26, 0xbfb8aa3b, v32
	v_exp_f32_e32 v26, v26
	v_add_f32_e32 v27, 1.0, v27
	v_rcp_f32_e32 v36, v27
	v_mul_f32_e32 v27, 0xbfb8aa3b, v33
	v_exp_f32_e32 v27, v27
	v_add_f32_e32 v26, 1.0, v26
	v_rcp_f32_e32 v26, v26
	v_add_f32_e32 v27, 1.0, v27
	v_rcp_f32_e32 v27, v27
	s_nop 0
	v_pk_mul_f32 v[32:33], v[32:33], v[26:27]
	v_mul_f32_e32 v26, 0xbfb8aa3b, v29
	v_exp_f32_e32 v26, v26
	v_cvt_pk_bf16_f32 v27, v32, v33
	v_add_f32_e32 v26, 1.0, v26
	v_rcp_f32_e32 v37, v26
	v_cvt_pk_bf16_f32 v26, v30, v31
	v_pk_mul_f32 v[36:37], v[28:29], v[36:37]
	v_cvt_pk_bf16_f32 v28, v34, v35
	v_cvt_pk_bf16_f32 v29, v36, v37
	global_store_dwordx4 v[90:91], v[26:29], off offset:256
	s_nop 1
	v_mul_f32_e32 v27, 0xbfb8aa3b, v18
	v_exp_f32_e32 v27, v27
	v_mul_f32_e32 v26, 0xbfb8aa3b, v22
	v_exp_f32_e32 v26, v26
	v_add_f32_e32 v27, 1.0, v27
	v_rcp_f32_e32 v28, v27
	v_mul_f32_e32 v27, 0xbfb8aa3b, v23
	v_exp_f32_e32 v27, v27
	v_add_f32_e32 v26, 1.0, v26
	v_rcp_f32_e32 v26, v26
	v_add_f32_e32 v27, 1.0, v27
	v_rcp_f32_e32 v27, v27
	s_nop 0
	v_pk_mul_f32 v[22:23], v[22:23], v[26:27]
	v_mul_f32_e32 v26, 0xbfb8aa3b, v19
	v_exp_f32_e32 v26, v26
	s_nop 0
	v_add_f32_e32 v26, 1.0, v26
	v_rcp_f32_e32 v29, v26
	s_nop 0
	v_pk_mul_f32 v[26:27], v[18:19], v[28:29]
	v_mul_f32_e32 v19, 0xbfb8aa3b, v20
	v_exp_f32_e32 v19, v19
	v_mul_f32_e32 v18, 0xbfb8aa3b, v24
	v_exp_f32_e32 v18, v18
	v_add_f32_e32 v19, 1.0, v19
	v_rcp_f32_e32 v28, v19
	v_mul_f32_e32 v19, 0xbfb8aa3b, v25
	v_exp_f32_e32 v19, v19
	v_add_f32_e32 v18, 1.0, v18
	v_rcp_f32_e32 v18, v18
	v_add_f32_e32 v19, 1.0, v19
	v_rcp_f32_e32 v19, v19
	s_nop 0
	v_pk_mul_f32 v[24:25], v[24:25], v[18:19]
	v_mul_f32_e32 v18, 0xbfb8aa3b, v21
	v_exp_f32_e32 v18, v18
	v_cvt_pk_bf16_f32 v19, v24, v25
	v_add_f32_e32 v18, 1.0, v18
	v_rcp_f32_e32 v29, v18
	v_cvt_pk_bf16_f32 v18, v22, v23
	v_pk_mul_f32 v[28:29], v[20:21], v[28:29]
	v_cvt_pk_bf16_f32 v20, v26, v27
	v_cvt_pk_bf16_f32 v21, v28, v29
	global_store_dwordx4 v[82:83], v[18:21], off offset:256
	s_nop 1
	v_mul_f32_e32 v19, 0xbfb8aa3b, v10
	v_exp_f32_e32 v19, v19
	v_mul_f32_e32 v18, 0xbfb8aa3b, v14
	v_exp_f32_e32 v18, v18
	v_add_f32_e32 v19, 1.0, v19
	v_rcp_f32_e32 v20, v19
	v_mul_f32_e32 v19, 0xbfb8aa3b, v15
	v_exp_f32_e32 v19, v19
	v_add_f32_e32 v18, 1.0, v18
	v_rcp_f32_e32 v18, v18
	v_add_f32_e32 v19, 1.0, v19
	v_rcp_f32_e32 v19, v19
	s_nop 0
	v_pk_mul_f32 v[14:15], v[14:15], v[18:19]
	v_mul_f32_e32 v18, 0xbfb8aa3b, v11
	v_exp_f32_e32 v18, v18
	s_nop 0
	v_add_f32_e32 v18, 1.0, v18
	v_rcp_f32_e32 v21, v18
	s_nop 0
	v_pk_mul_f32 v[18:19], v[10:11], v[20:21]
	v_mul_f32_e32 v11, 0xbfb8aa3b, v12
	v_exp_f32_e32 v11, v11
	v_mul_f32_e32 v10, 0xbfb8aa3b, v16
	v_exp_f32_e32 v10, v10
	v_add_f32_e32 v11, 1.0, v11
	v_rcp_f32_e32 v20, v11
	v_mul_f32_e32 v11, 0xbfb8aa3b, v17
	v_exp_f32_e32 v11, v11
	v_add_f32_e32 v10, 1.0, v10
	v_rcp_f32_e32 v10, v10
	v_add_f32_e32 v11, 1.0, v11
	v_rcp_f32_e32 v11, v11
	s_nop 0
	v_pk_mul_f32 v[16:17], v[16:17], v[10:11]
	v_mul_f32_e32 v10, 0xbfb8aa3b, v13
	v_exp_f32_e32 v10, v10
	v_cvt_pk_bf16_f32 v11, v16, v17
	v_add_f32_e32 v10, 1.0, v10
	v_rcp_f32_e32 v21, v10
	v_cvt_pk_bf16_f32 v10, v14, v15
	v_pk_mul_f32 v[20:21], v[12:13], v[20:21]
	v_cvt_pk_bf16_f32 v12, v18, v19
	v_cvt_pk_bf16_f32 v13, v20, v21
	global_store_dwordx4 v[74:75], v[10:13], off offset:256
	s_nop 1
	v_mul_f32_e32 v11, 0xbfb8aa3b, v2
	v_exp_f32_e32 v11, v11
	v_mul_f32_e32 v10, 0xbfb8aa3b, v6
	v_exp_f32_e32 v10, v10
	v_add_f32_e32 v11, 1.0, v11
	v_rcp_f32_e32 v12, v11
	v_mul_f32_e32 v11, 0xbfb8aa3b, v7
	v_exp_f32_e32 v11, v11
	v_add_f32_e32 v10, 1.0, v10
	v_rcp_f32_e32 v10, v10
	v_add_f32_e32 v11, 1.0, v11
	v_rcp_f32_e32 v11, v11
	s_nop 0
	v_pk_mul_f32 v[6:7], v[6:7], v[10:11]
	v_mul_f32_e32 v10, 0xbfb8aa3b, v3
	v_exp_f32_e32 v10, v10
	s_nop 0
	v_add_f32_e32 v10, 1.0, v10
	v_rcp_f32_e32 v13, v10
	s_nop 0
	v_pk_mul_f32 v[10:11], v[2:3], v[12:13]
	v_mul_f32_e32 v3, 0xbfb8aa3b, v4
	v_exp_f32_e32 v3, v3
	v_mul_f32_e32 v2, 0xbfb8aa3b, v8
	v_exp_f32_e32 v2, v2
	v_add_f32_e32 v3, 1.0, v3
	v_rcp_f32_e32 v12, v3
	v_mul_f32_e32 v3, 0xbfb8aa3b, v9
	v_exp_f32_e32 v3, v3
	v_add_f32_e32 v2, 1.0, v2
	v_rcp_f32_e32 v2, v2
	v_add_f32_e32 v3, 1.0, v3
	v_rcp_f32_e32 v3, v3
	s_nop 0
	v_pk_mul_f32 v[8:9], v[8:9], v[2:3]
	v_mul_f32_e32 v2, 0xbfb8aa3b, v5
	v_exp_f32_e32 v2, v2
	v_cvt_pk_bf16_f32 v3, v8, v9
	v_add_f32_e32 v2, 1.0, v2
	v_rcp_f32_e32 v13, v2
	v_cvt_pk_bf16_f32 v2, v6, v7
	v_pk_mul_f32 v[12:13], v[4:5], v[12:13]
	v_cvt_pk_bf16_f32 v4, v10, v11
	v_cvt_pk_bf16_f32 v5, v12, v13
	global_store_dwordx4 v[76:77], v[2:5], off offset:256
	s_cbranch_vccz .LBB0_1143
	s_waitcnt vmcnt(0)
	s_cmpk_gt_u32 s27, 0xff
	s_cbranch_scc1 .LBB0_1154
	s_barrier

.LBB0_1710:
	s_add_u32 s63, s10, 0x3c800000
	s_addc_u32 s64, s11, 0
	s_add_i32 s66, s55, 0x18000
	s_lshl_b32 s4, s4, 12
	v_lshl_add_u64 v[8:9], v[8:9], 0, s[24:25]
	s_mov_b32 m0, s66
	s_add_i32 s67, s55, 0x1a000
	s_lshl_b32 s65, s5, 13
	s_and_b32 s6, s4, 0x3000
	s_waitcnt vmcnt(2)
	s_barrier
	global_load_lds_dwordx4 v[8:9], off
	v_lshl_add_u64 v[6:7], v[6:7], 0, s[24:25]
	s_mov_b32 m0, s67
	s_add_i32 s68, s55, 0x8000
	s_add_i32 s69, s55, 0xa000
	global_load_lds_dwordx4 v[6:7], off
	v_lshl_add_u64 v[4:5], v[4:5], 0, s[24:25]
	s_mov_b32 m0, s68
	s_add_u32 s4, s12, 0x10080
	global_load_lds_dwordx4 v[4:5], off
	v_lshl_add_u64 v[2:3], v[2:3], 0, s[24:25]
	s_mov_b32 m0, s69
	s_addc_u32 s5, s13, 0
	s_add_i32 s70, s55, 0x1c000
	global_load_lds_dwordx4 v[2:3], off
	v_lshl_add_u64 v[2:3], s[4:5], 0, v[134:135]
	s_mov_b32 m0, s70
	s_add_i32 s71, s55, 0x1e000
	global_load_lds_dwordx4 v[2:3], off
	v_lshl_add_u64 v[2:3], s[4:5], 0, v[130:131]
	s_mov_b32 m0, s71
	s_mov_b32 s72, 0
	global_load_lds_dwordx4 v[2:3], off
	v_and_b32_e32 v2, 15, v0
	v_and_b32_e32 v3, 48, v0
	v_lshlrev_b32_e32 v0, 2, v0
	v_lshl_or_b32 v2, v2, 6, v3
	v_and_b32_e32 v0, 32, v0
	s_waitcnt vmcnt(6)
	v_xad_u32 v138, v2, v0, 0
	v_add_u32_e32 v0, s6, v138
	v_add_u32_e32 v139, 0x10000, v0
	v_add_u32_e32 v140, 0x10400, v0
	v_add_u32_e32 v141, 0x10800, v0
	v_add_u32_e32 v142, 0x10c00, v0
	v_add_u32_e32 v143, 0x14000, v0
	v_add_u32_e32 v144, 0x14400, v0
	v_add_u32_e32 v145, 0x14800, v0
	v_add_u32_e32 v146, 0x14c00, v0
	v_add_u32_e32 v147, 0x18000, v0
	v_add_u32_e32 v148, 0x18400, v0
	v_add_u32_e32 v149, 0x18800, v0
	v_add_u32_e32 v150, 0x18c00, v0
	v_add_u32_e32 v151, 0x1c000, v0
	v_add_u32_e32 v152, 0x1c400, v0
	v_add_u32_e32 v153, 0x1c800, v0
	v_add_u32_e32 v154, 0x1cc00, v0
	v_readlane_b32 s73, v253, 29
	v_readlane_b32 s34, v253, 57
	s_barrier
	v_readlane_b32 s35, v253, 58

.LBB0_1718:
	s_add_u32 s43, s14, s42
	s_addc_u32 s51, s15, 0
	s_add_u32 s46, s43, 0x100
	s_addc_u32 s47, s51, 0
	s_and_b64 s[44:45], s[40:41], exec
	s_cselect_b32 s47, s9, s47
	s_cselect_b32 s46, s35, s46
	s_add_u32 s42, s12, s42
	s_addc_u32 s44, s13, 0
	s_add_u32 s42, s42, 0x100
	s_addc_u32 s44, s44, 0
	s_and_b64 s[40:41], s[40:41], exec
	s_cselect_b32 s49, s7, s44
	s_cselect_b32 s48, s74, s42
	s_add_u32 s50, s43, 0x10080
	s_addc_u32 s51, s51, 0
	s_add_i32 m0, s55, 0xc000
	s_add_i32 s75, s55, 0xe000
	ds_read_b128 v[156:159], v139
	ds_read_b128 v[160:163], v140
	ds_read_b128 v[164:167], v141
	ds_read_b128 v[168:171], v142
	s_add_u32 s44, s48, 0x10000
	s_addc_u32 s45, s49, 0
	s_add_u32 s42, s46, 0x10000
	s_addc_u32 s43, s47, 0
	s_add_u32 s40, s48, 0x10080
	s_addc_u32 s41, s49, 0
	v_add_u32_e32 v0, s65, v138
	v_lshl_add_u64 v[184:185], s[50:51], 0, v[136:137]
	ds_read_b128 v[172:175], v0
	ds_read_b128 v[176:179], v0 offset:1024
	ds_read_b128 v[180:183], v0 offset:2048
	ds_read_b128 v[188:191], v0 offset:3072
	ds_read_b128 v[192:195], v0 offset:4096
	ds_read_b128 v[196:199], v0 offset:5120
	ds_read_b128 v[200:203], v0 offset:6144
	ds_read_b128 v[204:207], v0 offset:7168
	global_load_lds_dwordx4 v[184:185], off
	v_lshl_add_u64 v[184:185], s[50:51], 0, v[132:133]
	s_mov_b32 m0, s75
	s_nop 0
	global_load_lds_dwordx4 v[184:185], off
	ds_read_b128 v[208:211], v143
	ds_read_b128 v[212:215], v144
	ds_read_b128 v[216:219], v145
	ds_read_b128 v[232:235], v146
	s_waitcnt lgkmcnt(4)
	s_waitcnt vmcnt(8)
	s_barrier
	s_waitcnt lgkmcnt(0)
	s_setprio 1
	s_waitcnt lgkmcnt(0)
	v_mfma_f32_16x16x32_bf16 v[126:129], v[156:159], v[172:175], v[126:129]
	v_mfma_f32_16x16x32_bf16 v[122:125], v[164:167], v[172:175], v[122:125]
	v_mfma_f32_16x16x32_bf16 v[118:121], v[156:159], v[180:183], v[118:121]
	v_mfma_f32_16x16x32_bf16 v[114:117], v[164:167], v[180:183], v[114:117]
	v_mfma_f32_16x16x32_bf16 v[102:105], v[156:159], v[192:195], v[102:105]
	v_mfma_f32_16x16x32_bf16 v[98:101], v[164:167], v[192:195], v[98:101]
	v_mfma_f32_16x16x32_bf16 v[86:89], v[156:159], v[200:203], v[86:89]
	v_mfma_f32_16x16x32_bf16 v[82:85], v[164:167], v[200:203], v[82:85]
	v_mfma_f32_16x16x32_bf16 v[126:129], v[160:163], v[176:179], v[126:129]
	v_mfma_f32_16x16x32_bf16 v[122:125], v[168:171], v[176:179], v[122:125]
	v_mfma_f32_16x16x32_bf16 v[118:121], v[160:163], v[188:191], v[118:121]
	v_mfma_f32_16x16x32_bf16 v[114:117], v[168:171], v[188:191], v[114:117]
	v_mfma_f32_16x16x32_bf16 v[102:105], v[160:163], v[196:199], v[102:105]
	v_mfma_f32_16x16x32_bf16 v[98:101], v[168:171], v[196:199], v[98:101]
	v_mfma_f32_16x16x32_bf16 v[86:89], v[160:163], v[204:207], v[86:89]
	v_mfma_f32_16x16x32_bf16 v[82:85], v[168:171], v[204:207], v[82:85]
	v_mfma_f32_16x16x32_bf16 v[110:113], v[208:211], v[172:175], v[110:113]
	v_mfma_f32_16x16x32_bf16 v[106:109], v[216:219], v[172:175], v[106:109]
	v_mfma_f32_16x16x32_bf16 v[94:97], v[208:211], v[180:183], v[94:97]
	v_mfma_f32_16x16x32_bf16 v[90:93], v[216:219], v[180:183], v[90:93]
	v_mfma_f32_16x16x32_bf16 v[78:81], v[208:211], v[192:195], v[78:81]
	v_mfma_f32_16x16x32_bf16 v[74:77], v[216:219], v[192:195], v[74:77]
	v_mfma_f32_16x16x32_bf16 v[70:73], v[208:211], v[200:203], v[70:73]
	v_mfma_f32_16x16x32_bf16 v[66:69], v[216:219], v[200:203], v[66:69]
	v_mfma_f32_16x16x32_bf16 v[110:113], v[212:215], v[176:179], v[110:113]
	v_mfma_f32_16x16x32_bf16 v[106:109], v[232:235], v[176:179], v[106:109]
	v_mfma_f32_16x16x32_bf16 v[94:97], v[212:215], v[188:191], v[94:97]
	v_mfma_f32_16x16x32_bf16 v[90:93], v[232:235], v[188:191], v[90:93]
	v_mfma_f32_16x16x32_bf16 v[78:81], v[212:215], v[196:199], v[78:81]
	v_mfma_f32_16x16x32_bf16 v[74:77], v[232:235], v[196:199], v[74:77]
	v_mfma_f32_16x16x32_bf16 v[70:73], v[212:215], v[204:207], v[70:73]
	v_mfma_f32_16x16x32_bf16 v[66:69], v[232:235], v[204:207], v[66:69]
	s_setprio 0
	s_mov_b32 m0, s55
	v_lshl_add_u64 v[226:227], s[46:47], 0, v[136:137]
	s_barrier
	ds_read_b128 v[172:175], v0 offset:16384
	ds_read_b128 v[176:179], v0 offset:17408
	ds_read_b128 v[180:183], v0 offset:18432
	ds_read_b128 v[188:191], v0 offset:19456
	ds_read_b128 v[192:195], v0 offset:20480
	ds_read_b128 v[196:199], v0 offset:21504
	ds_read_b128 v[200:203], v0 offset:22528
	ds_read_b128 v[204:207], v0 offset:23552
	global_load_lds_dwordx4 v[226:227], off
	v_lshl_add_u64 v[236:237], s[46:47], 0, v[132:133]
	s_mov_b32 m0, s58
	s_nop 0
	global_load_lds_dwordx4 v[236:237], off
	s_mov_b32 m0, s56
	v_lshl_add_u64 v[184:185], s[48:49], 0, v[134:135]
	global_load_lds_dwordx4 v[184:185], off
	v_lshl_add_u64 v[220:221], s[48:49], 0, v[130:131]
	s_mov_b32 m0, s57
	s_nop 0
	global_load_lds_dwordx4 v[220:221], off
	s_barrier
	s_waitcnt lgkmcnt(0)
	s_setprio 1
	s_waitcnt lgkmcnt(0)
	v_mfma_f32_16x16x32_bf16 v[62:65], v[156:159], v[172:175], v[62:65]
	v_mfma_f32_16x16x32_bf16 v[58:61], v[164:167], v[172:175], v[58:61]
	v_mfma_f32_16x16x32_bf16 v[54:57], v[156:159], v[180:183], v[54:57]
	v_mfma_f32_16x16x32_bf16 v[50:53], v[164:167], v[180:183], v[50:53]
	v_mfma_f32_16x16x32_bf16 v[38:41], v[156:159], v[192:195], v[38:41]
	v_mfma_f32_16x16x32_bf16 v[34:37], v[164:167], v[192:195], v[34:37]
	v_mfma_f32_16x16x32_bf16 v[22:25], v[156:159], v[200:203], v[22:25]
	v_mfma_f32_16x16x32_bf16 v[18:21], v[164:167], v[200:203], v[18:21]
	v_mfma_f32_16x16x32_bf16 v[62:65], v[160:163], v[176:179], v[62:65]
	v_mfma_f32_16x16x32_bf16 v[58:61], v[168:171], v[176:179], v[58:61]
	v_mfma_f32_16x16x32_bf16 v[54:57], v[160:163], v[188:191], v[54:57]
	v_mfma_f32_16x16x32_bf16 v[50:53], v[168:171], v[188:191], v[50:53]
	v_mfma_f32_16x16x32_bf16 v[38:41], v[160:163], v[196:199], v[38:41]
	v_mfma_f32_16x16x32_bf16 v[34:37], v[168:171], v[196:199], v[34:37]
	v_mfma_f32_16x16x32_bf16 v[22:25], v[160:163], v[204:207], v[22:25]
	v_mfma_f32_16x16x32_bf16 v[18:21], v[168:171], v[204:207], v[18:21]
	s_setprio 0
	s_barrier
	s_mov_b32 m0, s59
	v_lshl_add_u64 v[156:157], s[44:45], 0, v[134:135]
	global_load_lds_dwordx4 v[156:157], off
	v_lshl_add_u64 v[156:157], s[44:45], 0, v[130:131]
	s_mov_b32 m0, s60
	s_nop 0
	global_load_lds_dwordx4 v[156:157], off
	s_waitcnt vmcnt(8)
	s_barrier
	s_setprio 1
	v_mfma_f32_16x16x32_bf16 v[46:49], v[208:211], v[172:175], v[46:49]
	v_mfma_f32_16x16x32_bf16 v[42:45], v[216:219], v[172:175], v[42:45]
	v_mfma_f32_16x16x32_bf16 v[30:33], v[208:211], v[180:183], v[30:33]
	v_mfma_f32_16x16x32_bf16 v[26:29], v[216:219], v[180:183], v[26:29]
	v_mfma_f32_16x16x32_bf16 v[14:17], v[208:211], v[192:195], v[14:17]
	v_mfma_f32_16x16x32_bf16 v[10:13], v[216:219], v[192:195], v[10:13]
	v_mfma_f32_16x16x32_bf16 v[6:9], v[208:211], v[200:203], v[6:9]
	v_mfma_f32_16x16x32_bf16 v[2:5], v[216:219], v[200:203], v[2:5]
	v_mfma_f32_16x16x32_bf16 v[46:49], v[212:215], v[176:179], v[46:49]
	v_mfma_f32_16x16x32_bf16 v[42:45], v[232:235], v[176:179], v[42:45]
	v_mfma_f32_16x16x32_bf16 v[30:33], v[212:215], v[188:191], v[30:33]
	v_mfma_f32_16x16x32_bf16 v[26:29], v[232:235], v[188:191], v[26:29]
	v_mfma_f32_16x16x32_bf16 v[14:17], v[212:215], v[196:199], v[14:17]
	v_mfma_f32_16x16x32_bf16 v[10:13], v[232:235], v[196:199], v[10:13]
	v_mfma_f32_16x16x32_bf16 v[6:9], v[212:215], v[204:207], v[6:9]
	v_mfma_f32_16x16x32_bf16 v[2:5], v[232:235], v[204:207], v[2:5]
	s_setprio 0
	s_barrier
	ds_read_b128 v[156:159], v147
	ds_read_b128 v[160:163], v148
	ds_read_b128 v[164:167], v149
	ds_read_b128 v[168:171], v150
	s_mov_b32 m0, s61
	v_lshl_add_u64 v[208:209], s[42:43], 0, v[136:137]
	ds_read_b128 v[172:175], v0 offset:32768
	ds_read_b128 v[176:179], v0 offset:33792
	ds_read_b128 v[180:183], v0 offset:34816
	ds_read_b128 v[188:191], v0 offset:35840
	ds_read_b128 v[192:195], v0 offset:36864
	ds_read_b128 v[196:199], v0 offset:37888
	ds_read_b128 v[200:203], v0 offset:38912
	ds_read_b128 v[204:207], v0 offset:39936
	global_load_lds_dwordx4 v[208:209], off
	v_lshl_add_u64 v[208:209], s[42:43], 0, v[132:133]
	s_mov_b32 m0, s62
	s_nop 0
	global_load_lds_dwordx4 v[208:209], off
	ds_read_b128 v[208:211], v151
	ds_read_b128 v[212:215], v152
	ds_read_b128 v[216:219], v153
	ds_read_b128 v[232:235], v154
	s_waitcnt lgkmcnt(4)
	s_waitcnt vmcnt(8)
	s_barrier
	s_waitcnt lgkmcnt(0)
	s_setprio 1
	s_waitcnt lgkmcnt(0)
	v_mfma_f32_16x16x32_bf16 v[126:129], v[156:159], v[172:175], v[126:129]
	v_mfma_f32_16x16x32_bf16 v[122:125], v[164:167], v[172:175], v[122:125]
	v_mfma_f32_16x16x32_bf16 v[118:121], v[156:159], v[180:183], v[118:121]
	v_mfma_f32_16x16x32_bf16 v[114:117], v[164:167], v[180:183], v[114:117]
	v_mfma_f32_16x16x32_bf16 v[102:105], v[156:159], v[192:195], v[102:105]
	v_mfma_f32_16x16x32_bf16 v[98:101], v[164:167], v[192:195], v[98:101]
	v_mfma_f32_16x16x32_bf16 v[86:89], v[156:159], v[200:203], v[86:89]
	v_mfma_f32_16x16x32_bf16 v[82:85], v[164:167], v[200:203], v[82:85]
	v_mfma_f32_16x16x32_bf16 v[126:129], v[160:163], v[176:179], v[126:129]
	v_mfma_f32_16x16x32_bf16 v[122:125], v[168:171], v[176:179], v[122:125]
	v_mfma_f32_16x16x32_bf16 v[118:121], v[160:163], v[188:191], v[118:121]
	v_mfma_f32_16x16x32_bf16 v[114:117], v[168:171], v[188:191], v[114:117]
	v_mfma_f32_16x16x32_bf16 v[102:105], v[160:163], v[196:199], v[102:105]
	v_mfma_f32_16x16x32_bf16 v[98:101], v[168:171], v[196:199], v[98:101]
	v_mfma_f32_16x16x32_bf16 v[86:89], v[160:163], v[204:207], v[86:89]
	v_mfma_f32_16x16x32_bf16 v[82:85], v[168:171], v[204:207], v[82:85]
	v_mfma_f32_16x16x32_bf16 v[110:113], v[208:211], v[172:175], v[110:113]
	v_mfma_f32_16x16x32_bf16 v[106:109], v[216:219], v[172:175], v[106:109]
	v_mfma_f32_16x16x32_bf16 v[94:97], v[208:211], v[180:183], v[94:97]
	v_mfma_f32_16x16x32_bf16 v[90:93], v[216:219], v[180:183], v[90:93]
	v_mfma_f32_16x16x32_bf16 v[78:81], v[208:211], v[192:195], v[78:81]
	v_mfma_f32_16x16x32_bf16 v[74:77], v[216:219], v[192:195], v[74:77]
	v_mfma_f32_16x16x32_bf16 v[70:73], v[208:211], v[200:203], v[70:73]
	v_mfma_f32_16x16x32_bf16 v[66:69], v[216:219], v[200:203], v[66:69]
	v_mfma_f32_16x16x32_bf16 v[110:113], v[212:215], v[176:179], v[110:113]
	v_mfma_f32_16x16x32_bf16 v[106:109], v[232:235], v[176:179], v[106:109]
	v_mfma_f32_16x16x32_bf16 v[94:97], v[212:215], v[188:191], v[94:97]
	v_mfma_f32_16x16x32_bf16 v[90:93], v[232:235], v[188:191], v[90:93]
	v_mfma_f32_16x16x32_bf16 v[78:81], v[212:215], v[196:199], v[78:81]
	v_mfma_f32_16x16x32_bf16 v[74:77], v[232:235], v[196:199], v[74:77]
	v_mfma_f32_16x16x32_bf16 v[70:73], v[212:215], v[204:207], v[70:73]
	v_mfma_f32_16x16x32_bf16 v[66:69], v[232:235], v[204:207], v[66:69]
	s_setprio 0
	s_barrier
	ds_read_b128 v[172:175], v0 offset:49152
	ds_read_b128 v[176:179], v0 offset:50176
	ds_read_b128 v[180:183], v0 offset:51200
	ds_read_b128 v[188:191], v0 offset:52224
	ds_read_b128 v[192:195], v0 offset:53248
	ds_read_b128 v[196:199], v0 offset:54272
	ds_read_b128 v[200:203], v0 offset:55296
	ds_read_b128 v[204:207], v0 offset:56320
	s_mov_b32 m0, s66
	v_lshl_add_u64 v[184:185], v[184:185], 0, s[24:25]
	global_load_lds_dwordx4 v[184:185], off
	v_lshl_add_u64 v[184:185], v[220:221], 0, s[24:25]
	s_mov_b32 m0, s67
	s_nop 0
	global_load_lds_dwordx4 v[184:185], off
	s_mov_b32 m0, s68
	v_lshl_add_u64 v[184:185], v[226:227], 0, s[24:25]
	global_load_lds_dwordx4 v[184:185], off
	v_lshl_add_u64 v[184:185], v[236:237], 0, s[24:25]
	s_mov_b32 m0, s69
	s_nop 0
	global_load_lds_dwordx4 v[184:185], off
	s_barrier
	s_waitcnt lgkmcnt(0)
	s_setprio 1
	s_waitcnt lgkmcnt(0)
	v_mfma_f32_16x16x32_bf16 v[62:65], v[156:159], v[172:175], v[62:65]
	v_mfma_f32_16x16x32_bf16 v[58:61], v[164:167], v[172:175], v[58:61]
	v_mfma_f32_16x16x32_bf16 v[54:57], v[156:159], v[180:183], v[54:57]
	v_mfma_f32_16x16x32_bf16 v[50:53], v[164:167], v[180:183], v[50:53]
	v_mfma_f32_16x16x32_bf16 v[38:41], v[156:159], v[192:195], v[38:41]
	v_mfma_f32_16x16x32_bf16 v[34:37], v[164:167], v[192:195], v[34:37]
	v_mfma_f32_16x16x32_bf16 v[22:25], v[156:159], v[200:203], v[22:25]
	v_mfma_f32_16x16x32_bf16 v[18:21], v[164:167], v[200:203], v[18:21]
	v_mfma_f32_16x16x32_bf16 v[62:65], v[160:163], v[176:179], v[62:65]
	v_mfma_f32_16x16x32_bf16 v[58:61], v[168:171], v[176:179], v[58:61]
	v_mfma_f32_16x16x32_bf16 v[54:57], v[160:163], v[188:191], v[54:57]
	v_mfma_f32_16x16x32_bf16 v[50:53], v[168:171], v[188:191], v[50:53]
	v_mfma_f32_16x16x32_bf16 v[38:41], v[160:163], v[196:199], v[38:41]
	v_mfma_f32_16x16x32_bf16 v[34:37], v[168:171], v[196:199], v[34:37]
	v_mfma_f32_16x16x32_bf16 v[22:25], v[160:163], v[204:207], v[22:25]
	v_mfma_f32_16x16x32_bf16 v[18:21], v[168:171], v[204:207], v[18:21]
	s_setprio 0
	s_barrier
	s_mov_b32 m0, s70
	v_lshl_add_u64 v[156:157], s[40:41], 0, v[134:135]
	global_load_lds_dwordx4 v[156:157], off
	v_lshl_add_u64 v[156:157], s[40:41], 0, v[130:131]
	s_mov_b32 m0, s71
	s_nop 0
	global_load_lds_dwordx4 v[156:157], off
	s_waitcnt vmcnt(8)
	s_barrier
	s_setprio 1
	v_mfma_f32_16x16x32_bf16 v[46:49], v[208:211], v[172:175], v[46:49]
	v_mfma_f32_16x16x32_bf16 v[42:45], v[216:219], v[172:175], v[42:45]
	v_mfma_f32_16x16x32_bf16 v[30:33], v[208:211], v[180:183], v[30:33]
	v_mfma_f32_16x16x32_bf16 v[26:29], v[216:219], v[180:183], v[26:29]
	v_mfma_f32_16x16x32_bf16 v[14:17], v[208:211], v[192:195], v[14:17]
	v_mfma_f32_16x16x32_bf16 v[10:13], v[216:219], v[192:195], v[10:13]
	v_mfma_f32_16x16x32_bf16 v[6:9], v[208:211], v[200:203], v[6:9]
	v_mfma_f32_16x16x32_bf16 v[2:5], v[216:219], v[200:203], v[2:5]
	v_mfma_f32_16x16x32_bf16 v[46:49], v[212:215], v[176:179], v[46:49]
	v_mfma_f32_16x16x32_bf16 v[42:45], v[232:235], v[176:179], v[42:45]
	v_mfma_f32_16x16x32_bf16 v[30:33], v[212:215], v[188:191], v[30:33]
	v_mfma_f32_16x16x32_bf16 v[26:29], v[232:235], v[188:191], v[26:29]
	v_mfma_f32_16x16x32_bf16 v[14:17], v[212:215], v[196:199], v[14:17]
	v_mfma_f32_16x16x32_bf16 v[10:13], v[232:235], v[196:199], v[10:13]
	v_mfma_f32_16x16x32_bf16 v[6:9], v[212:215], v[204:207], v[6:9]
	v_mfma_f32_16x16x32_bf16 v[2:5], v[232:235], v[204:207], v[2:5]
	s_setprio 0
	s_movk_i32 s42, 0x100
	s_andn2_b64 vcc, exec, s[38:39]
	s_mov_b64 s[40:41], -1
	s_mov_b64 s[38:39], 0
	s_barrier
	s_cbranch_vccz .LBB0_1718
	v_readlane_b32 s7, v252, 52
	v_readlane_b32 s9, v252, 51
	v_mbcnt_lo_u32_b32 v0, -1, 0
	v_mbcnt_hi_u32_b32 v0, -1, v0
	s_lshl_b32 s38, s7, 5
	v_and_b32_e32 v155, 15, v0
	s_ashr_i32 s35, s34, 31
	v_lshl_or_b32 v156, s9, 6, v155
	s_ashr_i32 s39, s38, 31
	s_lshl_b64 s[12:13], s[34:35], 19
	s_add_u32 s12, s63, s12
	v_cvt_pk_bf16_f32 v70, v70, v71
	v_cvt_pk_bf16_f32 v71, v72, v73
	v_cvt_pk_bf16_f32 v72, v66, v67
	v_add_u32_e32 v66, 0x80, v156
	v_ashrrev_i32_e32 v157, 31, v156
	s_addc_u32 s13, s64, s13
	s_lshl_b32 s14, s73, 8
	v_cvt_pk_bf16_f32 v110, v110, v111
	v_cvt_pk_bf16_f32 v111, v112, v113
	v_cvt_pk_bf16_f32 v112, v106, v107
	v_or_b32_e32 v106, 16, v156
	v_ashrrev_i32_e32 v67, 31, v66
	v_cvt_pk_bf16_f32 v46, v46, v47
	v_cvt_pk_bf16_f32 v47, v48, v49
	v_cvt_pk_bf16_f32 v48, v42, v43
	v_add_u32_e32 v42, 0x90, v156
	v_lshlrev_b64 v[158:159], 11, v[156:157]
	s_ashr_i32 s15, s14, 31
	v_ashrrev_i32_e32 v107, 31, v106
	v_cvt_pk_bf16_f32 v94, v94, v95
	v_cvt_pk_bf16_f32 v95, v96, v97
	v_cvt_pk_bf16_f32 v96, v90, v91
	v_or_b32_e32 v90, 32, v156
	v_lshlrev_b64 v[66:67], 11, v[66:67]
	v_ashrrev_i32_e32 v43, 31, v42
	v_cvt_pk_bf16_f32 v30, v30, v31
	v_cvt_pk_bf16_f32 v31, v32, v33
	v_cvt_pk_bf16_f32 v32, v26, v27
	v_add_u32_e32 v26, 0xa0, v156
	v_lshl_add_u64 v[158:159], s[12:13], 0, v[158:159]
	s_lshl_b64 s[14:15], s[14:15], 1
	v_lshlrev_b64 v[106:107], 11, v[106:107]
	v_ashrrev_i32_e32 v91, 31, v90
	v_cvt_pk_bf16_f32 v78, v78, v79
	v_cvt_pk_bf16_f32 v79, v80, v81
	v_cvt_pk_bf16_f32 v80, v74, v75
	v_or_b32_e32 v74, 48, v156
	v_lshl_add_u64 v[66:67], s[12:13], 0, v[66:67]
	v_lshlrev_b64 v[42:43], 11, v[42:43]
	v_ashrrev_i32_e32 v27, 31, v26
	v_cvt_pk_bf16_f32 v14, v14, v15
	v_cvt_pk_bf16_f32 v15, v16, v17
	v_cvt_pk_bf16_f32 v16, v10, v11
	v_add_u32_e32 v10, 0xb0, v156
	v_lshl_add_u64 v[158:159], v[158:159], 0, s[14:15]
	s_lshl_b64 s[34:35], s[38:39], 1
	v_lshl_add_u64 v[106:107], s[12:13], 0, v[106:107]
	v_lshlrev_b64 v[90:91], 11, v[90:91]
	v_ashrrev_i32_e32 v75, 31, v74
	v_lshl_add_u64 v[66:67], v[66:67], 0, s[14:15]
	v_lshl_add_u64 v[42:43], s[12:13], 0, v[42:43]
	v_lshlrev_b64 v[26:27], 11, v[26:27]
	v_ashrrev_i32_e32 v11, 31, v10
	v_lshl_add_u64 v[158:159], v[158:159], 0, s[34:35]
	v_and_b32_e32 v0, 48, v0
	v_lshl_add_u64 v[106:107], v[106:107], 0, s[14:15]
	v_lshl_add_u64 v[90:91], s[12:13], 0, v[90:91]
	v_lshlrev_b64 v[74:75], 11, v[74:75]
	v_lshl_add_u64 v[66:67], v[66:67], 0, s[34:35]
	v_lshl_add_u64 v[42:43], v[42:43], 0, s[14:15]
	v_lshl_add_u64 v[26:27], s[12:13], 0, v[26:27]
	v_lshlrev_b64 v[10:11], 11, v[10:11]
	v_lshl_add_u64 v[158:159], v[158:159], 0, v[0:1]
	v_cvt_pk_bf16_f32 v113, v108, v109
	v_lshl_add_u64 v[106:107], v[106:107], 0, s[34:35]
	v_lshl_add_u64 v[90:91], v[90:91], 0, s[14:15]
	v_lshl_add_u64 v[74:75], s[12:13], 0, v[74:75]
	v_lshl_add_u64 v[66:67], v[66:67], 0, v[0:1]
	v_cvt_pk_bf16_f32 v49, v44, v45
	v_lshl_add_u64 v[42:43], v[42:43], 0, s[34:35]
	v_lshl_add_u64 v[26:27], v[26:27], 0, s[14:15]
	v_lshl_add_u64 v[10:11], s[12:13], 0, v[10:11]
	global_store_dwordx4 v[158:159], v[110:113], off offset:256
	v_cvt_pk_bf16_f32 v97, v92, v93
	v_lshl_add_u64 v[90:91], v[90:91], 0, s[34:35]
	v_lshl_add_u64 v[110:111], v[106:107], 0, v[0:1]
	v_lshl_add_u64 v[74:75], v[74:75], 0, s[14:15]
	global_store_dwordx4 v[66:67], v[46:49], off offset:256
	v_cvt_pk_bf16_f32 v33, v28, v29
	v_lshl_add_u64 v[26:27], v[26:27], 0, s[34:35]
	v_lshl_add_u64 v[46:47], v[42:43], 0, v[0:1]
	v_lshl_add_u64 v[10:11], v[10:11], 0, s[14:15]
	global_store_dwordx4 v[110:111], v[94:97], off offset:256
	v_cvt_pk_bf16_f32 v81, v76, v77
	v_lshl_add_u64 v[74:75], v[74:75], 0, s[34:35]
	v_lshl_add_u64 v[94:95], v[90:91], 0, v[0:1]
	global_store_dwordx4 v[46:47], v[30:33], off offset:256
	v_cvt_pk_bf16_f32 v17, v12, v13
	v_lshl_add_u64 v[10:11], v[10:11], 0, s[34:35]
	v_lshl_add_u64 v[30:31], v[26:27], 0, v[0:1]
	v_cvt_pk_bf16_f32 v126, v126, v127
	v_cvt_pk_bf16_f32 v127, v128, v129
	v_cvt_pk_bf16_f32 v128, v122, v123
	v_cvt_pk_bf16_f32 v129, v124, v125
	v_cvt_pk_bf16_f32 v106, v118, v119
	v_cvt_pk_bf16_f32 v107, v120, v121
	v_cvt_pk_bf16_f32 v108, v114, v115
	v_cvt_pk_bf16_f32 v109, v116, v117
	v_cvt_pk_bf16_f32 v90, v102, v103
	v_cvt_pk_bf16_f32 v91, v104, v105
	v_cvt_pk_bf16_f32 v92, v98, v99
	v_cvt_pk_bf16_f32 v93, v100, v101
	global_store_dwordx4 v[94:95], v[78:81], off offset:256
	v_cvt_pk_bf16_f32 v76, v82, v83
	v_cvt_pk_bf16_f32 v77, v84, v85
	v_lshl_add_u64 v[78:79], v[74:75], 0, v[0:1]
	v_cvt_pk_bf16_f32 v74, v86, v87
	v_cvt_pk_bf16_f32 v75, v88, v89
	v_cvt_pk_bf16_f32 v73, v68, v69
	v_cvt_pk_bf16_f32 v62, v62, v63
	v_cvt_pk_bf16_f32 v63, v64, v65
	v_cvt_pk_bf16_f32 v64, v58, v59
	v_cvt_pk_bf16_f32 v65, v60, v61
	v_cvt_pk_bf16_f32 v42, v54, v55
	v_cvt_pk_bf16_f32 v43, v56, v57
	v_cvt_pk_bf16_f32 v44, v50, v51
	v_cvt_pk_bf16_f32 v45, v52, v53
	v_cvt_pk_bf16_f32 v26, v38, v39
	v_cvt_pk_bf16_f32 v27, v40, v41
	v_cvt_pk_bf16_f32 v28, v34, v35
	v_cvt_pk_bf16_f32 v29, v36, v37
	global_store_dwordx4 v[30:31], v[14:17], off offset:256
	v_cvt_pk_bf16_f32 v12, v18, v19
	v_cvt_pk_bf16_f32 v13, v20, v21
	v_lshl_add_u64 v[14:15], v[10:11], 0, v[0:1]
	v_cvt_pk_bf16_f32 v10, v22, v23
	v_cvt_pk_bf16_f32 v11, v24, v25
	v_cvt_pk_bf16_f32 v6, v6, v7
	v_cvt_pk_bf16_f32 v7, v8, v9
	v_cvt_pk_bf16_f32 v8, v2, v3
	v_cvt_pk_bf16_f32 v9, v4, v5
	s_and_b64 vcc, exec, s[4:5]
	s_mov_b32 s73, s6
	s_mov_b32 s34, s8
	s_mov_b64 s[12:13], s[20:21]
	s_mov_b64 s[14:15], s[10:11]
	global_store_dwordx4 v[158:159], v[126:129], off
	global_store_dwordx4 v[110:111], v[106:109], off
	global_store_dwordx4 v[94:95], v[90:93], off
	global_store_dwordx4 v[78:79], v[74:77], off
	global_store_dwordx4 v[78:79], v[70:73], off offset:256
	global_store_dwordx4 v[66:67], v[62:65], off
	global_store_dwordx4 v[46:47], v[42:45], off
	global_store_dwordx4 v[30:31], v[26:29], off
	global_store_dwordx4 v[14:15], v[10:13], off
	global_store_dwordx4 v[14:15], v[6:9], off offset:256
	s_cbranch_vccz .LBB0_1711
	s_waitcnt vmcnt(0)
	s_cmpk_gt_u32 s27, 0xff
	s_cbranch_scc1 .LBB0_1722
	s_barrier

.LBB0_1781:
	s_add_u32 s63, s6, 0xab000000
	s_addc_u32 s64, s7, 0
	s_lshl_b64 s[4:5], s[28:29], 2
	s_add_u32 s28, s8, s4
	s_addc_u32 s65, s9, s5
	s_add_i32 s67, s55, 0x18000
	s_lshl_b32 s4, s13, 12
	v_lshl_add_u64 v[8:9], v[8:9], 0, s[24:25]
	s_mov_b32 m0, s67
	s_add_i32 s68, s55, 0x1a000
	s_lshl_b32 s66, s12, 13
	s_and_b32 s6, s4, 0x3000
	s_waitcnt vmcnt(2)
	s_barrier
	global_load_lds_dwordx4 v[8:9], off
	v_lshl_add_u64 v[6:7], v[6:7], 0, s[24:25]
	s_mov_b32 m0, s68
	s_add_i32 s69, s55, 0x8000
	s_add_i32 s70, s55, 0xa000
	global_load_lds_dwordx4 v[6:7], off
	v_lshl_add_u64 v[4:5], v[4:5], 0, s[24:25]
	s_mov_b32 m0, s69
	s_add_u32 s4, s42, 0x20080
	global_load_lds_dwordx4 v[4:5], off
	v_lshl_add_u64 v[2:3], v[2:3], 0, s[24:25]
	s_mov_b32 m0, s70
	s_addc_u32 s5, s43, 0
	s_add_i32 s71, s55, 0x1c000
	global_load_lds_dwordx4 v[2:3], off
	v_lshl_add_u64 v[2:3], s[4:5], 0, v[0:1]
	s_mov_b32 m0, s71
	s_add_i32 s72, s55, 0x1e000
	global_load_lds_dwordx4 v[2:3], off
	v_lshl_add_u64 v[2:3], s[4:5], 0, v[150:151]
	s_mov_b32 m0, s72
	s_cmp_lt_u32 s46, 64
	global_load_lds_dwordx4 v[2:3], off
	v_and_b32_e32 v2, 15, v10
	v_and_b32_e32 v3, 48, v10
	v_lshl_or_b32 v2, v2, 6, v3
	v_lshlrev_b32_e32 v3, 2, v10
	v_and_b32_e32 v3, 32, v3
	v_xad_u32 v164, v2, v3, 0
	v_add_u32_e32 v2, s6, v164
	v_add_u32_e32 v165, 0x10000, v2
	v_add_u32_e32 v166, 0x10400, v2
	v_add_u32_e32 v167, 0x10800, v2
	v_add_u32_e32 v168, 0x10c00, v2
	v_add_u32_e32 v169, 0x14000, v2
	v_add_u32_e32 v170, 0x14400, v2
	v_add_u32_e32 v171, 0x14800, v2
	v_add_u32_e32 v172, 0x14c00, v2
	v_add_u32_e32 v173, 0x18000, v2
	v_add_u32_e32 v174, 0x18400, v2
	v_add_u32_e32 v175, 0x18800, v2
	v_add_u32_e32 v176, 0x18c00, v2
	v_add_u32_e32 v177, 0x1c000, v2
	v_add_u32_e32 v178, 0x1c400, v2
	v_add_u32_e32 v179, 0x1c800, v2
	v_add_u32_e32 v180, 0x1cc00, v2
	v_lshlrev_b32_e32 v2, 13, v11
	v_and_b32_e32 v2, 0xffffc000, v2
	v_lshl_add_u32 v2, v12, 10, v2
	v_and_b32_e32 v3, 1, v11
	v_lshl_or_b32 v2, v3, 6, v2
	v_lshl_add_u32 v152, v13, 1, v2
	v_lshlrev_b32_e32 v2, 13, v14
	v_and_b32_e32 v2, 0xffffc000, v2
	s_waitcnt vmcnt(6)
	v_lshl_add_u32 v2, v15, 10, v2
	v_and_b32_e32 v3, 1, v14
	v_lshl_or_b32 v2, v3, 6, v2
	s_cselect_b64 s[12:13], -1, 0
	v_mov_b32_e32 v153, v1
	v_lshl_add_u32 v154, v16, 1, v2
	v_mov_b32_e32 v155, v1
	s_mov_b32 s73, 0
	s_barrier
	s_branch .LBB0_1783

.LBB0_1791:
	s_ashr_i32 s21, s20, 31
	ds_read_b128 v[2:5], v165
	ds_read_b128 v[6:9], v166
	ds_read_b128 v[10:13], v167
	ds_read_b128 v[14:17], v168
	s_lshl_b64 s[34:35], s[20:21], 18
	s_add_u32 s34, s51, s34
	s_addc_u32 s35, s52, s35
	s_and_b64 s[6:7], s[6:7], exec
	s_cselect_b32 s15, s35, s45
	s_cselect_b32 s21, s34, s44
	s_lshl_b32 s40, s40, 8
	s_ashr_i32 s41, s40, 31
	s_add_u32 s6, s44, 0x20080
	s_addc_u32 s7, s45, 0
	s_add_i32 s39, s55, 0xc000
	v_add_u32_e32 v181, s66, v164
	v_lshl_add_u64 v[42:43], s[6:7], 0, v[146:147]
	s_mov_b32 m0, s39
	s_add_i32 s74, s55, 0xe000
	ds_read_b128 v[18:21], v181
	ds_read_b128 v[22:25], v181 offset:1024
	ds_read_b128 v[26:29], v181 offset:2048
	ds_read_b128 v[30:33], v181 offset:3072
	ds_read_b128 v[34:37], v181 offset:4096
	ds_read_b128 v[38:41], v181 offset:5120
	ds_read_b128 v[50:53], v181 offset:6144
	ds_read_b128 v[54:57], v181 offset:7168
	global_load_lds_dwordx4 v[42:43], off
	v_lshl_add_u64 v[42:43], s[6:7], 0, v[148:149]
	s_mov_b32 m0, s74
	s_nop 0
	global_load_lds_dwordx4 v[42:43], off
	ds_read_b128 v[188:191], v169
	ds_read_b128 v[192:195], v170
	ds_read_b128 v[196:199], v171
	ds_read_b128 v[200:203], v172
	s_waitcnt lgkmcnt(4)
	s_waitcnt vmcnt(8)
	s_barrier
	s_waitcnt lgkmcnt(0)
	s_setprio 1
	s_waitcnt lgkmcnt(0)
	v_mfma_f32_16x16x128_f8f6f4 v[142:145], v[2:9], v[18:25], 0
	v_mfma_f32_16x16x128_f8f6f4 v[138:141], v[10:17], v[18:25], 0
	v_mfma_f32_16x16x128_f8f6f4 v[134:137], v[2:9], v[26:33], 0
	v_mfma_f32_16x16x128_f8f6f4 v[130:133], v[10:17], v[26:33], 0
	v_mfma_f32_16x16x128_f8f6f4 v[122:125], v[2:9], v[34:41], 0
	v_mfma_f32_16x16x128_f8f6f4 v[114:117], v[10:17], v[34:41], 0
	v_mfma_f32_16x16x128_f8f6f4 v[106:109], v[2:9], v[50:57], 0
	v_mfma_f32_16x16x128_f8f6f4 v[98:101], v[10:17], v[50:57], 0
	v_lshl_add_u64 v[160:161], s[42:43], 0, v[0:1]
	s_mov_b64 s[6:7], 0x100
	v_lshl_add_u64 v[162:163], s[42:43], 0, v[150:151]
	v_mfma_f32_16x16x128_f8f6f4 v[78:81], v[188:195], v[18:25], 0
	v_mfma_f32_16x16x128_f8f6f4 v[74:77], v[196:203], v[18:25], 0
	v_mfma_f32_16x16x128_f8f6f4 v[70:73], v[188:195], v[26:33], 0
	v_mfma_f32_16x16x128_f8f6f4 v[66:69], v[196:203], v[26:33], 0
	v_mfma_f32_16x16x128_f8f6f4 v[62:65], v[188:195], v[34:41], 0
	v_mfma_f32_16x16x128_f8f6f4 v[58:61], v[196:203], v[34:41], 0
	v_mfma_f32_16x16x128_f8f6f4 v[46:49], v[188:195], v[50:57], 0
	v_mfma_f32_16x16x128_f8f6f4 v[42:45], v[196:203], v[50:57], 0
	s_setprio 0
	v_lshl_add_u64 v[156:157], s[44:45], 0, v[146:147]
	s_mov_b32 m0, s55
	v_lshl_add_u64 v[34:35], v[156:157], 0, s[6:7]
	v_lshl_add_u64 v[158:159], s[44:45], 0, v[148:149]
	s_barrier
	ds_read_b128 v[18:21], v181 offset:16384
	ds_read_b128 v[22:25], v181 offset:17408
	ds_read_b128 v[26:29], v181 offset:18432
	ds_read_b128 v[30:33], v181 offset:19456
	ds_read_b128 v[204:207], v181 offset:20480
	ds_read_b128 v[208:211], v181 offset:21504
	ds_read_b128 v[212:215], v181 offset:22528
	ds_read_b128 v[216:219], v181 offset:23552
	global_load_lds_dwordx4 v[34:35], off
	v_lshl_add_u64 v[34:35], v[158:159], 0, s[6:7]
	s_mov_b32 m0, s58
	s_nop 0
	global_load_lds_dwordx4 v[34:35], off
	s_mov_b32 m0, s56
	v_lshl_add_u64 v[34:35], v[160:161], 0, s[6:7]
	global_load_lds_dwordx4 v[34:35], off
	v_lshl_add_u64 v[34:35], v[162:163], 0, s[6:7]
	s_mov_b32 m0, s57
	s_nop 0
	global_load_lds_dwordx4 v[34:35], off
	s_barrier
	s_waitcnt lgkmcnt(0)
	s_setprio 1
	s_waitcnt lgkmcnt(0)
	v_mfma_f32_16x16x128_f8f6f4 v[126:129], v[2:9], v[18:25], 0
	v_mfma_f32_16x16x128_f8f6f4 v[118:121], v[10:17], v[18:25], 0
	v_mfma_f32_16x16x128_f8f6f4 v[110:113], v[2:9], v[26:33], 0
	v_mfma_f32_16x16x128_f8f6f4 v[102:105], v[10:17], v[26:33], 0
	v_mfma_f32_16x16x128_f8f6f4 v[94:97], v[2:9], v[204:211], 0
	v_mfma_f32_16x16x128_f8f6f4 v[90:93], v[10:17], v[204:211], 0
	v_mfma_f32_16x16x128_f8f6f4 v[86:89], v[2:9], v[212:219], 0
	v_mfma_f32_16x16x128_f8f6f4 v[82:85], v[10:17], v[212:219], 0
	s_setprio 0
	s_barrier
	s_add_u32 s6, s42, 0x20100
	s_addc_u32 s7, s43, 0
	s_mov_b32 m0, s59
	v_lshl_add_u64 v[2:3], s[6:7], 0, v[0:1]
	global_load_lds_dwordx4 v[2:3], off
	v_lshl_add_u64 v[2:3], s[6:7], 0, v[150:151]
	s_mov_b32 m0, s60
	s_nop 0
	global_load_lds_dwordx4 v[2:3], off
	s_waitcnt vmcnt(8)
	s_barrier
	s_setprio 1
	v_mfma_f32_16x16x128_f8f6f4 v[54:57], v[188:195], v[18:25], 0
	v_mfma_f32_16x16x128_f8f6f4 v[50:53], v[196:203], v[18:25], 0
	v_mfma_f32_16x16x128_f8f6f4 v[38:41], v[188:195], v[26:33], 0
	v_mfma_f32_16x16x128_f8f6f4 v[34:37], v[196:203], v[26:33], 0
	v_mfma_f32_16x16x128_f8f6f4 v[30:33], v[188:195], v[204:211], 0
	v_mfma_f32_16x16x128_f8f6f4 v[26:29], v[196:203], v[204:211], 0
	v_mfma_f32_16x16x128_f8f6f4 v[22:25], v[188:195], v[212:219], 0
	v_mfma_f32_16x16x128_f8f6f4 v[18:21], v[196:203], v[212:219], 0
	s_setprio 0
	s_barrier
	ds_read_b128 v[2:5], v173
	ds_read_b128 v[6:9], v174
	ds_read_b128 v[10:13], v175
	ds_read_b128 v[14:17], v176
	s_add_u32 s6, s44, 0x20100
	s_addc_u32 s7, s45, 0
	s_mov_b32 m0, s61
	v_lshl_add_u64 v[182:183], s[6:7], 0, v[146:147]
	ds_read_b128 v[188:191], v181 offset:32768
	ds_read_b128 v[192:195], v181 offset:33792
	ds_read_b128 v[196:199], v181 offset:34816
	ds_read_b128 v[200:203], v181 offset:35840
	ds_read_b128 v[204:207], v181 offset:36864
	ds_read_b128 v[208:211], v181 offset:37888
	ds_read_b128 v[212:215], v181 offset:38912
	ds_read_b128 v[216:219], v181 offset:39936
	global_load_lds_dwordx4 v[182:183], off
	v_lshl_add_u64 v[182:183], s[6:7], 0, v[148:149]
	s_mov_b32 m0, s62
	s_nop 0
	global_load_lds_dwordx4 v[182:183], off
	ds_read_b128 v[232:235], v177
	ds_read_b128 v[236:239], v178
	ds_read_b128 v[240:243], v179
	ds_read_b128 v[244:247], v180
	s_waitcnt lgkmcnt(4)
	s_waitcnt vmcnt(8)
	s_barrier
	s_waitcnt lgkmcnt(0)
	s_setprio 1
	s_waitcnt lgkmcnt(0)
	v_mfma_f32_16x16x128_f8f6f4 v[142:145], v[2:9], v[188:195], v[142:145]
	v_mfma_f32_16x16x128_f8f6f4 v[138:141], v[10:17], v[188:195], v[138:141]
	v_mfma_f32_16x16x128_f8f6f4 v[134:137], v[2:9], v[196:203], v[134:137]
	v_mfma_f32_16x16x128_f8f6f4 v[130:133], v[10:17], v[196:203], v[130:133]
	v_mfma_f32_16x16x128_f8f6f4 v[122:125], v[2:9], v[204:211], v[122:125]
	v_mfma_f32_16x16x128_f8f6f4 v[114:117], v[10:17], v[204:211], v[114:117]
	v_mfma_f32_16x16x128_f8f6f4 v[106:109], v[2:9], v[212:219], v[106:109]
	v_mfma_f32_16x16x128_f8f6f4 v[98:101], v[10:17], v[212:219], v[98:101]
	s_mov_b64 s[6:7], 0x180
	v_mfma_f32_16x16x128_f8f6f4 v[78:81], v[232:239], v[188:195], v[78:81]
	v_mfma_f32_16x16x128_f8f6f4 v[74:77], v[240:247], v[188:195], v[74:77]
	v_mfma_f32_16x16x128_f8f6f4 v[70:73], v[232:239], v[196:203], v[70:73]
	v_mfma_f32_16x16x128_f8f6f4 v[66:69], v[240:247], v[196:203], v[66:69]
	v_mfma_f32_16x16x128_f8f6f4 v[62:65], v[232:239], v[204:211], v[62:65]
	v_mfma_f32_16x16x128_f8f6f4 v[58:61], v[240:247], v[204:211], v[58:61]
	v_mfma_f32_16x16x128_f8f6f4 v[46:49], v[232:239], v[212:219], v[46:49]
	v_mfma_f32_16x16x128_f8f6f4 v[42:45], v[240:247], v[212:219], v[42:45]
	s_setprio 0
	s_mov_b32 m0, s69
	v_lshl_add_u64 v[156:157], v[156:157], 0, s[6:7]
	s_barrier
	ds_read_b128 v[188:191], v181 offset:49152
	ds_read_b128 v[192:195], v181 offset:50176
	ds_read_b128 v[196:199], v181 offset:51200
	ds_read_b128 v[200:203], v181 offset:52224
	ds_read_b128 v[204:207], v181 offset:53248
	ds_read_b128 v[208:211], v181 offset:54272
	ds_read_b128 v[212:215], v181 offset:55296
	ds_read_b128 v[216:219], v181 offset:56320
	global_load_lds_dwordx4 v[156:157], off
	v_lshl_add_u64 v[156:157], v[158:159], 0, s[6:7]
	s_mov_b32 m0, s70
	s_nop 0
	global_load_lds_dwordx4 v[156:157], off
	s_mov_b32 m0, s67
	v_lshl_add_u64 v[160:161], v[160:161], 0, s[6:7]
	global_load_lds_dwordx4 v[160:161], off
	v_lshl_add_u64 v[160:161], v[162:163], 0, s[6:7]
	s_mov_b32 m0, s68
	s_nop 0
	global_load_lds_dwordx4 v[160:161], off
	s_barrier
	s_waitcnt lgkmcnt(0)
	s_setprio 1
	s_waitcnt lgkmcnt(0)
	v_mfma_f32_16x16x128_f8f6f4 v[126:129], v[2:9], v[188:195], v[126:129]
	v_mfma_f32_16x16x128_f8f6f4 v[118:121], v[10:17], v[188:195], v[118:121]
	v_mfma_f32_16x16x128_f8f6f4 v[110:113], v[2:9], v[196:203], v[110:113]
	v_mfma_f32_16x16x128_f8f6f4 v[102:105], v[10:17], v[196:203], v[102:105]
	v_mfma_f32_16x16x128_f8f6f4 v[94:97], v[2:9], v[204:211], v[94:97]
	v_mfma_f32_16x16x128_f8f6f4 v[90:93], v[10:17], v[204:211], v[90:93]
	v_mfma_f32_16x16x128_f8f6f4 v[86:89], v[2:9], v[212:219], v[86:89]
	v_mfma_f32_16x16x128_f8f6f4 v[82:85], v[10:17], v[212:219], v[82:85]
	s_setprio 0
	s_barrier
	s_add_u32 s6, s42, 0x20180
	s_addc_u32 s7, s43, 0
	s_mov_b32 m0, s71
	v_lshl_add_u64 v[2:3], s[6:7], 0, v[0:1]
	global_load_lds_dwordx4 v[2:3], off
	v_lshl_add_u64 v[2:3], s[6:7], 0, v[150:151]
	s_mov_b32 m0, s72
	s_nop 0
	global_load_lds_dwordx4 v[2:3], off
	s_waitcnt vmcnt(8)
	s_barrier
	s_setprio 1
	v_mfma_f32_16x16x128_f8f6f4 v[54:57], v[232:239], v[188:195], v[54:57]
	v_mfma_f32_16x16x128_f8f6f4 v[50:53], v[240:247], v[188:195], v[50:53]
	v_mfma_f32_16x16x128_f8f6f4 v[38:41], v[232:239], v[196:203], v[38:41]
	v_mfma_f32_16x16x128_f8f6f4 v[34:37], v[240:247], v[196:203], v[34:37]
	v_mfma_f32_16x16x128_f8f6f4 v[30:33], v[232:239], v[204:211], v[30:33]
	v_mfma_f32_16x16x128_f8f6f4 v[26:29], v[240:247], v[204:211], v[26:29]
	v_mfma_f32_16x16x128_f8f6f4 v[22:25], v[232:239], v[212:219], v[22:25]
	v_mfma_f32_16x16x128_f8f6f4 v[18:21], v[240:247], v[212:219], v[18:21]
	s_setprio 0
	s_lshl_b64 s[6:7], s[40:41], 2
	s_add_u32 s41, s28, s6
	s_addc_u32 s75, s65, s7
	s_add_u32 s44, s44, 0x20180
	s_addc_u32 s45, s45, 0
	s_add_u32 s76, s42, 0x200
	s_addc_u32 s77, s43, 0
	s_mov_b32 s78, 0
	s_barrier
	s_branch .LBB0_1793
.LBB0_1792:
	ds_read_b128 v[10:13], v165
	ds_read_b128 v[14:17], v166
	ds_read_b128 v[156:159], v167
	ds_read_b128 v[160:163], v168
	s_add_u32 s79, s44, 0xfffe0080
	s_addc_u32 s80, s45, -1
	s_and_b64 s[6:7], s[42:43], exec
	s_cselect_b32 s43, s15, s80
	s_cselect_b32 s42, s21, s79
	s_cselect_b32 s7, s9, s77
	s_cselect_b32 s6, s8, s76
	s_mov_b32 m0, s39
	v_lshl_add_u64 v[2:3], s[44:45], 0, v[152:153]
	ds_read_b128 v[188:191], v181
	ds_read_b128 v[192:195], v181 offset:1024
	ds_read_b128 v[196:199], v181 offset:2048
	ds_read_b128 v[200:203], v181 offset:3072
	ds_read_b128 v[204:207], v181 offset:4096
	ds_read_b128 v[208:211], v181 offset:5120
	ds_read_b128 v[212:215], v181 offset:6144
	ds_read_b128 v[216:219], v181 offset:7168
	global_load_lds_dwordx4 v[2:3], off
	v_lshl_add_u64 v[2:3], s[44:45], 0, v[154:155]
	s_mov_b32 m0, s74
	s_nop 0
	global_load_lds_dwordx4 v[2:3], off
	ds_read_b128 v[232:235], v169
	ds_read_b128 v[236:239], v170
	ds_read_b128 v[240:243], v171
	ds_read_b128 v[244:247], v172
	s_waitcnt lgkmcnt(4)
	s_waitcnt vmcnt(8)
	s_barrier
	s_waitcnt lgkmcnt(0)
	s_setprio 1
	s_waitcnt lgkmcnt(0)
	v_mfma_f32_16x16x128_f8f6f4 v[142:145], v[10:17], v[188:195], v[142:145]
	v_mfma_f32_16x16x128_f8f6f4 v[138:141], v[156:163], v[188:195], v[138:141]
	v_mfma_f32_16x16x128_f8f6f4 v[134:137], v[10:17], v[196:203], v[134:137]
	v_mfma_f32_16x16x128_f8f6f4 v[130:133], v[156:163], v[196:203], v[130:133]
	v_mfma_f32_16x16x128_f8f6f4 v[122:125], v[10:17], v[204:211], v[122:125]
	v_mfma_f32_16x16x128_f8f6f4 v[114:117], v[156:163], v[204:211], v[114:117]
	v_mfma_f32_16x16x128_f8f6f4 v[106:109], v[10:17], v[212:219], v[106:109]
	v_mfma_f32_16x16x128_f8f6f4 v[98:101], v[156:163], v[212:219], v[98:101]
	v_mfma_f32_16x16x128_f8f6f4 v[78:81], v[232:239], v[188:195], v[78:81]
	v_mfma_f32_16x16x128_f8f6f4 v[74:77], v[240:247], v[188:195], v[74:77]
	v_mfma_f32_16x16x128_f8f6f4 v[70:73], v[232:239], v[196:203], v[70:73]
	v_mfma_f32_16x16x128_f8f6f4 v[66:69], v[240:247], v[196:203], v[66:69]
	v_mfma_f32_16x16x128_f8f6f4 v[62:65], v[232:239], v[204:211], v[62:65]
	v_mfma_f32_16x16x128_f8f6f4 v[58:61], v[240:247], v[204:211], v[58:61]
	v_mfma_f32_16x16x128_f8f6f4 v[46:49], v[232:239], v[212:219], v[46:49]
	v_mfma_f32_16x16x128_f8f6f4 v[42:45], v[240:247], v[212:219], v[42:45]
	s_setprio 0
	s_mov_b32 m0, s55
	v_lshl_add_u64 v[2:3], s[42:43], 0, v[146:147]
	s_barrier
	ds_read_b128 v[188:191], v181 offset:16384
	ds_read_b128 v[192:195], v181 offset:17408
	ds_read_b128 v[196:199], v181 offset:18432
	ds_read_b128 v[200:203], v181 offset:19456
	ds_read_b128 v[204:207], v181 offset:20480
	ds_read_b128 v[208:211], v181 offset:21504
	ds_read_b128 v[212:215], v181 offset:22528
	ds_read_b128 v[216:219], v181 offset:23552
	global_load_lds_dwordx4 v[2:3], off
	v_lshl_add_u64 v[4:5], s[42:43], 0, v[148:149]
	s_mov_b32 m0, s58
	s_nop 0
	global_load_lds_dwordx4 v[4:5], off
	s_mov_b32 m0, s56
	v_lshl_add_u64 v[6:7], s[6:7], 0, v[0:1]
	global_load_lds_dwordx4 v[6:7], off
	v_lshl_add_u64 v[8:9], s[6:7], 0, v[150:151]
	s_mov_b32 m0, s57
	s_nop 0
	global_load_lds_dwordx4 v[8:9], off
	s_barrier
	s_waitcnt lgkmcnt(0)
	s_setprio 1
	s_waitcnt lgkmcnt(0)
	v_mfma_f32_16x16x128_f8f6f4 v[126:129], v[10:17], v[188:195], v[126:129]
	v_mfma_f32_16x16x128_f8f6f4 v[118:121], v[156:163], v[188:195], v[118:121]
	v_mfma_f32_16x16x128_f8f6f4 v[110:113], v[10:17], v[196:203], v[110:113]
	v_mfma_f32_16x16x128_f8f6f4 v[102:105], v[156:163], v[196:203], v[102:105]
	v_mfma_f32_16x16x128_f8f6f4 v[94:97], v[10:17], v[204:211], v[94:97]
	v_mfma_f32_16x16x128_f8f6f4 v[90:93], v[156:163], v[204:211], v[90:93]
	v_mfma_f32_16x16x128_f8f6f4 v[86:89], v[10:17], v[212:219], v[86:89]
	v_mfma_f32_16x16x128_f8f6f4 v[82:85], v[156:163], v[212:219], v[82:85]
	s_setprio 0
	s_barrier
	s_add_u32 s80, s6, 0x20000
	s_addc_u32 s81, s7, 0
	s_mov_b32 m0, s59
	v_lshl_add_u64 v[10:11], s[80:81], 0, v[0:1]
	global_load_lds_dwordx4 v[10:11], off
	v_lshl_add_u64 v[10:11], s[80:81], 0, v[150:151]
	s_mov_b32 m0, s60
	s_nop 0
	global_load_lds_dwordx4 v[10:11], off
	s_waitcnt vmcnt(8)
	s_barrier
	s_setprio 1
	v_mfma_f32_16x16x128_f8f6f4 v[54:57], v[232:239], v[188:195], v[54:57]
	v_mfma_f32_16x16x128_f8f6f4 v[50:53], v[240:247], v[188:195], v[50:53]
	v_mfma_f32_16x16x128_f8f6f4 v[38:41], v[232:239], v[196:203], v[38:41]
	v_mfma_f32_16x16x128_f8f6f4 v[34:37], v[240:247], v[196:203], v[34:37]
	v_mfma_f32_16x16x128_f8f6f4 v[30:33], v[232:239], v[204:211], v[30:33]
	v_mfma_f32_16x16x128_f8f6f4 v[26:29], v[240:247], v[204:211], v[26:29]
	v_mfma_f32_16x16x128_f8f6f4 v[22:25], v[232:239], v[212:219], v[22:25]
	v_mfma_f32_16x16x128_f8f6f4 v[18:21], v[240:247], v[212:219], v[18:21]
	s_setprio 0
	s_barrier
	ds_read_b128 v[10:13], v173
	ds_read_b128 v[14:17], v174
	ds_read_b128 v[156:159], v175
	ds_read_b128 v[160:163], v176
	s_add_u32 s42, s42, 0x20000
	s_addc_u32 s43, s43, 0
	s_mov_b32 m0, s61
	v_lshl_add_u64 v[182:183], s[42:43], 0, v[146:147]
	ds_read_b128 v[188:191], v181 offset:32768
	ds_read_b128 v[192:195], v181 offset:33792
	ds_read_b128 v[196:199], v181 offset:34816
	ds_read_b128 v[200:203], v181 offset:35840
	ds_read_b128 v[204:207], v181 offset:36864
	ds_read_b128 v[208:211], v181 offset:37888
	ds_read_b128 v[212:215], v181 offset:38912
	ds_read_b128 v[216:219], v181 offset:39936
	global_load_lds_dwordx4 v[182:183], off
	v_lshl_add_u64 v[182:183], s[42:43], 0, v[148:149]
	s_mov_b32 m0, s62
	s_nop 0
	global_load_lds_dwordx4 v[182:183], off
	ds_read_b128 v[232:235], v177
	ds_read_b128 v[236:239], v178
	ds_read_b128 v[240:243], v179
	ds_read_b128 v[244:247], v180
	s_waitcnt lgkmcnt(4)
	s_waitcnt vmcnt(8)
	s_barrier
	s_waitcnt lgkmcnt(0)
	s_setprio 1
	s_waitcnt lgkmcnt(0)
	v_mfma_f32_16x16x128_f8f6f4 v[142:145], v[10:17], v[188:195], v[142:145]
	v_mfma_f32_16x16x128_f8f6f4 v[138:141], v[156:163], v[188:195], v[138:141]
	v_mfma_f32_16x16x128_f8f6f4 v[134:137], v[10:17], v[196:203], v[134:137]
	v_mfma_f32_16x16x128_f8f6f4 v[130:133], v[156:163], v[196:203], v[130:133]
	v_mfma_f32_16x16x128_f8f6f4 v[122:125], v[10:17], v[204:211], v[122:125]
	v_mfma_f32_16x16x128_f8f6f4 v[114:117], v[156:163], v[204:211], v[114:117]
	v_mfma_f32_16x16x128_f8f6f4 v[106:109], v[10:17], v[212:219], v[106:109]
	v_mfma_f32_16x16x128_f8f6f4 v[98:101], v[156:163], v[212:219], v[98:101]
	v_mfma_f32_16x16x128_f8f6f4 v[78:81], v[232:239], v[188:195], v[78:81]
	v_mfma_f32_16x16x128_f8f6f4 v[74:77], v[240:247], v[188:195], v[74:77]
	v_mfma_f32_16x16x128_f8f6f4 v[70:73], v[232:239], v[196:203], v[70:73]
	v_mfma_f32_16x16x128_f8f6f4 v[66:69], v[240:247], v[196:203], v[66:69]
	v_mfma_f32_16x16x128_f8f6f4 v[62:65], v[232:239], v[204:211], v[62:65]
	v_mfma_f32_16x16x128_f8f6f4 v[58:61], v[240:247], v[204:211], v[58:61]
	v_mfma_f32_16x16x128_f8f6f4 v[46:49], v[232:239], v[212:219], v[46:49]
	v_mfma_f32_16x16x128_f8f6f4 v[42:45], v[240:247], v[212:219], v[42:45]
	s_setprio 0
	s_mov_b32 m0, s69
	v_lshl_add_u64 v[2:3], v[2:3], 0, s[24:25]
	s_barrier
	ds_read_b128 v[188:191], v181 offset:49152
	ds_read_b128 v[192:195], v181 offset:50176
	ds_read_b128 v[196:199], v181 offset:51200
	ds_read_b128 v[200:203], v181 offset:52224
	ds_read_b128 v[204:207], v181 offset:53248
	ds_read_b128 v[208:211], v181 offset:54272
	ds_read_b128 v[212:215], v181 offset:55296
	ds_read_b128 v[216:219], v181 offset:56320
	global_load_lds_dwordx4 v[2:3], off
	v_lshl_add_u64 v[2:3], v[4:5], 0, s[24:25]
	s_mov_b32 m0, s70
	s_nop 0
	global_load_lds_dwordx4 v[2:3], off
	s_mov_b32 m0, s67
	v_lshl_add_u64 v[6:7], v[6:7], 0, s[24:25]
	global_load_lds_dwordx4 v[6:7], off
	v_lshl_add_u64 v[6:7], v[8:9], 0, s[24:25]
	s_mov_b32 m0, s68
	s_nop 0
	global_load_lds_dwordx4 v[6:7], off
	s_barrier
	s_waitcnt lgkmcnt(0)
	s_setprio 1
	s_waitcnt lgkmcnt(0)
	v_mfma_f32_16x16x128_f8f6f4 v[126:129], v[10:17], v[188:195], v[126:129]
	v_mfma_f32_16x16x128_f8f6f4 v[118:121], v[156:163], v[188:195], v[118:121]
	v_mfma_f32_16x16x128_f8f6f4 v[110:113], v[10:17], v[196:203], v[110:113]
	v_mfma_f32_16x16x128_f8f6f4 v[102:105], v[156:163], v[196:203], v[102:105]
	v_mfma_f32_16x16x128_f8f6f4 v[94:97], v[10:17], v[204:211], v[94:97]
	v_mfma_f32_16x16x128_f8f6f4 v[90:93], v[156:163], v[204:211], v[90:93]
	v_mfma_f32_16x16x128_f8f6f4 v[86:89], v[10:17], v[212:219], v[86:89]
	v_mfma_f32_16x16x128_f8f6f4 v[82:85], v[156:163], v[212:219], v[82:85]
	s_setprio 0
	s_barrier
	s_add_u32 s6, s6, 0x20080
	s_addc_u32 s7, s7, 0
	s_mov_b32 m0, s71
	v_lshl_add_u64 v[2:3], s[6:7], 0, v[0:1]
	global_load_lds_dwordx4 v[2:3], off
	v_lshl_add_u64 v[2:3], s[6:7], 0, v[150:151]
	s_mov_b32 m0, s72
	s_nop 0
	global_load_lds_dwordx4 v[2:3], off
	s_waitcnt vmcnt(8)
	s_barrier
	s_setprio 1
	v_mfma_f32_16x16x128_f8f6f4 v[54:57], v[232:239], v[188:195], v[54:57]
	v_mfma_f32_16x16x128_f8f6f4 v[50:53], v[240:247], v[188:195], v[50:53]
	v_mfma_f32_16x16x128_f8f6f4 v[38:41], v[232:239], v[196:203], v[38:41]
	v_mfma_f32_16x16x128_f8f6f4 v[34:37], v[240:247], v[196:203], v[34:37]
	v_mfma_f32_16x16x128_f8f6f4 v[30:33], v[232:239], v[204:211], v[30:33]
	v_mfma_f32_16x16x128_f8f6f4 v[26:29], v[240:247], v[204:211], v[26:29]
	v_mfma_f32_16x16x128_f8f6f4 v[22:25], v[232:239], v[212:219], v[22:25]
	v_mfma_f32_16x16x128_f8f6f4 v[18:21], v[240:247], v[212:219], v[18:21]
	s_setprio 0
	s_add_i32 s78, s78, 2
	s_add_u32 s44, s44, 0x100
	s_addc_u32 s45, s45, 0
	s_add_u32 s76, s76, 0x100
	s_addc_u32 s77, s77, 0
	s_cmp_gt_u32 s78, 5
	s_barrier
	s_cbranch_scc1 .LBB0_1782

.LBB0_1915:
	s_lshl_b32 s10, s10, 12
	s_lshl_b32 s55, s11, 13
	s_and_b32 s12, s10, 0x3000
	s_add_u32 s10, s4, 0xbc000000
	s_addc_u32 s11, s5, 0
	s_add_u32 s56, s4, 0x3c800000
	s_addc_u32 s57, s5, 0
	s_add_i32 s58, s47, 0x18000
	v_lshl_add_u64 v[8:9], v[8:9], 0, s[24:25]
	s_mov_b32 m0, s58
	s_add_i32 s59, s47, 0x1a000
	s_waitcnt vmcnt(2)
	s_barrier
	global_load_lds_dwordx4 v[8:9], off
	v_lshl_add_u64 v[6:7], v[6:7], 0, s[24:25]
	s_mov_b32 m0, s59
	s_add_i32 s60, s47, 0x8000
	s_add_i32 s61, s47, 0xa000
	global_load_lds_dwordx4 v[6:7], off
	v_lshl_add_u64 v[4:5], v[4:5], 0, s[24:25]
	s_mov_b32 m0, s60
	s_add_u32 s4, s40, 0x20080
	global_load_lds_dwordx4 v[4:5], off
	v_lshl_add_u64 v[2:3], v[2:3], 0, s[24:25]
	s_mov_b32 m0, s61
	s_addc_u32 s5, s41, 0
	s_add_i32 s62, s47, 0x1c000
	global_load_lds_dwordx4 v[2:3], off
	v_lshl_add_u64 v[2:3], s[4:5], 0, v[200:201]
	s_mov_b32 m0, s62
	s_add_i32 s63, s47, 0x1e000
	global_load_lds_dwordx4 v[2:3], off
	v_lshl_add_u64 v[2:3], s[4:5], 0, v[196:197]
	s_mov_b32 m0, s63
	s_cmp_lg_u64 s[8:9], 0
	global_load_lds_dwordx4 v[2:3], off
	v_and_b32_e32 v2, 15, v10
	v_and_b32_e32 v3, 48, v10
	v_lshl_or_b32 v2, v2, 6, v3
	v_lshlrev_b32_e32 v3, 2, v10
	v_and_b32_e32 v3, 32, v3
	v_xad_u32 v232, v2, v3, 0
	v_add_u32_e32 v2, s12, v232
	v_add_u32_e32 v233, 0x10000, v2
	v_add_u32_e32 v234, 0x10400, v2
	v_add_u32_e32 v235, 0x10800, v2
	v_add_u32_e32 v236, 0x10c00, v2
	v_add_u32_e32 v237, 0x14000, v2
	v_add_u32_e32 v238, 0x14400, v2
	v_add_u32_e32 v239, 0x14800, v2
	v_add_u32_e32 v240, 0x14c00, v2
	v_add_u32_e32 v241, 0x18000, v2
	v_add_u32_e32 v242, 0x18400, v2
	v_add_u32_e32 v243, 0x18800, v2
	v_add_u32_e32 v244, 0x18c00, v2
	v_add_u32_e32 v245, 0x1c000, v2
	v_add_u32_e32 v246, 0x1c400, v2
	v_add_u32_e32 v247, 0x1c800, v2
	v_add_u32_e32 v248, 0x1cc00, v2
	v_lshlrev_b32_e32 v2, 13, v14
	v_and_b32_e32 v2, 0xffffc000, v2
	v_lshl_add_u32 v2, v13, 10, v2
	v_and_b32_e32 v3, 1, v14
	v_lshl_or_b32 v2, v3, 6, v2
	v_lshl_add_u32 v204, v15, 1, v2
	v_lshlrev_b32_e32 v2, 13, v0
	v_and_b32_e32 v2, 0xffffc000, v2
	s_waitcnt vmcnt(6)
	v_lshl_add_u32 v2, v11, 10, v2
	v_and_b32_e32 v0, 1, v0
	v_lshl_or_b32 v0, v0, 6, v2
	v_readlane_b32 s4, v253, 57
	s_cselect_b64 s[12:13], -1, 0
	v_mov_b32_e32 v205, v1
	v_lshl_add_u32 v206, v12, 1, v0
	v_mov_b32_e32 v207, v1
	s_mov_b32 s64, 0
	v_readlane_b32 s65, v253, 29
	s_mov_b32 s66, s4
	s_barrier
	v_readlane_b32 s5, v253, 58
	s_branch .LBB0_1918

.LBB0_1925:
	ds_read_b128 v[2:5], v233
	ds_read_b128 v[6:9], v234
	ds_read_b128 v[10:13], v235
	ds_read_b128 v[14:17], v236
	s_add_u32 s40, s6, 0xfffe0080
	s_addc_u32 s41, s7, -1
	s_cmp_eq_u32 s71, 4
	s_cselect_b32 s43, s21, s41
	s_cselect_b32 s42, s67, s40
	s_cselect_b32 s41, s15, s70
	s_cselect_b32 s40, s68, s69
	v_add_u32_e32 v0, s55, v232
	v_lshl_add_u64 v[146:147], s[6:7], 0, v[204:205]
	s_add_i32 m0, s47, 0xc000
	ds_read_b128 v[150:153], v0
	ds_read_b128 v[154:157], v0 offset:1024
	ds_read_b128 v[158:161], v0 offset:2048
	ds_read_b128 v[162:165], v0 offset:3072
	ds_read_b128 v[166:169], v0 offset:4096
	ds_read_b128 v[170:173], v0 offset:5120
	ds_read_b128 v[174:177], v0 offset:6144
	ds_read_b128 v[178:181], v0 offset:7168
	global_load_lds_dwordx4 v[146:147], off
	v_lshl_add_u64 v[146:147], s[6:7], 0, v[206:207]
	s_add_i32 m0, s47, 0xe000
	s_nop 0
	global_load_lds_dwordx4 v[146:147], off
	ds_read_b128 v[188:191], v237
	ds_read_b128 v[192:195], v238
	ds_read_b128 v[208:211], v239
	ds_read_b128 v[212:215], v240
	s_waitcnt lgkmcnt(4)
	s_waitcnt vmcnt(8)
	s_barrier
	s_waitcnt lgkmcnt(0)
	s_setprio 1
	s_waitcnt lgkmcnt(0)
	v_mfma_f32_16x16x128_f8f6f4 v[142:145], v[2:9], v[150:157], v[142:145]
	v_mfma_f32_16x16x128_f8f6f4 v[138:141], v[10:17], v[150:157], v[138:141]
	v_mfma_f32_16x16x128_f8f6f4 v[126:129], v[2:9], v[158:165], v[126:129]
	v_mfma_f32_16x16x128_f8f6f4 v[122:125], v[10:17], v[158:165], v[122:125]
	v_mfma_f32_16x16x128_f8f6f4 v[110:113], v[2:9], v[166:173], v[110:113]
	v_mfma_f32_16x16x128_f8f6f4 v[106:109], v[10:17], v[166:173], v[106:109]
	v_mfma_f32_16x16x128_f8f6f4 v[94:97], v[2:9], v[174:181], v[94:97]
	v_mfma_f32_16x16x128_f8f6f4 v[90:93], v[10:17], v[174:181], v[90:93]
	v_mfma_f32_16x16x128_f8f6f4 v[134:137], v[188:195], v[150:157], v[134:137]
	v_mfma_f32_16x16x128_f8f6f4 v[130:133], v[208:215], v[150:157], v[130:133]
	v_mfma_f32_16x16x128_f8f6f4 v[118:121], v[188:195], v[158:165], v[118:121]
	v_mfma_f32_16x16x128_f8f6f4 v[114:117], v[208:215], v[158:165], v[114:117]
	v_mfma_f32_16x16x128_f8f6f4 v[102:105], v[188:195], v[166:173], v[102:105]
	v_mfma_f32_16x16x128_f8f6f4 v[98:101], v[208:215], v[166:173], v[98:101]
	v_mfma_f32_16x16x128_f8f6f4 v[86:89], v[188:195], v[174:181], v[86:89]
	v_mfma_f32_16x16x128_f8f6f4 v[82:85], v[208:215], v[174:181], v[82:85]
	s_setprio 0
	s_mov_b32 m0, s47
	v_lshl_add_u64 v[150:151], s[42:43], 0, v[202:203]
	s_barrier
	ds_read_b128 v[154:157], v0 offset:16384
	ds_read_b128 v[158:161], v0 offset:17408
	ds_read_b128 v[162:165], v0 offset:18432
	ds_read_b128 v[166:169], v0 offset:19456
	ds_read_b128 v[170:173], v0 offset:20480
	ds_read_b128 v[174:177], v0 offset:21504
	ds_read_b128 v[178:181], v0 offset:22528
	ds_read_b128 v[182:185], v0 offset:23552
	global_load_lds_dwordx4 v[150:151], off
	v_lshl_add_u64 v[152:153], s[42:43], 0, v[198:199]
	s_mov_b32 m0, s50
	s_nop 0
	global_load_lds_dwordx4 v[152:153], off
	s_mov_b32 m0, s48
	v_lshl_add_u64 v[146:147], s[40:41], 0, v[200:201]
	global_load_lds_dwordx4 v[146:147], off
	v_lshl_add_u64 v[148:149], s[40:41], 0, v[196:197]
	s_mov_b32 m0, s49
	s_nop 0
	global_load_lds_dwordx4 v[148:149], off
	s_barrier
	s_waitcnt lgkmcnt(0)
	s_setprio 1
	s_waitcnt lgkmcnt(0)
	v_mfma_f32_16x16x128_f8f6f4 v[78:81], v[2:9], v[154:161], v[78:81]
	v_mfma_f32_16x16x128_f8f6f4 v[74:77], v[10:17], v[154:161], v[74:77]
	v_mfma_f32_16x16x128_f8f6f4 v[62:65], v[2:9], v[162:169], v[62:65]
	v_mfma_f32_16x16x128_f8f6f4 v[58:61], v[10:17], v[162:169], v[58:61]
	v_mfma_f32_16x16x128_f8f6f4 v[46:49], v[2:9], v[170:177], v[46:49]
	v_mfma_f32_16x16x128_f8f6f4 v[42:45], v[10:17], v[170:177], v[42:45]
	v_mfma_f32_16x16x128_f8f6f4 v[30:33], v[2:9], v[178:185], v[30:33]
	v_mfma_f32_16x16x128_f8f6f4 v[26:29], v[10:17], v[178:185], v[26:29]
	s_setprio 0
	s_barrier
	s_add_u32 s72, s40, 0x20000
	s_addc_u32 s73, s41, 0
	s_mov_b32 m0, s51
	v_lshl_add_u64 v[2:3], s[72:73], 0, v[200:201]
	global_load_lds_dwordx4 v[2:3], off
	v_lshl_add_u64 v[2:3], s[72:73], 0, v[196:197]
	s_mov_b32 m0, s52
	s_nop 0
	global_load_lds_dwordx4 v[2:3], off
	s_waitcnt vmcnt(8)
	s_barrier
	s_setprio 1
	v_mfma_f32_16x16x128_f8f6f4 v[70:73], v[188:195], v[154:161], v[70:73]
	v_mfma_f32_16x16x128_f8f6f4 v[66:69], v[208:215], v[154:161], v[66:69]
	v_mfma_f32_16x16x128_f8f6f4 v[54:57], v[188:195], v[162:169], v[54:57]
	v_mfma_f32_16x16x128_f8f6f4 v[50:53], v[208:215], v[162:169], v[50:53]
	v_mfma_f32_16x16x128_f8f6f4 v[38:41], v[188:195], v[170:177], v[38:41]
	v_mfma_f32_16x16x128_f8f6f4 v[34:37], v[208:215], v[170:177], v[34:37]
	v_mfma_f32_16x16x128_f8f6f4 v[22:25], v[188:195], v[178:185], v[22:25]
	v_mfma_f32_16x16x128_f8f6f4 v[18:21], v[208:215], v[178:185], v[18:21]
	s_setprio 0
	s_barrier
	ds_read_b128 v[2:5], v241
	ds_read_b128 v[6:9], v242
	ds_read_b128 v[10:13], v243
	ds_read_b128 v[14:17], v244
	s_add_u32 s42, s42, 0x20000
	s_addc_u32 s43, s43, 0
	s_mov_b32 m0, s53
	v_lshl_add_u64 v[188:189], s[42:43], 0, v[202:203]
	ds_read_b128 v[154:157], v0 offset:32768
	ds_read_b128 v[158:161], v0 offset:33792
	ds_read_b128 v[162:165], v0 offset:34816
	ds_read_b128 v[166:169], v0 offset:35840
	ds_read_b128 v[170:173], v0 offset:36864
	ds_read_b128 v[174:177], v0 offset:37888
	ds_read_b128 v[178:181], v0 offset:38912
	ds_read_b128 v[182:185], v0 offset:39936
	global_load_lds_dwordx4 v[188:189], off
	v_lshl_add_u64 v[188:189], s[42:43], 0, v[198:199]
	s_mov_b32 m0, s54
	s_nop 0
	global_load_lds_dwordx4 v[188:189], off
	ds_read_b128 v[188:191], v245
	ds_read_b128 v[192:195], v246
	ds_read_b128 v[208:211], v247
	ds_read_b128 v[212:215], v248
	s_waitcnt lgkmcnt(4)
	s_waitcnt vmcnt(8)
	s_barrier
	s_waitcnt lgkmcnt(0)
	s_setprio 1
	s_waitcnt lgkmcnt(0)
	v_mfma_f32_16x16x128_f8f6f4 v[142:145], v[2:9], v[154:161], v[142:145]
	v_mfma_f32_16x16x128_f8f6f4 v[138:141], v[10:17], v[154:161], v[138:141]
	v_mfma_f32_16x16x128_f8f6f4 v[126:129], v[2:9], v[162:169], v[126:129]
	v_mfma_f32_16x16x128_f8f6f4 v[122:125], v[10:17], v[162:169], v[122:125]
	v_mfma_f32_16x16x128_f8f6f4 v[110:113], v[2:9], v[170:177], v[110:113]
	v_mfma_f32_16x16x128_f8f6f4 v[106:109], v[10:17], v[170:177], v[106:109]
	v_mfma_f32_16x16x128_f8f6f4 v[94:97], v[2:9], v[178:185], v[94:97]
	v_mfma_f32_16x16x128_f8f6f4 v[90:93], v[10:17], v[178:185], v[90:93]
	v_mfma_f32_16x16x128_f8f6f4 v[134:137], v[188:195], v[154:161], v[134:137]
	v_mfma_f32_16x16x128_f8f6f4 v[130:133], v[208:215], v[154:161], v[130:133]
	v_mfma_f32_16x16x128_f8f6f4 v[118:121], v[188:195], v[162:169], v[118:121]
	v_mfma_f32_16x16x128_f8f6f4 v[114:117], v[208:215], v[162:169], v[114:117]
	v_mfma_f32_16x16x128_f8f6f4 v[102:105], v[188:195], v[170:177], v[102:105]
	v_mfma_f32_16x16x128_f8f6f4 v[98:101], v[208:215], v[170:177], v[98:101]
	v_mfma_f32_16x16x128_f8f6f4 v[86:89], v[188:195], v[178:185], v[86:89]
	v_mfma_f32_16x16x128_f8f6f4 v[82:85], v[208:215], v[178:185], v[82:85]
	s_setprio 0
	s_barrier
	ds_read_b128 v[154:157], v0 offset:49152
	ds_read_b128 v[158:161], v0 offset:50176
	ds_read_b128 v[162:165], v0 offset:51200
	ds_read_b128 v[166:169], v0 offset:52224
	ds_read_b128 v[170:173], v0 offset:53248
	ds_read_b128 v[174:177], v0 offset:54272
	ds_read_b128 v[178:181], v0 offset:55296
	ds_read_b128 v[182:185], v0 offset:56320
	s_mov_b32 m0, s58
	v_lshl_add_u64 v[146:147], v[146:147], 0, s[24:25]
	global_load_lds_dwordx4 v[146:147], off
	v_lshl_add_u64 v[146:147], v[148:149], 0, s[24:25]
	s_mov_b32 m0, s59
	s_nop 0
	global_load_lds_dwordx4 v[146:147], off
	s_mov_b32 m0, s60
	v_lshl_add_u64 v[146:147], v[150:151], 0, s[24:25]
	global_load_lds_dwordx4 v[146:147], off
	v_lshl_add_u64 v[146:147], v[152:153], 0, s[24:25]
	s_mov_b32 m0, s61
	s_nop 0
	global_load_lds_dwordx4 v[146:147], off
	s_barrier
	s_waitcnt lgkmcnt(0)
	s_setprio 1
	s_waitcnt lgkmcnt(0)
	v_mfma_f32_16x16x128_f8f6f4 v[78:81], v[2:9], v[154:161], v[78:81]
	v_mfma_f32_16x16x128_f8f6f4 v[74:77], v[10:17], v[154:161], v[74:77]
	v_mfma_f32_16x16x128_f8f6f4 v[62:65], v[2:9], v[162:169], v[62:65]
	v_mfma_f32_16x16x128_f8f6f4 v[58:61], v[10:17], v[162:169], v[58:61]
	v_mfma_f32_16x16x128_f8f6f4 v[46:49], v[2:9], v[170:177], v[46:49]
	v_mfma_f32_16x16x128_f8f6f4 v[42:45], v[10:17], v[170:177], v[42:45]
	v_mfma_f32_16x16x128_f8f6f4 v[30:33], v[2:9], v[178:185], v[30:33]
	v_mfma_f32_16x16x128_f8f6f4 v[26:29], v[10:17], v[178:185], v[26:29]
	s_setprio 0
	s_barrier
	s_add_u32 s40, s40, 0x20080
	s_addc_u32 s41, s41, 0
	s_mov_b32 m0, s62
	v_lshl_add_u64 v[2:3], s[40:41], 0, v[200:201]
	global_load_lds_dwordx4 v[2:3], off
	v_lshl_add_u64 v[2:3], s[40:41], 0, v[196:197]
	s_mov_b32 m0, s63
	s_nop 0
	global_load_lds_dwordx4 v[2:3], off
	s_waitcnt vmcnt(8)
	s_barrier
	s_setprio 1
	v_mfma_f32_16x16x128_f8f6f4 v[70:73], v[188:195], v[154:161], v[70:73]
	v_mfma_f32_16x16x128_f8f6f4 v[66:69], v[208:215], v[154:161], v[66:69]
	v_mfma_f32_16x16x128_f8f6f4 v[54:57], v[188:195], v[162:169], v[54:57]
	v_mfma_f32_16x16x128_f8f6f4 v[50:53], v[208:215], v[162:169], v[50:53]
	v_mfma_f32_16x16x128_f8f6f4 v[38:41], v[188:195], v[170:177], v[38:41]
	v_mfma_f32_16x16x128_f8f6f4 v[34:37], v[208:215], v[170:177], v[34:37]
	v_mfma_f32_16x16x128_f8f6f4 v[22:25], v[188:195], v[178:185], v[22:25]
	v_mfma_f32_16x16x128_f8f6f4 v[18:21], v[208:215], v[178:185], v[18:21]
	s_setprio 0
	s_add_i32 s71, s71, 2
	s_add_u32 s6, s6, 0x100
	s_addc_u32 s7, s7, 0
	s_add_u32 s69, s69, 0x100
	s_addc_u32 s70, s70, 0
	s_cmp_gt_u32 s71, 5
	s_barrier
	s_cbranch_scc0 .LBB0_1925
	v_readlane_b32 s21, v252, 52
	v_readlane_b32 s6, v252, 51
	s_nop 15
	s_nop 15
	v_mbcnt_lo_u32_b32 v0, -1, 0
	v_mbcnt_hi_u32_b32 v0, -1, v0
	s_lshl_b32 s42, s6, 6
	s_lshl_b32 s6, s65, 8
	s_ashr_i32 s7, s6, 31
	s_lshl_b32 s40, s21, 5
	s_lshl_b32 s15, s66, 8
	s_ashr_i32 s41, s40, 31
	s_lshl_b64 s[66:67], s[6:7], 1
	s_add_u32 s21, s10, s66
	s_addc_u32 s43, s11, s67
	s_lshl_b64 s[68:69], s[40:41], 1
	s_add_u32 s70, s21, s68
	s_addc_u32 s71, s43, s69
	s_add_u32 s21, s56, s66
	v_and_b32_e32 v249, 15, v0
	v_lshrrev_b32_e32 v0, 1, v0
	s_addc_u32 s43, s57, s67
	v_and_b32_e32 v217, 24, v0
	s_add_u32 s66, s21, s68
	v_lshlrev_b32_e32 v0, 1, v217
	s_addc_u32 s67, s43, s69
	v_or_b32_e32 v2, s15, v249
	v_lshl_add_u64 v[210:211], s[70:71], 0, v[0:1]
	v_lshl_add_u64 v[212:213], s[66:67], 0, v[0:1]
	v_or_b32_e32 v0, s42, v249
	v_add_u32_e32 v2, s42, v2
	v_add_u32_e32 v216, s15, v0
	v_ashrrev_i32_e32 v3, 31, v2
	v_or_b32_e32 v214, 32, v216
	v_lshlrev_b64 v[4:5], 11, v[2:3]
	v_ashrrev_i32_e32 v215, 31, v214
	v_lshl_add_u64 v[6:7], v[210:211], 0, v[4:5]
	v_lshl_add_u64 v[4:5], v[212:213], 0, v[4:5]
	v_lshlrev_b64 v[8:9], 11, v[214:215]
	global_load_dwordx4 v[188:191], v[6:7], off
	global_load_dwordx4 v[192:195], v[4:5], off
	v_lshl_add_u64 v[10:11], v[210:211], 0, v[8:9]
	v_lshl_add_u64 v[8:9], v[212:213], 0, v[8:9]
	global_load_dwordx4 v[182:185], v[6:7], off offset:256
	global_load_dwordx4 v[178:181], v[4:5], off offset:256
	global_load_dwordx4 v[166:169], v[10:11], off
	global_load_dwordx4 v[158:161], v[10:11], off offset:256
	global_load_dwordx4 v[162:165], v[8:9], off
	global_load_dwordx4 v[154:157], v[8:9], off offset:256
	v_or_b32_e32 v2, 16, v2
	v_or_b32_e32 v6, 48, v216
	v_ashrrev_i32_e32 v3, 31, v2
	v_ashrrev_i32_e32 v7, 31, v6
	v_lshlrev_b64 v[2:3], 11, v[2:3]
	v_lshlrev_b64 v[6:7], 11, v[6:7]
	v_lshl_add_u64 v[4:5], v[210:211], 0, v[2:3]
	v_lshl_add_u64 v[2:3], v[212:213], 0, v[2:3]
	v_lshl_add_u64 v[8:9], v[210:211], 0, v[6:7]
	v_lshl_add_u64 v[208:209], v[212:213], 0, v[6:7]
	global_load_dwordx4 v[174:177], v[4:5], off
	global_load_dwordx4 v[14:17], v[4:5], off offset:256
	global_load_dwordx4 v[170:173], v[2:3], off
	global_load_dwordx4 v[10:13], v[2:3], off offset:256
	global_load_dwordx4 v[150:153], v[8:9], off
	s_nop 0
	global_load_dwordx4 v[6:9], v[8:9], off offset:256
	s_nop 0
	global_load_dwordx4 v[146:149], v[208:209], off
	global_load_dwordx4 v[2:5], v[208:209], off offset:256
	v_pk_mul_f32 v[144:145], v[144:145], s[18:19] op_sel_hi:[1,0]
	v_pk_mul_f32 v[142:143], v[142:143], s[18:19] op_sel_hi:[1,0]
	v_pk_mul_f32 v[140:141], v[140:141], s[18:19] op_sel_hi:[1,0]
	v_pk_mul_f32 v[138:139], v[138:139], s[18:19] op_sel_hi:[1,0]
	v_exp_f32_e32 v142, v142
	v_exp_f32_e32 v138, v138
	v_exp_f32_e32 v143, v143
	v_exp_f32_e32 v139, v139
	v_exp_f32_e32 v144, v144
	v_exp_f32_e32 v145, v145
	v_exp_f32_e32 v140, v140
	v_exp_f32_e32 v141, v141
	v_pk_add_f32 v[142:143], v[142:143], 1.0 op_sel_hi:[1,0]
	v_pk_add_f32 v[144:145], v[144:145], 1.0 op_sel_hi:[1,0]
	v_pk_add_f32 v[138:139], v[138:139], 1.0 op_sel_hi:[1,0]
	v_pk_add_f32 v[140:141], v[140:141], 1.0 op_sel_hi:[1,0]
	v_rcp_f32_e32 v142, v142
	v_rcp_f32_e32 v230, v138
	v_rcp_f32_e32 v143, v143
	v_rcp_f32_e32 v231, v139
	v_rcp_f32_e32 v138, v144
	v_rcp_f32_e32 v139, v145
	v_rcp_f32_e32 v144, v140
	v_rcp_f32_e32 v145, v141
	v_or_b32_e32 v208, s40, v217
	v_mov_b32_e32 v209, s41
	v_ashrrev_i32_e32 v217, 31, v216
	v_lshl_add_u64 v[208:209], v[208:209], 0, s[6:7]
	v_lshlrev_b64 v[216:217], 10, v[216:217]
	v_lshl_add_u64 v[220:221], v[216:217], 0, v[208:209]
	s_and_b64 vcc, exec, s[12:13]
	s_waitcnt vmcnt(0)
	v_lshlrev_b32_e32 v218, 16, v188
	v_and_b32_e32 v219, 0xffff0000, v188
	v_lshlrev_b32_e32 v188, 16, v189
	v_and_b32_e32 v189, 0xffff0000, v189
	v_lshlrev_b32_e32 v226, 16, v190
	v_and_b32_e32 v227, 0xffff0000, v190
	v_lshlrev_b32_e32 v190, 16, v191
	v_and_b32_e32 v191, 0xffff0000, v191
	v_lshlrev_b32_e32 v250, 16, v192
	v_and_b32_e32 v251, 0xffff0000, v192
	v_lshlrev_b32_e32 v192, 16, v193
	v_and_b32_e32 v193, 0xffff0000, v193
	v_lshlrev_b32_e32 v224, 16, v194
	v_and_b32_e32 v225, 0xffff0000, v194
	v_lshlrev_b32_e32 v194, 16, v195
	v_and_b32_e32 v195, 0xffff0000, v195
	v_pk_fma_f32 v[140:141], v[138:139], v[192:193], v[188:189]
	v_pk_fma_f32 v[138:139], v[142:143], v[250:251], v[218:219]
	v_pk_fma_f32 v[144:145], v[144:145], v[194:195], v[190:191]
	v_pk_fma_f32 v[142:143], v[230:231], v[224:225], v[226:227]
	v_lshl_add_u64 v[218:219], v[220:221], 2, s[8:9]
	s_cbranch_vccz .LBB0_1973
	global_store_dwordx4 v[218:219], v[138:141], off
	global_store_dwordx4 v[218:219], v[142:145], off offset:16
	v_mov_b64_e32 v[250:251], v[186:187]
	s_cbranch_execnz .LBB0_1929
